# conversion loops as a rotating 2-buffer pipeline over the 4 items of a claim (loads of item k+2 issued as soon as item k is stored), bit-identical
# speedup vs baseline: 1.0070x; 1.0030x over previous
; template <int DQK, int KB>
; __device__ __forceinline__ void qkt(f32x16& p0, f32x16& p1, const char* K_lds, int r32, int hi, const bf16x8* qr) {
;     constexpr int ROWB = DQK * 2, SHM_K = 64 * ROWB;
;     p0 = f32x16{}; p1 = f32x16{};
;     const char* kb[4];
; #pragma unroll
;     for (int dd = 0; dd < 4; ++dd) kb[dd] = K_lds + KB * SHM_K + r32 * ROWB + (((dd * 16 + hi * 8) * 2) ^ ((r32 & 7) << 4));
; #pragma unroll
;     for (int d0 = 0; d0 < DQK / 16; ++d0) { const char* a = kb[d0 & 3] + (d0 >> 2) * 128;
;         bf16x8 b0 = *reinterpret_cast<const bf16x8*>(a);
;         bf16x8 b1 = *reinterpret_cast<const bf16x8*>(a + 32 * ROWB);
;         p0 = __builtin_amdgcn_mfma_f32_32x32x16_bf16(b0, qr[d0], p0, 0, 0, 0);
;         p1 = __builtin_amdgcn_mfma_f32_32x32x16_bf16(b1, qr[d0], p1, 0, 0, 0); }
.LBB0_548:
	s_or_b64 exec, exec, s[8:9]
	v_readlane_b32 s8, v255, 18
	v_subrev_u32_e32 v132, s77, v134
	s_nop 0
	v_add_u32_e32 v2, s8, v134
	s_movk_i32 s8, 0x2200
	v_mad_i64_i32 v[2:3], s[8:9], v2, s8, v[140:141]
	global_load_dwordx4 v[126:129], v[2:3], off
	global_load_dwordx4 v[122:125], v[2:3], off offset:32
	global_load_dwordx4 v[118:121], v[2:3], off offset:64
	global_load_dwordx4 v[114:117], v[2:3], off offset:96
	global_load_dwordx4 v[110:113], v[2:3], off offset:128
	global_load_dwordx4 v[106:109], v[2:3], off offset:160
	global_load_dwordx4 v[102:105], v[2:3], off offset:192
	global_load_dwordx4 v[98:101], v[2:3], off offset:224
	s_cmp_gt_u32 s80, 1
	ds_read_b128 v[190:193], v166
	ds_read_b128 v[194:197], v166 offset:8192
	ds_read_b128 v[198:201], v167
	ds_read_b128 v[202:205], v167 offset:8192
	ds_read_b128 v[206:209], v168
	ds_read_b128 v[210:213], v168 offset:8192
	ds_read_b128 v[214:217], v169
	ds_read_b128 v[218:221], v169 offset:8192
	ds_read_b128 v[222:225], v166 offset:128
	ds_read_b128 v[226:229], v166 offset:8320
	ds_read_b128 v[230:233], v167 offset:128
	ds_read_b128 v[234:237], v167 offset:8320
	ds_read_b128 v[238:241], v168 offset:128
	s_waitcnt vmcnt(7) lgkmcnt(12)
	v_mfma_f32_32x32x16_bf16 v[18:33], v[190:193], v[126:129], 0
	ds_read_b128 v[242:245], v168 offset:8320
	s_waitcnt lgkmcnt(12)
	v_mfma_f32_32x32x16_bf16 v[2:17], v[194:197], v[126:129], 0
	ds_read_b128 v[246:249], v169 offset:128
	s_waitcnt vmcnt(6) lgkmcnt(12)
	v_mfma_f32_32x32x16_bf16 v[18:33], v[198:201], v[122:125], v[18:33]
	ds_read_b128 v[198:201], v169 offset:8320
	s_waitcnt lgkmcnt(12)
	v_mfma_f32_32x32x16_bf16 v[2:17], v[202:205], v[122:125], v[2:17]
	s_waitcnt vmcnt(5) lgkmcnt(11)
	v_mfma_f32_32x32x16_bf16 v[18:33], v[206:209], v[118:121], v[18:33]
	s_waitcnt lgkmcnt(10)
	v_mfma_f32_32x32x16_bf16 v[2:17], v[210:213], v[118:121], v[2:17]
	s_waitcnt vmcnt(4) lgkmcnt(9)
	v_mfma_f32_32x32x16_bf16 v[18:33], v[214:217], v[114:117], v[18:33]
	s_waitcnt lgkmcnt(8)
	v_mfma_f32_32x32x16_bf16 v[2:17], v[218:221], v[114:117], v[2:17]
	s_waitcnt vmcnt(3) lgkmcnt(7)
	v_mfma_f32_32x32x16_bf16 v[18:33], v[222:225], v[110:113], v[18:33]
	s_waitcnt lgkmcnt(6)
	v_mfma_f32_32x32x16_bf16 v[2:17], v[226:229], v[110:113], v[2:17]
	s_waitcnt vmcnt(2) lgkmcnt(5)
	v_mfma_f32_32x32x16_bf16 v[18:33], v[230:233], v[106:109], v[18:33]
	s_waitcnt lgkmcnt(4)
	v_mfma_f32_32x32x16_bf16 v[2:17], v[234:237], v[106:109], v[2:17]
	s_waitcnt vmcnt(1) lgkmcnt(3)
	v_mfma_f32_32x32x16_bf16 v[18:33], v[238:241], v[102:105], v[18:33]
	s_waitcnt lgkmcnt(2)
	v_mfma_f32_32x32x16_bf16 v[2:17], v[242:245], v[102:105], v[2:17]
	s_waitcnt vmcnt(0) lgkmcnt(1)
	v_mfma_f32_32x32x16_bf16 v[18:33], v[246:249], v[98:101], v[18:33]
	v_mov_b32_e32 v34, v151
	s_nop 0
	v_mul_f32_e32 v36, v34, v155
	v_fma_f32 v42, v34, s34, v36
	v_fma_f32 v43, v34, s35, v36
	v_fma_f32 v44, v34, s2, v36
	v_fma_f32 v45, v34, s3, v36
	v_pk_fma_f32 v[46:47], v[34:35], s[36:37], v[36:37] op_sel_hi:[0,1,0]
	s_waitcnt lgkmcnt(0)
	s_waitcnt lgkmcnt(0)
	v_mfma_f32_32x32x16_bf16 v[2:17], v[198:201], v[98:101], v[2:17]
	v_mov_b32_e32 v41, v34
	v_mul_f32_e32 v38, 0x42000000, v34
	v_fma_f32 v40, 0, v34, v36
	v_fmac_f32_e32 v41, v41, v155
	v_fma_f32 v48, v34, s38, v36
	v_fma_f32 v49, v34, s39, v36
	v_pk_fma_f32 v[50:51], v[34:35], s[40:41], v[36:37] op_sel_hi:[0,1,0]
	v_pk_fma_f32 v[52:53], v[34:35], s[42:43], v[36:37] op_sel_hi:[0,1,0]
	v_pk_fma_f32 v[34:35], v[34:35], s[44:45], v[36:37] op_sel_hi:[0,1,0]
	v_pk_add_f32 v[32:33], v[32:33], v[34:35]
	v_pk_add_f32 v[28:29], v[28:29], v[50:51]
	v_pk_add_f32 v[26:27], v[26:27], v[48:49]
	v_pk_add_f32 v[24:25], v[24:25], v[46:47]
	v_pk_add_f32 v[22:23], v[22:23], v[44:45]
	v_pk_add_f32 v[20:21], v[20:21], v[42:43]
	v_pk_add_f32 v[54:55], v[38:39], v[42:43] op_sel_hi:[0,1]
	v_pk_add_f32 v[44:45], v[38:39], v[44:45] op_sel_hi:[0,1]
	v_pk_add_f32 v[42:43], v[38:39], v[46:47] op_sel_hi:[0,1]
	v_pk_add_f32 v[46:47], v[38:39], v[48:49] op_sel_hi:[0,1]
	v_pk_add_f32 v[48:49], v[38:39], v[50:51] op_sel_hi:[0,1]
	v_pk_add_f32 v[36:37], v[38:39], v[52:53] op_sel_hi:[0,1]
	v_pk_add_f32 v[34:35], v[38:39], v[34:35] op_sel_hi:[0,1]
	v_pk_add_f32 v[50:51], v[38:39], v[40:41] op_sel_hi:[0,1]
	v_pk_add_f32 v[30:31], v[30:31], v[52:53]
	v_pk_add_f32 v[18:19], v[18:19], v[40:41]
	v_pk_add_f32 v[34:35], v[16:17], v[34:35]
	v_pk_add_f32 v[36:37], v[14:15], v[36:37]
	v_pk_add_f32 v[38:39], v[12:13], v[48:49]
	v_pk_add_f32 v[40:41], v[10:11], v[46:47]
	v_pk_add_f32 v[42:43], v[8:9], v[42:43]
	v_pk_add_f32 v[44:45], v[6:7], v[44:45]
	v_pk_add_f32 v[46:47], v[4:5], v[54:55]
	v_pk_add_f32 v[48:49], v[2:3], v[50:51]
	s_cbranch_scc1 .LBB0_550
; __device__ __forceinline__ void mask_tile(f32x16& p0, f32x16& p1, int dq) {
;     const float NEG = -__builtin_inff();
; #pragma unroll
;     for (int r = 0; r < 16; ++r) {
;         const int c = (r & 3) + 8 * (r >> 2);
;         if (dq - c < 0) p0[r] = NEG;
;         if (dq - c - 32 < 0) p1[r] = NEG;
;     }
; }
	v_sub_u32_e32 v2, v132, v154
	v_cmp_gt_i32_e64 s[66:67], 26, v2
	v_cmp_gt_i32_e64 s[68:69], 27, v2
	v_cmp_gt_i32_e64 s[64:65], 25, v2
	s_and_b64 s[66:67], s[68:69], s[66:67]
	v_cmp_gt_i32_e64 s[62:63], 24, v2
	s_and_b64 s[64:65], s[66:67], s[64:65]
	v_cmp_gt_i32_e64 s[60:61], 19, v2
	s_and_b64 s[62:63], s[64:65], s[62:63]
	v_cmp_gt_i32_e64 s[58:59], 18, v2
	s_and_b64 s[60:61], s[62:63], s[60:61]
	v_cmp_gt_i32_e64 s[56:57], 17, v2
	s_and_b64 s[58:59], s[60:61], s[58:59]
	v_cmp_gt_i32_e64 s[54:55], 16, v2
	s_and_b64 s[56:57], s[58:59], s[56:57]
	v_cmp_gt_i32_e64 s[52:53], 11, v2
	s_and_b64 s[54:55], s[56:57], s[54:55]
	v_cmp_gt_i32_e64 s[50:51], 10, v2
	s_and_b64 s[52:53], s[54:55], s[52:53]
	v_cmp_gt_i32_e64 s[48:49], 9, v2
	s_and_b64 s[50:51], s[52:53], s[50:51]
	v_cmp_gt_i32_e64 s[46:47], 8, v2
	s_and_b64 s[48:49], s[50:51], s[48:49]
	v_cmp_gt_i32_e64 s[44:45], 3, v2
	s_and_b64 s[46:47], s[48:49], s[46:47]
	v_cmp_gt_i32_e64 s[42:43], 2, v2
	s_and_b64 s[44:45], s[46:47], s[44:45]
	v_cmp_gt_i32_e64 s[40:41], 1, v2
	s_and_b64 s[42:43], s[44:45], s[42:43]
	v_cmp_gt_i32_e64 s[38:39], 0, v2
	s_and_b64 s[40:41], s[42:43], s[40:41]
	s_and_b64 s[38:39], s[40:41], s[38:39]
	v_cmp_gt_i32_e64 s[36:37], 58, v2
	v_cndmask_b32_e64 v18, v18, v147, s[38:39]
	v_cmp_gt_i32_e64 s[38:39], 59, v2
	v_cmp_gt_i32_e64 s[34:35], 57, v2
	s_and_b64 s[36:37], s[38:39], s[36:37]
	v_cmp_gt_i32_e64 s[30:31], 56, v2
	s_and_b64 s[34:35], s[36:37], s[34:35]
	v_cmp_gt_i32_e64 s[28:29], 51, v2
	s_and_b64 s[30:31], s[34:35], s[30:31]
	v_cmp_gt_i32_e64 s[26:27], 50, v2
	s_and_b64 s[28:29], s[30:31], s[28:29]
	v_cmp_gt_i32_e64 s[24:25], 49, v2
	s_and_b64 s[26:27], s[28:29], s[26:27]
	v_cmp_gt_i32_e64 s[22:23], 48, v2
	s_and_b64 s[24:25], s[26:27], s[24:25]
	v_cmp_gt_i32_e64 s[20:21], 43, v2
	s_and_b64 s[22:23], s[24:25], s[22:23]
	v_cmp_gt_i32_e64 s[18:19], 42, v2
	s_and_b64 s[20:21], s[22:23], s[20:21]
	v_cmp_gt_i32_e64 s[16:17], 41, v2
	s_and_b64 s[18:19], s[20:21], s[18:19]
	v_cmp_gt_i32_e64 s[14:15], 40, v2
	s_and_b64 s[16:17], s[18:19], s[16:17]
	v_cmp_gt_i32_e64 s[12:13], 35, v2
	s_and_b64 s[14:15], s[16:17], s[14:15]
	v_cmp_gt_i32_e64 s[10:11], 34, v2
	s_and_b64 s[12:13], s[14:15], s[12:13]
	v_cmp_gt_i32_e64 s[8:9], 33, v2
	s_and_b64 s[10:11], s[12:13], s[10:11]
	v_cmp_gt_i32_e32 vcc, 32, v2
	s_and_b64 s[8:9], s[10:11], s[8:9]
	v_cndmask_b32_e64 v21, v21, v147, s[44:45]
	s_mov_b32 s44, 0x41d00000
	v_cndmask_b32_e64 v20, v20, v147, s[42:43]
	s_mov_b32 s42, 0x41c00000
	v_cndmask_b32_e64 v19, v19, v147, s[40:41]
	s_mov_b32 s40, 0x41900000
	v_cndmask_b32_e64 v35, v35, v147, s[38:39]
	s_mov_b32 s38, 0x41800000
	v_cndmask_b32_e64 v34, v34, v147, s[36:37]
	s_mov_b32 s36, 0x41200000
	v_cndmask_b32_e64 v37, v37, v147, s[34:35]
	s_mov_b32 s34, 2.0
	s_and_b64 vcc, s[8:9], vcc
	v_cndmask_b32_e64 v33, v33, v147, s[68:69]
	v_cndmask_b32_e64 v32, v32, v147, s[66:67]
	v_cndmask_b32_e64 v31, v31, v147, s[64:65]
	v_cndmask_b32_e64 v30, v30, v147, s[62:63]
	v_cndmask_b32_e64 v29, v29, v147, s[60:61]
	v_cndmask_b32_e64 v28, v28, v147, s[58:59]
	v_cndmask_b32_e64 v27, v27, v147, s[56:57]
	v_cndmask_b32_e64 v26, v26, v147, s[54:55]
	v_cndmask_b32_e64 v25, v25, v147, s[52:53]
	v_cndmask_b32_e64 v24, v24, v147, s[50:51]
	v_cndmask_b32_e64 v23, v23, v147, s[48:49]
	v_cndmask_b32_e64 v22, v22, v147, s[46:47]
	s_mov_b32 s45, 0x41d80000
	s_mov_b32 s43, 0x41c80000
	s_mov_b32 s41, 0x41980000
	s_mov_b32 s39, 0x41880000
	s_mov_b32 s37, 0x41300000
	s_mov_b32 s35, 0x40400000
	v_cndmask_b32_e64 v36, v36, v147, s[30:31]
	v_cndmask_b32_e64 v39, v39, v147, s[28:29]
	v_cndmask_b32_e64 v38, v38, v147, s[26:27]
	v_cndmask_b32_e64 v41, v41, v147, s[24:25]
	v_cndmask_b32_e64 v40, v40, v147, s[22:23]
	v_cndmask_b32_e64 v43, v43, v147, s[20:21]
	v_cndmask_b32_e64 v42, v42, v147, s[18:19]
	v_cndmask_b32_e64 v45, v45, v147, s[16:17]
	v_cndmask_b32_e64 v44, v44, v147, s[14:15]
	v_cndmask_b32_e64 v47, v47, v147, s[12:13]
	v_cndmask_b32_e64 v46, v46, v147, s[10:11]
	v_cndmask_b32_e64 v49, v49, v147, s[8:9]
	v_cndmask_b32_e32 v48, v48, v147, vcc

; __device__ __forceinline__ void cv_load(const float* W, int N, int nblk, int item, int lane, f32x4 (&tv)[16]) {
;     const int kb = item / nblk, nb = item - kb * nblk; const float* p = W + (size_t)(64 * kb + 16 * (lane >> 4)) * N + 64 * nb + 4 * (lane & 15);
; #pragma unroll
;     for (int i = 0; i < 16; ++i) tv[i] = __builtin_nontemporal_load((const f32x4*)(p + (size_t)i * N));
; }
; template <int MODE> __device__ __forceinline__ void cv_run4(const float* W, int K, int N, unsigned char* WT, int item0, int lane) {
;     const int nblk = N / 64; f32x4 ta[16];
; #pragma unroll 1
;     for (int j = 0; j < 4; ++j) { cv_load(W, N, nblk, item0 + j, lane, ta); cv_finish<MODE>(ta, K, nblk, WT, item0 + j, lane); }
; }
.LBB0_729:
	s_lshr_b32 s21, s10, 5
	s_lshl_b32 s22, s21, 11
	v_lshl_or_b32 v132, s21, 6, v1
	s_sub_i32 s21, s11, s22
	v_subrev_u32_e32 v21, s22, v4
	v_lshlrev_b64 v[22:23], 13, v[132:133]
	s_add_i32 s22, s12, s21
	v_lshl_add_u64 v[22:23], s[4:5], 0, v[22:23]
	s_ashr_i32 s23, s22, 31
	v_lshlrev_b32_e32 v2, 2, v130
	v_mov_b32_e32 v3, v133
	v_lshl_add_u64 v[22:23], s[22:23], 2, v[22:23]
	s_movk_i32 s13, 0x2000
	v_lshl_add_u64 v[2:3], v[22:23], 0, v[2:3]
	v_add_co_u32_e32 v34, vcc, s13, v2
	s_movk_i32 s14, 0x6000
	s_nop 0
	v_addc_co_u32_e32 v35, vcc, 0, v3, vcc
	v_add_co_u32_e32 v36, vcc, s1, v2
	s_mov_b32 s15, 0xa000
	s_nop 0
	v_addc_co_u32_e32 v37, vcc, 0, v3, vcc
	v_add_co_u32_e32 v38, vcc, s14, v2
	s_mov_b32 s16, 0xe000
	s_nop 0
	v_addc_co_u32_e32 v39, vcc, 0, v3, vcc
	v_add_co_u32_e32 v40, vcc, s78, v2
	s_mov_b32 s17, 0x12000
	s_nop 0
	v_addc_co_u32_e32 v41, vcc, 0, v3, vcc
	v_add_co_u32_e32 v42, vcc, s15, v2
	s_mov_b32 s18, 0x16000
	s_nop 0
	v_addc_co_u32_e32 v43, vcc, 0, v3, vcc
	v_add_co_u32_e32 v46, vcc, s79, v2
	s_mov_b32 s19, 0x1a000
	s_nop 0
	v_addc_co_u32_e32 v47, vcc, 0, v3, vcc
	v_add_co_u32_e32 v50, vcc, s16, v2
	v_add_u32_e32 v24, s12, v21
	s_nop 0
	v_addc_co_u32_e32 v51, vcc, 0, v3, vcc
	v_add_co_u32_e32 v54, vcc, s86, v2
	v_ashrrev_i32_e32 v25, 31, v24
	s_nop 0
	v_addc_co_u32_e32 v55, vcc, 0, v3, vcc
	v_add_co_u32_e32 v58, vcc, s17, v2
	v_add_u32_e32 v28, 1, v24
	s_nop 0
	v_addc_co_u32_e32 v59, vcc, 0, v3, vcc
	v_add_co_u32_e32 v62, vcc, s87, v2
	v_add_u32_e32 v30, 2, v24
	s_nop 0
	v_addc_co_u32_e32 v63, vcc, 0, v3, vcc
	v_add_co_u32_e32 v66, vcc, s18, v2
	v_add_u32_e32 v32, 3, v24
	s_nop 0
	v_addc_co_u32_e32 v67, vcc, 0, v3, vcc
	v_add_co_u32_e32 v70, vcc, s85, v2
	s_mov_b32 s20, 0x1e000
	s_nop 0
	v_addc_co_u32_e32 v71, vcc, 0, v3, vcc
	v_add_co_u32_e32 v74, vcc, s19, v2
	v_lshl_add_u64 v[26:27], s[6:7], 0, v[132:133]
	s_nop 0
	v_addc_co_u32_e32 v75, vcc, 0, v3, vcc
	v_add_co_u32_e32 v78, vcc, s82, v2
	v_lshlrev_b64 v[24:25], 11, v[24:25]
	v_ashrrev_i32_e32 v29, 31, v28
	v_ashrrev_i32_e32 v31, 31, v30
	v_ashrrev_i32_e32 v33, 31, v32
	v_addc_co_u32_e32 v79, vcc, 0, v3, vcc
	v_lshl_add_u64 v[86:87], v[26:27], 0, v[24:25]
	v_lshlrev_b64 v[28:29], 11, v[28:29]
	v_lshlrev_b64 v[30:31], 11, v[30:31]
	v_lshlrev_b64 v[32:33], 11, v[32:33]
	global_load_dwordx4 v[22:25], v[2:3], off nt
	v_add_co_u32_e32 v2, vcc, s20, v2
	v_lshl_add_u64 v[88:89], v[26:27], 0, v[28:29]
	s_nop 0
	v_addc_co_u32_e32 v3, vcc, 0, v3, vcc
	v_lshl_add_u64 v[90:91], v[26:27], 0, v[30:31]
	v_lshl_add_u64 v[92:93], v[26:27], 0, v[32:33]
	global_load_dwordx4 v[26:29], v[34:35], off nt
	global_load_dwordx4 v[30:33], v[36:37], off nt
	s_nop 0
	global_load_dwordx4 v[34:37], v[38:39], off nt
	s_nop 0
	global_load_dwordx4 v[38:41], v[40:41], off nt
	s_nop 0
	global_load_dwordx4 v[42:45], v[42:43], off nt
	s_nop 0
	global_load_dwordx4 v[46:49], v[46:47], off nt
	s_nop 0
	global_load_dwordx4 v[50:53], v[50:51], off nt
	s_nop 0
	global_load_dwordx4 v[54:57], v[54:55], off nt
	s_nop 0
	global_load_dwordx4 v[58:61], v[58:59], off nt
	s_nop 0
	global_load_dwordx4 v[62:65], v[62:63], off nt
	s_nop 0
	global_load_dwordx4 v[66:69], v[66:67], off nt
	s_nop 0
	global_load_dwordx4 v[70:73], v[70:71], off nt
	s_nop 0
	global_load_dwordx4 v[74:77], v[74:75], off nt
	s_nop 0
	global_load_dwordx4 v[78:81], v[78:79], off nt
	s_nop 0
	global_load_dwordx4 v[82:85], v[2:3], off nt
	v_mov_b32_e32 v5, v133
	v_mov_b32_e32 v6, v133
	v_mov_b32_e32 v7, v133
	v_mov_b32_e32 v8, v133
	v_mov_b32_e32 v9, v133
	v_mov_b32_e32 v10, v133
	v_mov_b32_e32 v11, v133
	v_mov_b32_e32 v12, v133
	v_mov_b32_e32 v13, v133
	v_mov_b32_e32 v14, v133
	v_mov_b32_e32 v15, v133
	v_mov_b32_e32 v16, v133
	v_mov_b32_e32 v17, v133
	v_mov_b32_e32 v18, v133
	v_mov_b32_e32 v19, v133
	v_mov_b32_e32 v20, v133
	s_add_i32 s10, s10, 1
	s_add_i32 s12, s12, 64
	v_mov_b32_e32 v211, v133
	s_lshr_b32 s21, s10, 5
	s_lshl_b32 s22, s21, 11
	v_lshl_or_b32 v210, s21, 6, v1
	s_sub_i32 s21, s11, s22
	v_subrev_u32_e32 v115, s22, v4
	v_lshlrev_b64 v[116:117], 13, v[210:211]
	s_add_i32 s22, s12, s21
	v_lshl_add_u64 v[116:117], s[4:5], 0, v[116:117]
	s_ashr_i32 s23, s22, 31
	v_lshlrev_b32_e32 v98, 2, v130
	v_mov_b32_e32 v99, v211
	v_lshl_add_u64 v[116:117], s[22:23], 2, v[116:117]
	s_movk_i32 s13, 0x2000
	v_lshl_add_u64 v[98:99], v[116:117], 0, v[98:99]
	v_add_co_u32_e32 v136, vcc, s13, v98
	s_movk_i32 s14, 0x6000
	s_nop 0
	v_addc_co_u32_e32 v137, vcc, 0, v99, vcc
	v_add_co_u32_e32 v138, vcc, s1, v98
	s_mov_b32 s15, 0xa000
	s_nop 0
	v_addc_co_u32_e32 v139, vcc, 0, v99, vcc
	v_add_co_u32_e32 v140, vcc, s14, v98
	s_mov_b32 s16, 0xe000
	s_nop 0
	v_addc_co_u32_e32 v141, vcc, 0, v99, vcc
	v_add_co_u32_e32 v142, vcc, s78, v98
	s_mov_b32 s17, 0x12000
	s_nop 0
	v_addc_co_u32_e32 v143, vcc, 0, v99, vcc
	v_add_co_u32_e32 v152, vcc, s15, v98
	s_mov_b32 s18, 0x16000
	s_nop 0
	v_addc_co_u32_e32 v153, vcc, 0, v99, vcc
	v_add_co_u32_e32 v156, vcc, s79, v98
	s_mov_b32 s19, 0x1a000
	s_nop 0
	v_addc_co_u32_e32 v157, vcc, 0, v99, vcc
	v_add_co_u32_e32 v160, vcc, s16, v98
	v_add_u32_e32 v118, s12, v115
	s_nop 0
	v_addc_co_u32_e32 v161, vcc, 0, v99, vcc
	v_add_co_u32_e32 v164, vcc, s86, v98
	v_ashrrev_i32_e32 v119, 31, v118
	s_nop 0
	v_addc_co_u32_e32 v165, vcc, 0, v99, vcc
	v_add_co_u32_e32 v174, vcc, s17, v98
	v_add_u32_e32 v122, 1, v118
	s_nop 0
	v_addc_co_u32_e32 v175, vcc, 0, v99, vcc
	v_add_co_u32_e32 v178, vcc, s87, v98
	v_add_u32_e32 v124, 2, v118
	s_nop 0
	v_addc_co_u32_e32 v179, vcc, 0, v99, vcc
	v_add_co_u32_e32 v182, vcc, s18, v98
	v_add_u32_e32 v126, 3, v118
	s_nop 0
	v_addc_co_u32_e32 v183, vcc, 0, v99, vcc
	v_add_co_u32_e32 v186, vcc, s85, v98
; __device__ __forceinline__ void cv_load(const float* W, int N, int nblk, int item, int lane, f32x4 (&tv)[16]) {
;     const int kb = item / nblk, nb = item - kb * nblk; const float* p = W + (size_t)(64 * kb + 16 * (lane >> 4)) * N + 64 * nb + 4 * (lane & 15);
; #pragma unroll
;     for (int i = 0; i < 16; ++i) tv[i] = __builtin_nontemporal_load((const f32x4*)(p + (size_t)i * N));
; }
; template <int MODE> __device__ __forceinline__ void cv_finish(const f32x4 (&tv)[16], int K, int nblk, unsigned char* WT, int item, int lane) {
;     const int kb = item / nblk, nb = item - kb * nblk, k0 = 64 * kb + 16 * (lane >> 4), n0 = 64 * nb + 4 * (lane & 15);
;     unsigned D[16];
; #pragma unroll
;     for (int i = 0; i < 16; ++i) { const f32x2 a = (f32x2){tv[i].x, tv[i].y} * (f32x2){1024.f, 1024.f}, b = (f32x2){tv[i].z, tv[i].w} * (f32x2){1024.f, 1024.f};
;         D[i] = pk4_fp8(a.x, a.y, b.x, b.y); }
	s_mov_b32 s20, 0x1e000
	s_nop 0
	v_addc_co_u32_e32 v187, vcc, 0, v99, vcc
	v_add_co_u32_e32 v190, vcc, s19, v98
	v_lshl_add_u64 v[120:121], s[6:7], 0, v[210:211]
	s_nop 0
	v_addc_co_u32_e32 v191, vcc, 0, v99, vcc
	v_add_co_u32_e32 v194, vcc, s82, v98
	v_lshlrev_b64 v[118:119], 11, v[118:119]
	v_ashrrev_i32_e32 v123, 31, v122
	v_ashrrev_i32_e32 v125, 31, v124
	v_ashrrev_i32_e32 v127, 31, v126
	v_addc_co_u32_e32 v195, vcc, 0, v99, vcc
	v_lshl_add_u64 v[128:129], v[120:121], 0, v[118:119]
	v_lshlrev_b64 v[122:123], 11, v[122:123]
	v_lshlrev_b64 v[124:125], 11, v[124:125]
	v_lshlrev_b64 v[126:127], 11, v[126:127]
	global_load_dwordx4 v[116:119], v[98:99], off nt
	v_add_co_u32_e32 v98, vcc, s20, v98
	v_lshl_add_u64 v[168:169], v[120:121], 0, v[122:123]
	s_nop 0
	v_addc_co_u32_e32 v99, vcc, 0, v99, vcc
	v_lshl_add_u64 v[202:203], v[120:121], 0, v[124:125]
	v_lshl_add_u64 v[204:205], v[120:121], 0, v[126:127]
	global_load_dwordx4 v[120:123], v[136:137], off nt
	global_load_dwordx4 v[124:127], v[138:139], off nt
	s_nop 0
	global_load_dwordx4 v[136:139], v[140:141], off nt
	s_nop 0
	global_load_dwordx4 v[140:143], v[142:143], off nt
	s_nop 0
	global_load_dwordx4 v[152:155], v[152:153], off nt
	s_nop 0
	global_load_dwordx4 v[156:159], v[156:157], off nt
	s_nop 0
	global_load_dwordx4 v[160:163], v[160:161], off nt
	s_nop 0
	global_load_dwordx4 v[164:167], v[164:165], off nt
	s_nop 0
	global_load_dwordx4 v[174:177], v[174:175], off nt
	s_nop 0
	global_load_dwordx4 v[178:181], v[178:179], off nt
	s_nop 0
	global_load_dwordx4 v[182:185], v[182:183], off nt
	s_nop 0
	global_load_dwordx4 v[186:189], v[186:187], off nt
	s_nop 0
	global_load_dwordx4 v[190:193], v[190:191], off nt
	s_nop 0
	global_load_dwordx4 v[194:197], v[194:195], off nt
	s_nop 0
	global_load_dwordx4 v[198:201], v[98:99], off nt
	v_mov_b32_e32 v97, v211
	v_mov_b32_e32 v100, v211
	v_mov_b32_e32 v101, v211
	v_mov_b32_e32 v102, v211
	v_mov_b32_e32 v103, v211
	v_mov_b32_e32 v104, v211
	v_mov_b32_e32 v105, v211
	v_mov_b32_e32 v106, v211
	v_mov_b32_e32 v107, v211
	v_mov_b32_e32 v108, v211
	v_mov_b32_e32 v109, v211
	v_mov_b32_e32 v110, v211
	v_mov_b32_e32 v111, v211
	v_mov_b32_e32 v112, v211
	v_mov_b32_e32 v113, v211
	v_mov_b32_e32 v114, v211
	s_add_i32 s10, s10, 1
	s_add_i32 s12, s12, 64
	s_waitcnt vmcnt(31)
	v_pk_mul_f32 v[2:3], v[22:23], s[84:85] op_sel_hi:[1,0]
	v_pk_mul_f32 v[22:23], v[24:25], s[84:85] op_sel_hi:[1,0]
	v_med3_f32 v21, v2, s96, v150
	v_med3_f32 v94, v3, s96, v150
	v_med3_f32 v95, v22, s96, v150
	v_med3_f32 v96, v23, s96, v150
	s_waitcnt vmcnt(30)
	v_pk_mul_f32 v[2:3], v[26:27], s[84:85] op_sel_hi:[1,0]
	v_pk_mul_f32 v[22:23], v[28:29], s[84:85] op_sel_hi:[1,0]
	s_waitcnt vmcnt(29)
	v_pk_mul_f32 v[24:25], v[30:31], s[84:85] op_sel_hi:[1,0]
	v_pk_mul_f32 v[26:27], v[32:33], s[84:85] op_sel_hi:[1,0]
	s_waitcnt vmcnt(28)
	v_pk_mul_f32 v[28:29], v[34:35], s[84:85] op_sel_hi:[1,0]
	v_pk_mul_f32 v[30:31], v[36:37], s[84:85] op_sel_hi:[1,0]
	s_waitcnt vmcnt(27)
	v_pk_mul_f32 v[32:33], v[38:39], s[84:85] op_sel_hi:[1,0]
	v_pk_mul_f32 v[34:35], v[40:41], s[84:85] op_sel_hi:[1,0]
	s_waitcnt vmcnt(26)
	v_pk_mul_f32 v[36:37], v[42:43], s[84:85] op_sel_hi:[1,0]
	v_pk_mul_f32 v[38:39], v[44:45], s[84:85] op_sel_hi:[1,0]
	s_waitcnt vmcnt(25)
	v_pk_mul_f32 v[40:41], v[46:47], s[84:85] op_sel_hi:[1,0]
	v_pk_mul_f32 v[42:43], v[48:49], s[84:85] op_sel_hi:[1,0]
	s_waitcnt vmcnt(24)
	v_pk_mul_f32 v[44:45], v[50:51], s[84:85] op_sel_hi:[1,0]
	v_pk_mul_f32 v[46:47], v[52:53], s[84:85] op_sel_hi:[1,0]
	s_waitcnt vmcnt(23)
	v_pk_mul_f32 v[48:49], v[54:55], s[84:85] op_sel_hi:[1,0]
	v_pk_mul_f32 v[50:51], v[56:57], s[84:85] op_sel_hi:[1,0]
	s_waitcnt vmcnt(22)
	v_pk_mul_f32 v[52:53], v[58:59], s[84:85] op_sel_hi:[1,0]
	v_pk_mul_f32 v[54:55], v[60:61], s[84:85] op_sel_hi:[1,0]
	s_waitcnt vmcnt(21)
	v_pk_mul_f32 v[56:57], v[62:63], s[84:85] op_sel_hi:[1,0]
	v_pk_mul_f32 v[58:59], v[64:65], s[84:85] op_sel_hi:[1,0]
	s_waitcnt vmcnt(20)
	v_pk_mul_f32 v[60:61], v[66:67], s[84:85] op_sel_hi:[1,0]
	v_pk_mul_f32 v[62:63], v[68:69], s[84:85] op_sel_hi:[1,0]
	s_waitcnt vmcnt(19)
	v_pk_mul_f32 v[64:65], v[70:71], s[84:85] op_sel_hi:[1,0]
	v_pk_mul_f32 v[66:67], v[72:73], s[84:85] op_sel_hi:[1,0]
	s_waitcnt vmcnt(18)
	v_pk_mul_f32 v[68:69], v[74:75], s[84:85] op_sel_hi:[1,0]
	v_pk_mul_f32 v[70:71], v[76:77], s[84:85] op_sel_hi:[1,0]
	s_waitcnt vmcnt(17)
	v_pk_mul_f32 v[72:73], v[78:79], s[84:85] op_sel_hi:[1,0]
	v_pk_mul_f32 v[74:75], v[80:81], s[84:85] op_sel_hi:[1,0]
	s_waitcnt vmcnt(16)
; __device__ __forceinline__ void cv_load(const float* W, int N, int nblk, int item, int lane, f32x4 (&tv)[16]) {
;     const int kb = item / nblk, nb = item - kb * nblk; const float* p = W + (size_t)(64 * kb + 16 * (lane >> 4)) * N + 64 * nb + 4 * (lane & 15);
; #pragma unroll
;     for (int i = 0; i < 16; ++i) tv[i] = __builtin_nontemporal_load((const f32x4*)(p + (size_t)i * N));
; }
; template <int MODE> __device__ __forceinline__ void cv_finish(const f32x4 (&tv)[16], int K, int nblk, unsigned char* WT, int item, int lane) {
;     const int kb = item / nblk, nb = item - kb * nblk, k0 = 64 * kb + 16 * (lane >> 4), n0 = 64 * nb + 4 * (lane & 15);
;     unsigned D[16];
; #pragma unroll
;     for (int i = 0; i < 16; ++i) { const f32x2 a = (f32x2){tv[i].x, tv[i].y} * (f32x2){1024.f, 1024.f}, b = (f32x2){tv[i].z, tv[i].w} * (f32x2){1024.f, 1024.f};
;         D[i] = pk4_fp8(a.x, a.y, b.x, b.y); }
;     unsigned O[4][4];
; #pragma unroll
;     for (int q = 0; q < 4; ++q) { const unsigned a = D[4 * q], b = D[4 * q + 1], c = D[4 * q + 2], d = D[4 * q + 3];
;         const unsigned t0 = __builtin_amdgcn_perm(b, a, 0x05010400u), t1 = __builtin_amdgcn_perm(b, a, 0x07030602u), u0 = __builtin_amdgcn_perm(d, c, 0x05010400u), u1 = __builtin_amdgcn_perm(d, c, 0x07030602u);
;         O[0][q] = __builtin_amdgcn_perm(u0, t0, 0x05040100u); O[1][q] = __builtin_amdgcn_perm(u0, t0, 0x07060302u); O[2][q] = __builtin_amdgcn_perm(u1, t1, 0x05040100u); O[3][q] = __builtin_amdgcn_perm(u1, t1, 0x07060302u); }
; #pragma unroll
;     for (int j = 0; j < 4; ++j) { u32x4 o; o.x = O[j][0]; o.y = O[j][1]; o.z = O[j][2]; o.w = O[j][3];
;         __builtin_nontemporal_store(o, (u32x4*)(WT + (size_t)drow<MODE>(n0 + j) * K + k0)); }
; }
	v_pk_mul_f32 v[76:77], v[82:83], s[84:85] op_sel_hi:[1,0]
	v_cvt_pk_fp8_f32 v5, v21, v94
	v_med3_f32 v2, v2, s96, v150
	v_med3_f32 v3, v3, s96, v150
	v_med3_f32 v21, v22, s96, v150
	v_med3_f32 v22, v23, s96, v150
	v_med3_f32 v23, v24, s96, v150
	v_med3_f32 v24, v25, s96, v150
	v_med3_f32 v25, v26, s96, v150
	v_med3_f32 v26, v27, s96, v150
	v_med3_f32 v27, v28, s96, v150
	v_med3_f32 v28, v29, s96, v150
	v_med3_f32 v29, v30, s96, v150
	v_med3_f32 v30, v31, s96, v150
	v_med3_f32 v31, v32, s96, v150
	v_med3_f32 v32, v33, s96, v150
	v_med3_f32 v33, v34, s96, v150
	v_med3_f32 v34, v35, s96, v150
	v_med3_f32 v35, v36, s96, v150
	v_med3_f32 v36, v37, s96, v150
	v_med3_f32 v37, v38, s96, v150
	v_med3_f32 v38, v39, s96, v150
	v_med3_f32 v39, v40, s96, v150
	v_med3_f32 v40, v41, s96, v150
	v_med3_f32 v41, v42, s96, v150
	v_med3_f32 v42, v43, s96, v150
	v_med3_f32 v43, v44, s96, v150
	v_med3_f32 v44, v45, s96, v150
	v_med3_f32 v45, v46, s96, v150
	v_med3_f32 v46, v47, s96, v150
	v_med3_f32 v47, v48, s96, v150
	v_med3_f32 v48, v49, s96, v150
	v_med3_f32 v49, v50, s96, v150
	v_med3_f32 v50, v51, s96, v150
	v_med3_f32 v51, v52, s96, v150
	v_med3_f32 v52, v53, s96, v150
	v_med3_f32 v53, v54, s96, v150
	v_med3_f32 v54, v55, s96, v150
	v_med3_f32 v55, v56, s96, v150
	v_med3_f32 v56, v57, s96, v150
	v_med3_f32 v57, v58, s96, v150
	v_med3_f32 v58, v59, s96, v150
	v_med3_f32 v59, v60, s96, v150
	v_med3_f32 v60, v61, s96, v150
	v_med3_f32 v61, v62, s96, v150
	v_med3_f32 v62, v63, s96, v150
	v_med3_f32 v63, v64, s96, v150
	v_med3_f32 v64, v65, s96, v150
	v_med3_f32 v65, v66, s96, v150
	v_med3_f32 v66, v67, s96, v150
	v_med3_f32 v67, v68, s96, v150
	v_med3_f32 v68, v69, s96, v150
	v_med3_f32 v69, v70, s96, v150
	v_med3_f32 v70, v71, s96, v150
	v_med3_f32 v71, v72, s96, v150
	v_med3_f32 v72, v73, s96, v150
	v_med3_f32 v73, v74, s96, v150
	v_med3_f32 v74, v75, s96, v150
	v_med3_f32 v75, v76, s96, v150
	v_med3_f32 v76, v77, s96, v150
	v_cvt_pk_fp8_f32 v6, v2, v3
	v_cvt_pk_fp8_f32 v7, v23, v24
	v_cvt_pk_fp8_f32 v8, v27, v28
	v_cvt_pk_fp8_f32 v9, v31, v32
	v_cvt_pk_fp8_f32 v10, v35, v36
	v_cvt_pk_fp8_f32 v11, v39, v40
	v_cvt_pk_fp8_f32 v12, v43, v44
	v_cvt_pk_fp8_f32 v13, v47, v48
	v_cvt_pk_fp8_f32 v14, v51, v52
	v_cvt_pk_fp8_f32 v15, v55, v56
	v_cvt_pk_fp8_f32 v16, v59, v60
	v_cvt_pk_fp8_f32 v17, v63, v64
	v_cvt_pk_fp8_f32 v18, v67, v68
	v_cvt_pk_fp8_f32 v19, v71, v72
	v_cvt_pk_fp8_f32 v20, v75, v76
	v_pk_mul_f32 v[78:79], v[84:85], s[84:85] op_sel_hi:[1,0]
	v_cvt_pk_fp8_f32 v5, v95, v96 op_sel:[0,0,1]
	v_med3_f32 v77, v78, s96, v150
	v_med3_f32 v78, v79, s96, v150
	v_cvt_pk_fp8_f32 v6, v21, v22 op_sel:[0,0,1]
	v_cvt_pk_fp8_f32 v7, v25, v26 op_sel:[0,0,1]
	v_cvt_pk_fp8_f32 v8, v29, v30 op_sel:[0,0,1]
	v_cvt_pk_fp8_f32 v9, v33, v34 op_sel:[0,0,1]
	v_cvt_pk_fp8_f32 v10, v37, v38 op_sel:[0,0,1]
	v_cvt_pk_fp8_f32 v11, v41, v42 op_sel:[0,0,1]
	v_cvt_pk_fp8_f32 v12, v45, v46 op_sel:[0,0,1]
	v_cvt_pk_fp8_f32 v13, v49, v50 op_sel:[0,0,1]
	v_cvt_pk_fp8_f32 v14, v53, v54 op_sel:[0,0,1]
	v_cvt_pk_fp8_f32 v15, v57, v58 op_sel:[0,0,1]
	v_cvt_pk_fp8_f32 v16, v61, v62 op_sel:[0,0,1]
	v_cvt_pk_fp8_f32 v17, v65, v66 op_sel:[0,0,1]
	v_cvt_pk_fp8_f32 v18, v69, v70 op_sel:[0,0,1]
	v_cvt_pk_fp8_f32 v19, v73, v74 op_sel:[0,0,1]
	v_cvt_pk_fp8_f32 v20, v77, v78 op_sel:[0,0,1]
	v_perm_b32 v2, v6, v5, s97
	v_perm_b32 v3, v6, v5, s70
	v_perm_b32 v5, v8, v7, s97
	v_perm_b32 v7, v8, v7, s70
	v_perm_b32 v8, v10, v9, s97
	v_perm_b32 v9, v10, v9, s70
	v_perm_b32 v21, v12, v11, s97
	v_perm_b32 v12, v12, v11, s70
	v_perm_b32 v22, v14, v13, s97
	v_perm_b32 v23, v16, v15, s97
	v_perm_b32 v25, v18, v17, s97
	v_perm_b32 v26, v18, v17, s70
	v_perm_b32 v17, v20, v19, s97
	v_perm_b32 v13, v14, v13, s70
	v_perm_b32 v24, v16, v15, s70
	v_perm_b32 v27, v20, v19, s70
	v_perm_b32 v6, v5, v2, s71
	v_perm_b32 v14, v7, v3, s71
	v_perm_b32 v18, v7, v3, s72
	v_perm_b32 v7, v21, v8, s71
	v_perm_b32 v11, v21, v8, s72
	v_perm_b32 v15, v12, v9, s71
	v_perm_b32 v19, v12, v9, s72
	v_perm_b32 v8, v23, v22, s71
	v_perm_b32 v9, v17, v25, s71
	v_perm_b32 v10, v5, v2, s72
	v_perm_b32 v12, v23, v22, s72
	v_perm_b32 v16, v24, v13, s71
	v_perm_b32 v20, v24, v13, s72
	v_perm_b32 v13, v17, v25, s72
	v_perm_b32 v17, v27, v26, s71
	v_perm_b32 v21, v27, v26, s72
	global_store_dwordx4 v[86:87], v[6:9], off nt
	global_store_dwordx4 v[88:89], v[10:13], off nt
	global_store_dwordx4 v[90:91], v[14:17], off nt
	global_store_dwordx4 v[92:93], v[18:21], off nt
	s_lshr_b32 s21, s10, 5
	s_lshl_b32 s22, s21, 11
	v_lshl_or_b32 v132, s21, 6, v1
	s_sub_i32 s21, s11, s22
	v_subrev_u32_e32 v21, s22, v4
	v_lshlrev_b64 v[22:23], 13, v[132:133]
	s_add_i32 s22, s12, s21
	v_lshl_add_u64 v[22:23], s[4:5], 0, v[22:23]
	s_ashr_i32 s23, s22, 31
	v_lshlrev_b32_e32 v2, 2, v130
	v_mov_b32_e32 v3, v133
	v_lshl_add_u64 v[22:23], s[22:23], 2, v[22:23]
	s_movk_i32 s13, 0x2000
	v_lshl_add_u64 v[2:3], v[22:23], 0, v[2:3]
	v_add_co_u32_e32 v34, vcc, s13, v2
	s_movk_i32 s14, 0x6000
	s_nop 0
	v_addc_co_u32_e32 v35, vcc, 0, v3, vcc
	v_add_co_u32_e32 v36, vcc, s1, v2
	s_mov_b32 s15, 0xa000
	s_nop 0
	v_addc_co_u32_e32 v37, vcc, 0, v3, vcc
	v_add_co_u32_e32 v38, vcc, s14, v2
	s_mov_b32 s16, 0xe000
	s_nop 0
	v_addc_co_u32_e32 v39, vcc, 0, v3, vcc
	v_add_co_u32_e32 v40, vcc, s78, v2
	s_mov_b32 s17, 0x12000
	s_nop 0
	v_addc_co_u32_e32 v41, vcc, 0, v3, vcc
	v_add_co_u32_e32 v42, vcc, s15, v2
	s_mov_b32 s18, 0x16000
	s_nop 0
	v_addc_co_u32_e32 v43, vcc, 0, v3, vcc
	v_add_co_u32_e32 v46, vcc, s79, v2
	s_mov_b32 s19, 0x1a000
	s_nop 0
	v_addc_co_u32_e32 v47, vcc, 0, v3, vcc
	v_add_co_u32_e32 v50, vcc, s16, v2
	v_add_u32_e32 v24, s12, v21
	s_nop 0
	v_addc_co_u32_e32 v51, vcc, 0, v3, vcc
; __device__ __forceinline__ void cv_load(const float* W, int N, int nblk, int item, int lane, f32x4 (&tv)[16]) {
;     const int kb = item / nblk, nb = item - kb * nblk; const float* p = W + (size_t)(64 * kb + 16 * (lane >> 4)) * N + 64 * nb + 4 * (lane & 15);
; #pragma unroll
;     for (int i = 0; i < 16; ++i) tv[i] = __builtin_nontemporal_load((const f32x4*)(p + (size_t)i * N));
; }
; template <int MODE> __device__ __forceinline__ void cv_finish(const f32x4 (&tv)[16], int K, int nblk, unsigned char* WT, int item, int lane) {
;     const int kb = item / nblk, nb = item - kb * nblk, k0 = 64 * kb + 16 * (lane >> 4), n0 = 64 * nb + 4 * (lane & 15);
;     unsigned D[16];
; #pragma unroll
;     for (int i = 0; i < 16; ++i) { const f32x2 a = (f32x2){tv[i].x, tv[i].y} * (f32x2){1024.f, 1024.f}, b = (f32x2){tv[i].z, tv[i].w} * (f32x2){1024.f, 1024.f};
;         D[i] = pk4_fp8(a.x, a.y, b.x, b.y); }
	v_add_co_u32_e32 v54, vcc, s86, v2
	v_ashrrev_i32_e32 v25, 31, v24
	s_nop 0
	v_addc_co_u32_e32 v55, vcc, 0, v3, vcc
	v_add_co_u32_e32 v58, vcc, s17, v2
	v_add_u32_e32 v28, 1, v24
	s_nop 0
	v_addc_co_u32_e32 v59, vcc, 0, v3, vcc
	v_add_co_u32_e32 v62, vcc, s87, v2
	v_add_u32_e32 v30, 2, v24
	s_nop 0
	v_addc_co_u32_e32 v63, vcc, 0, v3, vcc
	v_add_co_u32_e32 v66, vcc, s18, v2
	v_add_u32_e32 v32, 3, v24
	s_nop 0
	v_addc_co_u32_e32 v67, vcc, 0, v3, vcc
	v_add_co_u32_e32 v70, vcc, s85, v2
	s_mov_b32 s20, 0x1e000
	s_nop 0
	v_addc_co_u32_e32 v71, vcc, 0, v3, vcc
	v_add_co_u32_e32 v74, vcc, s19, v2
	v_lshl_add_u64 v[26:27], s[6:7], 0, v[132:133]
	s_nop 0
	v_addc_co_u32_e32 v75, vcc, 0, v3, vcc
	v_add_co_u32_e32 v78, vcc, s82, v2
	v_lshlrev_b64 v[24:25], 11, v[24:25]
	v_ashrrev_i32_e32 v29, 31, v28
	v_ashrrev_i32_e32 v31, 31, v30
	v_ashrrev_i32_e32 v33, 31, v32
	v_addc_co_u32_e32 v79, vcc, 0, v3, vcc
	v_lshl_add_u64 v[86:87], v[26:27], 0, v[24:25]
	v_lshlrev_b64 v[28:29], 11, v[28:29]
	v_lshlrev_b64 v[30:31], 11, v[30:31]
	v_lshlrev_b64 v[32:33], 11, v[32:33]
	global_load_dwordx4 v[22:25], v[2:3], off nt
	v_add_co_u32_e32 v2, vcc, s20, v2
	v_lshl_add_u64 v[88:89], v[26:27], 0, v[28:29]
	s_nop 0
	v_addc_co_u32_e32 v3, vcc, 0, v3, vcc
	v_lshl_add_u64 v[90:91], v[26:27], 0, v[30:31]
	v_lshl_add_u64 v[92:93], v[26:27], 0, v[32:33]
	global_load_dwordx4 v[26:29], v[34:35], off nt
	global_load_dwordx4 v[30:33], v[36:37], off nt
	s_nop 0
	global_load_dwordx4 v[34:37], v[38:39], off nt
	s_nop 0
	global_load_dwordx4 v[38:41], v[40:41], off nt
	s_nop 0
	global_load_dwordx4 v[42:45], v[42:43], off nt
	s_nop 0
	global_load_dwordx4 v[46:49], v[46:47], off nt
	s_nop 0
	global_load_dwordx4 v[50:53], v[50:51], off nt
	s_nop 0
	global_load_dwordx4 v[54:57], v[54:55], off nt
	s_nop 0
	global_load_dwordx4 v[58:61], v[58:59], off nt
	s_nop 0
	global_load_dwordx4 v[62:65], v[62:63], off nt
	s_nop 0
	global_load_dwordx4 v[66:69], v[66:67], off nt
	s_nop 0
	global_load_dwordx4 v[70:73], v[70:71], off nt
	s_nop 0
	global_load_dwordx4 v[74:77], v[74:75], off nt
	s_nop 0
	global_load_dwordx4 v[78:81], v[78:79], off nt
	s_nop 0
	global_load_dwordx4 v[82:85], v[2:3], off nt
	v_mov_b32_e32 v5, v133
	v_mov_b32_e32 v6, v133
	v_mov_b32_e32 v7, v133
	v_mov_b32_e32 v8, v133
	v_mov_b32_e32 v9, v133
	v_mov_b32_e32 v10, v133
	v_mov_b32_e32 v11, v133
	v_mov_b32_e32 v12, v133
	v_mov_b32_e32 v13, v133
	v_mov_b32_e32 v14, v133
	v_mov_b32_e32 v15, v133
	v_mov_b32_e32 v16, v133
	v_mov_b32_e32 v17, v133
	v_mov_b32_e32 v18, v133
	v_mov_b32_e32 v19, v133
	v_mov_b32_e32 v20, v133
	s_add_i32 s10, s10, 1
	s_add_i32 s12, s12, 64
	s_waitcnt vmcnt(35)
	v_pk_mul_f32 v[98:99], v[116:117], s[84:85] op_sel_hi:[1,0]
	v_pk_mul_f32 v[116:117], v[118:119], s[84:85] op_sel_hi:[1,0]
	v_med3_f32 v115, v98, s96, v150
	v_med3_f32 v206, v99, s96, v150
	v_med3_f32 v145, v116, s96, v150
	v_med3_f32 v208, v117, s96, v150
	s_waitcnt vmcnt(34)
	v_pk_mul_f32 v[98:99], v[120:121], s[84:85] op_sel_hi:[1,0]
	v_pk_mul_f32 v[116:117], v[122:123], s[84:85] op_sel_hi:[1,0]
	s_waitcnt vmcnt(33)
	v_pk_mul_f32 v[118:119], v[124:125], s[84:85] op_sel_hi:[1,0]
	v_pk_mul_f32 v[120:121], v[126:127], s[84:85] op_sel_hi:[1,0]
	s_waitcnt vmcnt(32)
	v_pk_mul_f32 v[122:123], v[136:137], s[84:85] op_sel_hi:[1,0]
	v_pk_mul_f32 v[124:125], v[138:139], s[84:85] op_sel_hi:[1,0]
	s_waitcnt vmcnt(31)
	v_pk_mul_f32 v[126:127], v[140:141], s[84:85] op_sel_hi:[1,0]
	v_pk_mul_f32 v[136:137], v[142:143], s[84:85] op_sel_hi:[1,0]
	s_waitcnt vmcnt(30)
	v_pk_mul_f32 v[138:139], v[152:153], s[84:85] op_sel_hi:[1,0]
	v_pk_mul_f32 v[140:141], v[154:155], s[84:85] op_sel_hi:[1,0]
	s_waitcnt vmcnt(29)
	v_pk_mul_f32 v[142:143], v[156:157], s[84:85] op_sel_hi:[1,0]
	v_pk_mul_f32 v[152:153], v[158:159], s[84:85] op_sel_hi:[1,0]
	s_waitcnt vmcnt(28)
	v_pk_mul_f32 v[154:155], v[160:161], s[84:85] op_sel_hi:[1,0]
	v_pk_mul_f32 v[156:157], v[162:163], s[84:85] op_sel_hi:[1,0]
	s_waitcnt vmcnt(27)
	v_pk_mul_f32 v[158:159], v[164:165], s[84:85] op_sel_hi:[1,0]
	v_pk_mul_f32 v[160:161], v[166:167], s[84:85] op_sel_hi:[1,0]
	s_waitcnt vmcnt(26)
	v_pk_mul_f32 v[162:163], v[174:175], s[84:85] op_sel_hi:[1,0]
	v_pk_mul_f32 v[164:165], v[176:177], s[84:85] op_sel_hi:[1,0]
	s_waitcnt vmcnt(25)
	v_pk_mul_f32 v[166:167], v[178:179], s[84:85] op_sel_hi:[1,0]
	v_pk_mul_f32 v[174:175], v[180:181], s[84:85] op_sel_hi:[1,0]
	s_waitcnt vmcnt(24)
	v_pk_mul_f32 v[176:177], v[182:183], s[84:85] op_sel_hi:[1,0]
	v_pk_mul_f32 v[178:179], v[184:185], s[84:85] op_sel_hi:[1,0]
	s_waitcnt vmcnt(23)
	v_pk_mul_f32 v[180:181], v[186:187], s[84:85] op_sel_hi:[1,0]
	v_pk_mul_f32 v[182:183], v[188:189], s[84:85] op_sel_hi:[1,0]
	s_waitcnt vmcnt(22)
	v_pk_mul_f32 v[184:185], v[190:191], s[84:85] op_sel_hi:[1,0]
	v_pk_mul_f32 v[186:187], v[192:193], s[84:85] op_sel_hi:[1,0]
	s_waitcnt vmcnt(21)
	v_pk_mul_f32 v[188:189], v[194:195], s[84:85] op_sel_hi:[1,0]
	v_pk_mul_f32 v[190:191], v[196:197], s[84:85] op_sel_hi:[1,0]
	s_waitcnt vmcnt(20)
; __device__ __forceinline__ void cv_load(const float* W, int N, int nblk, int item, int lane, f32x4 (&tv)[16]) {
;     const int kb = item / nblk, nb = item - kb * nblk; const float* p = W + (size_t)(64 * kb + 16 * (lane >> 4)) * N + 64 * nb + 4 * (lane & 15);
; #pragma unroll
;     for (int i = 0; i < 16; ++i) tv[i] = __builtin_nontemporal_load((const f32x4*)(p + (size_t)i * N));
; }
; template <int MODE> __device__ __forceinline__ void cv_finish(const f32x4 (&tv)[16], int K, int nblk, unsigned char* WT, int item, int lane) {
;     const int kb = item / nblk, nb = item - kb * nblk, k0 = 64 * kb + 16 * (lane >> 4), n0 = 64 * nb + 4 * (lane & 15);
;     unsigned D[16];
; #pragma unroll
;     for (int i = 0; i < 16; ++i) { const f32x2 a = (f32x2){tv[i].x, tv[i].y} * (f32x2){1024.f, 1024.f}, b = (f32x2){tv[i].z, tv[i].w} * (f32x2){1024.f, 1024.f};
;         D[i] = pk4_fp8(a.x, a.y, b.x, b.y); }
;     unsigned O[4][4];
; #pragma unroll
;     for (int q = 0; q < 4; ++q) { const unsigned a = D[4 * q], b = D[4 * q + 1], c = D[4 * q + 2], d = D[4 * q + 3];
;         const unsigned t0 = __builtin_amdgcn_perm(b, a, 0x05010400u), t1 = __builtin_amdgcn_perm(b, a, 0x07030602u), u0 = __builtin_amdgcn_perm(d, c, 0x05010400u), u1 = __builtin_amdgcn_perm(d, c, 0x07030602u);
;         O[0][q] = __builtin_amdgcn_perm(u0, t0, 0x05040100u); O[1][q] = __builtin_amdgcn_perm(u0, t0, 0x07060302u); O[2][q] = __builtin_amdgcn_perm(u1, t1, 0x05040100u); O[3][q] = __builtin_amdgcn_perm(u1, t1, 0x07060302u); }
; #pragma unroll
;     for (int j = 0; j < 4; ++j) { u32x4 o; o.x = O[j][0]; o.y = O[j][1]; o.z = O[j][2]; o.w = O[j][3];
;         __builtin_nontemporal_store(o, (u32x4*)(WT + (size_t)drow<MODE>(n0 + j) * K + k0)); }
; }
	v_pk_mul_f32 v[192:193], v[198:199], s[84:85] op_sel_hi:[1,0]
	v_cvt_pk_fp8_f32 v97, v115, v206
	v_med3_f32 v98, v98, s96, v150
	v_med3_f32 v99, v99, s96, v150
	v_med3_f32 v115, v116, s96, v150
	v_med3_f32 v116, v117, s96, v150
	v_med3_f32 v117, v118, s96, v150
	v_med3_f32 v118, v119, s96, v150
	v_med3_f32 v119, v120, s96, v150
	v_med3_f32 v120, v121, s96, v150
	v_med3_f32 v121, v122, s96, v150
	v_med3_f32 v122, v123, s96, v150
	v_med3_f32 v123, v124, s96, v150
	v_med3_f32 v124, v125, s96, v150
	v_med3_f32 v125, v126, s96, v150
	v_med3_f32 v126, v127, s96, v150
	v_med3_f32 v127, v136, s96, v150
	v_med3_f32 v136, v137, s96, v150
	v_med3_f32 v137, v138, s96, v150
	v_med3_f32 v138, v139, s96, v150
	v_med3_f32 v139, v140, s96, v150
	v_med3_f32 v140, v141, s96, v150
	v_med3_f32 v141, v142, s96, v150
	v_med3_f32 v142, v143, s96, v150
	v_med3_f32 v143, v152, s96, v150
	v_med3_f32 v152, v153, s96, v150
	v_med3_f32 v153, v154, s96, v150
	v_med3_f32 v154, v155, s96, v150
	v_med3_f32 v155, v156, s96, v150
	v_med3_f32 v156, v157, s96, v150
	v_med3_f32 v157, v158, s96, v150
	v_med3_f32 v158, v159, s96, v150
	v_med3_f32 v159, v160, s96, v150
	v_med3_f32 v160, v161, s96, v150
	v_med3_f32 v161, v162, s96, v150
	v_med3_f32 v162, v163, s96, v150
	v_med3_f32 v163, v164, s96, v150
	v_med3_f32 v164, v165, s96, v150
	v_med3_f32 v165, v166, s96, v150
	v_med3_f32 v166, v167, s96, v150
	v_med3_f32 v167, v174, s96, v150
	v_med3_f32 v174, v175, s96, v150
	v_med3_f32 v175, v176, s96, v150
	v_med3_f32 v176, v177, s96, v150
	v_med3_f32 v177, v178, s96, v150
	v_med3_f32 v178, v179, s96, v150
	v_med3_f32 v179, v180, s96, v150
	v_med3_f32 v180, v181, s96, v150
	v_med3_f32 v181, v182, s96, v150
	v_med3_f32 v182, v183, s96, v150
	v_med3_f32 v183, v184, s96, v150
	v_med3_f32 v184, v185, s96, v150
	v_med3_f32 v185, v186, s96, v150
	v_med3_f32 v186, v187, s96, v150
	v_med3_f32 v187, v188, s96, v150
	v_med3_f32 v188, v189, s96, v150
	v_med3_f32 v189, v190, s96, v150
	v_med3_f32 v190, v191, s96, v150
	v_med3_f32 v191, v192, s96, v150
	v_med3_f32 v192, v193, s96, v150
	v_cvt_pk_fp8_f32 v100, v98, v99
	v_cvt_pk_fp8_f32 v101, v117, v118
	v_cvt_pk_fp8_f32 v102, v121, v122
	v_cvt_pk_fp8_f32 v103, v125, v126
	v_cvt_pk_fp8_f32 v104, v137, v138
	v_cvt_pk_fp8_f32 v105, v141, v142
	v_cvt_pk_fp8_f32 v106, v153, v154
	v_cvt_pk_fp8_f32 v107, v157, v158
	v_cvt_pk_fp8_f32 v108, v161, v162
	v_cvt_pk_fp8_f32 v109, v165, v166
	v_cvt_pk_fp8_f32 v110, v175, v176
	v_cvt_pk_fp8_f32 v111, v179, v180
	v_cvt_pk_fp8_f32 v112, v183, v184
	v_cvt_pk_fp8_f32 v113, v187, v188
	v_cvt_pk_fp8_f32 v114, v191, v192
	v_pk_mul_f32 v[194:195], v[200:201], s[84:85] op_sel_hi:[1,0]
	v_cvt_pk_fp8_f32 v97, v145, v208 op_sel:[0,0,1]
	v_med3_f32 v193, v194, s96, v150
	v_med3_f32 v194, v195, s96, v150
	v_cvt_pk_fp8_f32 v100, v115, v116 op_sel:[0,0,1]
	v_cvt_pk_fp8_f32 v101, v119, v120 op_sel:[0,0,1]
	v_cvt_pk_fp8_f32 v102, v123, v124 op_sel:[0,0,1]
	v_cvt_pk_fp8_f32 v103, v127, v136 op_sel:[0,0,1]
	v_cvt_pk_fp8_f32 v104, v139, v140 op_sel:[0,0,1]
	v_cvt_pk_fp8_f32 v105, v143, v152 op_sel:[0,0,1]
	v_cvt_pk_fp8_f32 v106, v155, v156 op_sel:[0,0,1]
	v_cvt_pk_fp8_f32 v107, v159, v160 op_sel:[0,0,1]
	v_cvt_pk_fp8_f32 v108, v163, v164 op_sel:[0,0,1]
	v_cvt_pk_fp8_f32 v109, v167, v174 op_sel:[0,0,1]
	v_cvt_pk_fp8_f32 v110, v177, v178 op_sel:[0,0,1]
	v_cvt_pk_fp8_f32 v111, v181, v182 op_sel:[0,0,1]
	v_cvt_pk_fp8_f32 v112, v185, v186 op_sel:[0,0,1]
	v_cvt_pk_fp8_f32 v113, v189, v190 op_sel:[0,0,1]
	v_cvt_pk_fp8_f32 v114, v193, v194 op_sel:[0,0,1]
	v_perm_b32 v98, v100, v97, s97
	v_perm_b32 v99, v100, v97, s70
	v_perm_b32 v97, v102, v101, s97
	v_perm_b32 v101, v102, v101, s70
	v_perm_b32 v102, v104, v103, s97
	v_perm_b32 v103, v104, v103, s70
	v_perm_b32 v115, v106, v105, s97
	v_perm_b32 v106, v106, v105, s70
	v_perm_b32 v116, v108, v107, s97
	v_perm_b32 v117, v110, v109, s97
	v_perm_b32 v119, v112, v111, s97
	v_perm_b32 v120, v112, v111, s70
	v_perm_b32 v111, v114, v113, s97
	v_perm_b32 v107, v108, v107, s70
	v_perm_b32 v118, v110, v109, s70
	v_perm_b32 v121, v114, v113, s70
	v_perm_b32 v100, v97, v98, s71
	v_perm_b32 v108, v101, v99, s71
	v_perm_b32 v112, v101, v99, s72
	v_perm_b32 v101, v115, v102, s71
	v_perm_b32 v105, v115, v102, s72
	v_perm_b32 v109, v106, v103, s71
	v_perm_b32 v113, v106, v103, s72
	v_perm_b32 v102, v117, v116, s71
	v_perm_b32 v103, v111, v119, s71
	v_perm_b32 v104, v97, v98, s72
	v_perm_b32 v106, v117, v116, s72
	v_perm_b32 v110, v118, v107, s71
	v_perm_b32 v114, v118, v107, s72
	v_perm_b32 v107, v111, v119, s72
	v_perm_b32 v111, v121, v120, s71
	v_perm_b32 v115, v121, v120, s72
	global_store_dwordx4 v[128:129], v[100:103], off nt
	global_store_dwordx4 v[168:169], v[104:107], off nt
	global_store_dwordx4 v[202:203], v[108:111], off nt
	global_store_dwordx4 v[204:205], v[112:115], off nt
	v_mov_b32_e32 v211, v133
	s_lshr_b32 s21, s10, 5
	s_lshl_b32 s22, s21, 11
	v_lshl_or_b32 v210, s21, 6, v1
	s_sub_i32 s21, s11, s22
	v_subrev_u32_e32 v115, s22, v4
	v_lshlrev_b64 v[116:117], 13, v[210:211]
	s_add_i32 s22, s12, s21
	v_lshl_add_u64 v[116:117], s[4:5], 0, v[116:117]
	s_ashr_i32 s23, s22, 31
	v_lshlrev_b32_e32 v98, 2, v130
	v_mov_b32_e32 v99, v211
	v_lshl_add_u64 v[116:117], s[22:23], 2, v[116:117]
	s_movk_i32 s13, 0x2000
	v_lshl_add_u64 v[98:99], v[116:117], 0, v[98:99]
	v_add_co_u32_e32 v136, vcc, s13, v98
	s_movk_i32 s14, 0x6000
	s_nop 0
	v_addc_co_u32_e32 v137, vcc, 0, v99, vcc
	v_add_co_u32_e32 v138, vcc, s1, v98
	s_mov_b32 s15, 0xa000
	s_nop 0
	v_addc_co_u32_e32 v139, vcc, 0, v99, vcc
	v_add_co_u32_e32 v140, vcc, s14, v98
	s_mov_b32 s16, 0xe000
	s_nop 0
	v_addc_co_u32_e32 v141, vcc, 0, v99, vcc
; __device__ __forceinline__ void cv_load(const float* W, int N, int nblk, int item, int lane, f32x4 (&tv)[16]) {
;     const int kb = item / nblk, nb = item - kb * nblk; const float* p = W + (size_t)(64 * kb + 16 * (lane >> 4)) * N + 64 * nb + 4 * (lane & 15);
; #pragma unroll
;     for (int i = 0; i < 16; ++i) tv[i] = __builtin_nontemporal_load((const f32x4*)(p + (size_t)i * N));
; }
; template <int MODE> __device__ __forceinline__ void cv_finish(const f32x4 (&tv)[16], int K, int nblk, unsigned char* WT, int item, int lane) {
;     const int kb = item / nblk, nb = item - kb * nblk, k0 = 64 * kb + 16 * (lane >> 4), n0 = 64 * nb + 4 * (lane & 15);
;     unsigned D[16];
; #pragma unroll
;     for (int i = 0; i < 16; ++i) { const f32x2 a = (f32x2){tv[i].x, tv[i].y} * (f32x2){1024.f, 1024.f}, b = (f32x2){tv[i].z, tv[i].w} * (f32x2){1024.f, 1024.f};
;         D[i] = pk4_fp8(a.x, a.y, b.x, b.y); }
	v_add_co_u32_e32 v142, vcc, s78, v98
	s_mov_b32 s17, 0x12000
	s_nop 0
	v_addc_co_u32_e32 v143, vcc, 0, v99, vcc
	v_add_co_u32_e32 v152, vcc, s15, v98
	s_mov_b32 s18, 0x16000
	s_nop 0
	v_addc_co_u32_e32 v153, vcc, 0, v99, vcc
	v_add_co_u32_e32 v156, vcc, s79, v98
	s_mov_b32 s19, 0x1a000
	s_nop 0
	v_addc_co_u32_e32 v157, vcc, 0, v99, vcc
	v_add_co_u32_e32 v160, vcc, s16, v98
	v_add_u32_e32 v118, s12, v115
	s_nop 0
	v_addc_co_u32_e32 v161, vcc, 0, v99, vcc
	v_add_co_u32_e32 v164, vcc, s86, v98
	v_ashrrev_i32_e32 v119, 31, v118
	s_nop 0
	v_addc_co_u32_e32 v165, vcc, 0, v99, vcc
	v_add_co_u32_e32 v174, vcc, s17, v98
	v_add_u32_e32 v122, 1, v118
	s_nop 0
	v_addc_co_u32_e32 v175, vcc, 0, v99, vcc
	v_add_co_u32_e32 v178, vcc, s87, v98
	v_add_u32_e32 v124, 2, v118
	s_nop 0
	v_addc_co_u32_e32 v179, vcc, 0, v99, vcc
	v_add_co_u32_e32 v182, vcc, s18, v98
	v_add_u32_e32 v126, 3, v118
	s_nop 0
	v_addc_co_u32_e32 v183, vcc, 0, v99, vcc
	v_add_co_u32_e32 v186, vcc, s85, v98
	s_mov_b32 s20, 0x1e000
	s_nop 0
	v_addc_co_u32_e32 v187, vcc, 0, v99, vcc
	v_add_co_u32_e32 v190, vcc, s19, v98
	v_lshl_add_u64 v[120:121], s[6:7], 0, v[210:211]
	s_nop 0
	v_addc_co_u32_e32 v191, vcc, 0, v99, vcc
	v_add_co_u32_e32 v194, vcc, s82, v98
	v_lshlrev_b64 v[118:119], 11, v[118:119]
	v_ashrrev_i32_e32 v123, 31, v122
	v_ashrrev_i32_e32 v125, 31, v124
	v_ashrrev_i32_e32 v127, 31, v126
	v_addc_co_u32_e32 v195, vcc, 0, v99, vcc
	v_lshl_add_u64 v[128:129], v[120:121], 0, v[118:119]
	v_lshlrev_b64 v[122:123], 11, v[122:123]
	v_lshlrev_b64 v[124:125], 11, v[124:125]
	v_lshlrev_b64 v[126:127], 11, v[126:127]
	global_load_dwordx4 v[116:119], v[98:99], off nt
	v_add_co_u32_e32 v98, vcc, s20, v98
	v_lshl_add_u64 v[168:169], v[120:121], 0, v[122:123]
	s_nop 0
	v_addc_co_u32_e32 v99, vcc, 0, v99, vcc
	v_lshl_add_u64 v[202:203], v[120:121], 0, v[124:125]
	v_lshl_add_u64 v[204:205], v[120:121], 0, v[126:127]
	global_load_dwordx4 v[120:123], v[136:137], off nt
	global_load_dwordx4 v[124:127], v[138:139], off nt
	s_nop 0
	global_load_dwordx4 v[136:139], v[140:141], off nt
	s_nop 0
	global_load_dwordx4 v[140:143], v[142:143], off nt
	s_nop 0
	global_load_dwordx4 v[152:155], v[152:153], off nt
	s_nop 0
	global_load_dwordx4 v[156:159], v[156:157], off nt
	s_nop 0
	global_load_dwordx4 v[160:163], v[160:161], off nt
	s_nop 0
	global_load_dwordx4 v[164:167], v[164:165], off nt
	s_nop 0
	global_load_dwordx4 v[174:177], v[174:175], off nt
	s_nop 0
	global_load_dwordx4 v[178:181], v[178:179], off nt
	s_nop 0
	global_load_dwordx4 v[182:185], v[182:183], off nt
	s_nop 0
	global_load_dwordx4 v[186:189], v[186:187], off nt
	s_nop 0
	global_load_dwordx4 v[190:193], v[190:191], off nt
	s_nop 0
	global_load_dwordx4 v[194:197], v[194:195], off nt
	s_nop 0
	global_load_dwordx4 v[198:201], v[98:99], off nt
	v_mov_b32_e32 v97, v211
	v_mov_b32_e32 v100, v211
	v_mov_b32_e32 v101, v211
	v_mov_b32_e32 v102, v211
	v_mov_b32_e32 v103, v211
	v_mov_b32_e32 v104, v211
	v_mov_b32_e32 v105, v211
	v_mov_b32_e32 v106, v211
	v_mov_b32_e32 v107, v211
	v_mov_b32_e32 v108, v211
	v_mov_b32_e32 v109, v211
	v_mov_b32_e32 v110, v211
	v_mov_b32_e32 v111, v211
	v_mov_b32_e32 v112, v211
	v_mov_b32_e32 v113, v211
	v_mov_b32_e32 v114, v211
	s_add_i32 s10, s10, 1
	s_add_i32 s12, s12, 64
	s_cmpk_eq_i32 s12, 0x100
	s_waitcnt vmcnt(35)
	v_pk_mul_f32 v[2:3], v[22:23], s[84:85] op_sel_hi:[1,0]
	v_pk_mul_f32 v[22:23], v[24:25], s[84:85] op_sel_hi:[1,0]
	v_med3_f32 v21, v2, s96, v150
	v_med3_f32 v94, v3, s96, v150
	v_med3_f32 v95, v22, s96, v150
	v_med3_f32 v96, v23, s96, v150
	s_waitcnt vmcnt(34)
	v_pk_mul_f32 v[2:3], v[26:27], s[84:85] op_sel_hi:[1,0]
	v_pk_mul_f32 v[22:23], v[28:29], s[84:85] op_sel_hi:[1,0]
	s_waitcnt vmcnt(33)
	v_pk_mul_f32 v[24:25], v[30:31], s[84:85] op_sel_hi:[1,0]
	v_pk_mul_f32 v[26:27], v[32:33], s[84:85] op_sel_hi:[1,0]
	s_waitcnt vmcnt(32)
	v_pk_mul_f32 v[28:29], v[34:35], s[84:85] op_sel_hi:[1,0]
	v_pk_mul_f32 v[30:31], v[36:37], s[84:85] op_sel_hi:[1,0]
	s_waitcnt vmcnt(31)
	v_pk_mul_f32 v[32:33], v[38:39], s[84:85] op_sel_hi:[1,0]
	v_pk_mul_f32 v[34:35], v[40:41], s[84:85] op_sel_hi:[1,0]
	s_waitcnt vmcnt(30)
	v_pk_mul_f32 v[36:37], v[42:43], s[84:85] op_sel_hi:[1,0]
	v_pk_mul_f32 v[38:39], v[44:45], s[84:85] op_sel_hi:[1,0]
	s_waitcnt vmcnt(29)
	v_pk_mul_f32 v[40:41], v[46:47], s[84:85] op_sel_hi:[1,0]
	v_pk_mul_f32 v[42:43], v[48:49], s[84:85] op_sel_hi:[1,0]
	s_waitcnt vmcnt(28)
	v_pk_mul_f32 v[44:45], v[50:51], s[84:85] op_sel_hi:[1,0]
	v_pk_mul_f32 v[46:47], v[52:53], s[84:85] op_sel_hi:[1,0]
	s_waitcnt vmcnt(27)
	v_pk_mul_f32 v[48:49], v[54:55], s[84:85] op_sel_hi:[1,0]
	v_pk_mul_f32 v[50:51], v[56:57], s[84:85] op_sel_hi:[1,0]
	s_waitcnt vmcnt(26)
	v_pk_mul_f32 v[52:53], v[58:59], s[84:85] op_sel_hi:[1,0]
	v_pk_mul_f32 v[54:55], v[60:61], s[84:85] op_sel_hi:[1,0]
	s_waitcnt vmcnt(25)
	v_pk_mul_f32 v[56:57], v[62:63], s[84:85] op_sel_hi:[1,0]
	v_pk_mul_f32 v[58:59], v[64:65], s[84:85] op_sel_hi:[1,0]
	s_waitcnt vmcnt(24)
	v_pk_mul_f32 v[60:61], v[66:67], s[84:85] op_sel_hi:[1,0]
	v_pk_mul_f32 v[62:63], v[68:69], s[84:85] op_sel_hi:[1,0]
	s_waitcnt vmcnt(23)
	v_pk_mul_f32 v[64:65], v[70:71], s[84:85] op_sel_hi:[1,0]
	v_pk_mul_f32 v[66:67], v[72:73], s[84:85] op_sel_hi:[1,0]
	s_waitcnt vmcnt(22)
	v_pk_mul_f32 v[68:69], v[74:75], s[84:85] op_sel_hi:[1,0]
	v_pk_mul_f32 v[70:71], v[76:77], s[84:85] op_sel_hi:[1,0]
	s_waitcnt vmcnt(21)
	v_pk_mul_f32 v[72:73], v[78:79], s[84:85] op_sel_hi:[1,0]
	v_pk_mul_f32 v[74:75], v[80:81], s[84:85] op_sel_hi:[1,0]
	s_waitcnt vmcnt(20)
; template <int MODE> __device__ __forceinline__ void cv_finish(const f32x4 (&tv)[16], int K, int nblk, unsigned char* WT, int item, int lane) {
;     const int kb = item / nblk, nb = item - kb * nblk, k0 = 64 * kb + 16 * (lane >> 4), n0 = 64 * nb + 4 * (lane & 15);
;     unsigned D[16];
; #pragma unroll
;     for (int i = 0; i < 16; ++i) { const f32x2 a = (f32x2){tv[i].x, tv[i].y} * (f32x2){1024.f, 1024.f}, b = (f32x2){tv[i].z, tv[i].w} * (f32x2){1024.f, 1024.f};
;         D[i] = pk4_fp8(a.x, a.y, b.x, b.y); }
;     unsigned O[4][4];
; #pragma unroll
;     for (int q = 0; q < 4; ++q) { const unsigned a = D[4 * q], b = D[4 * q + 1], c = D[4 * q + 2], d = D[4 * q + 3];
;         const unsigned t0 = __builtin_amdgcn_perm(b, a, 0x05010400u), t1 = __builtin_amdgcn_perm(b, a, 0x07030602u), u0 = __builtin_amdgcn_perm(d, c, 0x05010400u), u1 = __builtin_amdgcn_perm(d, c, 0x07030602u);
;         O[0][q] = __builtin_amdgcn_perm(u0, t0, 0x05040100u); O[1][q] = __builtin_amdgcn_perm(u0, t0, 0x07060302u); O[2][q] = __builtin_amdgcn_perm(u1, t1, 0x05040100u); O[3][q] = __builtin_amdgcn_perm(u1, t1, 0x07060302u); }
; #pragma unroll
;     for (int j = 0; j < 4; ++j) { u32x4 o; o.x = O[j][0]; o.y = O[j][1]; o.z = O[j][2]; o.w = O[j][3];
;         __builtin_nontemporal_store(o, (u32x4*)(WT + (size_t)drow<MODE>(n0 + j) * K + k0)); }
; }
	v_pk_mul_f32 v[76:77], v[82:83], s[84:85] op_sel_hi:[1,0]
	v_cvt_pk_fp8_f32 v5, v21, v94
	v_med3_f32 v2, v2, s96, v150
	v_med3_f32 v3, v3, s96, v150
	v_med3_f32 v21, v22, s96, v150
	v_med3_f32 v22, v23, s96, v150
	v_med3_f32 v23, v24, s96, v150
	v_med3_f32 v24, v25, s96, v150
	v_med3_f32 v25, v26, s96, v150
	v_med3_f32 v26, v27, s96, v150
	v_med3_f32 v27, v28, s96, v150
	v_med3_f32 v28, v29, s96, v150
	v_med3_f32 v29, v30, s96, v150
	v_med3_f32 v30, v31, s96, v150
	v_med3_f32 v31, v32, s96, v150
	v_med3_f32 v32, v33, s96, v150
	v_med3_f32 v33, v34, s96, v150
	v_med3_f32 v34, v35, s96, v150
	v_med3_f32 v35, v36, s96, v150
	v_med3_f32 v36, v37, s96, v150
	v_med3_f32 v37, v38, s96, v150
	v_med3_f32 v38, v39, s96, v150
	v_med3_f32 v39, v40, s96, v150
	v_med3_f32 v40, v41, s96, v150
	v_med3_f32 v41, v42, s96, v150
	v_med3_f32 v42, v43, s96, v150
	v_med3_f32 v43, v44, s96, v150
	v_med3_f32 v44, v45, s96, v150
	v_med3_f32 v45, v46, s96, v150
	v_med3_f32 v46, v47, s96, v150
	v_med3_f32 v47, v48, s96, v150
	v_med3_f32 v48, v49, s96, v150
	v_med3_f32 v49, v50, s96, v150
	v_med3_f32 v50, v51, s96, v150
	v_med3_f32 v51, v52, s96, v150
	v_med3_f32 v52, v53, s96, v150
	v_med3_f32 v53, v54, s96, v150
	v_med3_f32 v54, v55, s96, v150
	v_med3_f32 v55, v56, s96, v150
	v_med3_f32 v56, v57, s96, v150
	v_med3_f32 v57, v58, s96, v150
	v_med3_f32 v58, v59, s96, v150
	v_med3_f32 v59, v60, s96, v150
	v_med3_f32 v60, v61, s96, v150
	v_med3_f32 v61, v62, s96, v150
	v_med3_f32 v62, v63, s96, v150
	v_med3_f32 v63, v64, s96, v150
	v_med3_f32 v64, v65, s96, v150
	v_med3_f32 v65, v66, s96, v150
	v_med3_f32 v66, v67, s96, v150
	v_med3_f32 v67, v68, s96, v150
	v_med3_f32 v68, v69, s96, v150
	v_med3_f32 v69, v70, s96, v150
	v_med3_f32 v70, v71, s96, v150
	v_med3_f32 v71, v72, s96, v150
	v_med3_f32 v72, v73, s96, v150
	v_med3_f32 v73, v74, s96, v150
	v_med3_f32 v74, v75, s96, v150
	v_med3_f32 v75, v76, s96, v150
	v_med3_f32 v76, v77, s96, v150
	v_cvt_pk_fp8_f32 v6, v2, v3
	v_cvt_pk_fp8_f32 v7, v23, v24
	v_cvt_pk_fp8_f32 v8, v27, v28
	v_cvt_pk_fp8_f32 v9, v31, v32
	v_cvt_pk_fp8_f32 v10, v35, v36
	v_cvt_pk_fp8_f32 v11, v39, v40
	v_cvt_pk_fp8_f32 v12, v43, v44
	v_cvt_pk_fp8_f32 v13, v47, v48
	v_cvt_pk_fp8_f32 v14, v51, v52
	v_cvt_pk_fp8_f32 v15, v55, v56
	v_cvt_pk_fp8_f32 v16, v59, v60
	v_cvt_pk_fp8_f32 v17, v63, v64
	v_cvt_pk_fp8_f32 v18, v67, v68
	v_cvt_pk_fp8_f32 v19, v71, v72
	v_cvt_pk_fp8_f32 v20, v75, v76
	v_pk_mul_f32 v[78:79], v[84:85], s[84:85] op_sel_hi:[1,0]
	v_cvt_pk_fp8_f32 v5, v95, v96 op_sel:[0,0,1]
	v_med3_f32 v77, v78, s96, v150
	v_med3_f32 v78, v79, s96, v150
	v_cvt_pk_fp8_f32 v6, v21, v22 op_sel:[0,0,1]
	v_cvt_pk_fp8_f32 v7, v25, v26 op_sel:[0,0,1]
	v_cvt_pk_fp8_f32 v8, v29, v30 op_sel:[0,0,1]
	v_cvt_pk_fp8_f32 v9, v33, v34 op_sel:[0,0,1]
	v_cvt_pk_fp8_f32 v10, v37, v38 op_sel:[0,0,1]
	v_cvt_pk_fp8_f32 v11, v41, v42 op_sel:[0,0,1]
	v_cvt_pk_fp8_f32 v12, v45, v46 op_sel:[0,0,1]
	v_cvt_pk_fp8_f32 v13, v49, v50 op_sel:[0,0,1]
	v_cvt_pk_fp8_f32 v14, v53, v54 op_sel:[0,0,1]
	v_cvt_pk_fp8_f32 v15, v57, v58 op_sel:[0,0,1]
	v_cvt_pk_fp8_f32 v16, v61, v62 op_sel:[0,0,1]
	v_cvt_pk_fp8_f32 v17, v65, v66 op_sel:[0,0,1]
	v_cvt_pk_fp8_f32 v18, v69, v70 op_sel:[0,0,1]
	v_cvt_pk_fp8_f32 v19, v73, v74 op_sel:[0,0,1]
	v_cvt_pk_fp8_f32 v20, v77, v78 op_sel:[0,0,1]
	v_perm_b32 v2, v6, v5, s97
	v_perm_b32 v3, v6, v5, s70
	v_perm_b32 v5, v8, v7, s97
	v_perm_b32 v7, v8, v7, s70
	v_perm_b32 v8, v10, v9, s97
	v_perm_b32 v9, v10, v9, s70
	v_perm_b32 v21, v12, v11, s97
	v_perm_b32 v12, v12, v11, s70
	v_perm_b32 v22, v14, v13, s97
	v_perm_b32 v23, v16, v15, s97
	v_perm_b32 v25, v18, v17, s97
	v_perm_b32 v26, v18, v17, s70
	v_perm_b32 v17, v20, v19, s97
	v_perm_b32 v13, v14, v13, s70
	v_perm_b32 v24, v16, v15, s70
	v_perm_b32 v27, v20, v19, s70
	v_perm_b32 v6, v5, v2, s71
	v_perm_b32 v14, v7, v3, s71
	v_perm_b32 v18, v7, v3, s72
	v_perm_b32 v7, v21, v8, s71
	v_perm_b32 v11, v21, v8, s72
	v_perm_b32 v15, v12, v9, s71
	v_perm_b32 v19, v12, v9, s72
	v_perm_b32 v8, v23, v22, s71
	v_perm_b32 v9, v17, v25, s71
	v_perm_b32 v10, v5, v2, s72
	v_perm_b32 v12, v23, v22, s72
	v_perm_b32 v16, v24, v13, s71
	v_perm_b32 v20, v24, v13, s72
	v_perm_b32 v13, v17, v25, s72
	v_perm_b32 v17, v27, v26, s71
	v_perm_b32 v21, v27, v26, s72
	global_store_dwordx4 v[86:87], v[6:9], off nt
	global_store_dwordx4 v[88:89], v[10:13], off nt
	global_store_dwordx4 v[90:91], v[14:17], off nt
	global_store_dwordx4 v[92:93], v[18:21], off nt
	s_waitcnt vmcnt(19)
	v_pk_mul_f32 v[98:99], v[116:117], s[84:85] op_sel_hi:[1,0]
	v_pk_mul_f32 v[116:117], v[118:119], s[84:85] op_sel_hi:[1,0]
	v_med3_f32 v115, v98, s96, v150
	v_med3_f32 v206, v99, s96, v150
	v_med3_f32 v145, v116, s96, v150
	v_med3_f32 v208, v117, s96, v150
	s_waitcnt vmcnt(18)
	v_pk_mul_f32 v[98:99], v[120:121], s[84:85] op_sel_hi:[1,0]
	v_pk_mul_f32 v[116:117], v[122:123], s[84:85] op_sel_hi:[1,0]
	s_waitcnt vmcnt(17)
	v_pk_mul_f32 v[118:119], v[124:125], s[84:85] op_sel_hi:[1,0]
	v_pk_mul_f32 v[120:121], v[126:127], s[84:85] op_sel_hi:[1,0]
	s_waitcnt vmcnt(16)
	v_pk_mul_f32 v[122:123], v[136:137], s[84:85] op_sel_hi:[1,0]
	v_pk_mul_f32 v[124:125], v[138:139], s[84:85] op_sel_hi:[1,0]
	s_waitcnt vmcnt(15)
	v_pk_mul_f32 v[126:127], v[140:141], s[84:85] op_sel_hi:[1,0]
	v_pk_mul_f32 v[136:137], v[142:143], s[84:85] op_sel_hi:[1,0]
	s_waitcnt vmcnt(14)
	v_pk_mul_f32 v[138:139], v[152:153], s[84:85] op_sel_hi:[1,0]
	v_pk_mul_f32 v[140:141], v[154:155], s[84:85] op_sel_hi:[1,0]
	s_waitcnt vmcnt(13)
	v_pk_mul_f32 v[142:143], v[156:157], s[84:85] op_sel_hi:[1,0]
	v_pk_mul_f32 v[152:153], v[158:159], s[84:85] op_sel_hi:[1,0]
	s_waitcnt vmcnt(12)
; __device__ __forceinline__ unsigned pk4_fp8(float a, float b, float c, float d) {
;     a = __builtin_fminf(__builtin_fmaxf(a, -448.f), 448.f); b = __builtin_fminf(__builtin_fmaxf(b, -448.f), 448.f); c = __builtin_fminf(__builtin_fmaxf(c, -448.f), 448.f); d = __builtin_fminf(__builtin_fmaxf(d, -448.f), 448.f);
;     int w = 0; w = __builtin_amdgcn_cvt_pk_fp8_f32(a, b, w, false); w = __builtin_amdgcn_cvt_pk_fp8_f32(c, d, w, true); return (unsigned)w;
; template <int MODE> __device__ __forceinline__ void cv_finish(const f32x4 (&tv)[16], int K, int nblk, unsigned char* WT, int item, int lane) {
;     const int kb = item / nblk, nb = item - kb * nblk, k0 = 64 * kb + 16 * (lane >> 4), n0 = 64 * nb + 4 * (lane & 15);
;     unsigned D[16];
; #pragma unroll
;     for (int i = 0; i < 16; ++i) { const f32x2 a = (f32x2){tv[i].x, tv[i].y} * (f32x2){1024.f, 1024.f}, b = (f32x2){tv[i].z, tv[i].w} * (f32x2){1024.f, 1024.f};
;         D[i] = pk4_fp8(a.x, a.y, b.x, b.y); }
;     unsigned O[4][4];
; #pragma unroll
;     for (int q = 0; q < 4; ++q) { const unsigned a = D[4 * q], b = D[4 * q + 1], c = D[4 * q + 2], d = D[4 * q + 3];
;         const unsigned t0 = __builtin_amdgcn_perm(b, a, 0x05010400u), t1 = __builtin_amdgcn_perm(b, a, 0x07030602u), u0 = __builtin_amdgcn_perm(d, c, 0x05010400u), u1 = __builtin_amdgcn_perm(d, c, 0x07030602u);
;         O[0][q] = __builtin_amdgcn_perm(u0, t0, 0x05040100u); O[1][q] = __builtin_amdgcn_perm(u0, t0, 0x07060302u); O[2][q] = __builtin_amdgcn_perm(u1, t1, 0x05040100u); O[3][q] = __builtin_amdgcn_perm(u1, t1, 0x07060302u); }
; #pragma unroll
;     for (int j = 0; j < 4; ++j) { u32x4 o; o.x = O[j][0]; o.y = O[j][1]; o.z = O[j][2]; o.w = O[j][3];
;         __builtin_nontemporal_store(o, (u32x4*)(WT + (size_t)drow<MODE>(n0 + j) * K + k0)); }
; }
	v_pk_mul_f32 v[154:155], v[160:161], s[84:85] op_sel_hi:[1,0]
	v_pk_mul_f32 v[156:157], v[162:163], s[84:85] op_sel_hi:[1,0]
	s_waitcnt vmcnt(11)
	v_pk_mul_f32 v[158:159], v[164:165], s[84:85] op_sel_hi:[1,0]
	v_pk_mul_f32 v[160:161], v[166:167], s[84:85] op_sel_hi:[1,0]
	s_waitcnt vmcnt(10)
	v_pk_mul_f32 v[162:163], v[174:175], s[84:85] op_sel_hi:[1,0]
	v_pk_mul_f32 v[164:165], v[176:177], s[84:85] op_sel_hi:[1,0]
	s_waitcnt vmcnt(9)
	v_pk_mul_f32 v[166:167], v[178:179], s[84:85] op_sel_hi:[1,0]
	v_pk_mul_f32 v[174:175], v[180:181], s[84:85] op_sel_hi:[1,0]
	s_waitcnt vmcnt(8)
	v_pk_mul_f32 v[176:177], v[182:183], s[84:85] op_sel_hi:[1,0]
	v_pk_mul_f32 v[178:179], v[184:185], s[84:85] op_sel_hi:[1,0]
	s_waitcnt vmcnt(7)
	v_pk_mul_f32 v[180:181], v[186:187], s[84:85] op_sel_hi:[1,0]
	v_pk_mul_f32 v[182:183], v[188:189], s[84:85] op_sel_hi:[1,0]
	s_waitcnt vmcnt(6)
	v_pk_mul_f32 v[184:185], v[190:191], s[84:85] op_sel_hi:[1,0]
	v_pk_mul_f32 v[186:187], v[192:193], s[84:85] op_sel_hi:[1,0]
	s_waitcnt vmcnt(5)
	v_pk_mul_f32 v[188:189], v[194:195], s[84:85] op_sel_hi:[1,0]
	v_pk_mul_f32 v[190:191], v[196:197], s[84:85] op_sel_hi:[1,0]
	s_waitcnt vmcnt(4)
	v_pk_mul_f32 v[192:193], v[198:199], s[84:85] op_sel_hi:[1,0]
	v_cvt_pk_fp8_f32 v97, v115, v206
	v_med3_f32 v98, v98, s96, v150
	v_med3_f32 v99, v99, s96, v150
	v_med3_f32 v115, v116, s96, v150
	v_med3_f32 v116, v117, s96, v150
	v_med3_f32 v117, v118, s96, v150
	v_med3_f32 v118, v119, s96, v150
	v_med3_f32 v119, v120, s96, v150
	v_med3_f32 v120, v121, s96, v150
	v_med3_f32 v121, v122, s96, v150
	v_med3_f32 v122, v123, s96, v150
	v_med3_f32 v123, v124, s96, v150
	v_med3_f32 v124, v125, s96, v150
	v_med3_f32 v125, v126, s96, v150
	v_med3_f32 v126, v127, s96, v150
	v_med3_f32 v127, v136, s96, v150
	v_med3_f32 v136, v137, s96, v150
	v_med3_f32 v137, v138, s96, v150
	v_med3_f32 v138, v139, s96, v150
	v_med3_f32 v139, v140, s96, v150
	v_med3_f32 v140, v141, s96, v150
	v_med3_f32 v141, v142, s96, v150
	v_med3_f32 v142, v143, s96, v150
	v_med3_f32 v143, v152, s96, v150
	v_med3_f32 v152, v153, s96, v150
	v_med3_f32 v153, v154, s96, v150
	v_med3_f32 v154, v155, s96, v150
	v_med3_f32 v155, v156, s96, v150
	v_med3_f32 v156, v157, s96, v150
	v_med3_f32 v157, v158, s96, v150
	v_med3_f32 v158, v159, s96, v150
	v_med3_f32 v159, v160, s96, v150
	v_med3_f32 v160, v161, s96, v150
	v_med3_f32 v161, v162, s96, v150
	v_med3_f32 v162, v163, s96, v150
	v_med3_f32 v163, v164, s96, v150
	v_med3_f32 v164, v165, s96, v150
	v_med3_f32 v165, v166, s96, v150
	v_med3_f32 v166, v167, s96, v150
	v_med3_f32 v167, v174, s96, v150
	v_med3_f32 v174, v175, s96, v150
	v_med3_f32 v175, v176, s96, v150
	v_med3_f32 v176, v177, s96, v150
	v_med3_f32 v177, v178, s96, v150
	v_med3_f32 v178, v179, s96, v150
	v_med3_f32 v179, v180, s96, v150
	v_med3_f32 v180, v181, s96, v150
	v_med3_f32 v181, v182, s96, v150
	v_med3_f32 v182, v183, s96, v150
	v_med3_f32 v183, v184, s96, v150
	v_med3_f32 v184, v185, s96, v150
	v_med3_f32 v185, v186, s96, v150
	v_med3_f32 v186, v187, s96, v150
	v_med3_f32 v187, v188, s96, v150
	v_med3_f32 v188, v189, s96, v150
	v_med3_f32 v189, v190, s96, v150
	v_med3_f32 v190, v191, s96, v150
	v_med3_f32 v191, v192, s96, v150
	v_med3_f32 v192, v193, s96, v150
	v_cvt_pk_fp8_f32 v100, v98, v99
	v_cvt_pk_fp8_f32 v101, v117, v118
	v_cvt_pk_fp8_f32 v102, v121, v122
	v_cvt_pk_fp8_f32 v103, v125, v126
	v_cvt_pk_fp8_f32 v104, v137, v138
	v_cvt_pk_fp8_f32 v105, v141, v142
	v_cvt_pk_fp8_f32 v106, v153, v154
	v_cvt_pk_fp8_f32 v107, v157, v158
	v_cvt_pk_fp8_f32 v108, v161, v162
	v_cvt_pk_fp8_f32 v109, v165, v166
	v_cvt_pk_fp8_f32 v110, v175, v176
	v_cvt_pk_fp8_f32 v111, v179, v180
	v_cvt_pk_fp8_f32 v112, v183, v184
	v_cvt_pk_fp8_f32 v113, v187, v188
	v_cvt_pk_fp8_f32 v114, v191, v192
	v_pk_mul_f32 v[194:195], v[200:201], s[84:85] op_sel_hi:[1,0]
	v_cvt_pk_fp8_f32 v97, v145, v208 op_sel:[0,0,1]
	v_med3_f32 v193, v194, s96, v150
	v_med3_f32 v194, v195, s96, v150
	v_cvt_pk_fp8_f32 v100, v115, v116 op_sel:[0,0,1]
	v_cvt_pk_fp8_f32 v101, v119, v120 op_sel:[0,0,1]
	v_cvt_pk_fp8_f32 v102, v123, v124 op_sel:[0,0,1]
	v_cvt_pk_fp8_f32 v103, v127, v136 op_sel:[0,0,1]
	v_cvt_pk_fp8_f32 v104, v139, v140 op_sel:[0,0,1]
	v_cvt_pk_fp8_f32 v105, v143, v152 op_sel:[0,0,1]
	v_cvt_pk_fp8_f32 v106, v155, v156 op_sel:[0,0,1]
	v_cvt_pk_fp8_f32 v107, v159, v160 op_sel:[0,0,1]
	v_cvt_pk_fp8_f32 v108, v163, v164 op_sel:[0,0,1]
	v_cvt_pk_fp8_f32 v109, v167, v174 op_sel:[0,0,1]
	v_cvt_pk_fp8_f32 v110, v177, v178 op_sel:[0,0,1]
	v_cvt_pk_fp8_f32 v111, v181, v182 op_sel:[0,0,1]
	v_cvt_pk_fp8_f32 v112, v185, v186 op_sel:[0,0,1]
	v_cvt_pk_fp8_f32 v113, v189, v190 op_sel:[0,0,1]
	v_cvt_pk_fp8_f32 v114, v193, v194 op_sel:[0,0,1]
	v_perm_b32 v98, v100, v97, s97
	v_perm_b32 v99, v100, v97, s70
	v_perm_b32 v97, v102, v101, s97
	v_perm_b32 v101, v102, v101, s70
	v_perm_b32 v102, v104, v103, s97
	v_perm_b32 v103, v104, v103, s70
	v_perm_b32 v115, v106, v105, s97
	v_perm_b32 v106, v106, v105, s70
	v_perm_b32 v116, v108, v107, s97
	v_perm_b32 v117, v110, v109, s97
	v_perm_b32 v119, v112, v111, s97
	v_perm_b32 v120, v112, v111, s70
	v_perm_b32 v111, v114, v113, s97
	v_perm_b32 v107, v108, v107, s70
	v_perm_b32 v118, v110, v109, s70
	v_perm_b32 v121, v114, v113, s70
	v_perm_b32 v100, v97, v98, s71
	v_perm_b32 v108, v101, v99, s71
	v_perm_b32 v112, v101, v99, s72
	v_perm_b32 v101, v115, v102, s71
	v_perm_b32 v105, v115, v102, s72
	v_perm_b32 v109, v106, v103, s71
	v_perm_b32 v113, v106, v103, s72
	v_perm_b32 v102, v117, v116, s71
	v_perm_b32 v103, v111, v119, s71
	v_perm_b32 v104, v97, v98, s72
	v_perm_b32 v106, v117, v116, s72
	v_perm_b32 v110, v118, v107, s71
	v_perm_b32 v114, v118, v107, s72
	v_perm_b32 v107, v111, v119, s72
	v_perm_b32 v111, v121, v120, s71
	v_perm_b32 v115, v121, v120, s72
	global_store_dwordx4 v[128:129], v[100:103], off nt
	global_store_dwordx4 v[168:169], v[104:107], off nt
	global_store_dwordx4 v[202:203], v[108:111], off nt
	global_store_dwordx4 v[204:205], v[112:115], off nt
	s_cbranch_scc0 .LBB0_729
	s_mov_b64 s[4:5], 0

; template <int MODE> __device__ __forceinline__ int drow(int n) {
;     if (MODE == 1) { const int h = n / 192, nl = n - h * 192; return nl < 128 ? n : h * 192 + 128 + ((nl - 128) & 31) * 2 + ((nl - 128) >> 5); }
;     if (MODE == 2) { return n < FF ? ((n >> 7) * 256 + (n & 127)) : (((n - FF) >> 7) * 256 + 128 + ((n - FF) & 127)); }
;     return n;
; }
; __device__ __forceinline__ void cv_load(const float* W, int N, int nblk, int item, int lane, f32x4 (&tv)[16]) {
;     const int kb = item / nblk, nb = item - kb * nblk; const float* p = W + (size_t)(64 * kb + 16 * (lane >> 4)) * N + 64 * nb + 4 * (lane & 15);
; #pragma unroll
;     for (int i = 0; i < 16; ++i) tv[i] = __builtin_nontemporal_load((const f32x4*)(p + (size_t)i * N));
; }
.LBB0_734:
	s_ashr_i32 s8, s10, 31
	s_lshr_b32 s8, s8, 26
	s_add_i32 s8, s10, s8
	s_ashr_i32 s13, s8, 6
	s_andn2_b32 s8, s8, 63
	v_or_b32_e32 v66, s8, v1
	v_ashrrev_i32_e32 v67, 31, v66
	s_lshl_b32 s8, s13, 12
	v_lshlrev_b64 v[2:3], 14, v[66:67]
	s_sub_i32 s8, s11, s8
	v_lshl_add_u64 v[2:3], s[4:5], 0, v[2:3]
	s_ashr_i32 s9, s8, 31
	v_lshl_add_u64 v[2:3], s[8:9], 2, v[2:3]
	v_lshlrev_b32_e32 v132, 2, v130
	v_lshl_add_u64 v[2:3], v[2:3], 0, v[132:133]
	v_add_co_u32_e32 v4, vcc, s1, v2
	s_mov_b32 s9, 0x20000
	s_nop 0
	v_addc_co_u32_e32 v5, vcc, 0, v3, vcc
	global_load_dwordx4 v[62:65], v[2:3], off nt
	global_load_dwordx4 v[58:61], v[4:5], off nt
	v_add_co_u32_e32 v4, vcc, s78, v2
	v_add_u32_e32 v72, s8, v130
	s_nop 0
	v_addc_co_u32_e32 v5, vcc, 0, v3, vcc
	v_add_co_u32_e32 v6, vcc, s79, v2
	v_add_u32_e32 v68, s12, v70
	s_nop 0
	v_addc_co_u32_e32 v7, vcc, 0, v3, vcc
	global_load_dwordx4 v[54:57], v[4:5], off nt
	global_load_dwordx4 v[50:53], v[6:7], off nt
	v_add_co_u32_e32 v4, vcc, s86, v2
	s_lshl_b32 s8, s13, 13
	s_nop 0
	v_addc_co_u32_e32 v5, vcc, 0, v3, vcc
	v_add_co_u32_e32 v6, vcc, s87, v2
	v_subrev_u32_e32 v71, s8, v68
	s_nop 0
	v_addc_co_u32_e32 v7, vcc, 0, v3, vcc
	global_load_dwordx4 v[46:49], v[4:5], off nt
	global_load_dwordx4 v[42:45], v[6:7], off nt
	v_add_co_u32_e32 v4, vcc, s85, v2
	s_nop 1
	v_addc_co_u32_e32 v5, vcc, 0, v3, vcc
	v_add_co_u32_e32 v6, vcc, s82, v2
	s_nop 1
	v_addc_co_u32_e32 v7, vcc, 0, v3, vcc
	global_load_dwordx4 v[38:41], v[4:5], off nt
	global_load_dwordx4 v[34:37], v[6:7], off nt
	v_add_co_u32_e32 v4, vcc, s9, v2
	s_mov_b32 s9, 0x24000
	s_nop 0
	v_addc_co_u32_e32 v5, vcc, 0, v3, vcc
	v_add_co_u32_e32 v6, vcc, s9, v2
	s_mov_b32 s9, 0x28000
	s_nop 0
	v_addc_co_u32_e32 v7, vcc, 0, v3, vcc
	global_load_dwordx4 v[30:33], v[4:5], off nt
	global_load_dwordx4 v[26:29], v[6:7], off nt
	v_add_co_u32_e32 v4, vcc, s9, v2
	s_mov_b32 s9, 0x2c000
	s_nop 0
	v_addc_co_u32_e32 v5, vcc, 0, v3, vcc
	v_add_co_u32_e32 v6, vcc, s9, v2
	s_mov_b32 s9, 0x30000
	s_nop 0
	v_addc_co_u32_e32 v7, vcc, 0, v3, vcc
	global_load_dwordx4 v[22:25], v[4:5], off nt
	global_load_dwordx4 v[18:21], v[6:7], off nt
	v_add_co_u32_e32 v4, vcc, s9, v2
	s_mov_b32 s9, 0x34000
	s_nop 0
	v_addc_co_u32_e32 v5, vcc, 0, v3, vcc
	v_add_co_u32_e32 v6, vcc, s9, v2
	s_nop 1
	v_addc_co_u32_e32 v7, vcc, 0, v3, vcc
	global_load_dwordx4 v[14:17], v[4:5], off nt
	global_load_dwordx4 v[10:13], v[6:7], off nt
	v_add_co_u32_e32 v4, vcc, 0x38000, v2
	s_nop 1
	v_addc_co_u32_e32 v5, vcc, 0, v3, vcc
	v_add_co_u32_e32 v2, vcc, 0x3c000, v2
	s_nop 1
	v_addc_co_u32_e32 v3, vcc, 0, v3, vcc
	global_load_dwordx4 v[6:9], v[4:5], off nt
	s_nop 0
	global_load_dwordx4 v[2:5], v[2:3], off nt
	s_addk_i32 s12, 0x80
	s_add_i32 s11, s11, 64
	s_add_i32 s10, s10, 1
	s_ashr_i32 s8, s10, 31
	s_lshr_b32 s8, s8, 26
	s_add_i32 s8, s10, s8
	s_ashr_i32 s13, s8, 6
	s_andn2_b32 s8, s8, 63
	v_or_b32_e32 v156, s8, v1
	v_ashrrev_i32_e32 v157, 31, v156
	s_lshl_b32 s8, s13, 12
	v_lshlrev_b64 v[78:79], 14, v[156:157]
	s_sub_i32 s8, s11, s8
	v_lshl_add_u64 v[78:79], s[4:5], 0, v[78:79]
	s_ashr_i32 s9, s8, 31
	v_lshl_add_u64 v[78:79], s[8:9], 2, v[78:79]
	v_lshlrev_b32_e32 v132, 2, v130
	v_lshl_add_u64 v[78:79], v[78:79], 0, v[132:133]
	v_add_co_u32_e32 v80, vcc, s1, v78
	s_mov_b32 s9, 0x20000
	s_nop 0
	v_addc_co_u32_e32 v81, vcc, 0, v79, vcc
	global_load_dwordx4 v[152:155], v[78:79], off nt
	global_load_dwordx4 v[140:143], v[80:81], off nt
	v_add_co_u32_e32 v80, vcc, s78, v78
	v_add_u32_e32 v160, s8, v130
	s_nop 0
	v_addc_co_u32_e32 v81, vcc, 0, v79, vcc
	v_add_co_u32_e32 v82, vcc, s79, v78
	v_add_u32_e32 v158, s12, v70
	s_nop 0
	v_addc_co_u32_e32 v83, vcc, 0, v79, vcc
	global_load_dwordx4 v[136:139], v[80:81], off nt
	global_load_dwordx4 v[126:129], v[82:83], off nt
	v_add_co_u32_e32 v80, vcc, s86, v78
	s_lshl_b32 s8, s13, 13
	s_nop 0
	v_addc_co_u32_e32 v81, vcc, 0, v79, vcc
	v_add_co_u32_e32 v82, vcc, s87, v78
	v_subrev_u32_e32 v73, s8, v158
	s_nop 0
	v_addc_co_u32_e32 v83, vcc, 0, v79, vcc
	global_load_dwordx4 v[122:125], v[80:81], off nt
	global_load_dwordx4 v[118:121], v[82:83], off nt
	v_add_co_u32_e32 v80, vcc, s85, v78
	s_nop 1
	v_addc_co_u32_e32 v81, vcc, 0, v79, vcc
	v_add_co_u32_e32 v82, vcc, s82, v78
	s_nop 1
	v_addc_co_u32_e32 v83, vcc, 0, v79, vcc
	global_load_dwordx4 v[114:117], v[80:81], off nt
	global_load_dwordx4 v[110:113], v[82:83], off nt
	v_add_co_u32_e32 v80, vcc, s9, v78
	s_mov_b32 s9, 0x24000
	s_nop 0
	v_addc_co_u32_e32 v81, vcc, 0, v79, vcc
	v_add_co_u32_e32 v82, vcc, s9, v78
	s_mov_b32 s9, 0x28000
	s_nop 0
	v_addc_co_u32_e32 v83, vcc, 0, v79, vcc
	global_load_dwordx4 v[106:109], v[80:81], off nt
	global_load_dwordx4 v[102:105], v[82:83], off nt
	v_add_co_u32_e32 v80, vcc, s9, v78
	s_mov_b32 s9, 0x2c000
	s_nop 0
	v_addc_co_u32_e32 v81, vcc, 0, v79, vcc
	v_add_co_u32_e32 v82, vcc, s9, v78
	s_mov_b32 s9, 0x30000
	s_nop 0
	v_addc_co_u32_e32 v83, vcc, 0, v79, vcc
	global_load_dwordx4 v[98:101], v[80:81], off nt
	global_load_dwordx4 v[94:97], v[82:83], off nt
	v_add_co_u32_e32 v80, vcc, s9, v78
	s_mov_b32 s9, 0x34000
	s_nop 0
	v_addc_co_u32_e32 v81, vcc, 0, v79, vcc
	v_add_co_u32_e32 v82, vcc, s9, v78
	s_nop 1
	v_addc_co_u32_e32 v83, vcc, 0, v79, vcc
	global_load_dwordx4 v[90:93], v[80:81], off nt
	global_load_dwordx4 v[86:89], v[82:83], off nt
	v_add_co_u32_e32 v80, vcc, 0x38000, v78
	s_nop 1
	v_addc_co_u32_e32 v81, vcc, 0, v79, vcc
	v_add_co_u32_e32 v78, vcc, 0x3c000, v78
	s_nop 1
	v_addc_co_u32_e32 v79, vcc, 0, v79, vcc
	global_load_dwordx4 v[82:85], v[80:81], off nt
	s_nop 0
	global_load_dwordx4 v[78:81], v[78:79], off nt
	s_addk_i32 s12, 0x80
	s_add_i32 s11, s11, 64
	s_add_i32 s10, s10, 1
	v_cmp_lt_i32_e32 vcc, s73, v72
	s_and_saveexec_b64 s[8:9], vcc
	s_xor_b64 s[8:9], exec, s[8:9]
	v_add_u32_e32 v68, 0x7ffff000, v71
	v_and_b32_e32 v68, 0x7fffff00, v68
	v_and_b32_e32 v69, 0x7c, v72
	v_or3_b32 v68, v69, v68, s83
	s_andn2_saveexec_b64 s[8:9], s[8:9]
	v_and_b32_e32 v68, 0x7c, v72
	v_and_or_b32 v68, v71, s0, v68
	s_or_b64 exec, exec, s[8:9]
	s_waitcnt vmcnt(31)
; __device__ __forceinline__ unsigned pk4_fp8(float a, float b, float c, float d) {
;     a = __builtin_fminf(__builtin_fmaxf(a, -448.f), 448.f); b = __builtin_fminf(__builtin_fmaxf(b, -448.f), 448.f); c = __builtin_fminf(__builtin_fmaxf(c, -448.f), 448.f); d = __builtin_fminf(__builtin_fmaxf(d, -448.f), 448.f);
;     int w = 0; w = __builtin_amdgcn_cvt_pk_fp8_f32(a, b, w, false); w = __builtin_amdgcn_cvt_pk_fp8_f32(c, d, w, true); return (unsigned)w;
; template <int MODE> __device__ __forceinline__ void cv_finish(const f32x4 (&tv)[16], int K, int nblk, unsigned char* WT, int item, int lane) {
;     const int kb = item / nblk, nb = item - kb * nblk, k0 = 64 * kb + 16 * (lane >> 4), n0 = 64 * nb + 4 * (lane & 15);
;     unsigned D[16];
; #pragma unroll
;     for (int i = 0; i < 16; ++i) { const f32x2 a = (f32x2){tv[i].x, tv[i].y} * (f32x2){1024.f, 1024.f}, b = (f32x2){tv[i].z, tv[i].w} * (f32x2){1024.f, 1024.f};
;         D[i] = pk4_fp8(a.x, a.y, b.x, b.y); }
	v_pk_mul_f32 v[62:63], v[62:63], s[84:85] op_sel_hi:[1,0]
	v_pk_mul_f32 v[64:65], v[64:65], s[84:85] op_sel_hi:[1,0]
	v_med3_f32 v69, v62, s96, v150
	v_med3_f32 v63, v63, s96, v150
	v_mov_b32_e32 v62, v133
	v_cvt_pk_fp8_f32 v62, v69, v63
	v_med3_f32 v63, v64, s96, v150
	v_med3_f32 v64, v65, s96, v150
	s_waitcnt vmcnt(30)
	v_pk_mul_f32 v[58:59], v[58:59], s[84:85] op_sel_hi:[1,0]
	v_cvt_pk_fp8_f32 v62, v63, v64 op_sel:[0,0,1]
	v_med3_f32 v63, v58, s96, v150
	v_med3_f32 v59, v59, s96, v150
	v_mov_b32_e32 v58, v133
	v_cvt_pk_fp8_f32 v58, v63, v59
	v_pk_mul_f32 v[60:61], v[60:61], s[84:85] op_sel_hi:[1,0]
	s_waitcnt vmcnt(29)
	v_pk_mul_f32 v[54:55], v[54:55], s[84:85] op_sel_hi:[1,0]
	v_med3_f32 v59, v60, s96, v150
	v_med3_f32 v60, v61, s96, v150
	v_cvt_pk_fp8_f32 v58, v59, v60 op_sel:[0,0,1]
	v_med3_f32 v59, v54, s96, v150
	v_med3_f32 v55, v55, s96, v150
	v_mov_b32_e32 v54, v133
	v_cvt_pk_fp8_f32 v54, v59, v55
	v_pk_mul_f32 v[56:57], v[56:57], s[84:85] op_sel_hi:[1,0]
	s_waitcnt vmcnt(28)
	v_pk_mul_f32 v[50:51], v[50:51], s[84:85] op_sel_hi:[1,0]
	v_med3_f32 v55, v56, s96, v150
	v_med3_f32 v56, v57, s96, v150
	v_cvt_pk_fp8_f32 v54, v55, v56 op_sel:[0,0,1]
	v_med3_f32 v55, v50, s96, v150
	v_med3_f32 v51, v51, s96, v150
	v_mov_b32_e32 v50, v133
	v_cvt_pk_fp8_f32 v50, v55, v51
	v_pk_mul_f32 v[52:53], v[52:53], s[84:85] op_sel_hi:[1,0]
	s_waitcnt vmcnt(27)
	v_pk_mul_f32 v[46:47], v[46:47], s[84:85] op_sel_hi:[1,0]
	v_med3_f32 v51, v52, s96, v150
	v_med3_f32 v52, v53, s96, v150
	v_cvt_pk_fp8_f32 v50, v51, v52 op_sel:[0,0,1]
	v_med3_f32 v51, v46, s96, v150
	v_med3_f32 v47, v47, s96, v150
	v_mov_b32_e32 v46, v133
	v_cvt_pk_fp8_f32 v46, v51, v47
	v_pk_mul_f32 v[48:49], v[48:49], s[84:85] op_sel_hi:[1,0]
	s_waitcnt vmcnt(26)
	v_pk_mul_f32 v[42:43], v[42:43], s[84:85] op_sel_hi:[1,0]
	v_med3_f32 v47, v48, s96, v150
	v_med3_f32 v48, v49, s96, v150
	v_cvt_pk_fp8_f32 v46, v47, v48 op_sel:[0,0,1]
	v_med3_f32 v47, v42, s96, v150
	v_med3_f32 v43, v43, s96, v150
	v_mov_b32_e32 v42, v133
	v_cvt_pk_fp8_f32 v42, v47, v43
	v_pk_mul_f32 v[44:45], v[44:45], s[84:85] op_sel_hi:[1,0]
	s_waitcnt vmcnt(25)
	v_pk_mul_f32 v[38:39], v[38:39], s[84:85] op_sel_hi:[1,0]
	v_med3_f32 v43, v44, s96, v150
	v_med3_f32 v44, v45, s96, v150
	v_cvt_pk_fp8_f32 v42, v43, v44 op_sel:[0,0,1]
	v_med3_f32 v43, v38, s96, v150
	v_med3_f32 v39, v39, s96, v150
	v_mov_b32_e32 v38, v133
	v_cvt_pk_fp8_f32 v38, v43, v39
	v_pk_mul_f32 v[40:41], v[40:41], s[84:85] op_sel_hi:[1,0]
	s_waitcnt vmcnt(24)
	v_pk_mul_f32 v[34:35], v[34:35], s[84:85] op_sel_hi:[1,0]
	v_med3_f32 v39, v40, s96, v150
	v_med3_f32 v40, v41, s96, v150
	v_cvt_pk_fp8_f32 v38, v39, v40 op_sel:[0,0,1]
	v_med3_f32 v39, v34, s96, v150
	v_med3_f32 v35, v35, s96, v150
	v_mov_b32_e32 v34, v133
	v_cvt_pk_fp8_f32 v34, v39, v35
	v_pk_mul_f32 v[36:37], v[36:37], s[84:85] op_sel_hi:[1,0]
	s_waitcnt vmcnt(23)
	v_pk_mul_f32 v[30:31], v[30:31], s[84:85] op_sel_hi:[1,0]
	v_med3_f32 v35, v36, s96, v150
	v_med3_f32 v36, v37, s96, v150
	v_cvt_pk_fp8_f32 v34, v35, v36 op_sel:[0,0,1]
	v_med3_f32 v35, v30, s96, v150
	v_med3_f32 v31, v31, s96, v150
	v_mov_b32_e32 v30, v133
	v_cvt_pk_fp8_f32 v30, v35, v31
	v_pk_mul_f32 v[32:33], v[32:33], s[84:85] op_sel_hi:[1,0]
	s_waitcnt vmcnt(22)
	v_pk_mul_f32 v[26:27], v[26:27], s[84:85] op_sel_hi:[1,0]
	v_med3_f32 v31, v32, s96, v150
	v_med3_f32 v32, v33, s96, v150
	v_cvt_pk_fp8_f32 v30, v31, v32 op_sel:[0,0,1]
	v_med3_f32 v31, v26, s96, v150
	v_med3_f32 v27, v27, s96, v150
	v_mov_b32_e32 v26, v133
	v_cvt_pk_fp8_f32 v26, v31, v27
	v_pk_mul_f32 v[28:29], v[28:29], s[84:85] op_sel_hi:[1,0]
	s_waitcnt vmcnt(21)
	v_pk_mul_f32 v[22:23], v[22:23], s[84:85] op_sel_hi:[1,0]
	v_med3_f32 v27, v28, s96, v150
	v_med3_f32 v28, v29, s96, v150
	v_cvt_pk_fp8_f32 v26, v27, v28 op_sel:[0,0,1]
	v_med3_f32 v27, v22, s96, v150
	v_med3_f32 v23, v23, s96, v150
	v_mov_b32_e32 v22, v133
	v_cvt_pk_fp8_f32 v22, v27, v23
	v_pk_mul_f32 v[24:25], v[24:25], s[84:85] op_sel_hi:[1,0]
	s_waitcnt vmcnt(20)
	v_pk_mul_f32 v[18:19], v[18:19], s[84:85] op_sel_hi:[1,0]
	v_med3_f32 v23, v24, s96, v150
	v_med3_f32 v24, v25, s96, v150
	v_cvt_pk_fp8_f32 v22, v23, v24 op_sel:[0,0,1]
	v_med3_f32 v23, v18, s96, v150
	v_med3_f32 v19, v19, s96, v150
	v_mov_b32_e32 v18, v133
	v_cvt_pk_fp8_f32 v18, v23, v19
	v_pk_mul_f32 v[20:21], v[20:21], s[84:85] op_sel_hi:[1,0]
	s_waitcnt vmcnt(19)
	v_pk_mul_f32 v[14:15], v[14:15], s[84:85] op_sel_hi:[1,0]
	v_med3_f32 v19, v20, s96, v150
	v_med3_f32 v20, v21, s96, v150
	v_cvt_pk_fp8_f32 v18, v19, v20 op_sel:[0,0,1]
	v_med3_f32 v19, v14, s96, v150
	v_med3_f32 v15, v15, s96, v150
	v_mov_b32_e32 v14, v133
	v_cvt_pk_fp8_f32 v14, v19, v15
	v_pk_mul_f32 v[16:17], v[16:17], s[84:85] op_sel_hi:[1,0]
	s_waitcnt vmcnt(18)
	v_pk_mul_f32 v[10:11], v[10:11], s[84:85] op_sel_hi:[1,0]
	v_med3_f32 v15, v16, s96, v150
	v_med3_f32 v16, v17, s96, v150
	v_cvt_pk_fp8_f32 v14, v15, v16 op_sel:[0,0,1]
	v_med3_f32 v15, v10, s96, v150
	v_med3_f32 v11, v11, s96, v150
	v_mov_b32_e32 v10, v133
	v_cvt_pk_fp8_f32 v10, v15, v11
	v_pk_mul_f32 v[12:13], v[12:13], s[84:85] op_sel_hi:[1,0]
	s_waitcnt vmcnt(17)
	v_pk_mul_f32 v[6:7], v[6:7], s[84:85] op_sel_hi:[1,0]
	v_med3_f32 v11, v12, s96, v150
	v_med3_f32 v12, v13, s96, v150
	v_cvt_pk_fp8_f32 v10, v11, v12 op_sel:[0,0,1]
	v_med3_f32 v11, v6, s96, v150
	v_med3_f32 v7, v7, s96, v150
	v_mov_b32_e32 v6, v133
	v_cvt_pk_fp8_f32 v6, v11, v7
	v_pk_mul_f32 v[8:9], v[8:9], s[84:85] op_sel_hi:[1,0]
	s_waitcnt vmcnt(16)
; __device__ __forceinline__ void cv_load(const float* W, int N, int nblk, int item, int lane, f32x4 (&tv)[16]) {
;     const int kb = item / nblk, nb = item - kb * nblk; const float* p = W + (size_t)(64 * kb + 16 * (lane >> 4)) * N + 64 * nb + 4 * (lane & 15);
; #pragma unroll
;     for (int i = 0; i < 16; ++i) tv[i] = __builtin_nontemporal_load((const f32x4*)(p + (size_t)i * N));
; }
; template <int MODE> __device__ __forceinline__ void cv_finish(const f32x4 (&tv)[16], int K, int nblk, unsigned char* WT, int item, int lane) {
;     ...
;     unsigned O[4][4];
; #pragma unroll
;     for (int q = 0; q < 4; ++q) { const unsigned a = D[4 * q], b = D[4 * q + 1], c = D[4 * q + 2], d = D[4 * q + 3];
;         const unsigned t0 = __builtin_amdgcn_perm(b, a, 0x05010400u), t1 = __builtin_amdgcn_perm(b, a, 0x07030602u), u0 = __builtin_amdgcn_perm(d, c, 0x05010400u), u1 = __builtin_amdgcn_perm(d, c, 0x07030602u);
;         O[0][q] = __builtin_amdgcn_perm(u0, t0, 0x05040100u); O[1][q] = __builtin_amdgcn_perm(u0, t0, 0x07060302u); O[2][q] = __builtin_amdgcn_perm(u1, t1, 0x05040100u); O[3][q] = __builtin_amdgcn_perm(u1, t1, 0x07060302u); }
; #pragma unroll
;     for (int j = 0; j < 4; ++j) { u32x4 o; o.x = O[j][0]; o.y = O[j][1]; o.z = O[j][2]; o.w = O[j][3];
;         __builtin_nontemporal_store(o, (u32x4*)(WT + (size_t)drow<MODE>(n0 + j) * K + k0)); }
; }
	v_pk_mul_f32 v[2:3], v[2:3], s[84:85] op_sel_hi:[1,0]
	v_med3_f32 v7, v8, s96, v150
	v_med3_f32 v8, v9, s96, v150
	v_cvt_pk_fp8_f32 v6, v7, v8 op_sel:[0,0,1]
	v_med3_f32 v2, v2, s96, v150
	v_med3_f32 v3, v3, s96, v150
	v_mov_b32_e32 v7, v133
	v_cvt_pk_fp8_f32 v7, v2, v3
	v_pk_mul_f32 v[2:3], v[4:5], s[84:85] op_sel_hi:[1,0]
	v_ashrrev_i32_e32 v69, 31, v68
	v_med3_f32 v2, v2, s96, v150
	v_med3_f32 v3, v3, s96, v150
	v_cvt_pk_fp8_f32 v7, v2, v3 op_sel:[0,0,1]
	v_perm_b32 v5, v58, v62, s97
	v_perm_b32 v8, v50, v54, s97
	v_perm_b32 v9, v42, v46, s97
	v_perm_b32 v11, v34, v38, s97
	v_perm_b32 v12, v26, v30, s97
	v_perm_b32 v13, v18, v22, s97
	v_perm_b32 v15, v10, v14, s97
	v_perm_b32 v16, v7, v6, s97
	v_lshl_add_u64 v[2:3], s[6:7], 0, v[66:67]
	v_lshlrev_b64 v[20:21], 11, v[68:69]
	v_add_u32_e32 v17, 1, v72
	v_perm_b32 v74, v8, v5, s71
	v_perm_b32 v75, v11, v9, s71
	v_perm_b32 v76, v13, v12, s71
	v_perm_b32 v77, v16, v15, s71
	v_lshl_add_u64 v[20:21], v[2:3], 0, v[20:21]
	v_cmp_lt_i32_e32 vcc, s73, v17
	global_store_dwordx4 v[20:21], v[74:77], off nt
	s_and_saveexec_b64 s[8:9], vcc
	s_xor_b64 s[8:9], exec, s[8:9]
	v_add_u32_e32 v4, 0x7ffff002, v71
	v_and_b32_e32 v4, 0x7fffff00, v4
	v_and_b32_e32 v17, 0x7d, v17
	v_or3_b32 v4, v17, v4, s83
	s_andn2_saveexec_b64 s[8:9], s[8:9]
	v_add_u32_e32 v4, 2, v71
	v_and_b32_e32 v17, 0x7d, v17
	v_and_or_b32 v4, v4, s0, v17
	s_or_b64 exec, exec, s[8:9]
	v_perm_b32 v64, v8, v5, s72
	v_ashrrev_i32_e32 v5, 31, v4
	v_lshlrev_b64 v[4:5], 11, v[4:5]
	v_perm_b32 v65, v11, v9, s72
	v_perm_b32 v66, v13, v12, s72
	v_perm_b32 v67, v16, v15, s72
	v_lshl_add_u64 v[4:5], v[2:3], 0, v[4:5]
	global_store_dwordx4 v[4:5], v[64:67], off nt
	v_add_u32_e32 v5, 2, v72
	v_cmp_lt_i32_e32 vcc, s73, v5
	s_and_saveexec_b64 s[8:9], vcc
	s_xor_b64 s[8:9], exec, s[8:9]
	v_add_u32_e32 v4, 0x7ffff004, v71
	v_and_b32_e32 v4, 0x7fffff00, v4
	v_and_b32_e32 v5, 0x7e, v5
	v_or3_b32 v4, v5, v4, s83
	s_andn2_saveexec_b64 s[8:9], s[8:9]
	v_add_u32_e32 v4, 4, v71
	v_and_b32_e32 v5, 0x7e, v5
	v_and_or_b32 v4, v4, s0, v5
	s_or_b64 exec, exec, s[8:9]
	v_ashrrev_i32_e32 v5, 31, v4
	v_perm_b32 v8, v58, v62, s70
	v_perm_b32 v9, v50, v54, s70
	v_perm_b32 v11, v42, v46, s70
	v_perm_b32 v12, v34, v38, s70
	v_perm_b32 v13, v26, v30, s70
	v_perm_b32 v15, v18, v22, s70
	v_perm_b32 v10, v10, v14, s70
	v_perm_b32 v6, v7, v6, s70
	v_lshlrev_b64 v[4:5], 11, v[4:5]
	v_perm_b32 v16, v9, v8, s71
	v_perm_b32 v17, v12, v11, s71
	v_perm_b32 v18, v15, v13, s71
	v_perm_b32 v19, v6, v10, s71
	v_lshl_add_u64 v[4:5], v[2:3], 0, v[4:5]
	global_store_dwordx4 v[4:5], v[16:19], off nt
	v_add_u32_e32 v5, 3, v72
	v_cmp_lt_i32_e32 vcc, s73, v5
	s_and_saveexec_b64 s[8:9], vcc
	s_xor_b64 s[8:9], exec, s[8:9]
	v_add_u32_e32 v4, 0x7ffff006, v71
	v_and_b32_e32 v4, 0x7fffff00, v4
	v_and_b32_e32 v5, 0x7f, v5
	v_or3_b32 v4, v5, v4, s83
	s_andn2_saveexec_b64 s[8:9], s[8:9]
	v_add_u32_e32 v4, 6, v71
	v_and_b32_e32 v5, 0x7f, v5
	v_and_or_b32 v4, v4, s0, v5
	s_or_b64 exec, exec, s[8:9]
	v_ashrrev_i32_e32 v5, 31, v4
	v_lshlrev_b64 v[4:5], 11, v[4:5]
	v_perm_b32 v16, v9, v8, s72
	v_perm_b32 v17, v12, v11, s72
	v_perm_b32 v18, v15, v13, s72
	v_perm_b32 v19, v6, v10, s72
	v_lshl_add_u64 v[2:3], v[2:3], 0, v[4:5]
	global_store_dwordx4 v[2:3], v[16:19], off nt
	s_ashr_i32 s8, s10, 31
	s_lshr_b32 s8, s8, 26
	s_add_i32 s8, s10, s8
	s_ashr_i32 s13, s8, 6
	s_andn2_b32 s8, s8, 63
	v_or_b32_e32 v66, s8, v1
	v_ashrrev_i32_e32 v67, 31, v66
	s_lshl_b32 s8, s13, 12
	v_lshlrev_b64 v[2:3], 14, v[66:67]
	s_sub_i32 s8, s11, s8
	v_lshl_add_u64 v[2:3], s[4:5], 0, v[2:3]
	s_ashr_i32 s9, s8, 31
	v_lshl_add_u64 v[2:3], s[8:9], 2, v[2:3]
	v_lshlrev_b32_e32 v132, 2, v130
	v_lshl_add_u64 v[2:3], v[2:3], 0, v[132:133]
	v_add_co_u32_e32 v4, vcc, s1, v2
	s_mov_b32 s9, 0x20000
	s_nop 0
	v_addc_co_u32_e32 v5, vcc, 0, v3, vcc
	global_load_dwordx4 v[62:65], v[2:3], off nt
	global_load_dwordx4 v[58:61], v[4:5], off nt
	v_add_co_u32_e32 v4, vcc, s78, v2
	v_add_u32_e32 v72, s8, v130
	s_nop 0
	v_addc_co_u32_e32 v5, vcc, 0, v3, vcc
	v_add_co_u32_e32 v6, vcc, s79, v2
	v_add_u32_e32 v68, s12, v70
	s_nop 0
	v_addc_co_u32_e32 v7, vcc, 0, v3, vcc
	global_load_dwordx4 v[54:57], v[4:5], off nt
	global_load_dwordx4 v[50:53], v[6:7], off nt
	v_add_co_u32_e32 v4, vcc, s86, v2
	s_lshl_b32 s8, s13, 13
	s_nop 0
	v_addc_co_u32_e32 v5, vcc, 0, v3, vcc
	v_add_co_u32_e32 v6, vcc, s87, v2
	v_subrev_u32_e32 v71, s8, v68
	s_nop 0
	v_addc_co_u32_e32 v7, vcc, 0, v3, vcc
	global_load_dwordx4 v[46:49], v[4:5], off nt
	global_load_dwordx4 v[42:45], v[6:7], off nt
	v_add_co_u32_e32 v4, vcc, s85, v2
	s_nop 1
	v_addc_co_u32_e32 v5, vcc, 0, v3, vcc
	v_add_co_u32_e32 v6, vcc, s82, v2
	s_nop 1
	v_addc_co_u32_e32 v7, vcc, 0, v3, vcc
	global_load_dwordx4 v[38:41], v[4:5], off nt
	global_load_dwordx4 v[34:37], v[6:7], off nt
	v_add_co_u32_e32 v4, vcc, s9, v2
	s_mov_b32 s9, 0x24000
	s_nop 0
	v_addc_co_u32_e32 v5, vcc, 0, v3, vcc
	v_add_co_u32_e32 v6, vcc, s9, v2
	s_mov_b32 s9, 0x28000
	s_nop 0
	v_addc_co_u32_e32 v7, vcc, 0, v3, vcc
	global_load_dwordx4 v[30:33], v[4:5], off nt
	global_load_dwordx4 v[26:29], v[6:7], off nt
	v_add_co_u32_e32 v4, vcc, s9, v2
	s_mov_b32 s9, 0x2c000
	s_nop 0
	v_addc_co_u32_e32 v5, vcc, 0, v3, vcc
	v_add_co_u32_e32 v6, vcc, s9, v2
	s_mov_b32 s9, 0x30000
	s_nop 0
	v_addc_co_u32_e32 v7, vcc, 0, v3, vcc
	global_load_dwordx4 v[22:25], v[4:5], off nt
	global_load_dwordx4 v[18:21], v[6:7], off nt
	v_add_co_u32_e32 v4, vcc, s9, v2
	s_mov_b32 s9, 0x34000
	s_nop 0
	v_addc_co_u32_e32 v5, vcc, 0, v3, vcc
	v_add_co_u32_e32 v6, vcc, s9, v2
	s_nop 1
	v_addc_co_u32_e32 v7, vcc, 0, v3, vcc
	global_load_dwordx4 v[14:17], v[4:5], off nt
	global_load_dwordx4 v[10:13], v[6:7], off nt
	v_add_co_u32_e32 v4, vcc, 0x38000, v2
	s_nop 1
	v_addc_co_u32_e32 v5, vcc, 0, v3, vcc
	v_add_co_u32_e32 v2, vcc, 0x3c000, v2
	s_nop 1
	v_addc_co_u32_e32 v3, vcc, 0, v3, vcc
	global_load_dwordx4 v[6:9], v[4:5], off nt
	s_nop 0
	global_load_dwordx4 v[2:5], v[2:3], off nt
	s_addk_i32 s12, 0x80
	s_add_i32 s11, s11, 64
	s_add_i32 s10, s10, 1
	v_cmp_lt_i32_e32 vcc, s73, v160
	s_and_saveexec_b64 s[8:9], vcc
	s_xor_b64 s[8:9], exec, s[8:9]
	v_add_u32_e32 v158, 0x7ffff000, v73
	v_and_b32_e32 v158, 0x7fffff00, v158
	v_and_b32_e32 v159, 0x7c, v160
	v_or3_b32 v158, v159, v158, s83
	s_andn2_saveexec_b64 s[8:9], s[8:9]
	v_and_b32_e32 v158, 0x7c, v160
	v_and_or_b32 v158, v73, s0, v158
	s_or_b64 exec, exec, s[8:9]
	s_waitcnt vmcnt(35)
; __device__ __forceinline__ unsigned pk4_fp8(float a, float b, float c, float d) {
;     a = __builtin_fminf(__builtin_fmaxf(a, -448.f), 448.f); b = __builtin_fminf(__builtin_fmaxf(b, -448.f), 448.f); c = __builtin_fminf(__builtin_fmaxf(c, -448.f), 448.f); d = __builtin_fminf(__builtin_fmaxf(d, -448.f), 448.f);
;     int w = 0; w = __builtin_amdgcn_cvt_pk_fp8_f32(a, b, w, false); w = __builtin_amdgcn_cvt_pk_fp8_f32(c, d, w, true); return (unsigned)w;
; template <int MODE> __device__ __forceinline__ void cv_finish(const f32x4 (&tv)[16], int K, int nblk, unsigned char* WT, int item, int lane) {
;     const int kb = item / nblk, nb = item - kb * nblk, k0 = 64 * kb + 16 * (lane >> 4), n0 = 64 * nb + 4 * (lane & 15);
;     unsigned D[16];
; #pragma unroll
;     for (int i = 0; i < 16; ++i) { const f32x2 a = (f32x2){tv[i].x, tv[i].y} * (f32x2){1024.f, 1024.f}, b = (f32x2){tv[i].z, tv[i].w} * (f32x2){1024.f, 1024.f};
;         D[i] = pk4_fp8(a.x, a.y, b.x, b.y); }
	v_pk_mul_f32 v[152:153], v[152:153], s[84:85] op_sel_hi:[1,0]
	v_pk_mul_f32 v[154:155], v[154:155], s[84:85] op_sel_hi:[1,0]
	v_med3_f32 v159, v152, s96, v150
	v_med3_f32 v153, v153, s96, v150
	v_mov_b32_e32 v152, v133
	v_cvt_pk_fp8_f32 v152, v159, v153
	v_med3_f32 v153, v154, s96, v150
	v_med3_f32 v154, v155, s96, v150
	s_waitcnt vmcnt(34)
	v_pk_mul_f32 v[140:141], v[140:141], s[84:85] op_sel_hi:[1,0]
	v_cvt_pk_fp8_f32 v152, v153, v154 op_sel:[0,0,1]
	v_med3_f32 v153, v140, s96, v150
	v_med3_f32 v141, v141, s96, v150
	v_mov_b32_e32 v140, v133
	v_cvt_pk_fp8_f32 v140, v153, v141
	v_pk_mul_f32 v[142:143], v[142:143], s[84:85] op_sel_hi:[1,0]
	s_waitcnt vmcnt(33)
	v_pk_mul_f32 v[136:137], v[136:137], s[84:85] op_sel_hi:[1,0]
	v_med3_f32 v141, v142, s96, v150
	v_med3_f32 v142, v143, s96, v150
	v_cvt_pk_fp8_f32 v140, v141, v142 op_sel:[0,0,1]
	v_med3_f32 v141, v136, s96, v150
	v_med3_f32 v137, v137, s96, v150
	v_mov_b32_e32 v136, v133
	v_cvt_pk_fp8_f32 v136, v141, v137
	v_pk_mul_f32 v[138:139], v[138:139], s[84:85] op_sel_hi:[1,0]
	s_waitcnt vmcnt(32)
	v_pk_mul_f32 v[126:127], v[126:127], s[84:85] op_sel_hi:[1,0]
	v_med3_f32 v137, v138, s96, v150
	v_med3_f32 v138, v139, s96, v150
	v_cvt_pk_fp8_f32 v136, v137, v138 op_sel:[0,0,1]
	v_med3_f32 v137, v126, s96, v150
	v_med3_f32 v127, v127, s96, v150
	v_mov_b32_e32 v126, v133
	v_cvt_pk_fp8_f32 v126, v137, v127
	v_pk_mul_f32 v[128:129], v[128:129], s[84:85] op_sel_hi:[1,0]
	s_waitcnt vmcnt(31)
	v_pk_mul_f32 v[122:123], v[122:123], s[84:85] op_sel_hi:[1,0]
	v_med3_f32 v127, v128, s96, v150
	v_med3_f32 v128, v129, s96, v150
	v_cvt_pk_fp8_f32 v126, v127, v128 op_sel:[0,0,1]
	v_med3_f32 v127, v122, s96, v150
	v_med3_f32 v123, v123, s96, v150
	v_mov_b32_e32 v122, v133
	v_cvt_pk_fp8_f32 v122, v127, v123
	v_pk_mul_f32 v[124:125], v[124:125], s[84:85] op_sel_hi:[1,0]
	s_waitcnt vmcnt(30)
	v_pk_mul_f32 v[118:119], v[118:119], s[84:85] op_sel_hi:[1,0]
	v_med3_f32 v123, v124, s96, v150
	v_med3_f32 v124, v125, s96, v150
	v_cvt_pk_fp8_f32 v122, v123, v124 op_sel:[0,0,1]
	v_med3_f32 v123, v118, s96, v150
	v_med3_f32 v119, v119, s96, v150
	v_mov_b32_e32 v118, v133
	v_cvt_pk_fp8_f32 v118, v123, v119
	v_pk_mul_f32 v[120:121], v[120:121], s[84:85] op_sel_hi:[1,0]
	s_waitcnt vmcnt(29)
	v_pk_mul_f32 v[114:115], v[114:115], s[84:85] op_sel_hi:[1,0]
	v_med3_f32 v119, v120, s96, v150
	v_med3_f32 v120, v121, s96, v150
	v_cvt_pk_fp8_f32 v118, v119, v120 op_sel:[0,0,1]
	v_med3_f32 v119, v114, s96, v150
	v_med3_f32 v115, v115, s96, v150
	v_mov_b32_e32 v114, v133
	v_cvt_pk_fp8_f32 v114, v119, v115
	v_pk_mul_f32 v[116:117], v[116:117], s[84:85] op_sel_hi:[1,0]
	s_waitcnt vmcnt(28)
	v_pk_mul_f32 v[110:111], v[110:111], s[84:85] op_sel_hi:[1,0]
	v_med3_f32 v115, v116, s96, v150
	v_med3_f32 v116, v117, s96, v150
	v_cvt_pk_fp8_f32 v114, v115, v116 op_sel:[0,0,1]
	v_med3_f32 v115, v110, s96, v150
	v_med3_f32 v111, v111, s96, v150
	v_mov_b32_e32 v110, v133
	v_cvt_pk_fp8_f32 v110, v115, v111
	v_pk_mul_f32 v[112:113], v[112:113], s[84:85] op_sel_hi:[1,0]
	s_waitcnt vmcnt(27)
	v_pk_mul_f32 v[106:107], v[106:107], s[84:85] op_sel_hi:[1,0]
	v_med3_f32 v111, v112, s96, v150
	v_med3_f32 v112, v113, s96, v150
	v_cvt_pk_fp8_f32 v110, v111, v112 op_sel:[0,0,1]
	v_med3_f32 v111, v106, s96, v150
	v_med3_f32 v107, v107, s96, v150
	v_mov_b32_e32 v106, v133
	v_cvt_pk_fp8_f32 v106, v111, v107
	v_pk_mul_f32 v[108:109], v[108:109], s[84:85] op_sel_hi:[1,0]
	s_waitcnt vmcnt(26)
	v_pk_mul_f32 v[102:103], v[102:103], s[84:85] op_sel_hi:[1,0]
	v_med3_f32 v107, v108, s96, v150
	v_med3_f32 v108, v109, s96, v150
	v_cvt_pk_fp8_f32 v106, v107, v108 op_sel:[0,0,1]
	v_med3_f32 v107, v102, s96, v150
	v_med3_f32 v103, v103, s96, v150
	v_mov_b32_e32 v102, v133
	v_cvt_pk_fp8_f32 v102, v107, v103
	v_pk_mul_f32 v[104:105], v[104:105], s[84:85] op_sel_hi:[1,0]
	s_waitcnt vmcnt(25)
	v_pk_mul_f32 v[98:99], v[98:99], s[84:85] op_sel_hi:[1,0]
	v_med3_f32 v103, v104, s96, v150
	v_med3_f32 v104, v105, s96, v150
	v_cvt_pk_fp8_f32 v102, v103, v104 op_sel:[0,0,1]
	v_med3_f32 v103, v98, s96, v150
	v_med3_f32 v99, v99, s96, v150
	v_mov_b32_e32 v98, v133
	v_cvt_pk_fp8_f32 v98, v103, v99
	v_pk_mul_f32 v[100:101], v[100:101], s[84:85] op_sel_hi:[1,0]
	s_waitcnt vmcnt(24)
	v_pk_mul_f32 v[94:95], v[94:95], s[84:85] op_sel_hi:[1,0]
	v_med3_f32 v99, v100, s96, v150
	v_med3_f32 v100, v101, s96, v150
	v_cvt_pk_fp8_f32 v98, v99, v100 op_sel:[0,0,1]
	v_med3_f32 v99, v94, s96, v150
	v_med3_f32 v95, v95, s96, v150
	v_mov_b32_e32 v94, v133
	v_cvt_pk_fp8_f32 v94, v99, v95
	v_pk_mul_f32 v[96:97], v[96:97], s[84:85] op_sel_hi:[1,0]
	s_waitcnt vmcnt(23)
	v_pk_mul_f32 v[90:91], v[90:91], s[84:85] op_sel_hi:[1,0]
	v_med3_f32 v95, v96, s96, v150
	v_med3_f32 v96, v97, s96, v150
	v_cvt_pk_fp8_f32 v94, v95, v96 op_sel:[0,0,1]
	v_med3_f32 v95, v90, s96, v150
	v_med3_f32 v91, v91, s96, v150
	v_mov_b32_e32 v90, v133
	v_cvt_pk_fp8_f32 v90, v95, v91
	v_pk_mul_f32 v[92:93], v[92:93], s[84:85] op_sel_hi:[1,0]
	s_waitcnt vmcnt(22)
	v_pk_mul_f32 v[86:87], v[86:87], s[84:85] op_sel_hi:[1,0]
	v_med3_f32 v91, v92, s96, v150
	v_med3_f32 v92, v93, s96, v150
	v_cvt_pk_fp8_f32 v90, v91, v92 op_sel:[0,0,1]
	v_med3_f32 v91, v86, s96, v150
	v_med3_f32 v87, v87, s96, v150
	v_mov_b32_e32 v86, v133
	v_cvt_pk_fp8_f32 v86, v91, v87
	v_pk_mul_f32 v[88:89], v[88:89], s[84:85] op_sel_hi:[1,0]
	s_waitcnt vmcnt(21)
	v_pk_mul_f32 v[82:83], v[82:83], s[84:85] op_sel_hi:[1,0]
	v_med3_f32 v87, v88, s96, v150
	v_med3_f32 v88, v89, s96, v150
	v_cvt_pk_fp8_f32 v86, v87, v88 op_sel:[0,0,1]
	v_med3_f32 v87, v82, s96, v150
	v_med3_f32 v83, v83, s96, v150
	v_mov_b32_e32 v82, v133
	v_cvt_pk_fp8_f32 v82, v87, v83
	v_pk_mul_f32 v[84:85], v[84:85], s[84:85] op_sel_hi:[1,0]
	s_waitcnt vmcnt(20)
; __device__ __forceinline__ void cv_load(const float* W, int N, int nblk, int item, int lane, f32x4 (&tv)[16]) {
;     const int kb = item / nblk, nb = item - kb * nblk; const float* p = W + (size_t)(64 * kb + 16 * (lane >> 4)) * N + 64 * nb + 4 * (lane & 15);
; #pragma unroll
;     for (int i = 0; i < 16; ++i) tv[i] = __builtin_nontemporal_load((const f32x4*)(p + (size_t)i * N));
; }
; template <int MODE> __device__ __forceinline__ void cv_finish(const f32x4 (&tv)[16], int K, int nblk, unsigned char* WT, int item, int lane) {
;     ...
;     unsigned O[4][4];
; #pragma unroll
;     for (int q = 0; q < 4; ++q) { const unsigned a = D[4 * q], b = D[4 * q + 1], c = D[4 * q + 2], d = D[4 * q + 3];
;         const unsigned t0 = __builtin_amdgcn_perm(b, a, 0x05010400u), t1 = __builtin_amdgcn_perm(b, a, 0x07030602u), u0 = __builtin_amdgcn_perm(d, c, 0x05010400u), u1 = __builtin_amdgcn_perm(d, c, 0x07030602u);
;         O[0][q] = __builtin_amdgcn_perm(u0, t0, 0x05040100u); O[1][q] = __builtin_amdgcn_perm(u0, t0, 0x07060302u); O[2][q] = __builtin_amdgcn_perm(u1, t1, 0x05040100u); O[3][q] = __builtin_amdgcn_perm(u1, t1, 0x07060302u); }
; #pragma unroll
;     for (int j = 0; j < 4; ++j) { u32x4 o; o.x = O[j][0]; o.y = O[j][1]; o.z = O[j][2]; o.w = O[j][3];
;         __builtin_nontemporal_store(o, (u32x4*)(WT + (size_t)drow<MODE>(n0 + j) * K + k0)); }
; }
	v_pk_mul_f32 v[78:79], v[78:79], s[84:85] op_sel_hi:[1,0]
	v_med3_f32 v83, v84, s96, v150
	v_med3_f32 v84, v85, s96, v150
	v_cvt_pk_fp8_f32 v82, v83, v84 op_sel:[0,0,1]
	v_med3_f32 v78, v78, s96, v150
	v_med3_f32 v79, v79, s96, v150
	v_mov_b32_e32 v83, v133
	v_cvt_pk_fp8_f32 v83, v78, v79
	v_pk_mul_f32 v[78:79], v[80:81], s[84:85] op_sel_hi:[1,0]
	v_ashrrev_i32_e32 v159, 31, v158
	v_med3_f32 v78, v78, s96, v150
	v_med3_f32 v79, v79, s96, v150
	v_cvt_pk_fp8_f32 v83, v78, v79 op_sel:[0,0,1]
	v_perm_b32 v81, v140, v152, s97
	v_perm_b32 v84, v126, v136, s97
	v_perm_b32 v85, v118, v122, s97
	v_perm_b32 v87, v110, v114, s97
	v_perm_b32 v88, v102, v106, s97
	v_perm_b32 v89, v94, v98, s97
	v_perm_b32 v91, v86, v90, s97
	v_perm_b32 v92, v83, v82, s97
	v_lshl_add_u64 v[78:79], s[6:7], 0, v[156:157]
	v_lshlrev_b64 v[96:97], 11, v[158:159]
	v_add_u32_e32 v93, 1, v160
	v_perm_b32 v162, v84, v81, s71
	v_perm_b32 v163, v87, v85, s71
	v_perm_b32 v164, v89, v88, s71
	v_perm_b32 v165, v92, v91, s71
	v_lshl_add_u64 v[96:97], v[78:79], 0, v[96:97]
	v_cmp_lt_i32_e32 vcc, s73, v93
	global_store_dwordx4 v[96:97], v[162:165], off nt
	s_and_saveexec_b64 s[8:9], vcc
	s_xor_b64 s[8:9], exec, s[8:9]
	v_add_u32_e32 v80, 0x7ffff002, v73
	v_and_b32_e32 v80, 0x7fffff00, v80
	v_and_b32_e32 v93, 0x7d, v93
	v_or3_b32 v80, v93, v80, s83
	s_andn2_saveexec_b64 s[8:9], s[8:9]
	v_add_u32_e32 v80, 2, v73
	v_and_b32_e32 v93, 0x7d, v93
	v_and_or_b32 v80, v80, s0, v93
	s_or_b64 exec, exec, s[8:9]
	v_perm_b32 v154, v84, v81, s72
	v_ashrrev_i32_e32 v81, 31, v80
	v_lshlrev_b64 v[80:81], 11, v[80:81]
	v_perm_b32 v155, v87, v85, s72
	v_perm_b32 v156, v89, v88, s72
	v_perm_b32 v157, v92, v91, s72
	v_lshl_add_u64 v[80:81], v[78:79], 0, v[80:81]
	global_store_dwordx4 v[80:81], v[154:157], off nt
	v_add_u32_e32 v81, 2, v160
	v_cmp_lt_i32_e32 vcc, s73, v81
	s_and_saveexec_b64 s[8:9], vcc
	s_xor_b64 s[8:9], exec, s[8:9]
	v_add_u32_e32 v80, 0x7ffff004, v73
	v_and_b32_e32 v80, 0x7fffff00, v80
	v_and_b32_e32 v81, 0x7e, v81
	v_or3_b32 v80, v81, v80, s83
	s_andn2_saveexec_b64 s[8:9], s[8:9]
	v_add_u32_e32 v80, 4, v73
	v_and_b32_e32 v81, 0x7e, v81
	v_and_or_b32 v80, v80, s0, v81
	s_or_b64 exec, exec, s[8:9]
	v_ashrrev_i32_e32 v81, 31, v80
	v_perm_b32 v84, v140, v152, s70
	v_perm_b32 v85, v126, v136, s70
	v_perm_b32 v87, v118, v122, s70
	v_perm_b32 v88, v110, v114, s70
	v_perm_b32 v89, v102, v106, s70
	v_perm_b32 v91, v94, v98, s70
	v_perm_b32 v86, v86, v90, s70
	v_perm_b32 v82, v83, v82, s70
	v_lshlrev_b64 v[80:81], 11, v[80:81]
	v_perm_b32 v92, v85, v84, s71
	v_perm_b32 v93, v88, v87, s71
	v_perm_b32 v94, v91, v89, s71
	v_perm_b32 v95, v82, v86, s71
	v_lshl_add_u64 v[80:81], v[78:79], 0, v[80:81]
	global_store_dwordx4 v[80:81], v[92:95], off nt
	v_add_u32_e32 v81, 3, v160
	v_cmp_lt_i32_e32 vcc, s73, v81
	s_and_saveexec_b64 s[8:9], vcc
	s_xor_b64 s[8:9], exec, s[8:9]
	v_add_u32_e32 v80, 0x7ffff006, v73
	v_and_b32_e32 v80, 0x7fffff00, v80
	v_and_b32_e32 v81, 0x7f, v81
	v_or3_b32 v80, v81, v80, s83
	s_andn2_saveexec_b64 s[8:9], s[8:9]
	v_add_u32_e32 v80, 6, v73
	v_and_b32_e32 v81, 0x7f, v81
	v_and_or_b32 v80, v80, s0, v81
	s_or_b64 exec, exec, s[8:9]
	v_ashrrev_i32_e32 v81, 31, v80
	v_lshlrev_b64 v[80:81], 11, v[80:81]
	v_perm_b32 v92, v85, v84, s72
	v_perm_b32 v93, v88, v87, s72
	v_perm_b32 v94, v91, v89, s72
	v_perm_b32 v95, v82, v86, s72
	v_lshl_add_u64 v[78:79], v[78:79], 0, v[80:81]
	global_store_dwordx4 v[78:79], v[92:95], off nt
	s_ashr_i32 s8, s10, 31
	s_lshr_b32 s8, s8, 26
	s_add_i32 s8, s10, s8
	s_ashr_i32 s13, s8, 6
	s_andn2_b32 s8, s8, 63
	v_or_b32_e32 v156, s8, v1
	v_ashrrev_i32_e32 v157, 31, v156
	s_lshl_b32 s8, s13, 12
	v_lshlrev_b64 v[78:79], 14, v[156:157]
	s_sub_i32 s8, s11, s8
	v_lshl_add_u64 v[78:79], s[4:5], 0, v[78:79]
	s_ashr_i32 s9, s8, 31
	v_lshl_add_u64 v[78:79], s[8:9], 2, v[78:79]
	v_lshlrev_b32_e32 v132, 2, v130
	v_lshl_add_u64 v[78:79], v[78:79], 0, v[132:133]
	v_add_co_u32_e32 v80, vcc, s1, v78
	s_mov_b32 s9, 0x20000
	s_nop 0
	v_addc_co_u32_e32 v81, vcc, 0, v79, vcc
	global_load_dwordx4 v[152:155], v[78:79], off nt
	global_load_dwordx4 v[140:143], v[80:81], off nt
	v_add_co_u32_e32 v80, vcc, s78, v78
	v_add_u32_e32 v160, s8, v130
	s_nop 0
	v_addc_co_u32_e32 v81, vcc, 0, v79, vcc
	v_add_co_u32_e32 v82, vcc, s79, v78
	v_add_u32_e32 v158, s12, v70
	s_nop 0
	v_addc_co_u32_e32 v83, vcc, 0, v79, vcc
	global_load_dwordx4 v[136:139], v[80:81], off nt
	global_load_dwordx4 v[126:129], v[82:83], off nt
	v_add_co_u32_e32 v80, vcc, s86, v78
	s_lshl_b32 s8, s13, 13
	s_nop 0
	v_addc_co_u32_e32 v81, vcc, 0, v79, vcc
	v_add_co_u32_e32 v82, vcc, s87, v78
	v_subrev_u32_e32 v73, s8, v158
	s_nop 0
	v_addc_co_u32_e32 v83, vcc, 0, v79, vcc
	global_load_dwordx4 v[122:125], v[80:81], off nt
	global_load_dwordx4 v[118:121], v[82:83], off nt
	v_add_co_u32_e32 v80, vcc, s85, v78
	s_nop 1
	v_addc_co_u32_e32 v81, vcc, 0, v79, vcc
	v_add_co_u32_e32 v82, vcc, s82, v78
	s_nop 1
	v_addc_co_u32_e32 v83, vcc, 0, v79, vcc
	global_load_dwordx4 v[114:117], v[80:81], off nt
	global_load_dwordx4 v[110:113], v[82:83], off nt
	v_add_co_u32_e32 v80, vcc, s9, v78
	s_mov_b32 s9, 0x24000
	s_nop 0
	v_addc_co_u32_e32 v81, vcc, 0, v79, vcc
	v_add_co_u32_e32 v82, vcc, s9, v78
	s_mov_b32 s9, 0x28000
	s_nop 0
	v_addc_co_u32_e32 v83, vcc, 0, v79, vcc
	global_load_dwordx4 v[106:109], v[80:81], off nt
	global_load_dwordx4 v[102:105], v[82:83], off nt
	v_add_co_u32_e32 v80, vcc, s9, v78
	s_mov_b32 s9, 0x2c000
	s_nop 0
	v_addc_co_u32_e32 v81, vcc, 0, v79, vcc
	v_add_co_u32_e32 v82, vcc, s9, v78
	s_mov_b32 s9, 0x30000
	s_nop 0
	v_addc_co_u32_e32 v83, vcc, 0, v79, vcc
	global_load_dwordx4 v[98:101], v[80:81], off nt
	global_load_dwordx4 v[94:97], v[82:83], off nt
	v_add_co_u32_e32 v80, vcc, s9, v78
	s_mov_b32 s9, 0x34000
	s_nop 0
	v_addc_co_u32_e32 v81, vcc, 0, v79, vcc
	v_add_co_u32_e32 v82, vcc, s9, v78
	s_nop 1
	v_addc_co_u32_e32 v83, vcc, 0, v79, vcc
	global_load_dwordx4 v[90:93], v[80:81], off nt
	global_load_dwordx4 v[86:89], v[82:83], off nt
	v_add_co_u32_e32 v80, vcc, 0x38000, v78
	s_nop 1
	v_addc_co_u32_e32 v81, vcc, 0, v79, vcc
	v_add_co_u32_e32 v78, vcc, 0x3c000, v78
	s_nop 1
	v_addc_co_u32_e32 v79, vcc, 0, v79, vcc
	global_load_dwordx4 v[82:85], v[80:81], off nt
	s_nop 0
	global_load_dwordx4 v[78:81], v[78:79], off nt
	s_addk_i32 s12, 0x80
	s_add_i32 s11, s11, 64
	s_add_i32 s10, s10, 1
	v_cmp_lt_i32_e32 vcc, s73, v72
	s_and_saveexec_b64 s[8:9], vcc
	s_xor_b64 s[8:9], exec, s[8:9]
	v_add_u32_e32 v68, 0x7ffff000, v71
	v_and_b32_e32 v68, 0x7fffff00, v68
	v_and_b32_e32 v69, 0x7c, v72
	v_or3_b32 v68, v69, v68, s83
	s_andn2_saveexec_b64 s[8:9], s[8:9]
	v_and_b32_e32 v68, 0x7c, v72
	v_and_or_b32 v68, v71, s0, v68
	s_or_b64 exec, exec, s[8:9]
	s_waitcnt vmcnt(35)
; __device__ __forceinline__ unsigned pk4_fp8(float a, float b, float c, float d) {
;     a = __builtin_fminf(__builtin_fmaxf(a, -448.f), 448.f); b = __builtin_fminf(__builtin_fmaxf(b, -448.f), 448.f); c = __builtin_fminf(__builtin_fmaxf(c, -448.f), 448.f); d = __builtin_fminf(__builtin_fmaxf(d, -448.f), 448.f);
;     int w = 0; w = __builtin_amdgcn_cvt_pk_fp8_f32(a, b, w, false); w = __builtin_amdgcn_cvt_pk_fp8_f32(c, d, w, true); return (unsigned)w;
; template <int MODE> __device__ __forceinline__ void cv_finish(const f32x4 (&tv)[16], int K, int nblk, unsigned char* WT, int item, int lane) {
;     const int kb = item / nblk, nb = item - kb * nblk, k0 = 64 * kb + 16 * (lane >> 4), n0 = 64 * nb + 4 * (lane & 15);
;     unsigned D[16];
; #pragma unroll
;     for (int i = 0; i < 16; ++i) { const f32x2 a = (f32x2){tv[i].x, tv[i].y} * (f32x2){1024.f, 1024.f}, b = (f32x2){tv[i].z, tv[i].w} * (f32x2){1024.f, 1024.f};
;         D[i] = pk4_fp8(a.x, a.y, b.x, b.y); }
	v_pk_mul_f32 v[62:63], v[62:63], s[84:85] op_sel_hi:[1,0]
	v_pk_mul_f32 v[64:65], v[64:65], s[84:85] op_sel_hi:[1,0]
	v_med3_f32 v69, v62, s96, v150
	v_med3_f32 v63, v63, s96, v150
	v_mov_b32_e32 v62, v133
	v_cvt_pk_fp8_f32 v62, v69, v63
	v_med3_f32 v63, v64, s96, v150
	v_med3_f32 v64, v65, s96, v150
	s_waitcnt vmcnt(34)
	v_pk_mul_f32 v[58:59], v[58:59], s[84:85] op_sel_hi:[1,0]
	v_cvt_pk_fp8_f32 v62, v63, v64 op_sel:[0,0,1]
	v_med3_f32 v63, v58, s96, v150
	v_med3_f32 v59, v59, s96, v150
	v_mov_b32_e32 v58, v133
	v_cvt_pk_fp8_f32 v58, v63, v59
	v_pk_mul_f32 v[60:61], v[60:61], s[84:85] op_sel_hi:[1,0]
	s_waitcnt vmcnt(33)
	v_pk_mul_f32 v[54:55], v[54:55], s[84:85] op_sel_hi:[1,0]
	v_med3_f32 v59, v60, s96, v150
	v_med3_f32 v60, v61, s96, v150
	v_cvt_pk_fp8_f32 v58, v59, v60 op_sel:[0,0,1]
	v_med3_f32 v59, v54, s96, v150
	v_med3_f32 v55, v55, s96, v150
	v_mov_b32_e32 v54, v133
	v_cvt_pk_fp8_f32 v54, v59, v55
	v_pk_mul_f32 v[56:57], v[56:57], s[84:85] op_sel_hi:[1,0]
	s_waitcnt vmcnt(32)
	v_pk_mul_f32 v[50:51], v[50:51], s[84:85] op_sel_hi:[1,0]
	v_med3_f32 v55, v56, s96, v150
	v_med3_f32 v56, v57, s96, v150
	v_cvt_pk_fp8_f32 v54, v55, v56 op_sel:[0,0,1]
	v_med3_f32 v55, v50, s96, v150
	v_med3_f32 v51, v51, s96, v150
	v_mov_b32_e32 v50, v133
	v_cvt_pk_fp8_f32 v50, v55, v51
	v_pk_mul_f32 v[52:53], v[52:53], s[84:85] op_sel_hi:[1,0]
	s_waitcnt vmcnt(31)
	v_pk_mul_f32 v[46:47], v[46:47], s[84:85] op_sel_hi:[1,0]
	v_med3_f32 v51, v52, s96, v150
	v_med3_f32 v52, v53, s96, v150
	v_cvt_pk_fp8_f32 v50, v51, v52 op_sel:[0,0,1]
	v_med3_f32 v51, v46, s96, v150
	v_med3_f32 v47, v47, s96, v150
	v_mov_b32_e32 v46, v133
	v_cvt_pk_fp8_f32 v46, v51, v47
	v_pk_mul_f32 v[48:49], v[48:49], s[84:85] op_sel_hi:[1,0]
	s_waitcnt vmcnt(30)
	v_pk_mul_f32 v[42:43], v[42:43], s[84:85] op_sel_hi:[1,0]
	v_med3_f32 v47, v48, s96, v150
	v_med3_f32 v48, v49, s96, v150
	v_cvt_pk_fp8_f32 v46, v47, v48 op_sel:[0,0,1]
	v_med3_f32 v47, v42, s96, v150
	v_med3_f32 v43, v43, s96, v150
	v_mov_b32_e32 v42, v133
	v_cvt_pk_fp8_f32 v42, v47, v43
	v_pk_mul_f32 v[44:45], v[44:45], s[84:85] op_sel_hi:[1,0]
	s_waitcnt vmcnt(29)
	v_pk_mul_f32 v[38:39], v[38:39], s[84:85] op_sel_hi:[1,0]
	v_med3_f32 v43, v44, s96, v150
	v_med3_f32 v44, v45, s96, v150
	v_cvt_pk_fp8_f32 v42, v43, v44 op_sel:[0,0,1]
	v_med3_f32 v43, v38, s96, v150
	v_med3_f32 v39, v39, s96, v150
	v_mov_b32_e32 v38, v133
	v_cvt_pk_fp8_f32 v38, v43, v39
	v_pk_mul_f32 v[40:41], v[40:41], s[84:85] op_sel_hi:[1,0]
	s_waitcnt vmcnt(28)
	v_pk_mul_f32 v[34:35], v[34:35], s[84:85] op_sel_hi:[1,0]
	v_med3_f32 v39, v40, s96, v150
	v_med3_f32 v40, v41, s96, v150
	v_cvt_pk_fp8_f32 v38, v39, v40 op_sel:[0,0,1]
	v_med3_f32 v39, v34, s96, v150
	v_med3_f32 v35, v35, s96, v150
	v_mov_b32_e32 v34, v133
	v_cvt_pk_fp8_f32 v34, v39, v35
	v_pk_mul_f32 v[36:37], v[36:37], s[84:85] op_sel_hi:[1,0]
	s_waitcnt vmcnt(27)
	v_pk_mul_f32 v[30:31], v[30:31], s[84:85] op_sel_hi:[1,0]
	v_med3_f32 v35, v36, s96, v150
	v_med3_f32 v36, v37, s96, v150
	v_cvt_pk_fp8_f32 v34, v35, v36 op_sel:[0,0,1]
	v_med3_f32 v35, v30, s96, v150
	v_med3_f32 v31, v31, s96, v150
	v_mov_b32_e32 v30, v133
	v_cvt_pk_fp8_f32 v30, v35, v31
	v_pk_mul_f32 v[32:33], v[32:33], s[84:85] op_sel_hi:[1,0]
	s_waitcnt vmcnt(26)
	v_pk_mul_f32 v[26:27], v[26:27], s[84:85] op_sel_hi:[1,0]
	v_med3_f32 v31, v32, s96, v150
	v_med3_f32 v32, v33, s96, v150
	v_cvt_pk_fp8_f32 v30, v31, v32 op_sel:[0,0,1]
	v_med3_f32 v31, v26, s96, v150
	v_med3_f32 v27, v27, s96, v150
	v_mov_b32_e32 v26, v133
	v_cvt_pk_fp8_f32 v26, v31, v27
	v_pk_mul_f32 v[28:29], v[28:29], s[84:85] op_sel_hi:[1,0]
	s_waitcnt vmcnt(25)
	v_pk_mul_f32 v[22:23], v[22:23], s[84:85] op_sel_hi:[1,0]
	v_med3_f32 v27, v28, s96, v150
	v_med3_f32 v28, v29, s96, v150
	v_cvt_pk_fp8_f32 v26, v27, v28 op_sel:[0,0,1]
	v_med3_f32 v27, v22, s96, v150
	v_med3_f32 v23, v23, s96, v150
	v_mov_b32_e32 v22, v133
	v_cvt_pk_fp8_f32 v22, v27, v23
	v_pk_mul_f32 v[24:25], v[24:25], s[84:85] op_sel_hi:[1,0]
	s_waitcnt vmcnt(24)
	v_pk_mul_f32 v[18:19], v[18:19], s[84:85] op_sel_hi:[1,0]
	v_med3_f32 v23, v24, s96, v150
	v_med3_f32 v24, v25, s96, v150
	v_cvt_pk_fp8_f32 v22, v23, v24 op_sel:[0,0,1]
	v_med3_f32 v23, v18, s96, v150
	v_med3_f32 v19, v19, s96, v150
	v_mov_b32_e32 v18, v133
	v_cvt_pk_fp8_f32 v18, v23, v19
	v_pk_mul_f32 v[20:21], v[20:21], s[84:85] op_sel_hi:[1,0]
	s_waitcnt vmcnt(23)
	v_pk_mul_f32 v[14:15], v[14:15], s[84:85] op_sel_hi:[1,0]
	v_med3_f32 v19, v20, s96, v150
	v_med3_f32 v20, v21, s96, v150
	v_cvt_pk_fp8_f32 v18, v19, v20 op_sel:[0,0,1]
	v_med3_f32 v19, v14, s96, v150
	v_med3_f32 v15, v15, s96, v150
	v_mov_b32_e32 v14, v133
	v_cvt_pk_fp8_f32 v14, v19, v15
	v_pk_mul_f32 v[16:17], v[16:17], s[84:85] op_sel_hi:[1,0]
	s_waitcnt vmcnt(22)
	v_pk_mul_f32 v[10:11], v[10:11], s[84:85] op_sel_hi:[1,0]
	v_med3_f32 v15, v16, s96, v150
	v_med3_f32 v16, v17, s96, v150
	v_cvt_pk_fp8_f32 v14, v15, v16 op_sel:[0,0,1]
	v_med3_f32 v15, v10, s96, v150
	v_med3_f32 v11, v11, s96, v150
	v_mov_b32_e32 v10, v133
	v_cvt_pk_fp8_f32 v10, v15, v11
	v_pk_mul_f32 v[12:13], v[12:13], s[84:85] op_sel_hi:[1,0]
	s_waitcnt vmcnt(21)
	v_pk_mul_f32 v[6:7], v[6:7], s[84:85] op_sel_hi:[1,0]
	v_med3_f32 v11, v12, s96, v150
	v_med3_f32 v12, v13, s96, v150
	v_cvt_pk_fp8_f32 v10, v11, v12 op_sel:[0,0,1]
	v_med3_f32 v11, v6, s96, v150
	v_med3_f32 v7, v7, s96, v150
	v_mov_b32_e32 v6, v133
	v_cvt_pk_fp8_f32 v6, v11, v7
	v_pk_mul_f32 v[8:9], v[8:9], s[84:85] op_sel_hi:[1,0]
	s_waitcnt vmcnt(20)
; template <int MODE> __device__ __forceinline__ void cv_finish(const f32x4 (&tv)[16], int K, int nblk, unsigned char* WT, int item, int lane) {
;     const int kb = item / nblk, nb = item - kb * nblk, k0 = 64 * kb + 16 * (lane >> 4), n0 = 64 * nb + 4 * (lane & 15);
;     unsigned D[16];
; #pragma unroll
;     for (int i = 0; i < 16; ++i) { const f32x2 a = (f32x2){tv[i].x, tv[i].y} * (f32x2){1024.f, 1024.f}, b = (f32x2){tv[i].z, tv[i].w} * (f32x2){1024.f, 1024.f};
;         D[i] = pk4_fp8(a.x, a.y, b.x, b.y); }
;     unsigned O[4][4];
; #pragma unroll
;     for (int q = 0; q < 4; ++q) { const unsigned a = D[4 * q], b = D[4 * q + 1], c = D[4 * q + 2], d = D[4 * q + 3];
;         const unsigned t0 = __builtin_amdgcn_perm(b, a, 0x05010400u), t1 = __builtin_amdgcn_perm(b, a, 0x07030602u), u0 = __builtin_amdgcn_perm(d, c, 0x05010400u), u1 = __builtin_amdgcn_perm(d, c, 0x07030602u);
;         O[0][q] = __builtin_amdgcn_perm(u0, t0, 0x05040100u); O[1][q] = __builtin_amdgcn_perm(u0, t0, 0x07060302u); O[2][q] = __builtin_amdgcn_perm(u1, t1, 0x05040100u); O[3][q] = __builtin_amdgcn_perm(u1, t1, 0x07060302u); }
; #pragma unroll
;     for (int j = 0; j < 4; ++j) { u32x4 o; o.x = O[j][0]; o.y = O[j][1]; o.z = O[j][2]; o.w = O[j][3];
;         __builtin_nontemporal_store(o, (u32x4*)(WT + (size_t)drow<MODE>(n0 + j) * K + k0)); }
; }
	v_pk_mul_f32 v[2:3], v[2:3], s[84:85] op_sel_hi:[1,0]
	v_med3_f32 v7, v8, s96, v150
	v_med3_f32 v8, v9, s96, v150
	v_cvt_pk_fp8_f32 v6, v7, v8 op_sel:[0,0,1]
	v_med3_f32 v2, v2, s96, v150
	v_med3_f32 v3, v3, s96, v150
	v_mov_b32_e32 v7, v133
	v_cvt_pk_fp8_f32 v7, v2, v3
	v_pk_mul_f32 v[2:3], v[4:5], s[84:85] op_sel_hi:[1,0]
	v_ashrrev_i32_e32 v69, 31, v68
	v_med3_f32 v2, v2, s96, v150
	v_med3_f32 v3, v3, s96, v150
	v_cvt_pk_fp8_f32 v7, v2, v3 op_sel:[0,0,1]
	v_perm_b32 v5, v58, v62, s97
	v_perm_b32 v8, v50, v54, s97
	v_perm_b32 v9, v42, v46, s97
	v_perm_b32 v11, v34, v38, s97
	v_perm_b32 v12, v26, v30, s97
	v_perm_b32 v13, v18, v22, s97
	v_perm_b32 v15, v10, v14, s97
	v_perm_b32 v16, v7, v6, s97
	v_lshl_add_u64 v[2:3], s[6:7], 0, v[66:67]
	v_lshlrev_b64 v[20:21], 11, v[68:69]
	v_add_u32_e32 v17, 1, v72
	v_perm_b32 v74, v8, v5, s71
	v_perm_b32 v75, v11, v9, s71
	v_perm_b32 v76, v13, v12, s71
	v_perm_b32 v77, v16, v15, s71
	v_lshl_add_u64 v[20:21], v[2:3], 0, v[20:21]
	v_cmp_lt_i32_e32 vcc, s73, v17
	global_store_dwordx4 v[20:21], v[74:77], off nt
	s_and_saveexec_b64 s[8:9], vcc
	s_xor_b64 s[8:9], exec, s[8:9]
	v_add_u32_e32 v4, 0x7ffff002, v71
	v_and_b32_e32 v4, 0x7fffff00, v4
	v_and_b32_e32 v17, 0x7d, v17
	v_or3_b32 v4, v17, v4, s83
	s_andn2_saveexec_b64 s[8:9], s[8:9]
	v_add_u32_e32 v4, 2, v71
	v_and_b32_e32 v17, 0x7d, v17
	v_and_or_b32 v4, v4, s0, v17
	s_or_b64 exec, exec, s[8:9]
	v_perm_b32 v64, v8, v5, s72
	v_ashrrev_i32_e32 v5, 31, v4
	v_lshlrev_b64 v[4:5], 11, v[4:5]
	v_perm_b32 v65, v11, v9, s72
	v_perm_b32 v66, v13, v12, s72
	v_perm_b32 v67, v16, v15, s72
	v_lshl_add_u64 v[4:5], v[2:3], 0, v[4:5]
	global_store_dwordx4 v[4:5], v[64:67], off nt
	v_add_u32_e32 v5, 2, v72
	v_cmp_lt_i32_e32 vcc, s73, v5
	s_and_saveexec_b64 s[8:9], vcc
	s_xor_b64 s[8:9], exec, s[8:9]
	v_add_u32_e32 v4, 0x7ffff004, v71
	v_and_b32_e32 v4, 0x7fffff00, v4
	v_and_b32_e32 v5, 0x7e, v5
	v_or3_b32 v4, v5, v4, s83
	s_andn2_saveexec_b64 s[8:9], s[8:9]
	v_add_u32_e32 v4, 4, v71
	v_and_b32_e32 v5, 0x7e, v5
	v_and_or_b32 v4, v4, s0, v5
	s_or_b64 exec, exec, s[8:9]
	v_ashrrev_i32_e32 v5, 31, v4
	v_perm_b32 v8, v58, v62, s70
	v_perm_b32 v9, v50, v54, s70
	v_perm_b32 v11, v42, v46, s70
	v_perm_b32 v12, v34, v38, s70
	v_perm_b32 v13, v26, v30, s70
	v_perm_b32 v15, v18, v22, s70
	v_perm_b32 v10, v10, v14, s70
	v_perm_b32 v6, v7, v6, s70
	v_lshlrev_b64 v[4:5], 11, v[4:5]
	v_perm_b32 v16, v9, v8, s71
	v_perm_b32 v17, v12, v11, s71
	v_perm_b32 v18, v15, v13, s71
	v_perm_b32 v19, v6, v10, s71
	v_lshl_add_u64 v[4:5], v[2:3], 0, v[4:5]
	global_store_dwordx4 v[4:5], v[16:19], off nt
	v_add_u32_e32 v5, 3, v72
	v_cmp_lt_i32_e32 vcc, s73, v5
	s_and_saveexec_b64 s[8:9], vcc
	s_xor_b64 s[8:9], exec, s[8:9]
	v_add_u32_e32 v4, 0x7ffff006, v71
	v_and_b32_e32 v4, 0x7fffff00, v4
	v_and_b32_e32 v5, 0x7f, v5
	v_or3_b32 v4, v5, v4, s83
	s_andn2_saveexec_b64 s[8:9], s[8:9]
	v_add_u32_e32 v4, 6, v71
	v_and_b32_e32 v5, 0x7f, v5
	v_and_or_b32 v4, v4, s0, v5
	s_or_b64 exec, exec, s[8:9]
	v_ashrrev_i32_e32 v5, 31, v4
	v_lshlrev_b64 v[4:5], 11, v[4:5]
	v_perm_b32 v16, v9, v8, s72
	v_perm_b32 v17, v12, v11, s72
	v_perm_b32 v18, v15, v13, s72
	v_perm_b32 v19, v6, v10, s72
	v_lshl_add_u64 v[2:3], v[2:3], 0, v[4:5]
	global_store_dwordx4 v[2:3], v[16:19], off nt
	v_cmp_lt_i32_e32 vcc, s73, v160
	s_and_saveexec_b64 s[8:9], vcc
	s_xor_b64 s[8:9], exec, s[8:9]
	v_add_u32_e32 v158, 0x7ffff000, v73
	v_and_b32_e32 v158, 0x7fffff00, v158
	v_and_b32_e32 v159, 0x7c, v160
	v_or3_b32 v158, v159, v158, s83
	s_andn2_saveexec_b64 s[8:9], s[8:9]
	v_and_b32_e32 v158, 0x7c, v160
	v_and_or_b32 v158, v73, s0, v158
	s_or_b64 exec, exec, s[8:9]
	s_waitcnt vmcnt(19)
	v_pk_mul_f32 v[152:153], v[152:153], s[84:85] op_sel_hi:[1,0]
	v_pk_mul_f32 v[154:155], v[154:155], s[84:85] op_sel_hi:[1,0]
	v_med3_f32 v159, v152, s96, v150
	v_med3_f32 v153, v153, s96, v150
	v_mov_b32_e32 v152, v133
	v_cvt_pk_fp8_f32 v152, v159, v153
	v_med3_f32 v153, v154, s96, v150
	v_med3_f32 v154, v155, s96, v150
	s_waitcnt vmcnt(18)
	v_pk_mul_f32 v[140:141], v[140:141], s[84:85] op_sel_hi:[1,0]
	v_cvt_pk_fp8_f32 v152, v153, v154 op_sel:[0,0,1]
	v_med3_f32 v153, v140, s96, v150
	v_med3_f32 v141, v141, s96, v150
	v_mov_b32_e32 v140, v133
	v_cvt_pk_fp8_f32 v140, v153, v141
	v_pk_mul_f32 v[142:143], v[142:143], s[84:85] op_sel_hi:[1,0]
	s_waitcnt vmcnt(17)
	v_pk_mul_f32 v[136:137], v[136:137], s[84:85] op_sel_hi:[1,0]
	v_med3_f32 v141, v142, s96, v150
	v_med3_f32 v142, v143, s96, v150
	v_cvt_pk_fp8_f32 v140, v141, v142 op_sel:[0,0,1]
	v_med3_f32 v141, v136, s96, v150
	v_med3_f32 v137, v137, s96, v150
	v_mov_b32_e32 v136, v133
	v_cvt_pk_fp8_f32 v136, v141, v137
	v_pk_mul_f32 v[138:139], v[138:139], s[84:85] op_sel_hi:[1,0]
	s_waitcnt vmcnt(16)
	v_pk_mul_f32 v[126:127], v[126:127], s[84:85] op_sel_hi:[1,0]
	v_med3_f32 v137, v138, s96, v150
	v_med3_f32 v138, v139, s96, v150
	v_cvt_pk_fp8_f32 v136, v137, v138 op_sel:[0,0,1]
	v_med3_f32 v137, v126, s96, v150
	v_med3_f32 v127, v127, s96, v150
	v_mov_b32_e32 v126, v133
	v_cvt_pk_fp8_f32 v126, v137, v127
	v_pk_mul_f32 v[128:129], v[128:129], s[84:85] op_sel_hi:[1,0]
	s_waitcnt vmcnt(15)
	v_pk_mul_f32 v[122:123], v[122:123], s[84:85] op_sel_hi:[1,0]
	v_med3_f32 v127, v128, s96, v150
	v_med3_f32 v128, v129, s96, v150
	v_cvt_pk_fp8_f32 v126, v127, v128 op_sel:[0,0,1]
	v_med3_f32 v127, v122, s96, v150
	v_med3_f32 v123, v123, s96, v150
	v_mov_b32_e32 v122, v133
	v_cvt_pk_fp8_f32 v122, v127, v123
	v_pk_mul_f32 v[124:125], v[124:125], s[84:85] op_sel_hi:[1,0]
	s_waitcnt vmcnt(14)
; __device__ __forceinline__ unsigned pk4_fp8(float a, float b, float c, float d) {
;     a = __builtin_fminf(__builtin_fmaxf(a, -448.f), 448.f); b = __builtin_fminf(__builtin_fmaxf(b, -448.f), 448.f); c = __builtin_fminf(__builtin_fmaxf(c, -448.f), 448.f); d = __builtin_fminf(__builtin_fmaxf(d, -448.f), 448.f);
;     int w = 0; w = __builtin_amdgcn_cvt_pk_fp8_f32(a, b, w, false); w = __builtin_amdgcn_cvt_pk_fp8_f32(c, d, w, true); return (unsigned)w;
; template <int MODE> __device__ __forceinline__ void cv_finish(const f32x4 (&tv)[16], int K, int nblk, unsigned char* WT, int item, int lane) {
;     const int kb = item / nblk, nb = item - kb * nblk, k0 = 64 * kb + 16 * (lane >> 4), n0 = 64 * nb + 4 * (lane & 15);
;     unsigned D[16];
; #pragma unroll
;     for (int i = 0; i < 16; ++i) { const f32x2 a = (f32x2){tv[i].x, tv[i].y} * (f32x2){1024.f, 1024.f}, b = (f32x2){tv[i].z, tv[i].w} * (f32x2){1024.f, 1024.f};
;         D[i] = pk4_fp8(a.x, a.y, b.x, b.y); }
	v_pk_mul_f32 v[118:119], v[118:119], s[84:85] op_sel_hi:[1,0]
	v_med3_f32 v123, v124, s96, v150
	v_med3_f32 v124, v125, s96, v150
	v_cvt_pk_fp8_f32 v122, v123, v124 op_sel:[0,0,1]
	v_med3_f32 v123, v118, s96, v150
	v_med3_f32 v119, v119, s96, v150
	v_mov_b32_e32 v118, v133
	v_cvt_pk_fp8_f32 v118, v123, v119
	v_pk_mul_f32 v[120:121], v[120:121], s[84:85] op_sel_hi:[1,0]
	s_waitcnt vmcnt(13)
	v_pk_mul_f32 v[114:115], v[114:115], s[84:85] op_sel_hi:[1,0]
	v_med3_f32 v119, v120, s96, v150
	v_med3_f32 v120, v121, s96, v150
	v_cvt_pk_fp8_f32 v118, v119, v120 op_sel:[0,0,1]
	v_med3_f32 v119, v114, s96, v150
	v_med3_f32 v115, v115, s96, v150
	v_mov_b32_e32 v114, v133
	v_cvt_pk_fp8_f32 v114, v119, v115
	v_pk_mul_f32 v[116:117], v[116:117], s[84:85] op_sel_hi:[1,0]
	s_waitcnt vmcnt(12)
	v_pk_mul_f32 v[110:111], v[110:111], s[84:85] op_sel_hi:[1,0]
	v_med3_f32 v115, v116, s96, v150
	v_med3_f32 v116, v117, s96, v150
	v_cvt_pk_fp8_f32 v114, v115, v116 op_sel:[0,0,1]
	v_med3_f32 v115, v110, s96, v150
	v_med3_f32 v111, v111, s96, v150
	v_mov_b32_e32 v110, v133
	v_cvt_pk_fp8_f32 v110, v115, v111
	v_pk_mul_f32 v[112:113], v[112:113], s[84:85] op_sel_hi:[1,0]
	s_waitcnt vmcnt(11)
	v_pk_mul_f32 v[106:107], v[106:107], s[84:85] op_sel_hi:[1,0]
	v_med3_f32 v111, v112, s96, v150
	v_med3_f32 v112, v113, s96, v150
	v_cvt_pk_fp8_f32 v110, v111, v112 op_sel:[0,0,1]
	v_med3_f32 v111, v106, s96, v150
	v_med3_f32 v107, v107, s96, v150
	v_mov_b32_e32 v106, v133
	v_cvt_pk_fp8_f32 v106, v111, v107
	v_pk_mul_f32 v[108:109], v[108:109], s[84:85] op_sel_hi:[1,0]
	s_waitcnt vmcnt(10)
	v_pk_mul_f32 v[102:103], v[102:103], s[84:85] op_sel_hi:[1,0]
	v_med3_f32 v107, v108, s96, v150
	v_med3_f32 v108, v109, s96, v150
	v_cvt_pk_fp8_f32 v106, v107, v108 op_sel:[0,0,1]
	v_med3_f32 v107, v102, s96, v150
	v_med3_f32 v103, v103, s96, v150
	v_mov_b32_e32 v102, v133
	v_cvt_pk_fp8_f32 v102, v107, v103
	v_pk_mul_f32 v[104:105], v[104:105], s[84:85] op_sel_hi:[1,0]
	s_waitcnt vmcnt(9)
	v_pk_mul_f32 v[98:99], v[98:99], s[84:85] op_sel_hi:[1,0]
	v_med3_f32 v103, v104, s96, v150
	v_med3_f32 v104, v105, s96, v150
	v_cvt_pk_fp8_f32 v102, v103, v104 op_sel:[0,0,1]
	v_med3_f32 v103, v98, s96, v150
	v_med3_f32 v99, v99, s96, v150
	v_mov_b32_e32 v98, v133
	v_cvt_pk_fp8_f32 v98, v103, v99
	v_pk_mul_f32 v[100:101], v[100:101], s[84:85] op_sel_hi:[1,0]
	s_waitcnt vmcnt(8)
	v_pk_mul_f32 v[94:95], v[94:95], s[84:85] op_sel_hi:[1,0]
	v_med3_f32 v99, v100, s96, v150
	v_med3_f32 v100, v101, s96, v150
	v_cvt_pk_fp8_f32 v98, v99, v100 op_sel:[0,0,1]
	v_med3_f32 v99, v94, s96, v150
	v_med3_f32 v95, v95, s96, v150
	v_mov_b32_e32 v94, v133
	v_cvt_pk_fp8_f32 v94, v99, v95
	v_pk_mul_f32 v[96:97], v[96:97], s[84:85] op_sel_hi:[1,0]
	s_waitcnt vmcnt(7)
	v_pk_mul_f32 v[90:91], v[90:91], s[84:85] op_sel_hi:[1,0]
	v_med3_f32 v95, v96, s96, v150
	v_med3_f32 v96, v97, s96, v150
	v_cvt_pk_fp8_f32 v94, v95, v96 op_sel:[0,0,1]
	v_med3_f32 v95, v90, s96, v150
	v_med3_f32 v91, v91, s96, v150
	v_mov_b32_e32 v90, v133
	v_cvt_pk_fp8_f32 v90, v95, v91
	v_pk_mul_f32 v[92:93], v[92:93], s[84:85] op_sel_hi:[1,0]
	s_waitcnt vmcnt(6)
	v_pk_mul_f32 v[86:87], v[86:87], s[84:85] op_sel_hi:[1,0]
	v_med3_f32 v91, v92, s96, v150
	v_med3_f32 v92, v93, s96, v150
	v_cvt_pk_fp8_f32 v90, v91, v92 op_sel:[0,0,1]
	v_med3_f32 v91, v86, s96, v150
	v_med3_f32 v87, v87, s96, v150
	v_mov_b32_e32 v86, v133
	v_cvt_pk_fp8_f32 v86, v91, v87
	v_pk_mul_f32 v[88:89], v[88:89], s[84:85] op_sel_hi:[1,0]
	s_waitcnt vmcnt(5)
	v_pk_mul_f32 v[82:83], v[82:83], s[84:85] op_sel_hi:[1,0]
	v_med3_f32 v87, v88, s96, v150
	v_med3_f32 v88, v89, s96, v150
	v_cvt_pk_fp8_f32 v86, v87, v88 op_sel:[0,0,1]
	v_med3_f32 v87, v82, s96, v150
	v_med3_f32 v83, v83, s96, v150
	v_mov_b32_e32 v82, v133
	v_cvt_pk_fp8_f32 v82, v87, v83
	v_pk_mul_f32 v[84:85], v[84:85], s[84:85] op_sel_hi:[1,0]
	s_waitcnt vmcnt(4)
; template <int MODE> __device__ __forceinline__ void cv_finish(const f32x4 (&tv)[16], int K, int nblk, unsigned char* WT, int item, int lane) {
;     ...
;     unsigned O[4][4];
; #pragma unroll
;     for (int q = 0; q < 4; ++q) { const unsigned a = D[4 * q], b = D[4 * q + 1], c = D[4 * q + 2], d = D[4 * q + 3];
;         const unsigned t0 = __builtin_amdgcn_perm(b, a, 0x05010400u), t1 = __builtin_amdgcn_perm(b, a, 0x07030602u), u0 = __builtin_amdgcn_perm(d, c, 0x05010400u), u1 = __builtin_amdgcn_perm(d, c, 0x07030602u);
;         O[0][q] = __builtin_amdgcn_perm(u0, t0, 0x05040100u); O[1][q] = __builtin_amdgcn_perm(u0, t0, 0x07060302u); O[2][q] = __builtin_amdgcn_perm(u1, t1, 0x05040100u); O[3][q] = __builtin_amdgcn_perm(u1, t1, 0x07060302u); }
; #pragma unroll
;     for (int j = 0; j < 4; ++j) { u32x4 o; o.x = O[j][0]; o.y = O[j][1]; o.z = O[j][2]; o.w = O[j][3];
;         __builtin_nontemporal_store(o, (u32x4*)(WT + (size_t)drow<MODE>(n0 + j) * K + k0)); }
; }
; template <int MODE> __device__ __forceinline__ void cv_run4(const float* W, int K, int N, unsigned char* WT, int item0, int lane) {
;     const int nblk = N / 64; f32x4 ta[16];
; #pragma unroll 1
;     for (int j = 0; j < 4; ++j) { cv_load(W, N, nblk, item0 + j, lane, ta); cv_finish<MODE>(ta, K, nblk, WT, item0 + j, lane); }
	v_pk_mul_f32 v[78:79], v[78:79], s[84:85] op_sel_hi:[1,0]
	v_med3_f32 v83, v84, s96, v150
	v_med3_f32 v84, v85, s96, v150
	v_cvt_pk_fp8_f32 v82, v83, v84 op_sel:[0,0,1]
	v_med3_f32 v78, v78, s96, v150
	v_med3_f32 v79, v79, s96, v150
	v_mov_b32_e32 v83, v133
	v_cvt_pk_fp8_f32 v83, v78, v79
	v_pk_mul_f32 v[78:79], v[80:81], s[84:85] op_sel_hi:[1,0]
	v_ashrrev_i32_e32 v159, 31, v158
	v_med3_f32 v78, v78, s96, v150
	v_med3_f32 v79, v79, s96, v150
	v_cvt_pk_fp8_f32 v83, v78, v79 op_sel:[0,0,1]
	v_perm_b32 v81, v140, v152, s97
	v_perm_b32 v84, v126, v136, s97
	v_perm_b32 v85, v118, v122, s97
	v_perm_b32 v87, v110, v114, s97
	v_perm_b32 v88, v102, v106, s97
	v_perm_b32 v89, v94, v98, s97
	v_perm_b32 v91, v86, v90, s97
	v_perm_b32 v92, v83, v82, s97
	v_lshl_add_u64 v[78:79], s[6:7], 0, v[156:157]
	v_lshlrev_b64 v[96:97], 11, v[158:159]
	v_add_u32_e32 v93, 1, v160
	v_perm_b32 v162, v84, v81, s71
	v_perm_b32 v163, v87, v85, s71
	v_perm_b32 v164, v89, v88, s71
	v_perm_b32 v165, v92, v91, s71
	v_lshl_add_u64 v[96:97], v[78:79], 0, v[96:97]
	v_cmp_lt_i32_e32 vcc, s73, v93
	global_store_dwordx4 v[96:97], v[162:165], off nt
	s_and_saveexec_b64 s[8:9], vcc
	s_xor_b64 s[8:9], exec, s[8:9]
	v_add_u32_e32 v80, 0x7ffff002, v73
	v_and_b32_e32 v80, 0x7fffff00, v80
	v_and_b32_e32 v93, 0x7d, v93
	v_or3_b32 v80, v93, v80, s83
	s_andn2_saveexec_b64 s[8:9], s[8:9]
	v_add_u32_e32 v80, 2, v73
	v_and_b32_e32 v93, 0x7d, v93
	v_and_or_b32 v80, v80, s0, v93
	s_or_b64 exec, exec, s[8:9]
	v_perm_b32 v154, v84, v81, s72
	v_ashrrev_i32_e32 v81, 31, v80
	v_lshlrev_b64 v[80:81], 11, v[80:81]
	v_perm_b32 v155, v87, v85, s72
	v_perm_b32 v156, v89, v88, s72
	v_perm_b32 v157, v92, v91, s72
	v_lshl_add_u64 v[80:81], v[78:79], 0, v[80:81]
	global_store_dwordx4 v[80:81], v[154:157], off nt
	v_add_u32_e32 v81, 2, v160
	v_cmp_lt_i32_e32 vcc, s73, v81
	s_and_saveexec_b64 s[8:9], vcc
	s_xor_b64 s[8:9], exec, s[8:9]
	v_add_u32_e32 v80, 0x7ffff004, v73
	v_and_b32_e32 v80, 0x7fffff00, v80
	v_and_b32_e32 v81, 0x7e, v81
	v_or3_b32 v80, v81, v80, s83
	s_andn2_saveexec_b64 s[8:9], s[8:9]
	v_add_u32_e32 v80, 4, v73
	v_and_b32_e32 v81, 0x7e, v81
	v_and_or_b32 v80, v80, s0, v81
	s_or_b64 exec, exec, s[8:9]
	v_ashrrev_i32_e32 v81, 31, v80
	v_perm_b32 v84, v140, v152, s70
	v_perm_b32 v85, v126, v136, s70
	v_perm_b32 v87, v118, v122, s70
	v_perm_b32 v88, v110, v114, s70
	v_perm_b32 v89, v102, v106, s70
	v_perm_b32 v91, v94, v98, s70
	v_perm_b32 v86, v86, v90, s70
	v_perm_b32 v82, v83, v82, s70
	v_lshlrev_b64 v[80:81], 11, v[80:81]
	v_perm_b32 v92, v85, v84, s71
	v_perm_b32 v93, v88, v87, s71
	v_perm_b32 v94, v91, v89, s71
	v_perm_b32 v95, v82, v86, s71
	v_lshl_add_u64 v[80:81], v[78:79], 0, v[80:81]
	global_store_dwordx4 v[80:81], v[92:95], off nt
	v_add_u32_e32 v81, 3, v160
	v_cmp_lt_i32_e32 vcc, s73, v81
	s_and_saveexec_b64 s[8:9], vcc
	s_xor_b64 s[8:9], exec, s[8:9]
	v_add_u32_e32 v80, 0x7ffff006, v73
	v_and_b32_e32 v80, 0x7fffff00, v80
	v_and_b32_e32 v81, 0x7f, v81
	v_or3_b32 v80, v81, v80, s83
	s_andn2_saveexec_b64 s[8:9], s[8:9]
	v_add_u32_e32 v80, 6, v73
	v_and_b32_e32 v81, 0x7f, v81
	v_and_or_b32 v80, v80, s0, v81
	s_or_b64 exec, exec, s[8:9]
	v_ashrrev_i32_e32 v81, 31, v80
	v_lshlrev_b64 v[80:81], 11, v[80:81]
	v_perm_b32 v92, v85, v84, s72
	v_perm_b32 v93, v88, v87, s72
	v_perm_b32 v94, v91, v89, s72
	v_perm_b32 v95, v82, v86, s72
	v_lshl_add_u64 v[78:79], v[78:79], 0, v[80:81]
	global_store_dwordx4 v[78:79], v[92:95], off nt
	s_cmpk_eq_i32 s12, 0x200
	s_cbranch_scc0 .LBB0_734
	s_branch .LBB0_719

; __device__ __forceinline__ void cv_load(const float* W, int N, int nblk, int item, int lane, f32x4 (&tv)[16]) {
;     const int kb = item / nblk, nb = item - kb * nblk; const float* p = W + (size_t)(64 * kb + 16 * (lane >> 4)) * N + 64 * nb + 4 * (lane & 15);
; #pragma unroll
;     for (int i = 0; i < 16; ++i) tv[i] = __builtin_nontemporal_load((const f32x4*)(p + (size_t)i * N));
; }
.LBB0_761:
	s_lshr_b32 s41, s2, 5
	s_lshl_b32 s42, s41, 11
	v_mov_b32_e32 v3, v67
	v_lshl_or_b32 v2, s41, 6, v1
	s_sub_i32 s41, s39, s42
	v_subrev_u32_e32 v8, s42, v4
	v_lshlrev_b64 v[6:7], 13, v[2:3]
	s_add_i32 s42, s40, s41
	v_lshl_add_u64 v[6:7], s[6:7], 0, v[6:7]
	s_ashr_i32 s43, s42, 31
	v_lshl_add_u64 v[6:7], s[42:43], 2, v[6:7]
	v_lshl_add_u64 v[16:17], v[6:7], 0, v[66:67]
	v_add_co_u32_e32 v18, vcc, s0, v16
	v_add_u32_e32 v8, s40, v8
	s_nop 0
	v_addc_co_u32_e32 v19, vcc, 0, v17, vcc
	v_add_co_u32_e32 v20, vcc, s1, v16
	v_ashrrev_i32_e32 v9, 31, v8
	s_nop 0
	v_addc_co_u32_e32 v21, vcc, 0, v17, vcc
	v_add_co_u32_e32 v22, vcc, s5, v16
	v_add_u32_e32 v10, 1, v8
	s_nop 0
	v_addc_co_u32_e32 v23, vcc, 0, v17, vcc
	v_add_co_u32_e32 v24, vcc, s12, v16
	v_add_u32_e32 v12, 2, v8
	s_nop 0
	v_addc_co_u32_e32 v25, vcc, 0, v17, vcc
	v_add_co_u32_e32 v26, vcc, s13, v16
	v_add_u32_e32 v14, 3, v8
	s_nop 0
	v_addc_co_u32_e32 v27, vcc, 0, v17, vcc
	v_add_co_u32_e32 v30, vcc, s14, v16
	v_lshl_add_u64 v[2:3], s[8:9], 0, v[2:3]
	s_nop 0
	v_addc_co_u32_e32 v31, vcc, 0, v17, vcc
	v_add_co_u32_e32 v34, vcc, s15, v16
	v_lshlrev_b64 v[8:9], 11, v[8:9]
	s_nop 0
	v_addc_co_u32_e32 v35, vcc, 0, v17, vcc
	v_add_co_u32_e32 v38, vcc, s16, v16
	v_ashrrev_i32_e32 v11, 31, v10
	s_nop 0
	v_addc_co_u32_e32 v39, vcc, 0, v17, vcc
	v_add_co_u32_e32 v42, vcc, s17, v16
	v_ashrrev_i32_e32 v13, 31, v12
	s_nop 0
	v_addc_co_u32_e32 v43, vcc, 0, v17, vcc
	v_add_co_u32_e32 v46, vcc, s18, v16
	v_ashrrev_i32_e32 v15, 31, v14
	s_nop 0
	v_addc_co_u32_e32 v47, vcc, 0, v17, vcc
	v_add_co_u32_e32 v50, vcc, s19, v16
	v_lshl_add_u64 v[74:75], v[2:3], 0, v[8:9]
	s_nop 0
	v_addc_co_u32_e32 v51, vcc, 0, v17, vcc
	v_add_co_u32_e32 v54, vcc, s20, v16
	v_lshlrev_b64 v[10:11], 11, v[10:11]
	s_nop 0
	v_addc_co_u32_e32 v55, vcc, 0, v17, vcc
	v_add_co_u32_e32 v58, vcc, s21, v16
	v_lshlrev_b64 v[12:13], 11, v[12:13]
	s_nop 0
	v_addc_co_u32_e32 v59, vcc, 0, v17, vcc
	v_add_co_u32_e32 v62, vcc, s22, v16
	v_lshlrev_b64 v[14:15], 11, v[14:15]
	s_nop 0
	v_addc_co_u32_e32 v63, vcc, 0, v17, vcc
	v_add_co_u32_e32 v68, vcc, s23, v16
	global_load_dwordx4 v[6:9], v[16:17], off nt
	s_nop 0
	v_addc_co_u32_e32 v69, vcc, 0, v17, vcc
	v_lshl_add_u64 v[76:77], v[2:3], 0, v[10:11]
	v_lshl_add_u64 v[78:79], v[2:3], 0, v[12:13]
	v_lshl_add_u64 v[2:3], v[2:3], 0, v[14:15]
	global_load_dwordx4 v[10:13], v[18:19], off nt
	global_load_dwordx4 v[14:17], v[20:21], off nt
	s_nop 0
	global_load_dwordx4 v[18:21], v[22:23], off nt
	s_nop 0
	global_load_dwordx4 v[22:25], v[24:25], off nt
	s_nop 0
	global_load_dwordx4 v[26:29], v[26:27], off nt
	s_nop 0
	global_load_dwordx4 v[30:33], v[30:31], off nt
	s_nop 0
	global_load_dwordx4 v[34:37], v[34:35], off nt
	s_nop 0
	global_load_dwordx4 v[38:41], v[38:39], off nt
	s_nop 0
	global_load_dwordx4 v[42:45], v[42:43], off nt
	s_nop 0
	global_load_dwordx4 v[46:49], v[46:47], off nt
	s_nop 0
	global_load_dwordx4 v[50:53], v[50:51], off nt
	s_nop 0
	global_load_dwordx4 v[54:57], v[54:55], off nt
	s_nop 0
	global_load_dwordx4 v[58:61], v[58:59], off nt
	s_nop 0
	global_load_dwordx4 v[62:65], v[62:63], off nt
	s_nop 0
	global_load_dwordx4 v[68:71], v[68:69], off nt
	v_mov_b32_e32 v5, v67
	v_mov_b32_e32 v73, v67
	v_mov_b32_e32 v80, v67
	v_mov_b32_e32 v81, v67
	v_mov_b32_e32 v82, v67
	v_mov_b32_e32 v83, v67
	v_mov_b32_e32 v84, v67
	v_mov_b32_e32 v85, v67
	v_mov_b32_e32 v86, v67
	v_mov_b32_e32 v87, v67
	v_mov_b32_e32 v88, v67
	v_mov_b32_e32 v89, v67
	v_mov_b32_e32 v90, v67
	v_mov_b32_e32 v91, v67
	v_mov_b32_e32 v92, v67
	v_mov_b32_e32 v93, v67
	s_add_i32 s2, s2, 1
	s_add_i32 s40, s40, 64
	s_lshr_b32 s41, s2, 5
	s_lshl_b32 s42, s41, 11
	v_mov_b32_e32 v99, v67
	v_lshl_or_b32 v98, s41, 6, v1
	s_sub_i32 s41, s39, s42
	v_subrev_u32_e32 v104, s42, v4
	v_lshlrev_b64 v[102:103], 13, v[98:99]
	s_add_i32 s42, s40, s41
	v_lshl_add_u64 v[102:103], s[6:7], 0, v[102:103]
	s_ashr_i32 s43, s42, 31
	v_lshl_add_u64 v[102:103], s[42:43], 2, v[102:103]
	v_lshl_add_u64 v[112:113], v[102:103], 0, v[66:67]
	v_add_co_u32_e32 v114, vcc, s0, v112
	v_add_u32_e32 v104, s40, v104
	s_nop 0
	v_addc_co_u32_e32 v115, vcc, 0, v113, vcc
	v_add_co_u32_e32 v116, vcc, s1, v112
	v_ashrrev_i32_e32 v105, 31, v104
	s_nop 0
	v_addc_co_u32_e32 v117, vcc, 0, v113, vcc
	v_add_co_u32_e32 v118, vcc, s5, v112
	v_add_u32_e32 v106, 1, v104
	s_nop 0
	v_addc_co_u32_e32 v119, vcc, 0, v113, vcc
	v_add_co_u32_e32 v120, vcc, s12, v112
	v_add_u32_e32 v108, 2, v104
	s_nop 0
	v_addc_co_u32_e32 v121, vcc, 0, v113, vcc
	v_add_co_u32_e32 v122, vcc, s13, v112
	v_add_u32_e32 v110, 3, v104
	s_nop 0
	v_addc_co_u32_e32 v123, vcc, 0, v113, vcc
	v_add_co_u32_e32 v126, vcc, s14, v112
	v_lshl_add_u64 v[98:99], s[8:9], 0, v[98:99]
	s_nop 0
	v_addc_co_u32_e32 v127, vcc, 0, v113, vcc
	v_add_co_u32_e32 v132, vcc, s15, v112
	v_lshlrev_b64 v[104:105], 11, v[104:105]
	s_nop 0
	v_addc_co_u32_e32 v133, vcc, 0, v113, vcc
	v_add_co_u32_e32 v136, vcc, s16, v112
	v_ashrrev_i32_e32 v107, 31, v106
	s_nop 0
	v_addc_co_u32_e32 v137, vcc, 0, v113, vcc
	v_add_co_u32_e32 v140, vcc, s17, v112
	v_ashrrev_i32_e32 v109, 31, v108
	s_nop 0
	v_addc_co_u32_e32 v141, vcc, 0, v113, vcc
	v_add_co_u32_e32 v144, vcc, s18, v112
	v_ashrrev_i32_e32 v111, 31, v110
	s_nop 0
	v_addc_co_u32_e32 v145, vcc, 0, v113, vcc
	v_add_co_u32_e32 v148, vcc, s19, v112
	v_lshl_add_u64 v[174:175], v[98:99], 0, v[104:105]
	s_nop 0
	v_addc_co_u32_e32 v149, vcc, 0, v113, vcc
	v_add_co_u32_e32 v152, vcc, s20, v112
	v_lshlrev_b64 v[106:107], 11, v[106:107]
	s_nop 0
	v_addc_co_u32_e32 v153, vcc, 0, v113, vcc
	v_add_co_u32_e32 v156, vcc, s21, v112
	v_lshlrev_b64 v[108:109], 11, v[108:109]
	s_nop 0
	v_addc_co_u32_e32 v157, vcc, 0, v113, vcc
; __device__ __forceinline__ unsigned pk4_fp8(float a, float b, float c, float d) {
;     a = __builtin_fminf(__builtin_fmaxf(a, -448.f), 448.f); b = __builtin_fminf(__builtin_fmaxf(b, -448.f), 448.f); c = __builtin_fminf(__builtin_fmaxf(c, -448.f), 448.f); d = __builtin_fminf(__builtin_fmaxf(d, -448.f), 448.f);
;     int w = 0; w = __builtin_amdgcn_cvt_pk_fp8_f32(a, b, w, false); w = __builtin_amdgcn_cvt_pk_fp8_f32(c, d, w, true); return (unsigned)w;
; __device__ __forceinline__ void cv_load(const float* W, int N, int nblk, int item, int lane, f32x4 (&tv)[16]) {
;     const int kb = item / nblk, nb = item - kb * nblk; const float* p = W + (size_t)(64 * kb + 16 * (lane >> 4)) * N + 64 * nb + 4 * (lane & 15);
; #pragma unroll
;     for (int i = 0; i < 16; ++i) tv[i] = __builtin_nontemporal_load((const f32x4*)(p + (size_t)i * N));
; }
; template <int MODE> __device__ __forceinline__ void cv_finish(const f32x4 (&tv)[16], int K, int nblk, unsigned char* WT, int item, int lane) {
;     const int kb = item / nblk, nb = item - kb * nblk, k0 = 64 * kb + 16 * (lane >> 4), n0 = 64 * nb + 4 * (lane & 15);
;     unsigned D[16];
; #pragma unroll
;     for (int i = 0; i < 16; ++i) { const f32x2 a = (f32x2){tv[i].x, tv[i].y} * (f32x2){1024.f, 1024.f}, b = (f32x2){tv[i].z, tv[i].w} * (f32x2){1024.f, 1024.f};
;         D[i] = pk4_fp8(a.x, a.y, b.x, b.y); }
	v_add_co_u32_e32 v160, vcc, s22, v112
	v_lshlrev_b64 v[110:111], 11, v[110:111]
	s_nop 0
	v_addc_co_u32_e32 v161, vcc, 0, v113, vcc
	v_add_co_u32_e32 v164, vcc, s23, v112
	global_load_dwordx4 v[102:105], v[112:113], off nt
	s_nop 0
	v_addc_co_u32_e32 v165, vcc, 0, v113, vcc
	v_lshl_add_u64 v[176:177], v[98:99], 0, v[106:107]
	v_lshl_add_u64 v[178:179], v[98:99], 0, v[108:109]
	v_lshl_add_u64 v[98:99], v[98:99], 0, v[110:111]
	global_load_dwordx4 v[106:109], v[114:115], off nt
	global_load_dwordx4 v[110:113], v[116:117], off nt
	s_nop 0
	global_load_dwordx4 v[114:117], v[118:119], off nt
	s_nop 0
	global_load_dwordx4 v[118:121], v[120:121], off nt
	s_nop 0
	global_load_dwordx4 v[122:125], v[122:123], off nt
	s_nop 0
	global_load_dwordx4 v[126:129], v[126:127], off nt
	s_nop 0
	global_load_dwordx4 v[132:135], v[132:133], off nt
	s_nop 0
	global_load_dwordx4 v[136:139], v[136:137], off nt
	s_nop 0
	global_load_dwordx4 v[140:143], v[140:141], off nt
	s_nop 0
	global_load_dwordx4 v[144:147], v[144:145], off nt
	s_nop 0
	global_load_dwordx4 v[148:151], v[148:149], off nt
	s_nop 0
	global_load_dwordx4 v[152:155], v[152:153], off nt
	s_nop 0
	global_load_dwordx4 v[156:159], v[156:157], off nt
	s_nop 0
	global_load_dwordx4 v[160:163], v[160:161], off nt
	s_nop 0
	global_load_dwordx4 v[164:167], v[164:165], off nt
	v_mov_b32_e32 v101, v67
	v_mov_b32_e32 v169, v67
	v_mov_b32_e32 v100, v67
	v_mov_b32_e32 v171, v67
	v_mov_b32_e32 v168, v67
	v_mov_b32_e32 v173, v67
	v_mov_b32_e32 v180, v67
	v_mov_b32_e32 v181, v67
	v_mov_b32_e32 v182, v67
	v_mov_b32_e32 v183, v67
	v_mov_b32_e32 v184, v67
	v_mov_b32_e32 v185, v67
	v_mov_b32_e32 v186, v67
	v_mov_b32_e32 v187, v67
	v_mov_b32_e32 v188, v67
	v_mov_b32_e32 v189, v67
	s_add_i32 s2, s2, 1
	s_add_i32 s40, s40, 64
	s_waitcnt vmcnt(31)
	v_pk_mul_f32 v[6:7], v[6:7], s[4:5] op_sel_hi:[1,0]
	s_nop 0
	v_med3_f32 v94, v6, s24, v72
	v_med3_f32 v95, v7, s24, v72
	s_waitcnt vmcnt(30)
	v_pk_mul_f32 v[6:7], v[10:11], s[4:5] op_sel_hi:[1,0]
	s_waitcnt vmcnt(29)
	v_pk_mul_f32 v[10:11], v[14:15], s[4:5] op_sel_hi:[1,0]
	s_waitcnt vmcnt(28)
	v_pk_mul_f32 v[14:15], v[18:19], s[4:5] op_sel_hi:[1,0]
	s_waitcnt vmcnt(27)
	v_pk_mul_f32 v[18:19], v[22:23], s[4:5] op_sel_hi:[1,0]
	s_waitcnt vmcnt(26)
	v_pk_mul_f32 v[22:23], v[26:27], s[4:5] op_sel_hi:[1,0]
	s_waitcnt vmcnt(25)
	v_pk_mul_f32 v[26:27], v[30:31], s[4:5] op_sel_hi:[1,0]
	s_waitcnt vmcnt(24)
	v_pk_mul_f32 v[30:31], v[34:35], s[4:5] op_sel_hi:[1,0]
	s_waitcnt vmcnt(23)
	v_pk_mul_f32 v[34:35], v[38:39], s[4:5] op_sel_hi:[1,0]
	s_waitcnt vmcnt(22)
	v_pk_mul_f32 v[38:39], v[42:43], s[4:5] op_sel_hi:[1,0]
	s_waitcnt vmcnt(21)
	v_pk_mul_f32 v[42:43], v[46:47], s[4:5] op_sel_hi:[1,0]
	s_waitcnt vmcnt(20)
	v_pk_mul_f32 v[46:47], v[50:51], s[4:5] op_sel_hi:[1,0]
	s_waitcnt vmcnt(19)
	v_pk_mul_f32 v[50:51], v[54:55], s[4:5] op_sel_hi:[1,0]
	s_waitcnt vmcnt(18)
	v_pk_mul_f32 v[54:55], v[58:59], s[4:5] op_sel_hi:[1,0]
	s_waitcnt vmcnt(17)
	v_pk_mul_f32 v[58:59], v[62:63], s[4:5] op_sel_hi:[1,0]
	s_waitcnt vmcnt(16)
	v_pk_mul_f32 v[62:63], v[68:69], s[4:5] op_sel_hi:[1,0]
	v_med3_f32 v6, v6, s24, v72
	v_med3_f32 v7, v7, s24, v72
	v_med3_f32 v10, v10, s24, v72
	v_med3_f32 v11, v11, s24, v72
	v_med3_f32 v14, v14, s24, v72
	v_med3_f32 v15, v15, s24, v72
	v_med3_f32 v18, v18, s24, v72
	v_med3_f32 v19, v19, s24, v72
	v_med3_f32 v22, v22, s24, v72
	v_med3_f32 v23, v23, s24, v72
	v_med3_f32 v26, v26, s24, v72
	v_med3_f32 v27, v27, s24, v72
	v_med3_f32 v30, v30, s24, v72
	v_med3_f32 v31, v31, s24, v72
	v_med3_f32 v34, v34, s24, v72
	v_med3_f32 v35, v35, s24, v72
	v_med3_f32 v38, v38, s24, v72
	v_med3_f32 v39, v39, s24, v72
	v_med3_f32 v42, v42, s24, v72
	v_med3_f32 v43, v43, s24, v72
	v_med3_f32 v46, v46, s24, v72
	v_med3_f32 v47, v47, s24, v72
	v_med3_f32 v50, v50, s24, v72
	v_med3_f32 v51, v51, s24, v72
	v_med3_f32 v54, v54, s24, v72
	v_med3_f32 v55, v55, s24, v72
	v_med3_f32 v58, v58, s24, v72
	v_med3_f32 v59, v59, s24, v72
	v_med3_f32 v62, v62, s24, v72
	v_med3_f32 v63, v63, s24, v72
	v_cvt_pk_fp8_f32 v5, v94, v95
	v_cvt_pk_fp8_f32 v73, v6, v7
	v_cvt_pk_fp8_f32 v80, v10, v11
	v_cvt_pk_fp8_f32 v81, v14, v15
	v_cvt_pk_fp8_f32 v82, v18, v19
	v_cvt_pk_fp8_f32 v83, v22, v23
	v_cvt_pk_fp8_f32 v84, v26, v27
	v_cvt_pk_fp8_f32 v85, v30, v31
	v_cvt_pk_fp8_f32 v86, v34, v35
	v_cvt_pk_fp8_f32 v87, v38, v39
	v_cvt_pk_fp8_f32 v88, v42, v43
	v_cvt_pk_fp8_f32 v89, v46, v47
	v_cvt_pk_fp8_f32 v90, v50, v51
	v_cvt_pk_fp8_f32 v91, v54, v55
	v_cvt_pk_fp8_f32 v92, v58, v59
	v_cvt_pk_fp8_f32 v93, v62, v63
	v_pk_mul_f32 v[8:9], v[8:9], s[4:5] op_sel_hi:[1,0]
	s_nop 0
	v_med3_f32 v96, v8, s24, v72
	v_med3_f32 v97, v9, s24, v72
	v_pk_mul_f32 v[8:9], v[12:13], s[4:5] op_sel_hi:[1,0]
	v_pk_mul_f32 v[12:13], v[16:17], s[4:5] op_sel_hi:[1,0]
	v_pk_mul_f32 v[16:17], v[20:21], s[4:5] op_sel_hi:[1,0]
	v_pk_mul_f32 v[20:21], v[24:25], s[4:5] op_sel_hi:[1,0]
	v_pk_mul_f32 v[24:25], v[28:29], s[4:5] op_sel_hi:[1,0]
	v_pk_mul_f32 v[28:29], v[32:33], s[4:5] op_sel_hi:[1,0]
	v_pk_mul_f32 v[32:33], v[36:37], s[4:5] op_sel_hi:[1,0]
	v_pk_mul_f32 v[36:37], v[40:41], s[4:5] op_sel_hi:[1,0]
	v_pk_mul_f32 v[40:41], v[44:45], s[4:5] op_sel_hi:[1,0]
	v_pk_mul_f32 v[44:45], v[48:49], s[4:5] op_sel_hi:[1,0]
	v_pk_mul_f32 v[48:49], v[52:53], s[4:5] op_sel_hi:[1,0]
	v_pk_mul_f32 v[52:53], v[56:57], s[4:5] op_sel_hi:[1,0]
	v_pk_mul_f32 v[56:57], v[60:61], s[4:5] op_sel_hi:[1,0]
	v_pk_mul_f32 v[60:61], v[64:65], s[4:5] op_sel_hi:[1,0]
	v_pk_mul_f32 v[64:65], v[70:71], s[4:5] op_sel_hi:[1,0]
	v_med3_f32 v8, v8, s24, v72
	v_med3_f32 v9, v9, s24, v72
	v_med3_f32 v12, v12, s24, v72
	v_med3_f32 v13, v13, s24, v72
	v_med3_f32 v16, v16, s24, v72
; __device__ __forceinline__ void cv_load(const float* W, int N, int nblk, int item, int lane, f32x4 (&tv)[16]) {
;     const int kb = item / nblk, nb = item - kb * nblk; const float* p = W + (size_t)(64 * kb + 16 * (lane >> 4)) * N + 64 * nb + 4 * (lane & 15);
; #pragma unroll
;     for (int i = 0; i < 16; ++i) tv[i] = __builtin_nontemporal_load((const f32x4*)(p + (size_t)i * N));
; }
; template <int MODE> __device__ __forceinline__ void cv_finish(const f32x4 (&tv)[16], int K, int nblk, unsigned char* WT, int item, int lane) {
;     const int kb = item / nblk, nb = item - kb * nblk, k0 = 64 * kb + 16 * (lane >> 4), n0 = 64 * nb + 4 * (lane & 15);
;     unsigned D[16];
; #pragma unroll
;     for (int i = 0; i < 16; ++i) { const f32x2 a = (f32x2){tv[i].x, tv[i].y} * (f32x2){1024.f, 1024.f}, b = (f32x2){tv[i].z, tv[i].w} * (f32x2){1024.f, 1024.f};
;         D[i] = pk4_fp8(a.x, a.y, b.x, b.y); }
;     unsigned O[4][4];
; #pragma unroll
;     for (int q = 0; q < 4; ++q) { const unsigned a = D[4 * q], b = D[4 * q + 1], c = D[4 * q + 2], d = D[4 * q + 3];
;         const unsigned t0 = __builtin_amdgcn_perm(b, a, 0x05010400u), t1 = __builtin_amdgcn_perm(b, a, 0x07030602u), u0 = __builtin_amdgcn_perm(d, c, 0x05010400u), u1 = __builtin_amdgcn_perm(d, c, 0x07030602u);
;         O[0][q] = __builtin_amdgcn_perm(u0, t0, 0x05040100u); O[1][q] = __builtin_amdgcn_perm(u0, t0, 0x07060302u); O[2][q] = __builtin_amdgcn_perm(u1, t1, 0x05040100u); O[3][q] = __builtin_amdgcn_perm(u1, t1, 0x07060302u); }
; #pragma unroll
;     for (int j = 0; j < 4; ++j) { u32x4 o; o.x = O[j][0]; o.y = O[j][1]; o.z = O[j][2]; o.w = O[j][3];
;         __builtin_nontemporal_store(o, (u32x4*)(WT + (size_t)drow<MODE>(n0 + j) * K + k0)); }
; }
	v_med3_f32 v17, v17, s24, v72
	v_med3_f32 v20, v20, s24, v72
	v_med3_f32 v21, v21, s24, v72
	v_med3_f32 v24, v24, s24, v72
	v_med3_f32 v25, v25, s24, v72
	v_med3_f32 v28, v28, s24, v72
	v_med3_f32 v29, v29, s24, v72
	v_med3_f32 v32, v32, s24, v72
	v_med3_f32 v33, v33, s24, v72
	v_med3_f32 v36, v36, s24, v72
	v_med3_f32 v37, v37, s24, v72
	v_med3_f32 v40, v40, s24, v72
	v_med3_f32 v41, v41, s24, v72
	v_med3_f32 v44, v44, s24, v72
	v_med3_f32 v45, v45, s24, v72
	v_med3_f32 v48, v48, s24, v72
	v_med3_f32 v49, v49, s24, v72
	v_med3_f32 v52, v52, s24, v72
	v_med3_f32 v53, v53, s24, v72
	v_med3_f32 v56, v56, s24, v72
	v_med3_f32 v57, v57, s24, v72
	v_med3_f32 v60, v60, s24, v72
	v_med3_f32 v61, v61, s24, v72
	v_med3_f32 v64, v64, s24, v72
	v_med3_f32 v65, v65, s24, v72
	v_cvt_pk_fp8_f32 v5, v96, v97 op_sel:[0,0,1]
	v_cvt_pk_fp8_f32 v73, v8, v9 op_sel:[0,0,1]
	v_cvt_pk_fp8_f32 v80, v12, v13 op_sel:[0,0,1]
	v_cvt_pk_fp8_f32 v81, v16, v17 op_sel:[0,0,1]
	v_cvt_pk_fp8_f32 v82, v20, v21 op_sel:[0,0,1]
	v_cvt_pk_fp8_f32 v83, v24, v25 op_sel:[0,0,1]
	v_cvt_pk_fp8_f32 v84, v28, v29 op_sel:[0,0,1]
	v_cvt_pk_fp8_f32 v85, v32, v33 op_sel:[0,0,1]
	v_cvt_pk_fp8_f32 v86, v36, v37 op_sel:[0,0,1]
	v_cvt_pk_fp8_f32 v87, v40, v41 op_sel:[0,0,1]
	v_cvt_pk_fp8_f32 v88, v44, v45 op_sel:[0,0,1]
	v_cvt_pk_fp8_f32 v89, v48, v49 op_sel:[0,0,1]
	v_cvt_pk_fp8_f32 v90, v52, v53 op_sel:[0,0,1]
	v_cvt_pk_fp8_f32 v91, v56, v57 op_sel:[0,0,1]
	v_cvt_pk_fp8_f32 v92, v60, v61 op_sel:[0,0,1]
	v_cvt_pk_fp8_f32 v93, v64, v65 op_sel:[0,0,1]
	v_perm_b32 v7, v73, v5, s25
	v_perm_b32 v5, v73, v5, s26
	v_perm_b32 v8, v81, v80, s25
	v_perm_b32 v9, v81, v80, s26
	v_perm_b32 v11, v83, v82, s25
	v_perm_b32 v13, v85, v84, s25
	v_perm_b32 v17, v87, v86, s25
	v_perm_b32 v21, v89, v88, s25
	v_perm_b32 v23, v91, v90, s25
	v_perm_b32 v25, v93, v92, s25
	v_perm_b32 v12, v83, v82, s26
	v_perm_b32 v16, v85, v84, s26
	v_perm_b32 v20, v87, v86, s26
	v_perm_b32 v22, v89, v88, s26
	v_perm_b32 v24, v91, v90, s26
	v_perm_b32 v26, v93, v92, s26
	v_perm_b32 v6, v8, v7, s27
	v_perm_b32 v10, v8, v7, s28
	v_perm_b32 v14, v9, v5, s27
	v_perm_b32 v18, v9, v5, s28
	v_perm_b32 v7, v13, v11, s27
	v_perm_b32 v8, v21, v17, s27
	v_perm_b32 v9, v25, v23, s27
	v_perm_b32 v11, v13, v11, s28
	v_perm_b32 v15, v16, v12, s27
	v_perm_b32 v19, v16, v12, s28
	v_perm_b32 v12, v21, v17, s28
	v_perm_b32 v16, v22, v20, s27
	v_perm_b32 v20, v22, v20, s28
	v_perm_b32 v13, v25, v23, s28
	v_perm_b32 v17, v26, v24, s27
	v_perm_b32 v21, v26, v24, s28
	global_store_dwordx4 v[74:75], v[6:9], off nt
	global_store_dwordx4 v[76:77], v[10:13], off nt
	global_store_dwordx4 v[78:79], v[14:17], off nt
	global_store_dwordx4 v[2:3], v[18:21], off nt
	s_lshr_b32 s41, s2, 5
	s_lshl_b32 s42, s41, 11
	v_mov_b32_e32 v3, v67
	v_lshl_or_b32 v2, s41, 6, v1
	s_sub_i32 s41, s39, s42
	v_subrev_u32_e32 v8, s42, v4
	v_lshlrev_b64 v[6:7], 13, v[2:3]
	s_add_i32 s42, s40, s41
	v_lshl_add_u64 v[6:7], s[6:7], 0, v[6:7]
	s_ashr_i32 s43, s42, 31
	v_lshl_add_u64 v[6:7], s[42:43], 2, v[6:7]
	v_lshl_add_u64 v[16:17], v[6:7], 0, v[66:67]
	v_add_co_u32_e32 v18, vcc, s0, v16
	v_add_u32_e32 v8, s40, v8
	s_nop 0
	v_addc_co_u32_e32 v19, vcc, 0, v17, vcc
	v_add_co_u32_e32 v20, vcc, s1, v16
	v_ashrrev_i32_e32 v9, 31, v8
	s_nop 0
	v_addc_co_u32_e32 v21, vcc, 0, v17, vcc
	v_add_co_u32_e32 v22, vcc, s5, v16
	v_add_u32_e32 v10, 1, v8
	s_nop 0
	v_addc_co_u32_e32 v23, vcc, 0, v17, vcc
	v_add_co_u32_e32 v24, vcc, s12, v16
	v_add_u32_e32 v12, 2, v8
	s_nop 0
	v_addc_co_u32_e32 v25, vcc, 0, v17, vcc
	v_add_co_u32_e32 v26, vcc, s13, v16
	v_add_u32_e32 v14, 3, v8
	s_nop 0
	v_addc_co_u32_e32 v27, vcc, 0, v17, vcc
	v_add_co_u32_e32 v30, vcc, s14, v16
	v_lshl_add_u64 v[2:3], s[8:9], 0, v[2:3]
	s_nop 0
	v_addc_co_u32_e32 v31, vcc, 0, v17, vcc
	v_add_co_u32_e32 v34, vcc, s15, v16
	v_lshlrev_b64 v[8:9], 11, v[8:9]
	s_nop 0
	v_addc_co_u32_e32 v35, vcc, 0, v17, vcc
	v_add_co_u32_e32 v38, vcc, s16, v16
	v_ashrrev_i32_e32 v11, 31, v10
	s_nop 0
	v_addc_co_u32_e32 v39, vcc, 0, v17, vcc
	v_add_co_u32_e32 v42, vcc, s17, v16
	v_ashrrev_i32_e32 v13, 31, v12
	s_nop 0
	v_addc_co_u32_e32 v43, vcc, 0, v17, vcc
	v_add_co_u32_e32 v46, vcc, s18, v16
	v_ashrrev_i32_e32 v15, 31, v14
	s_nop 0
	v_addc_co_u32_e32 v47, vcc, 0, v17, vcc
	v_add_co_u32_e32 v50, vcc, s19, v16
	v_lshl_add_u64 v[74:75], v[2:3], 0, v[8:9]
	s_nop 0
	v_addc_co_u32_e32 v51, vcc, 0, v17, vcc
	v_add_co_u32_e32 v54, vcc, s20, v16
	v_lshlrev_b64 v[10:11], 11, v[10:11]
	s_nop 0
	v_addc_co_u32_e32 v55, vcc, 0, v17, vcc
	v_add_co_u32_e32 v58, vcc, s21, v16
	v_lshlrev_b64 v[12:13], 11, v[12:13]
	s_nop 0
	v_addc_co_u32_e32 v59, vcc, 0, v17, vcc
	v_add_co_u32_e32 v62, vcc, s22, v16
	v_lshlrev_b64 v[14:15], 11, v[14:15]
	s_nop 0
	v_addc_co_u32_e32 v63, vcc, 0, v17, vcc
	v_add_co_u32_e32 v68, vcc, s23, v16
	global_load_dwordx4 v[6:9], v[16:17], off nt
	s_nop 0
	v_addc_co_u32_e32 v69, vcc, 0, v17, vcc
	v_lshl_add_u64 v[76:77], v[2:3], 0, v[10:11]
	v_lshl_add_u64 v[78:79], v[2:3], 0, v[12:13]
	v_lshl_add_u64 v[2:3], v[2:3], 0, v[14:15]
	global_load_dwordx4 v[10:13], v[18:19], off nt
	global_load_dwordx4 v[14:17], v[20:21], off nt
	s_nop 0
	global_load_dwordx4 v[18:21], v[22:23], off nt
	s_nop 0
	global_load_dwordx4 v[22:25], v[24:25], off nt
	s_nop 0
	global_load_dwordx4 v[26:29], v[26:27], off nt
	s_nop 0
	global_load_dwordx4 v[30:33], v[30:31], off nt
	s_nop 0
	global_load_dwordx4 v[34:37], v[34:35], off nt
	s_nop 0
	global_load_dwordx4 v[38:41], v[38:39], off nt
	s_nop 0
	global_load_dwordx4 v[42:45], v[42:43], off nt
	s_nop 0
	global_load_dwordx4 v[46:49], v[46:47], off nt
	s_nop 0
	global_load_dwordx4 v[50:53], v[50:51], off nt
	s_nop 0
	global_load_dwordx4 v[54:57], v[54:55], off nt
	s_nop 0
	global_load_dwordx4 v[58:61], v[58:59], off nt
	s_nop 0
	global_load_dwordx4 v[62:65], v[62:63], off nt
	s_nop 0
	global_load_dwordx4 v[68:71], v[68:69], off nt
	v_mov_b32_e32 v5, v67
	v_mov_b32_e32 v73, v67
	v_mov_b32_e32 v80, v67
	v_mov_b32_e32 v81, v67
	v_mov_b32_e32 v82, v67
	v_mov_b32_e32 v83, v67
	v_mov_b32_e32 v84, v67
	v_mov_b32_e32 v85, v67
	v_mov_b32_e32 v86, v67
	v_mov_b32_e32 v87, v67
	v_mov_b32_e32 v88, v67
	v_mov_b32_e32 v89, v67
	v_mov_b32_e32 v90, v67
	v_mov_b32_e32 v91, v67
	v_mov_b32_e32 v92, v67
	v_mov_b32_e32 v93, v67
	s_add_i32 s2, s2, 1
	s_add_i32 s40, s40, 64
	s_waitcnt vmcnt(35)
; __device__ __forceinline__ unsigned pk4_fp8(float a, float b, float c, float d) {
;     a = __builtin_fminf(__builtin_fmaxf(a, -448.f), 448.f); b = __builtin_fminf(__builtin_fmaxf(b, -448.f), 448.f); c = __builtin_fminf(__builtin_fmaxf(c, -448.f), 448.f); d = __builtin_fminf(__builtin_fmaxf(d, -448.f), 448.f);
;     int w = 0; w = __builtin_amdgcn_cvt_pk_fp8_f32(a, b, w, false); w = __builtin_amdgcn_cvt_pk_fp8_f32(c, d, w, true); return (unsigned)w;
; template <int MODE> __device__ __forceinline__ void cv_finish(const f32x4 (&tv)[16], int K, int nblk, unsigned char* WT, int item, int lane) {
;     const int kb = item / nblk, nb = item - kb * nblk, k0 = 64 * kb + 16 * (lane >> 4), n0 = 64 * nb + 4 * (lane & 15);
;     unsigned D[16];
; #pragma unroll
;     for (int i = 0; i < 16; ++i) { const f32x2 a = (f32x2){tv[i].x, tv[i].y} * (f32x2){1024.f, 1024.f}, b = (f32x2){tv[i].z, tv[i].w} * (f32x2){1024.f, 1024.f};
;         D[i] = pk4_fp8(a.x, a.y, b.x, b.y); }
	v_pk_mul_f32 v[102:103], v[102:103], s[4:5] op_sel_hi:[1,0]
	s_nop 0
	v_med3_f32 v190, v102, s24, v72
	v_med3_f32 v191, v103, s24, v72
	s_waitcnt vmcnt(34)
	v_pk_mul_f32 v[102:103], v[106:107], s[4:5] op_sel_hi:[1,0]
	s_waitcnt vmcnt(33)
	v_pk_mul_f32 v[106:107], v[110:111], s[4:5] op_sel_hi:[1,0]
	s_waitcnt vmcnt(32)
	v_pk_mul_f32 v[110:111], v[114:115], s[4:5] op_sel_hi:[1,0]
	s_waitcnt vmcnt(31)
	v_pk_mul_f32 v[114:115], v[118:119], s[4:5] op_sel_hi:[1,0]
	s_waitcnt vmcnt(30)
	v_pk_mul_f32 v[118:119], v[122:123], s[4:5] op_sel_hi:[1,0]
	s_waitcnt vmcnt(29)
	v_pk_mul_f32 v[122:123], v[126:127], s[4:5] op_sel_hi:[1,0]
	s_waitcnt vmcnt(28)
	v_pk_mul_f32 v[126:127], v[132:133], s[4:5] op_sel_hi:[1,0]
	s_waitcnt vmcnt(27)
	v_pk_mul_f32 v[132:133], v[136:137], s[4:5] op_sel_hi:[1,0]
	s_waitcnt vmcnt(26)
	v_pk_mul_f32 v[136:137], v[140:141], s[4:5] op_sel_hi:[1,0]
	s_waitcnt vmcnt(25)
	v_pk_mul_f32 v[140:141], v[144:145], s[4:5] op_sel_hi:[1,0]
	s_waitcnt vmcnt(24)
	v_pk_mul_f32 v[144:145], v[148:149], s[4:5] op_sel_hi:[1,0]
	s_waitcnt vmcnt(23)
	v_pk_mul_f32 v[148:149], v[152:153], s[4:5] op_sel_hi:[1,0]
	s_waitcnt vmcnt(22)
	v_pk_mul_f32 v[152:153], v[156:157], s[4:5] op_sel_hi:[1,0]
	s_waitcnt vmcnt(21)
	v_pk_mul_f32 v[156:157], v[160:161], s[4:5] op_sel_hi:[1,0]
	s_waitcnt vmcnt(20)
	v_pk_mul_f32 v[160:161], v[164:165], s[4:5] op_sel_hi:[1,0]
	v_med3_f32 v102, v102, s24, v72
	v_med3_f32 v103, v103, s24, v72
	v_med3_f32 v106, v106, s24, v72
	v_med3_f32 v107, v107, s24, v72
	v_med3_f32 v110, v110, s24, v72
	v_med3_f32 v111, v111, s24, v72
	v_med3_f32 v114, v114, s24, v72
	v_med3_f32 v115, v115, s24, v72
	v_med3_f32 v118, v118, s24, v72
	v_med3_f32 v119, v119, s24, v72
	v_med3_f32 v122, v122, s24, v72
	v_med3_f32 v123, v123, s24, v72
	v_med3_f32 v126, v126, s24, v72
	v_med3_f32 v127, v127, s24, v72
	v_med3_f32 v132, v132, s24, v72
	v_med3_f32 v133, v133, s24, v72
	v_med3_f32 v136, v136, s24, v72
	v_med3_f32 v137, v137, s24, v72
	v_med3_f32 v140, v140, s24, v72
	v_med3_f32 v141, v141, s24, v72
	v_med3_f32 v144, v144, s24, v72
	v_med3_f32 v145, v145, s24, v72
	v_med3_f32 v148, v148, s24, v72
	v_med3_f32 v149, v149, s24, v72
	v_med3_f32 v152, v152, s24, v72
	v_med3_f32 v153, v153, s24, v72
	v_med3_f32 v156, v156, s24, v72
	v_med3_f32 v157, v157, s24, v72
	v_med3_f32 v160, v160, s24, v72
	v_med3_f32 v161, v161, s24, v72
	v_cvt_pk_fp8_f32 v101, v190, v191
	v_cvt_pk_fp8_f32 v169, v102, v103
	v_cvt_pk_fp8_f32 v100, v106, v107
	v_cvt_pk_fp8_f32 v171, v110, v111
	v_cvt_pk_fp8_f32 v168, v114, v115
	v_cvt_pk_fp8_f32 v173, v118, v119
	v_cvt_pk_fp8_f32 v180, v122, v123
	v_cvt_pk_fp8_f32 v181, v126, v127
	v_cvt_pk_fp8_f32 v182, v132, v133
	v_cvt_pk_fp8_f32 v183, v136, v137
	v_cvt_pk_fp8_f32 v184, v140, v141
	v_cvt_pk_fp8_f32 v185, v144, v145
	v_cvt_pk_fp8_f32 v186, v148, v149
	v_cvt_pk_fp8_f32 v187, v152, v153
	v_cvt_pk_fp8_f32 v188, v156, v157
	v_cvt_pk_fp8_f32 v189, v160, v161
	v_pk_mul_f32 v[104:105], v[104:105], s[4:5] op_sel_hi:[1,0]
	s_nop 0
	v_med3_f32 v192, v104, s24, v72
	v_med3_f32 v193, v105, s24, v72
	v_pk_mul_f32 v[104:105], v[108:109], s[4:5] op_sel_hi:[1,0]
	v_pk_mul_f32 v[108:109], v[112:113], s[4:5] op_sel_hi:[1,0]
	v_pk_mul_f32 v[112:113], v[116:117], s[4:5] op_sel_hi:[1,0]
	v_pk_mul_f32 v[116:117], v[120:121], s[4:5] op_sel_hi:[1,0]
	v_pk_mul_f32 v[120:121], v[124:125], s[4:5] op_sel_hi:[1,0]
	v_pk_mul_f32 v[124:125], v[128:129], s[4:5] op_sel_hi:[1,0]
	v_pk_mul_f32 v[128:129], v[134:135], s[4:5] op_sel_hi:[1,0]
	v_pk_mul_f32 v[134:135], v[138:139], s[4:5] op_sel_hi:[1,0]
	v_pk_mul_f32 v[138:139], v[142:143], s[4:5] op_sel_hi:[1,0]
	v_pk_mul_f32 v[142:143], v[146:147], s[4:5] op_sel_hi:[1,0]
	v_pk_mul_f32 v[146:147], v[150:151], s[4:5] op_sel_hi:[1,0]
	v_pk_mul_f32 v[150:151], v[154:155], s[4:5] op_sel_hi:[1,0]
	v_pk_mul_f32 v[154:155], v[158:159], s[4:5] op_sel_hi:[1,0]
	v_pk_mul_f32 v[158:159], v[162:163], s[4:5] op_sel_hi:[1,0]
	v_pk_mul_f32 v[162:163], v[166:167], s[4:5] op_sel_hi:[1,0]
	v_med3_f32 v104, v104, s24, v72
	v_med3_f32 v105, v105, s24, v72
	v_med3_f32 v108, v108, s24, v72
	v_med3_f32 v109, v109, s24, v72
	v_med3_f32 v112, v112, s24, v72
	v_med3_f32 v113, v113, s24, v72
	v_med3_f32 v116, v116, s24, v72
	v_med3_f32 v117, v117, s24, v72
	v_med3_f32 v120, v120, s24, v72
	v_med3_f32 v121, v121, s24, v72
	v_med3_f32 v124, v124, s24, v72
	v_med3_f32 v125, v125, s24, v72
	v_med3_f32 v128, v128, s24, v72
	v_med3_f32 v129, v129, s24, v72
	v_med3_f32 v134, v134, s24, v72
	v_med3_f32 v135, v135, s24, v72
	v_med3_f32 v138, v138, s24, v72
	v_med3_f32 v139, v139, s24, v72
	v_med3_f32 v142, v142, s24, v72
	v_med3_f32 v143, v143, s24, v72
	v_med3_f32 v146, v146, s24, v72
	v_med3_f32 v147, v147, s24, v72
	v_med3_f32 v150, v150, s24, v72
	v_med3_f32 v151, v151, s24, v72
	v_med3_f32 v154, v154, s24, v72
	v_med3_f32 v155, v155, s24, v72
	v_med3_f32 v158, v158, s24, v72
	v_med3_f32 v159, v159, s24, v72
	v_med3_f32 v162, v162, s24, v72
	v_med3_f32 v163, v163, s24, v72
	v_cvt_pk_fp8_f32 v101, v192, v193 op_sel:[0,0,1]
	v_cvt_pk_fp8_f32 v169, v104, v105 op_sel:[0,0,1]
	v_cvt_pk_fp8_f32 v100, v108, v109 op_sel:[0,0,1]
	v_cvt_pk_fp8_f32 v171, v112, v113 op_sel:[0,0,1]
	v_cvt_pk_fp8_f32 v168, v116, v117 op_sel:[0,0,1]
	v_cvt_pk_fp8_f32 v173, v120, v121 op_sel:[0,0,1]
	v_cvt_pk_fp8_f32 v180, v124, v125 op_sel:[0,0,1]
	v_cvt_pk_fp8_f32 v181, v128, v129 op_sel:[0,0,1]
	v_cvt_pk_fp8_f32 v182, v134, v135 op_sel:[0,0,1]
	v_cvt_pk_fp8_f32 v183, v138, v139 op_sel:[0,0,1]
	v_cvt_pk_fp8_f32 v184, v142, v143 op_sel:[0,0,1]
	v_cvt_pk_fp8_f32 v185, v146, v147 op_sel:[0,0,1]
	v_cvt_pk_fp8_f32 v186, v150, v151 op_sel:[0,0,1]
	v_cvt_pk_fp8_f32 v187, v154, v155 op_sel:[0,0,1]
; __device__ __forceinline__ void cv_load(const float* W, int N, int nblk, int item, int lane, f32x4 (&tv)[16]) {
;     const int kb = item / nblk, nb = item - kb * nblk; const float* p = W + (size_t)(64 * kb + 16 * (lane >> 4)) * N + 64 * nb + 4 * (lane & 15);
; #pragma unroll
;     for (int i = 0; i < 16; ++i) tv[i] = __builtin_nontemporal_load((const f32x4*)(p + (size_t)i * N));
; }
; template <int MODE> __device__ __forceinline__ void cv_finish(const f32x4 (&tv)[16], int K, int nblk, unsigned char* WT, int item, int lane) {
;     ...
;     unsigned O[4][4];
; #pragma unroll
;     for (int q = 0; q < 4; ++q) { const unsigned a = D[4 * q], b = D[4 * q + 1], c = D[4 * q + 2], d = D[4 * q + 3];
;         const unsigned t0 = __builtin_amdgcn_perm(b, a, 0x05010400u), t1 = __builtin_amdgcn_perm(b, a, 0x07030602u), u0 = __builtin_amdgcn_perm(d, c, 0x05010400u), u1 = __builtin_amdgcn_perm(d, c, 0x07030602u);
;         O[0][q] = __builtin_amdgcn_perm(u0, t0, 0x05040100u); O[1][q] = __builtin_amdgcn_perm(u0, t0, 0x07060302u); O[2][q] = __builtin_amdgcn_perm(u1, t1, 0x05040100u); O[3][q] = __builtin_amdgcn_perm(u1, t1, 0x07060302u); }
; #pragma unroll
;     for (int j = 0; j < 4; ++j) { u32x4 o; o.x = O[j][0]; o.y = O[j][1]; o.z = O[j][2]; o.w = O[j][3];
;         __builtin_nontemporal_store(o, (u32x4*)(WT + (size_t)drow<MODE>(n0 + j) * K + k0)); }
; }
	v_cvt_pk_fp8_f32 v188, v158, v159 op_sel:[0,0,1]
	v_cvt_pk_fp8_f32 v189, v162, v163 op_sel:[0,0,1]
	v_perm_b32 v103, v169, v101, s25
	v_perm_b32 v101, v169, v101, s26
	v_perm_b32 v104, v171, v100, s25
	v_perm_b32 v105, v171, v100, s26
	v_perm_b32 v107, v173, v168, s25
	v_perm_b32 v109, v181, v180, s25
	v_perm_b32 v113, v183, v182, s25
	v_perm_b32 v117, v185, v184, s25
	v_perm_b32 v119, v187, v186, s25
	v_perm_b32 v121, v189, v188, s25
	v_perm_b32 v108, v173, v168, s26
	v_perm_b32 v112, v181, v180, s26
	v_perm_b32 v116, v183, v182, s26
	v_perm_b32 v118, v185, v184, s26
	v_perm_b32 v120, v187, v186, s26
	v_perm_b32 v122, v189, v188, s26
	v_perm_b32 v102, v104, v103, s27
	v_perm_b32 v106, v104, v103, s28
	v_perm_b32 v110, v105, v101, s27
	v_perm_b32 v114, v105, v101, s28
	v_perm_b32 v103, v109, v107, s27
	v_perm_b32 v104, v117, v113, s27
	v_perm_b32 v105, v121, v119, s27
	v_perm_b32 v107, v109, v107, s28
	v_perm_b32 v111, v112, v108, s27
	v_perm_b32 v115, v112, v108, s28
	v_perm_b32 v108, v117, v113, s28
	v_perm_b32 v112, v118, v116, s27
	v_perm_b32 v116, v118, v116, s28
	v_perm_b32 v109, v121, v119, s28
	v_perm_b32 v113, v122, v120, s27
	v_perm_b32 v117, v122, v120, s28
	global_store_dwordx4 v[174:175], v[102:105], off nt
	global_store_dwordx4 v[176:177], v[106:109], off nt
	global_store_dwordx4 v[178:179], v[110:113], off nt
	global_store_dwordx4 v[98:99], v[114:117], off nt
	s_lshr_b32 s41, s2, 5
	s_lshl_b32 s42, s41, 11
	v_mov_b32_e32 v99, v67
	v_lshl_or_b32 v98, s41, 6, v1
	s_sub_i32 s41, s39, s42
	v_subrev_u32_e32 v104, s42, v4
	v_lshlrev_b64 v[102:103], 13, v[98:99]
	s_add_i32 s42, s40, s41
	v_lshl_add_u64 v[102:103], s[6:7], 0, v[102:103]
	s_ashr_i32 s43, s42, 31
	v_lshl_add_u64 v[102:103], s[42:43], 2, v[102:103]
	v_lshl_add_u64 v[112:113], v[102:103], 0, v[66:67]
	v_add_co_u32_e32 v114, vcc, s0, v112
	v_add_u32_e32 v104, s40, v104
	s_nop 0
	v_addc_co_u32_e32 v115, vcc, 0, v113, vcc
	v_add_co_u32_e32 v116, vcc, s1, v112
	v_ashrrev_i32_e32 v105, 31, v104
	s_nop 0
	v_addc_co_u32_e32 v117, vcc, 0, v113, vcc
	v_add_co_u32_e32 v118, vcc, s5, v112
	v_add_u32_e32 v106, 1, v104
	s_nop 0
	v_addc_co_u32_e32 v119, vcc, 0, v113, vcc
	v_add_co_u32_e32 v120, vcc, s12, v112
	v_add_u32_e32 v108, 2, v104
	s_nop 0
	v_addc_co_u32_e32 v121, vcc, 0, v113, vcc
	v_add_co_u32_e32 v122, vcc, s13, v112
	v_add_u32_e32 v110, 3, v104
	s_nop 0
	v_addc_co_u32_e32 v123, vcc, 0, v113, vcc
	v_add_co_u32_e32 v126, vcc, s14, v112
	v_lshl_add_u64 v[98:99], s[8:9], 0, v[98:99]
	s_nop 0
	v_addc_co_u32_e32 v127, vcc, 0, v113, vcc
	v_add_co_u32_e32 v132, vcc, s15, v112
	v_lshlrev_b64 v[104:105], 11, v[104:105]
	s_nop 0
	v_addc_co_u32_e32 v133, vcc, 0, v113, vcc
	v_add_co_u32_e32 v136, vcc, s16, v112
	v_ashrrev_i32_e32 v107, 31, v106
	s_nop 0
	v_addc_co_u32_e32 v137, vcc, 0, v113, vcc
	v_add_co_u32_e32 v140, vcc, s17, v112
	v_ashrrev_i32_e32 v109, 31, v108
	s_nop 0
	v_addc_co_u32_e32 v141, vcc, 0, v113, vcc
	v_add_co_u32_e32 v144, vcc, s18, v112
	v_ashrrev_i32_e32 v111, 31, v110
	s_nop 0
	v_addc_co_u32_e32 v145, vcc, 0, v113, vcc
	v_add_co_u32_e32 v148, vcc, s19, v112
	v_lshl_add_u64 v[174:175], v[98:99], 0, v[104:105]
	s_nop 0
	v_addc_co_u32_e32 v149, vcc, 0, v113, vcc
	v_add_co_u32_e32 v152, vcc, s20, v112
	v_lshlrev_b64 v[106:107], 11, v[106:107]
	s_nop 0
	v_addc_co_u32_e32 v153, vcc, 0, v113, vcc
	v_add_co_u32_e32 v156, vcc, s21, v112
	v_lshlrev_b64 v[108:109], 11, v[108:109]
	s_nop 0
	v_addc_co_u32_e32 v157, vcc, 0, v113, vcc
	v_add_co_u32_e32 v160, vcc, s22, v112
	v_lshlrev_b64 v[110:111], 11, v[110:111]
	s_nop 0
	v_addc_co_u32_e32 v161, vcc, 0, v113, vcc
	v_add_co_u32_e32 v164, vcc, s23, v112
	global_load_dwordx4 v[102:105], v[112:113], off nt
	s_nop 0
	v_addc_co_u32_e32 v165, vcc, 0, v113, vcc
	v_lshl_add_u64 v[176:177], v[98:99], 0, v[106:107]
	v_lshl_add_u64 v[178:179], v[98:99], 0, v[108:109]
	v_lshl_add_u64 v[98:99], v[98:99], 0, v[110:111]
	global_load_dwordx4 v[106:109], v[114:115], off nt
	global_load_dwordx4 v[110:113], v[116:117], off nt
	s_nop 0
	global_load_dwordx4 v[114:117], v[118:119], off nt
	s_nop 0
	global_load_dwordx4 v[118:121], v[120:121], off nt
	s_nop 0
	global_load_dwordx4 v[122:125], v[122:123], off nt
	s_nop 0
	global_load_dwordx4 v[126:129], v[126:127], off nt
	s_nop 0
	global_load_dwordx4 v[132:135], v[132:133], off nt
	s_nop 0
	global_load_dwordx4 v[136:139], v[136:137], off nt
	s_nop 0
	global_load_dwordx4 v[140:143], v[140:141], off nt
	s_nop 0
	global_load_dwordx4 v[144:147], v[144:145], off nt
	s_nop 0
	global_load_dwordx4 v[148:151], v[148:149], off nt
	s_nop 0
	global_load_dwordx4 v[152:155], v[152:153], off nt
	s_nop 0
	global_load_dwordx4 v[156:159], v[156:157], off nt
	s_nop 0
	global_load_dwordx4 v[160:163], v[160:161], off nt
	s_nop 0
	global_load_dwordx4 v[164:167], v[164:165], off nt
	v_mov_b32_e32 v101, v67
	v_mov_b32_e32 v169, v67
	v_mov_b32_e32 v100, v67
	v_mov_b32_e32 v171, v67
	v_mov_b32_e32 v168, v67
	v_mov_b32_e32 v173, v67
	v_mov_b32_e32 v180, v67
	v_mov_b32_e32 v181, v67
	v_mov_b32_e32 v182, v67
	v_mov_b32_e32 v183, v67
	v_mov_b32_e32 v184, v67
	v_mov_b32_e32 v185, v67
	v_mov_b32_e32 v186, v67
	v_mov_b32_e32 v187, v67
	v_mov_b32_e32 v188, v67
	v_mov_b32_e32 v189, v67
	s_add_i32 s2, s2, 1
	s_add_i32 s40, s40, 64
	s_cmpk_eq_i32 s40, 0x100
	s_waitcnt vmcnt(35)
	v_pk_mul_f32 v[6:7], v[6:7], s[4:5] op_sel_hi:[1,0]
	s_nop 0
	v_med3_f32 v94, v6, s24, v72
	v_med3_f32 v95, v7, s24, v72
	s_waitcnt vmcnt(34)
	v_pk_mul_f32 v[6:7], v[10:11], s[4:5] op_sel_hi:[1,0]
	s_waitcnt vmcnt(33)
	v_pk_mul_f32 v[10:11], v[14:15], s[4:5] op_sel_hi:[1,0]
	s_waitcnt vmcnt(32)
	v_pk_mul_f32 v[14:15], v[18:19], s[4:5] op_sel_hi:[1,0]
	s_waitcnt vmcnt(31)
; __device__ __forceinline__ unsigned pk4_fp8(float a, float b, float c, float d) {
;     a = __builtin_fminf(__builtin_fmaxf(a, -448.f), 448.f); b = __builtin_fminf(__builtin_fmaxf(b, -448.f), 448.f); c = __builtin_fminf(__builtin_fmaxf(c, -448.f), 448.f); d = __builtin_fminf(__builtin_fmaxf(d, -448.f), 448.f);
;     int w = 0; w = __builtin_amdgcn_cvt_pk_fp8_f32(a, b, w, false); w = __builtin_amdgcn_cvt_pk_fp8_f32(c, d, w, true); return (unsigned)w;
; template <int MODE> __device__ __forceinline__ void cv_finish(const f32x4 (&tv)[16], int K, int nblk, unsigned char* WT, int item, int lane) {
;     const int kb = item / nblk, nb = item - kb * nblk, k0 = 64 * kb + 16 * (lane >> 4), n0 = 64 * nb + 4 * (lane & 15);
;     unsigned D[16];
; #pragma unroll
;     for (int i = 0; i < 16; ++i) { const f32x2 a = (f32x2){tv[i].x, tv[i].y} * (f32x2){1024.f, 1024.f}, b = (f32x2){tv[i].z, tv[i].w} * (f32x2){1024.f, 1024.f};
;         D[i] = pk4_fp8(a.x, a.y, b.x, b.y); }
;     unsigned O[4][4];
; #pragma unroll
;     for (int q = 0; q < 4; ++q) { const unsigned a = D[4 * q], b = D[4 * q + 1], c = D[4 * q + 2], d = D[4 * q + 3];
;         const unsigned t0 = __builtin_amdgcn_perm(b, a, 0x05010400u), t1 = __builtin_amdgcn_perm(b, a, 0x07030602u), u0 = __builtin_amdgcn_perm(d, c, 0x05010400u), u1 = __builtin_amdgcn_perm(d, c, 0x07030602u);
;         O[0][q] = __builtin_amdgcn_perm(u0, t0, 0x05040100u); O[1][q] = __builtin_amdgcn_perm(u0, t0, 0x07060302u); O[2][q] = __builtin_amdgcn_perm(u1, t1, 0x05040100u); O[3][q] = __builtin_amdgcn_perm(u1, t1, 0x07060302u); }
; #pragma unroll
;     for (int j = 0; j < 4; ++j) { u32x4 o; o.x = O[j][0]; o.y = O[j][1]; o.z = O[j][2]; o.w = O[j][3];
;         __builtin_nontemporal_store(o, (u32x4*)(WT + (size_t)drow<MODE>(n0 + j) * K + k0)); }
; }
	v_pk_mul_f32 v[18:19], v[22:23], s[4:5] op_sel_hi:[1,0]
	s_waitcnt vmcnt(30)
	v_pk_mul_f32 v[22:23], v[26:27], s[4:5] op_sel_hi:[1,0]
	s_waitcnt vmcnt(29)
	v_pk_mul_f32 v[26:27], v[30:31], s[4:5] op_sel_hi:[1,0]
	s_waitcnt vmcnt(28)
	v_pk_mul_f32 v[30:31], v[34:35], s[4:5] op_sel_hi:[1,0]
	s_waitcnt vmcnt(27)
	v_pk_mul_f32 v[34:35], v[38:39], s[4:5] op_sel_hi:[1,0]
	s_waitcnt vmcnt(26)
	v_pk_mul_f32 v[38:39], v[42:43], s[4:5] op_sel_hi:[1,0]
	s_waitcnt vmcnt(25)
	v_pk_mul_f32 v[42:43], v[46:47], s[4:5] op_sel_hi:[1,0]
	s_waitcnt vmcnt(24)
	v_pk_mul_f32 v[46:47], v[50:51], s[4:5] op_sel_hi:[1,0]
	s_waitcnt vmcnt(23)
	v_pk_mul_f32 v[50:51], v[54:55], s[4:5] op_sel_hi:[1,0]
	s_waitcnt vmcnt(22)
	v_pk_mul_f32 v[54:55], v[58:59], s[4:5] op_sel_hi:[1,0]
	s_waitcnt vmcnt(21)
	v_pk_mul_f32 v[58:59], v[62:63], s[4:5] op_sel_hi:[1,0]
	s_waitcnt vmcnt(20)
	v_pk_mul_f32 v[62:63], v[68:69], s[4:5] op_sel_hi:[1,0]
	v_med3_f32 v6, v6, s24, v72
	v_med3_f32 v7, v7, s24, v72
	v_med3_f32 v10, v10, s24, v72
	v_med3_f32 v11, v11, s24, v72
	v_med3_f32 v14, v14, s24, v72
	v_med3_f32 v15, v15, s24, v72
	v_med3_f32 v18, v18, s24, v72
	v_med3_f32 v19, v19, s24, v72
	v_med3_f32 v22, v22, s24, v72
	v_med3_f32 v23, v23, s24, v72
	v_med3_f32 v26, v26, s24, v72
	v_med3_f32 v27, v27, s24, v72
	v_med3_f32 v30, v30, s24, v72
	v_med3_f32 v31, v31, s24, v72
	v_med3_f32 v34, v34, s24, v72
	v_med3_f32 v35, v35, s24, v72
	v_med3_f32 v38, v38, s24, v72
	v_med3_f32 v39, v39, s24, v72
	v_med3_f32 v42, v42, s24, v72
	v_med3_f32 v43, v43, s24, v72
	v_med3_f32 v46, v46, s24, v72
	v_med3_f32 v47, v47, s24, v72
	v_med3_f32 v50, v50, s24, v72
	v_med3_f32 v51, v51, s24, v72
	v_med3_f32 v54, v54, s24, v72
	v_med3_f32 v55, v55, s24, v72
	v_med3_f32 v58, v58, s24, v72
	v_med3_f32 v59, v59, s24, v72
	v_med3_f32 v62, v62, s24, v72
	v_med3_f32 v63, v63, s24, v72
	v_cvt_pk_fp8_f32 v5, v94, v95
	v_cvt_pk_fp8_f32 v73, v6, v7
	v_cvt_pk_fp8_f32 v80, v10, v11
	v_cvt_pk_fp8_f32 v81, v14, v15
	v_cvt_pk_fp8_f32 v82, v18, v19
	v_cvt_pk_fp8_f32 v83, v22, v23
	v_cvt_pk_fp8_f32 v84, v26, v27
	v_cvt_pk_fp8_f32 v85, v30, v31
	v_cvt_pk_fp8_f32 v86, v34, v35
	v_cvt_pk_fp8_f32 v87, v38, v39
	v_cvt_pk_fp8_f32 v88, v42, v43
	v_cvt_pk_fp8_f32 v89, v46, v47
	v_cvt_pk_fp8_f32 v90, v50, v51
	v_cvt_pk_fp8_f32 v91, v54, v55
	v_cvt_pk_fp8_f32 v92, v58, v59
	v_cvt_pk_fp8_f32 v93, v62, v63
	v_pk_mul_f32 v[8:9], v[8:9], s[4:5] op_sel_hi:[1,0]
	s_nop 0
	v_med3_f32 v96, v8, s24, v72
	v_med3_f32 v97, v9, s24, v72
	v_pk_mul_f32 v[8:9], v[12:13], s[4:5] op_sel_hi:[1,0]
	v_pk_mul_f32 v[12:13], v[16:17], s[4:5] op_sel_hi:[1,0]
	v_pk_mul_f32 v[16:17], v[20:21], s[4:5] op_sel_hi:[1,0]
	v_pk_mul_f32 v[20:21], v[24:25], s[4:5] op_sel_hi:[1,0]
	v_pk_mul_f32 v[24:25], v[28:29], s[4:5] op_sel_hi:[1,0]
	v_pk_mul_f32 v[28:29], v[32:33], s[4:5] op_sel_hi:[1,0]
	v_pk_mul_f32 v[32:33], v[36:37], s[4:5] op_sel_hi:[1,0]
	v_pk_mul_f32 v[36:37], v[40:41], s[4:5] op_sel_hi:[1,0]
	v_pk_mul_f32 v[40:41], v[44:45], s[4:5] op_sel_hi:[1,0]
	v_pk_mul_f32 v[44:45], v[48:49], s[4:5] op_sel_hi:[1,0]
	v_pk_mul_f32 v[48:49], v[52:53], s[4:5] op_sel_hi:[1,0]
	v_pk_mul_f32 v[52:53], v[56:57], s[4:5] op_sel_hi:[1,0]
	v_pk_mul_f32 v[56:57], v[60:61], s[4:5] op_sel_hi:[1,0]
	v_pk_mul_f32 v[60:61], v[64:65], s[4:5] op_sel_hi:[1,0]
	v_pk_mul_f32 v[64:65], v[70:71], s[4:5] op_sel_hi:[1,0]
	v_med3_f32 v8, v8, s24, v72
	v_med3_f32 v9, v9, s24, v72
	v_med3_f32 v12, v12, s24, v72
	v_med3_f32 v13, v13, s24, v72
	v_med3_f32 v16, v16, s24, v72
	v_med3_f32 v17, v17, s24, v72
	v_med3_f32 v20, v20, s24, v72
	v_med3_f32 v21, v21, s24, v72
	v_med3_f32 v24, v24, s24, v72
	v_med3_f32 v25, v25, s24, v72
	v_med3_f32 v28, v28, s24, v72
	v_med3_f32 v29, v29, s24, v72
	v_med3_f32 v32, v32, s24, v72
	v_med3_f32 v33, v33, s24, v72
	v_med3_f32 v36, v36, s24, v72
	v_med3_f32 v37, v37, s24, v72
	v_med3_f32 v40, v40, s24, v72
	v_med3_f32 v41, v41, s24, v72
	v_med3_f32 v44, v44, s24, v72
	v_med3_f32 v45, v45, s24, v72
	v_med3_f32 v48, v48, s24, v72
	v_med3_f32 v49, v49, s24, v72
	v_med3_f32 v52, v52, s24, v72
	v_med3_f32 v53, v53, s24, v72
	v_med3_f32 v56, v56, s24, v72
	v_med3_f32 v57, v57, s24, v72
	v_med3_f32 v60, v60, s24, v72
	v_med3_f32 v61, v61, s24, v72
	v_med3_f32 v64, v64, s24, v72
	v_med3_f32 v65, v65, s24, v72
	v_cvt_pk_fp8_f32 v5, v96, v97 op_sel:[0,0,1]
	v_cvt_pk_fp8_f32 v73, v8, v9 op_sel:[0,0,1]
	v_cvt_pk_fp8_f32 v80, v12, v13 op_sel:[0,0,1]
	v_cvt_pk_fp8_f32 v81, v16, v17 op_sel:[0,0,1]
	v_cvt_pk_fp8_f32 v82, v20, v21 op_sel:[0,0,1]
	v_cvt_pk_fp8_f32 v83, v24, v25 op_sel:[0,0,1]
	v_cvt_pk_fp8_f32 v84, v28, v29 op_sel:[0,0,1]
	v_cvt_pk_fp8_f32 v85, v32, v33 op_sel:[0,0,1]
	v_cvt_pk_fp8_f32 v86, v36, v37 op_sel:[0,0,1]
	v_cvt_pk_fp8_f32 v87, v40, v41 op_sel:[0,0,1]
	v_cvt_pk_fp8_f32 v88, v44, v45 op_sel:[0,0,1]
	v_cvt_pk_fp8_f32 v89, v48, v49 op_sel:[0,0,1]
	v_cvt_pk_fp8_f32 v90, v52, v53 op_sel:[0,0,1]
	v_cvt_pk_fp8_f32 v91, v56, v57 op_sel:[0,0,1]
	v_cvt_pk_fp8_f32 v92, v60, v61 op_sel:[0,0,1]
	v_cvt_pk_fp8_f32 v93, v64, v65 op_sel:[0,0,1]
	v_perm_b32 v7, v73, v5, s25
	v_perm_b32 v5, v73, v5, s26
	v_perm_b32 v8, v81, v80, s25
	v_perm_b32 v9, v81, v80, s26
	v_perm_b32 v11, v83, v82, s25
	v_perm_b32 v13, v85, v84, s25
	v_perm_b32 v17, v87, v86, s25
	v_perm_b32 v21, v89, v88, s25
	v_perm_b32 v23, v91, v90, s25
	v_perm_b32 v25, v93, v92, s25
	v_perm_b32 v12, v83, v82, s26
	v_perm_b32 v16, v85, v84, s26
	v_perm_b32 v20, v87, v86, s26
	v_perm_b32 v22, v89, v88, s26
	v_perm_b32 v24, v91, v90, s26
	v_perm_b32 v26, v93, v92, s26
	v_perm_b32 v6, v8, v7, s27
	v_perm_b32 v10, v8, v7, s28
	v_perm_b32 v14, v9, v5, s27
	v_perm_b32 v18, v9, v5, s28
	v_perm_b32 v7, v13, v11, s27
	v_perm_b32 v8, v21, v17, s27
	v_perm_b32 v9, v25, v23, s27
	v_perm_b32 v11, v13, v11, s28
	v_perm_b32 v15, v16, v12, s27
	v_perm_b32 v19, v16, v12, s28
	v_perm_b32 v12, v21, v17, s28
	v_perm_b32 v16, v22, v20, s27
	v_perm_b32 v20, v22, v20, s28
	v_perm_b32 v13, v25, v23, s28
	v_perm_b32 v17, v26, v24, s27
	v_perm_b32 v21, v26, v24, s28
	global_store_dwordx4 v[74:75], v[6:9], off nt
	global_store_dwordx4 v[76:77], v[10:13], off nt
	global_store_dwordx4 v[78:79], v[14:17], off nt
	global_store_dwordx4 v[2:3], v[18:21], off nt
	s_waitcnt vmcnt(19)
; template <int MODE> __device__ __forceinline__ void cv_finish(const f32x4 (&tv)[16], int K, int nblk, unsigned char* WT, int item, int lane) {
;     const int kb = item / nblk, nb = item - kb * nblk, k0 = 64 * kb + 16 * (lane >> 4), n0 = 64 * nb + 4 * (lane & 15);
;     unsigned D[16];
; #pragma unroll
;     for (int i = 0; i < 16; ++i) { const f32x2 a = (f32x2){tv[i].x, tv[i].y} * (f32x2){1024.f, 1024.f}, b = (f32x2){tv[i].z, tv[i].w} * (f32x2){1024.f, 1024.f};
;         D[i] = pk4_fp8(a.x, a.y, b.x, b.y); }
	v_pk_mul_f32 v[102:103], v[102:103], s[4:5] op_sel_hi:[1,0]
	s_nop 0
	v_med3_f32 v190, v102, s24, v72
	v_med3_f32 v191, v103, s24, v72
	s_waitcnt vmcnt(18)
	v_pk_mul_f32 v[102:103], v[106:107], s[4:5] op_sel_hi:[1,0]
	s_waitcnt vmcnt(17)
	v_pk_mul_f32 v[106:107], v[110:111], s[4:5] op_sel_hi:[1,0]
	s_waitcnt vmcnt(16)
	v_pk_mul_f32 v[110:111], v[114:115], s[4:5] op_sel_hi:[1,0]
	s_waitcnt vmcnt(15)
	v_pk_mul_f32 v[114:115], v[118:119], s[4:5] op_sel_hi:[1,0]
	s_waitcnt vmcnt(14)
	v_pk_mul_f32 v[118:119], v[122:123], s[4:5] op_sel_hi:[1,0]
	s_waitcnt vmcnt(13)
	v_pk_mul_f32 v[122:123], v[126:127], s[4:5] op_sel_hi:[1,0]
	s_waitcnt vmcnt(12)
	v_pk_mul_f32 v[126:127], v[132:133], s[4:5] op_sel_hi:[1,0]
	s_waitcnt vmcnt(11)
	v_pk_mul_f32 v[132:133], v[136:137], s[4:5] op_sel_hi:[1,0]
	s_waitcnt vmcnt(10)
	v_pk_mul_f32 v[136:137], v[140:141], s[4:5] op_sel_hi:[1,0]
	s_waitcnt vmcnt(9)
	v_pk_mul_f32 v[140:141], v[144:145], s[4:5] op_sel_hi:[1,0]
	s_waitcnt vmcnt(8)
	v_pk_mul_f32 v[144:145], v[148:149], s[4:5] op_sel_hi:[1,0]
	s_waitcnt vmcnt(7)
	v_pk_mul_f32 v[148:149], v[152:153], s[4:5] op_sel_hi:[1,0]
	s_waitcnt vmcnt(6)
	v_pk_mul_f32 v[152:153], v[156:157], s[4:5] op_sel_hi:[1,0]
	s_waitcnt vmcnt(5)
	v_pk_mul_f32 v[156:157], v[160:161], s[4:5] op_sel_hi:[1,0]
	s_waitcnt vmcnt(4)
; template <int MODE> __device__ __forceinline__ void cv_finish(const f32x4 (&tv)[16], int K, int nblk, unsigned char* WT, int item, int lane) {
;     const int kb = item / nblk, nb = item - kb * nblk, k0 = 64 * kb + 16 * (lane >> 4), n0 = 64 * nb + 4 * (lane & 15);
;     unsigned D[16];
; #pragma unroll
;     for (int i = 0; i < 16; ++i) { const f32x2 a = (f32x2){tv[i].x, tv[i].y} * (f32x2){1024.f, 1024.f}, b = (f32x2){tv[i].z, tv[i].w} * (f32x2){1024.f, 1024.f};
;         D[i] = pk4_fp8(a.x, a.y, b.x, b.y); }
;     unsigned O[4][4];
; #pragma unroll
;     for (int q = 0; q < 4; ++q) { const unsigned a = D[4 * q], b = D[4 * q + 1], c = D[4 * q + 2], d = D[4 * q + 3];
;         const unsigned t0 = __builtin_amdgcn_perm(b, a, 0x05010400u), t1 = __builtin_amdgcn_perm(b, a, 0x07030602u), u0 = __builtin_amdgcn_perm(d, c, 0x05010400u), u1 = __builtin_amdgcn_perm(d, c, 0x07030602u);
;         O[0][q] = __builtin_amdgcn_perm(u0, t0, 0x05040100u); O[1][q] = __builtin_amdgcn_perm(u0, t0, 0x07060302u); O[2][q] = __builtin_amdgcn_perm(u1, t1, 0x05040100u); O[3][q] = __builtin_amdgcn_perm(u1, t1, 0x07060302u); }
; #pragma unroll
;     for (int j = 0; j < 4; ++j) { u32x4 o; o.x = O[j][0]; o.y = O[j][1]; o.z = O[j][2]; o.w = O[j][3];
;         __builtin_nontemporal_store(o, (u32x4*)(WT + (size_t)drow<MODE>(n0 + j) * K + k0)); }
; }
; template <int MODE> __device__ __forceinline__ void cv_run4(const float* W, int K, int N, unsigned char* WT, int item0, int lane) {
;     const int nblk = N / 64; f32x4 ta[16];
; #pragma unroll 1
;     for (int j = 0; j < 4; ++j) { cv_load(W, N, nblk, item0 + j, lane, ta); cv_finish<MODE>(ta, K, nblk, WT, item0 + j, lane); }
	v_pk_mul_f32 v[160:161], v[164:165], s[4:5] op_sel_hi:[1,0]
	v_med3_f32 v102, v102, s24, v72
	v_med3_f32 v103, v103, s24, v72
	v_med3_f32 v106, v106, s24, v72
	v_med3_f32 v107, v107, s24, v72
	v_med3_f32 v110, v110, s24, v72
	v_med3_f32 v111, v111, s24, v72
	v_med3_f32 v114, v114, s24, v72
	v_med3_f32 v115, v115, s24, v72
	v_med3_f32 v118, v118, s24, v72
	v_med3_f32 v119, v119, s24, v72
	v_med3_f32 v122, v122, s24, v72
	v_med3_f32 v123, v123, s24, v72
	v_med3_f32 v126, v126, s24, v72
	v_med3_f32 v127, v127, s24, v72
	v_med3_f32 v132, v132, s24, v72
	v_med3_f32 v133, v133, s24, v72
	v_med3_f32 v136, v136, s24, v72
	v_med3_f32 v137, v137, s24, v72
	v_med3_f32 v140, v140, s24, v72
	v_med3_f32 v141, v141, s24, v72
	v_med3_f32 v144, v144, s24, v72
	v_med3_f32 v145, v145, s24, v72
	v_med3_f32 v148, v148, s24, v72
	v_med3_f32 v149, v149, s24, v72
	v_med3_f32 v152, v152, s24, v72
	v_med3_f32 v153, v153, s24, v72
	v_med3_f32 v156, v156, s24, v72
	v_med3_f32 v157, v157, s24, v72
	v_med3_f32 v160, v160, s24, v72
	v_med3_f32 v161, v161, s24, v72
	v_cvt_pk_fp8_f32 v101, v190, v191
	v_cvt_pk_fp8_f32 v169, v102, v103
	v_cvt_pk_fp8_f32 v100, v106, v107
	v_cvt_pk_fp8_f32 v171, v110, v111
	v_cvt_pk_fp8_f32 v168, v114, v115
	v_cvt_pk_fp8_f32 v173, v118, v119
	v_cvt_pk_fp8_f32 v180, v122, v123
	v_cvt_pk_fp8_f32 v181, v126, v127
	v_cvt_pk_fp8_f32 v182, v132, v133
	v_cvt_pk_fp8_f32 v183, v136, v137
	v_cvt_pk_fp8_f32 v184, v140, v141
	v_cvt_pk_fp8_f32 v185, v144, v145
	v_cvt_pk_fp8_f32 v186, v148, v149
	v_cvt_pk_fp8_f32 v187, v152, v153
	v_cvt_pk_fp8_f32 v188, v156, v157
	v_cvt_pk_fp8_f32 v189, v160, v161
	v_pk_mul_f32 v[104:105], v[104:105], s[4:5] op_sel_hi:[1,0]
	s_nop 0
	v_med3_f32 v192, v104, s24, v72
	v_med3_f32 v193, v105, s24, v72
	v_pk_mul_f32 v[104:105], v[108:109], s[4:5] op_sel_hi:[1,0]
	v_pk_mul_f32 v[108:109], v[112:113], s[4:5] op_sel_hi:[1,0]
	v_pk_mul_f32 v[112:113], v[116:117], s[4:5] op_sel_hi:[1,0]
	v_pk_mul_f32 v[116:117], v[120:121], s[4:5] op_sel_hi:[1,0]
	v_pk_mul_f32 v[120:121], v[124:125], s[4:5] op_sel_hi:[1,0]
	v_pk_mul_f32 v[124:125], v[128:129], s[4:5] op_sel_hi:[1,0]
	v_pk_mul_f32 v[128:129], v[134:135], s[4:5] op_sel_hi:[1,0]
	v_pk_mul_f32 v[134:135], v[138:139], s[4:5] op_sel_hi:[1,0]
	v_pk_mul_f32 v[138:139], v[142:143], s[4:5] op_sel_hi:[1,0]
	v_pk_mul_f32 v[142:143], v[146:147], s[4:5] op_sel_hi:[1,0]
	v_pk_mul_f32 v[146:147], v[150:151], s[4:5] op_sel_hi:[1,0]
	v_pk_mul_f32 v[150:151], v[154:155], s[4:5] op_sel_hi:[1,0]
	v_pk_mul_f32 v[154:155], v[158:159], s[4:5] op_sel_hi:[1,0]
	v_pk_mul_f32 v[158:159], v[162:163], s[4:5] op_sel_hi:[1,0]
	v_pk_mul_f32 v[162:163], v[166:167], s[4:5] op_sel_hi:[1,0]
	v_med3_f32 v104, v104, s24, v72
	v_med3_f32 v105, v105, s24, v72
	v_med3_f32 v108, v108, s24, v72
	v_med3_f32 v109, v109, s24, v72
	v_med3_f32 v112, v112, s24, v72
	v_med3_f32 v113, v113, s24, v72
	v_med3_f32 v116, v116, s24, v72
	v_med3_f32 v117, v117, s24, v72
	v_med3_f32 v120, v120, s24, v72
	v_med3_f32 v121, v121, s24, v72
	v_med3_f32 v124, v124, s24, v72
	v_med3_f32 v125, v125, s24, v72
	v_med3_f32 v128, v128, s24, v72
	v_med3_f32 v129, v129, s24, v72
	v_med3_f32 v134, v134, s24, v72
	v_med3_f32 v135, v135, s24, v72
	v_med3_f32 v138, v138, s24, v72
	v_med3_f32 v139, v139, s24, v72
	v_med3_f32 v142, v142, s24, v72
	v_med3_f32 v143, v143, s24, v72
	v_med3_f32 v146, v146, s24, v72
	v_med3_f32 v147, v147, s24, v72
	v_med3_f32 v150, v150, s24, v72
	v_med3_f32 v151, v151, s24, v72
	v_med3_f32 v154, v154, s24, v72
	v_med3_f32 v155, v155, s24, v72
	v_med3_f32 v158, v158, s24, v72
	v_med3_f32 v159, v159, s24, v72
	v_med3_f32 v162, v162, s24, v72
	v_med3_f32 v163, v163, s24, v72
	v_cvt_pk_fp8_f32 v101, v192, v193 op_sel:[0,0,1]
	v_cvt_pk_fp8_f32 v169, v104, v105 op_sel:[0,0,1]
	v_cvt_pk_fp8_f32 v100, v108, v109 op_sel:[0,0,1]
	v_cvt_pk_fp8_f32 v171, v112, v113 op_sel:[0,0,1]
	v_cvt_pk_fp8_f32 v168, v116, v117 op_sel:[0,0,1]
	v_cvt_pk_fp8_f32 v173, v120, v121 op_sel:[0,0,1]
	v_cvt_pk_fp8_f32 v180, v124, v125 op_sel:[0,0,1]
	v_cvt_pk_fp8_f32 v181, v128, v129 op_sel:[0,0,1]
	v_cvt_pk_fp8_f32 v182, v134, v135 op_sel:[0,0,1]
	v_cvt_pk_fp8_f32 v183, v138, v139 op_sel:[0,0,1]
	v_cvt_pk_fp8_f32 v184, v142, v143 op_sel:[0,0,1]
	v_cvt_pk_fp8_f32 v185, v146, v147 op_sel:[0,0,1]
	v_cvt_pk_fp8_f32 v186, v150, v151 op_sel:[0,0,1]
	v_cvt_pk_fp8_f32 v187, v154, v155 op_sel:[0,0,1]
	v_cvt_pk_fp8_f32 v188, v158, v159 op_sel:[0,0,1]
	v_cvt_pk_fp8_f32 v189, v162, v163 op_sel:[0,0,1]
	v_perm_b32 v103, v169, v101, s25
	v_perm_b32 v101, v169, v101, s26
	v_perm_b32 v104, v171, v100, s25
	v_perm_b32 v105, v171, v100, s26
	v_perm_b32 v107, v173, v168, s25
	v_perm_b32 v109, v181, v180, s25
	v_perm_b32 v113, v183, v182, s25
	v_perm_b32 v117, v185, v184, s25
	v_perm_b32 v119, v187, v186, s25
	v_perm_b32 v121, v189, v188, s25
	v_perm_b32 v108, v173, v168, s26
	v_perm_b32 v112, v181, v180, s26
	v_perm_b32 v116, v183, v182, s26
	v_perm_b32 v118, v185, v184, s26
	v_perm_b32 v120, v187, v186, s26
	v_perm_b32 v122, v189, v188, s26
	v_perm_b32 v102, v104, v103, s27
	v_perm_b32 v106, v104, v103, s28
	v_perm_b32 v110, v105, v101, s27
	v_perm_b32 v114, v105, v101, s28
	v_perm_b32 v103, v109, v107, s27
	v_perm_b32 v104, v117, v113, s27
	v_perm_b32 v105, v121, v119, s27
	v_perm_b32 v107, v109, v107, s28
	v_perm_b32 v111, v112, v108, s27
	v_perm_b32 v115, v112, v108, s28
	v_perm_b32 v108, v117, v113, s28
	v_perm_b32 v112, v118, v116, s27
	v_perm_b32 v116, v118, v116, s28
	v_perm_b32 v109, v121, v119, s28
	v_perm_b32 v113, v122, v120, s27
	v_perm_b32 v117, v122, v120, s28
	global_store_dwordx4 v[174:175], v[102:105], off nt
	global_store_dwordx4 v[176:177], v[106:109], off nt
	global_store_dwordx4 v[178:179], v[110:113], off nt
	global_store_dwordx4 v[98:99], v[114:117], off nt
	s_cbranch_scc0 .LBB0_761
	s_mov_b64 s[6:7], 0

; template <int MODE> __device__ __forceinline__ int drow(int n) {
;     if (MODE == 1) { const int h = n / 192, nl = n - h * 192; return nl < 128 ? n : h * 192 + 128 + ((nl - 128) & 31) * 2 + ((nl - 128) >> 5); }
;     if (MODE == 2) { return n < FF ? ((n >> 7) * 256 + (n & 127)) : (((n - FF) >> 7) * 256 + 128 + ((n - FF) & 127)); }
;     return n;
; }
; __device__ __forceinline__ void cv_load(const float* W, int N, int nblk, int item, int lane, f32x4 (&tv)[16]) {
;     const int kb = item / nblk, nb = item - kb * nblk; const float* p = W + (size_t)(64 * kb + 16 * (lane >> 4)) * N + 64 * nb + 4 * (lane & 15);
; #pragma unroll
;     for (int i = 0; i < 16; ++i) tv[i] = __builtin_nontemporal_load((const f32x4*)(p + (size_t)i * N));
; }
.LBB0_766:
	s_ashr_i32 s10, s2, 31
	s_lshr_b32 s10, s10, 26
	s_add_i32 s10, s2, s10
	s_ashr_i32 s41, s10, 6
	s_andn2_b32 s10, s10, 63
	v_or_b32_e32 v68, s10, v1
	v_ashrrev_i32_e32 v69, 31, v68
	s_lshl_b32 s10, s41, 12
	v_lshlrev_b64 v[2:3], 14, v[68:69]
	s_sub_i32 s10, s39, s10
	v_lshl_add_u64 v[2:3], s[6:7], 0, v[2:3]
	s_ashr_i32 s11, s10, 31
	v_lshl_add_u64 v[2:3], s[10:11], 2, v[2:3]
	v_lshl_add_u64 v[2:3], v[2:3], 0, v[66:67]
	v_add_co_u32_e32 v4, vcc, s1, v2
	v_add_u32_e32 v75, s10, v130
	s_nop 0
	v_addc_co_u32_e32 v5, vcc, 0, v3, vcc
	global_load_dwordx4 v[62:65], v[2:3], off nt
	global_load_dwordx4 v[58:61], v[4:5], off nt
	v_add_co_u32_e32 v4, vcc, s12, v2
	v_add_u32_e32 v70, s40, v73
	s_nop 0
	v_addc_co_u32_e32 v5, vcc, 0, v3, vcc
	v_add_co_u32_e32 v6, vcc, s14, v2
	s_lshl_b32 s10, s41, 13
	s_nop 0
	v_addc_co_u32_e32 v7, vcc, 0, v3, vcc
	global_load_dwordx4 v[54:57], v[4:5], off nt
	global_load_dwordx4 v[50:53], v[6:7], off nt
	v_add_co_u32_e32 v4, vcc, s16, v2
	v_subrev_u32_e32 v74, s10, v70
	s_nop 0
	v_addc_co_u32_e32 v5, vcc, 0, v3, vcc
	v_add_co_u32_e32 v6, vcc, s18, v2
	v_and_b32_e32 v71, 0x7c, v75
	s_nop 0
	v_addc_co_u32_e32 v7, vcc, 0, v3, vcc
	global_load_dwordx4 v[46:49], v[4:5], off nt
	global_load_dwordx4 v[42:45], v[6:7], off nt
	v_add_co_u32_e32 v4, vcc, s20, v2
	s_nop 1
	v_addc_co_u32_e32 v5, vcc, 0, v3, vcc
	v_add_co_u32_e32 v6, vcc, s22, v2
	s_nop 1
	v_addc_co_u32_e32 v7, vcc, 0, v3, vcc
	global_load_dwordx4 v[38:41], v[4:5], off nt
	global_load_dwordx4 v[34:37], v[6:7], off nt
	v_add_co_u32_e32 v4, vcc, s29, v2
	s_nop 1
	v_addc_co_u32_e32 v5, vcc, 0, v3, vcc
	v_add_co_u32_e32 v6, vcc, s30, v2
	s_nop 1
	v_addc_co_u32_e32 v7, vcc, 0, v3, vcc
	global_load_dwordx4 v[30:33], v[4:5], off nt
	global_load_dwordx4 v[26:29], v[6:7], off nt
	v_add_co_u32_e32 v4, vcc, s31, v2
	s_nop 1
	v_addc_co_u32_e32 v5, vcc, 0, v3, vcc
	v_add_co_u32_e32 v6, vcc, s33, v2
	s_nop 1
	v_addc_co_u32_e32 v7, vcc, 0, v3, vcc
	global_load_dwordx4 v[22:25], v[4:5], off nt
	global_load_dwordx4 v[18:21], v[6:7], off nt
	v_add_co_u32_e32 v4, vcc, s34, v2
	s_nop 1
	v_addc_co_u32_e32 v5, vcc, 0, v3, vcc
	v_add_co_u32_e32 v6, vcc, s35, v2
	s_nop 1
	v_addc_co_u32_e32 v7, vcc, 0, v3, vcc
	global_load_dwordx4 v[14:17], v[4:5], off nt
	global_load_dwordx4 v[10:13], v[6:7], off nt
	v_add_co_u32_e32 v4, vcc, 0x38000, v2
	s_nop 1
	v_addc_co_u32_e32 v5, vcc, 0, v3, vcc
	v_add_co_u32_e32 v2, vcc, 0x3c000, v2
	s_nop 1
	v_addc_co_u32_e32 v3, vcc, 0, v3, vcc
	global_load_dwordx4 v[6:9], v[4:5], off nt
	s_nop 0
	global_load_dwordx4 v[2:5], v[2:3], off nt
	s_addk_i32 s40, 0x80
	s_add_i32 s39, s39, 64
	s_add_i32 s2, s2, 1
	s_ashr_i32 s10, s2, 31
	s_lshr_b32 s10, s10, 26
	s_add_i32 s10, s2, s10
	s_ashr_i32 s41, s10, 6
	s_andn2_b32 s10, s10, 63
	v_or_b32_e32 v148, s10, v1
	v_ashrrev_i32_e32 v149, 31, v148
	s_lshl_b32 s10, s41, 12
	v_lshlrev_b64 v[80:81], 14, v[148:149]
	s_sub_i32 s10, s39, s10
	v_lshl_add_u64 v[80:81], s[6:7], 0, v[80:81]
	s_ashr_i32 s11, s10, 31
	v_lshl_add_u64 v[80:81], s[10:11], 2, v[80:81]
	v_lshl_add_u64 v[80:81], v[80:81], 0, v[66:67]
	v_add_co_u32_e32 v82, vcc, s1, v80
	v_add_u32_e32 v129, s10, v130
	s_nop 0
	v_addc_co_u32_e32 v83, vcc, 0, v81, vcc
	global_load_dwordx4 v[144:147], v[80:81], off nt
	global_load_dwordx4 v[140:143], v[82:83], off nt
	v_add_co_u32_e32 v82, vcc, s12, v80
	v_add_u32_e32 v150, s40, v73
	s_nop 0
	v_addc_co_u32_e32 v83, vcc, 0, v81, vcc
	v_add_co_u32_e32 v84, vcc, s14, v80
	s_lshl_b32 s10, s41, 13
	s_nop 0
	v_addc_co_u32_e32 v85, vcc, 0, v81, vcc
	global_load_dwordx4 v[136:139], v[82:83], off nt
	global_load_dwordx4 v[132:135], v[84:85], off nt
	v_add_co_u32_e32 v82, vcc, s16, v80
	v_subrev_u32_e32 v128, s10, v150
	s_nop 0
	v_addc_co_u32_e32 v83, vcc, 0, v81, vcc
	v_add_co_u32_e32 v84, vcc, s18, v80
	v_and_b32_e32 v151, 0x7c, v129
	s_nop 0
	v_addc_co_u32_e32 v85, vcc, 0, v81, vcc
	global_load_dwordx4 v[124:127], v[82:83], off nt
	global_load_dwordx4 v[120:123], v[84:85], off nt
	v_add_co_u32_e32 v82, vcc, s20, v80
	s_nop 1
	v_addc_co_u32_e32 v83, vcc, 0, v81, vcc
	v_add_co_u32_e32 v84, vcc, s22, v80
	s_nop 1
	v_addc_co_u32_e32 v85, vcc, 0, v81, vcc
	global_load_dwordx4 v[116:119], v[82:83], off nt
	global_load_dwordx4 v[112:115], v[84:85], off nt
	v_add_co_u32_e32 v82, vcc, s29, v80
	s_nop 1
	v_addc_co_u32_e32 v83, vcc, 0, v81, vcc
	v_add_co_u32_e32 v84, vcc, s30, v80
	s_nop 1
	v_addc_co_u32_e32 v85, vcc, 0, v81, vcc
	global_load_dwordx4 v[108:111], v[82:83], off nt
	global_load_dwordx4 v[104:107], v[84:85], off nt
	v_add_co_u32_e32 v82, vcc, s31, v80
	s_nop 1
	v_addc_co_u32_e32 v83, vcc, 0, v81, vcc
	v_add_co_u32_e32 v84, vcc, s33, v80
	s_nop 1
	v_addc_co_u32_e32 v85, vcc, 0, v81, vcc
	global_load_dwordx4 v[100:103], v[82:83], off nt
	global_load_dwordx4 v[96:99], v[84:85], off nt
	v_add_co_u32_e32 v82, vcc, s34, v80
	s_nop 1
	v_addc_co_u32_e32 v83, vcc, 0, v81, vcc
	v_add_co_u32_e32 v84, vcc, s35, v80
	s_nop 1
	v_addc_co_u32_e32 v85, vcc, 0, v81, vcc
	global_load_dwordx4 v[92:95], v[82:83], off nt
	global_load_dwordx4 v[88:91], v[84:85], off nt
	v_add_co_u32_e32 v82, vcc, 0x38000, v80
	s_nop 1
	v_addc_co_u32_e32 v83, vcc, 0, v81, vcc
	v_add_co_u32_e32 v80, vcc, 0x3c000, v80
	s_nop 1
	v_addc_co_u32_e32 v81, vcc, 0, v81, vcc
	global_load_dwordx4 v[84:87], v[82:83], off nt
	s_nop 0
	global_load_dwordx4 v[80:83], v[80:81], off nt
	s_addk_i32 s40, 0x80
	s_add_i32 s39, s39, 64
	s_add_i32 s2, s2, 1
	v_cmp_lt_i32_e32 vcc, s36, v75
	s_and_saveexec_b64 s[10:11], vcc
	s_xor_b64 s[10:11], exec, s[10:11]
	v_add_u32_e32 v70, 0x7ffff000, v74
	v_and_b32_e32 v70, 0x7fffff00, v70
	v_or3_b32 v70, v71, v70, s37
	s_andn2_saveexec_b64 s[10:11], s[10:11]
	v_and_or_b32 v70, v74, s38, v71
	s_or_b64 exec, exec, s[10:11]
	s_waitcnt vmcnt(31)
; __device__ __forceinline__ unsigned pk4_fp8(float a, float b, float c, float d) {
;     a = __builtin_fminf(__builtin_fmaxf(a, -448.f), 448.f); b = __builtin_fminf(__builtin_fmaxf(b, -448.f), 448.f); c = __builtin_fminf(__builtin_fmaxf(c, -448.f), 448.f); d = __builtin_fminf(__builtin_fmaxf(d, -448.f), 448.f);
;     int w = 0; w = __builtin_amdgcn_cvt_pk_fp8_f32(a, b, w, false); w = __builtin_amdgcn_cvt_pk_fp8_f32(c, d, w, true); return (unsigned)w;
; template <int MODE> __device__ __forceinline__ void cv_finish(const f32x4 (&tv)[16], int K, int nblk, unsigned char* WT, int item, int lane) {
;     const int kb = item / nblk, nb = item - kb * nblk, k0 = 64 * kb + 16 * (lane >> 4), n0 = 64 * nb + 4 * (lane & 15);
;     unsigned D[16];
; #pragma unroll
;     for (int i = 0; i < 16; ++i) { const f32x2 a = (f32x2){tv[i].x, tv[i].y} * (f32x2){1024.f, 1024.f}, b = (f32x2){tv[i].z, tv[i].w} * (f32x2){1024.f, 1024.f};
;         D[i] = pk4_fp8(a.x, a.y, b.x, b.y); }
	v_pk_mul_f32 v[62:63], v[62:63], s[4:5] op_sel_hi:[1,0]
	v_pk_mul_f32 v[64:65], v[64:65], s[4:5] op_sel_hi:[1,0]
	v_med3_f32 v71, v62, s24, v72
	v_med3_f32 v63, v63, s24, v72
	v_mov_b32_e32 v62, v67
	v_cvt_pk_fp8_f32 v62, v71, v63
	v_med3_f32 v63, v64, s24, v72
	v_med3_f32 v64, v65, s24, v72
	s_waitcnt vmcnt(30)
	v_pk_mul_f32 v[58:59], v[58:59], s[4:5] op_sel_hi:[1,0]
	v_cvt_pk_fp8_f32 v62, v63, v64 op_sel:[0,0,1]
	v_med3_f32 v63, v58, s24, v72
	v_med3_f32 v59, v59, s24, v72
	v_mov_b32_e32 v58, v67
	v_cvt_pk_fp8_f32 v58, v63, v59
	v_pk_mul_f32 v[60:61], v[60:61], s[4:5] op_sel_hi:[1,0]
	s_waitcnt vmcnt(29)
	v_pk_mul_f32 v[54:55], v[54:55], s[4:5] op_sel_hi:[1,0]
	v_med3_f32 v59, v60, s24, v72
	v_med3_f32 v60, v61, s24, v72
	v_cvt_pk_fp8_f32 v58, v59, v60 op_sel:[0,0,1]
	v_med3_f32 v59, v54, s24, v72
	v_med3_f32 v55, v55, s24, v72
	v_mov_b32_e32 v54, v67
	v_cvt_pk_fp8_f32 v54, v59, v55
	v_pk_mul_f32 v[56:57], v[56:57], s[4:5] op_sel_hi:[1,0]
	s_waitcnt vmcnt(28)
	v_pk_mul_f32 v[50:51], v[50:51], s[4:5] op_sel_hi:[1,0]
	v_med3_f32 v55, v56, s24, v72
	v_med3_f32 v56, v57, s24, v72
	v_cvt_pk_fp8_f32 v54, v55, v56 op_sel:[0,0,1]
	v_med3_f32 v55, v50, s24, v72
	v_med3_f32 v51, v51, s24, v72
	v_mov_b32_e32 v50, v67
	v_cvt_pk_fp8_f32 v50, v55, v51
	v_pk_mul_f32 v[52:53], v[52:53], s[4:5] op_sel_hi:[1,0]
	s_waitcnt vmcnt(27)
	v_pk_mul_f32 v[46:47], v[46:47], s[4:5] op_sel_hi:[1,0]
	v_med3_f32 v51, v52, s24, v72
	v_med3_f32 v52, v53, s24, v72
	v_cvt_pk_fp8_f32 v50, v51, v52 op_sel:[0,0,1]
	v_med3_f32 v51, v46, s24, v72
	v_med3_f32 v47, v47, s24, v72
	v_mov_b32_e32 v46, v67
	v_cvt_pk_fp8_f32 v46, v51, v47
	v_pk_mul_f32 v[48:49], v[48:49], s[4:5] op_sel_hi:[1,0]
	s_waitcnt vmcnt(26)
	v_pk_mul_f32 v[42:43], v[42:43], s[4:5] op_sel_hi:[1,0]
	v_med3_f32 v47, v48, s24, v72
	v_med3_f32 v48, v49, s24, v72
	v_cvt_pk_fp8_f32 v46, v47, v48 op_sel:[0,0,1]
	v_med3_f32 v47, v42, s24, v72
	v_med3_f32 v43, v43, s24, v72
	v_mov_b32_e32 v42, v67
	v_cvt_pk_fp8_f32 v42, v47, v43
	v_pk_mul_f32 v[44:45], v[44:45], s[4:5] op_sel_hi:[1,0]
	s_waitcnt vmcnt(25)
	v_pk_mul_f32 v[38:39], v[38:39], s[4:5] op_sel_hi:[1,0]
	v_med3_f32 v43, v44, s24, v72
	v_med3_f32 v44, v45, s24, v72
	v_cvt_pk_fp8_f32 v42, v43, v44 op_sel:[0,0,1]
	v_med3_f32 v43, v38, s24, v72
	v_med3_f32 v39, v39, s24, v72
	v_mov_b32_e32 v38, v67
	v_cvt_pk_fp8_f32 v38, v43, v39
	v_pk_mul_f32 v[40:41], v[40:41], s[4:5] op_sel_hi:[1,0]
	s_waitcnt vmcnt(24)
	v_pk_mul_f32 v[34:35], v[34:35], s[4:5] op_sel_hi:[1,0]
	v_med3_f32 v39, v40, s24, v72
	v_med3_f32 v40, v41, s24, v72
	v_cvt_pk_fp8_f32 v38, v39, v40 op_sel:[0,0,1]
	v_med3_f32 v39, v34, s24, v72
	v_med3_f32 v35, v35, s24, v72
	v_mov_b32_e32 v34, v67
	v_cvt_pk_fp8_f32 v34, v39, v35
	v_pk_mul_f32 v[36:37], v[36:37], s[4:5] op_sel_hi:[1,0]
	s_waitcnt vmcnt(23)
	v_pk_mul_f32 v[30:31], v[30:31], s[4:5] op_sel_hi:[1,0]
	v_med3_f32 v35, v36, s24, v72
	v_med3_f32 v36, v37, s24, v72
	v_cvt_pk_fp8_f32 v34, v35, v36 op_sel:[0,0,1]
	v_med3_f32 v35, v30, s24, v72
	v_med3_f32 v31, v31, s24, v72
	v_mov_b32_e32 v30, v67
	v_cvt_pk_fp8_f32 v30, v35, v31
	v_pk_mul_f32 v[32:33], v[32:33], s[4:5] op_sel_hi:[1,0]
	s_waitcnt vmcnt(22)
	v_pk_mul_f32 v[26:27], v[26:27], s[4:5] op_sel_hi:[1,0]
	v_med3_f32 v31, v32, s24, v72
	v_med3_f32 v32, v33, s24, v72
	v_cvt_pk_fp8_f32 v30, v31, v32 op_sel:[0,0,1]
	v_med3_f32 v31, v26, s24, v72
	v_med3_f32 v27, v27, s24, v72
	v_mov_b32_e32 v26, v67
	v_cvt_pk_fp8_f32 v26, v31, v27
	v_pk_mul_f32 v[28:29], v[28:29], s[4:5] op_sel_hi:[1,0]
	s_waitcnt vmcnt(21)
	v_pk_mul_f32 v[22:23], v[22:23], s[4:5] op_sel_hi:[1,0]
	v_med3_f32 v27, v28, s24, v72
	v_med3_f32 v28, v29, s24, v72
	v_cvt_pk_fp8_f32 v26, v27, v28 op_sel:[0,0,1]
	v_med3_f32 v27, v22, s24, v72
	v_med3_f32 v23, v23, s24, v72
	v_mov_b32_e32 v22, v67
	v_cvt_pk_fp8_f32 v22, v27, v23
	v_pk_mul_f32 v[24:25], v[24:25], s[4:5] op_sel_hi:[1,0]
	s_waitcnt vmcnt(20)
	v_pk_mul_f32 v[18:19], v[18:19], s[4:5] op_sel_hi:[1,0]
	v_med3_f32 v23, v24, s24, v72
	v_med3_f32 v24, v25, s24, v72
	v_cvt_pk_fp8_f32 v22, v23, v24 op_sel:[0,0,1]
	v_med3_f32 v23, v18, s24, v72
	v_med3_f32 v19, v19, s24, v72
	v_mov_b32_e32 v18, v67
	v_cvt_pk_fp8_f32 v18, v23, v19
	v_pk_mul_f32 v[20:21], v[20:21], s[4:5] op_sel_hi:[1,0]
	s_waitcnt vmcnt(19)
	v_pk_mul_f32 v[14:15], v[14:15], s[4:5] op_sel_hi:[1,0]
	v_med3_f32 v19, v20, s24, v72
	v_med3_f32 v20, v21, s24, v72
	v_cvt_pk_fp8_f32 v18, v19, v20 op_sel:[0,0,1]
	v_med3_f32 v19, v14, s24, v72
	v_med3_f32 v15, v15, s24, v72
	v_mov_b32_e32 v14, v67
	v_cvt_pk_fp8_f32 v14, v19, v15
	v_pk_mul_f32 v[16:17], v[16:17], s[4:5] op_sel_hi:[1,0]
	s_waitcnt vmcnt(18)
	v_pk_mul_f32 v[10:11], v[10:11], s[4:5] op_sel_hi:[1,0]
	v_med3_f32 v15, v16, s24, v72
	v_med3_f32 v16, v17, s24, v72
	v_cvt_pk_fp8_f32 v14, v15, v16 op_sel:[0,0,1]
	v_med3_f32 v15, v10, s24, v72
	v_med3_f32 v11, v11, s24, v72
	v_mov_b32_e32 v10, v67
	v_cvt_pk_fp8_f32 v10, v15, v11
	v_pk_mul_f32 v[12:13], v[12:13], s[4:5] op_sel_hi:[1,0]
	s_waitcnt vmcnt(17)
	v_pk_mul_f32 v[6:7], v[6:7], s[4:5] op_sel_hi:[1,0]
	v_med3_f32 v11, v12, s24, v72
	v_med3_f32 v12, v13, s24, v72
	v_cvt_pk_fp8_f32 v10, v11, v12 op_sel:[0,0,1]
	v_med3_f32 v11, v6, s24, v72
	v_med3_f32 v7, v7, s24, v72
	v_mov_b32_e32 v6, v67
	v_cvt_pk_fp8_f32 v6, v11, v7
	v_pk_mul_f32 v[8:9], v[8:9], s[4:5] op_sel_hi:[1,0]
	s_waitcnt vmcnt(16)
; __device__ __forceinline__ void cv_load(const float* W, int N, int nblk, int item, int lane, f32x4 (&tv)[16]) {
;     const int kb = item / nblk, nb = item - kb * nblk; const float* p = W + (size_t)(64 * kb + 16 * (lane >> 4)) * N + 64 * nb + 4 * (lane & 15);
; #pragma unroll
;     for (int i = 0; i < 16; ++i) tv[i] = __builtin_nontemporal_load((const f32x4*)(p + (size_t)i * N));
; }
; template <int MODE> __device__ __forceinline__ void cv_finish(const f32x4 (&tv)[16], int K, int nblk, unsigned char* WT, int item, int lane) {
;     ...
;     unsigned O[4][4];
; #pragma unroll
;     for (int q = 0; q < 4; ++q) { const unsigned a = D[4 * q], b = D[4 * q + 1], c = D[4 * q + 2], d = D[4 * q + 3];
;         const unsigned t0 = __builtin_amdgcn_perm(b, a, 0x05010400u), t1 = __builtin_amdgcn_perm(b, a, 0x07030602u), u0 = __builtin_amdgcn_perm(d, c, 0x05010400u), u1 = __builtin_amdgcn_perm(d, c, 0x07030602u);
;         O[0][q] = __builtin_amdgcn_perm(u0, t0, 0x05040100u); O[1][q] = __builtin_amdgcn_perm(u0, t0, 0x07060302u); O[2][q] = __builtin_amdgcn_perm(u1, t1, 0x05040100u); O[3][q] = __builtin_amdgcn_perm(u1, t1, 0x07060302u); }
; #pragma unroll
;     for (int j = 0; j < 4; ++j) { u32x4 o; o.x = O[j][0]; o.y = O[j][1]; o.z = O[j][2]; o.w = O[j][3];
;         __builtin_nontemporal_store(o, (u32x4*)(WT + (size_t)drow<MODE>(n0 + j) * K + k0)); }
; }
	v_pk_mul_f32 v[2:3], v[2:3], s[4:5] op_sel_hi:[1,0]
	v_med3_f32 v7, v8, s24, v72
	v_med3_f32 v8, v9, s24, v72
	v_cvt_pk_fp8_f32 v6, v7, v8 op_sel:[0,0,1]
	v_med3_f32 v2, v2, s24, v72
	v_med3_f32 v3, v3, s24, v72
	v_mov_b32_e32 v7, v67
	v_cvt_pk_fp8_f32 v7, v2, v3
	v_pk_mul_f32 v[2:3], v[4:5], s[4:5] op_sel_hi:[1,0]
	v_ashrrev_i32_e32 v71, 31, v70
	v_med3_f32 v2, v2, s24, v72
	v_med3_f32 v3, v3, s24, v72
	v_cvt_pk_fp8_f32 v7, v2, v3 op_sel:[0,0,1]
	v_perm_b32 v5, v58, v62, s25
	v_perm_b32 v8, v50, v54, s25
	v_perm_b32 v9, v42, v46, s25
	v_perm_b32 v11, v34, v38, s25
	v_perm_b32 v12, v26, v30, s25
	v_perm_b32 v13, v18, v22, s25
	v_perm_b32 v15, v10, v14, s25
	v_perm_b32 v16, v7, v6, s25
	v_lshl_add_u64 v[2:3], s[8:9], 0, v[68:69]
	v_lshlrev_b64 v[20:21], 11, v[70:71]
	v_add_u32_e32 v4, 1, v75
	v_perm_b32 v76, v8, v5, s27
	v_perm_b32 v77, v11, v9, s27
	v_perm_b32 v78, v13, v12, s27
	v_perm_b32 v79, v16, v15, s27
	v_lshl_add_u64 v[20:21], v[2:3], 0, v[20:21]
	v_cmp_lt_i32_e32 vcc, s36, v4
	v_and_b32_e32 v17, 0x7d, v4
	global_store_dwordx4 v[20:21], v[76:79], off nt
	s_and_saveexec_b64 s[10:11], vcc
	s_xor_b64 s[10:11], exec, s[10:11]
	v_add_u32_e32 v4, 0x7ffff002, v74
	v_and_b32_e32 v4, 0x7fffff00, v4
	v_or3_b32 v4, v17, v4, s37
	s_andn2_saveexec_b64 s[10:11], s[10:11]
	v_add_u32_e32 v4, 2, v74
	v_and_or_b32 v4, v4, s38, v17
	s_or_b64 exec, exec, s[10:11]
	v_perm_b32 v68, v8, v5, s28
	v_ashrrev_i32_e32 v5, 31, v4
	v_lshlrev_b64 v[4:5], 11, v[4:5]
	v_perm_b32 v69, v11, v9, s28
	v_perm_b32 v70, v13, v12, s28
	v_perm_b32 v71, v16, v15, s28
	v_lshl_add_u64 v[4:5], v[2:3], 0, v[4:5]
	global_store_dwordx4 v[4:5], v[68:71], off nt
	v_add_u32_e32 v4, 2, v75
	v_cmp_lt_i32_e32 vcc, s36, v4
	v_and_b32_e32 v5, 0x7e, v4
	s_and_saveexec_b64 s[10:11], vcc
	s_xor_b64 s[10:11], exec, s[10:11]
	v_add_u32_e32 v4, 0x7ffff004, v74
	v_and_b32_e32 v4, 0x7fffff00, v4
	v_or3_b32 v4, v5, v4, s37
	s_andn2_saveexec_b64 s[10:11], s[10:11]
	v_add_u32_e32 v4, 4, v74
	v_and_or_b32 v4, v4, s38, v5
	s_or_b64 exec, exec, s[10:11]
	v_ashrrev_i32_e32 v5, 31, v4
	v_perm_b32 v8, v58, v62, s26
	v_perm_b32 v9, v50, v54, s26
	v_perm_b32 v11, v42, v46, s26
	v_perm_b32 v12, v34, v38, s26
	v_perm_b32 v13, v26, v30, s26
	v_perm_b32 v15, v18, v22, s26
	v_perm_b32 v10, v10, v14, s26
	v_perm_b32 v6, v7, v6, s26
	v_lshlrev_b64 v[4:5], 11, v[4:5]
	v_perm_b32 v16, v9, v8, s27
	v_perm_b32 v17, v12, v11, s27
	v_perm_b32 v18, v15, v13, s27
	v_perm_b32 v19, v6, v10, s27
	v_lshl_add_u64 v[4:5], v[2:3], 0, v[4:5]
	global_store_dwordx4 v[4:5], v[16:19], off nt
	v_add_u32_e32 v4, 3, v75
	v_cmp_lt_i32_e32 vcc, s36, v4
	v_and_b32_e32 v5, 0x7f, v4
	s_and_saveexec_b64 s[10:11], vcc
	s_xor_b64 s[10:11], exec, s[10:11]
	v_add_u32_e32 v4, 0x7ffff006, v74
	v_and_b32_e32 v4, 0x7fffff00, v4
	v_or3_b32 v4, v5, v4, s37
	s_andn2_saveexec_b64 s[10:11], s[10:11]
	v_add_u32_e32 v4, 6, v74
	v_and_or_b32 v4, v4, s38, v5
	s_or_b64 exec, exec, s[10:11]
	v_ashrrev_i32_e32 v5, 31, v4
	v_lshlrev_b64 v[4:5], 11, v[4:5]
	v_perm_b32 v16, v9, v8, s28
	v_perm_b32 v17, v12, v11, s28
	v_perm_b32 v18, v15, v13, s28
	v_perm_b32 v19, v6, v10, s28
	v_lshl_add_u64 v[2:3], v[2:3], 0, v[4:5]
	global_store_dwordx4 v[2:3], v[16:19], off nt
	s_ashr_i32 s10, s2, 31
	s_lshr_b32 s10, s10, 26
	s_add_i32 s10, s2, s10
	s_ashr_i32 s41, s10, 6
	s_andn2_b32 s10, s10, 63
	v_or_b32_e32 v68, s10, v1
	v_ashrrev_i32_e32 v69, 31, v68
	s_lshl_b32 s10, s41, 12
	v_lshlrev_b64 v[2:3], 14, v[68:69]
	s_sub_i32 s10, s39, s10
	v_lshl_add_u64 v[2:3], s[6:7], 0, v[2:3]
	s_ashr_i32 s11, s10, 31
	v_lshl_add_u64 v[2:3], s[10:11], 2, v[2:3]
	v_lshl_add_u64 v[2:3], v[2:3], 0, v[66:67]
	v_add_co_u32_e32 v4, vcc, s1, v2
	v_add_u32_e32 v75, s10, v130
	s_nop 0
	v_addc_co_u32_e32 v5, vcc, 0, v3, vcc
	global_load_dwordx4 v[62:65], v[2:3], off nt
	global_load_dwordx4 v[58:61], v[4:5], off nt
	v_add_co_u32_e32 v4, vcc, s12, v2
	v_add_u32_e32 v70, s40, v73
	s_nop 0
	v_addc_co_u32_e32 v5, vcc, 0, v3, vcc
	v_add_co_u32_e32 v6, vcc, s14, v2
	s_lshl_b32 s10, s41, 13
	s_nop 0
	v_addc_co_u32_e32 v7, vcc, 0, v3, vcc
	global_load_dwordx4 v[54:57], v[4:5], off nt
	global_load_dwordx4 v[50:53], v[6:7], off nt
	v_add_co_u32_e32 v4, vcc, s16, v2
	v_subrev_u32_e32 v74, s10, v70
	s_nop 0
	v_addc_co_u32_e32 v5, vcc, 0, v3, vcc
	v_add_co_u32_e32 v6, vcc, s18, v2
	v_and_b32_e32 v71, 0x7c, v75
	s_nop 0
	v_addc_co_u32_e32 v7, vcc, 0, v3, vcc
	global_load_dwordx4 v[46:49], v[4:5], off nt
	global_load_dwordx4 v[42:45], v[6:7], off nt
	v_add_co_u32_e32 v4, vcc, s20, v2
	s_nop 1
	v_addc_co_u32_e32 v5, vcc, 0, v3, vcc
	v_add_co_u32_e32 v6, vcc, s22, v2
	s_nop 1
	v_addc_co_u32_e32 v7, vcc, 0, v3, vcc
	global_load_dwordx4 v[38:41], v[4:5], off nt
	global_load_dwordx4 v[34:37], v[6:7], off nt
	v_add_co_u32_e32 v4, vcc, s29, v2
	s_nop 1
	v_addc_co_u32_e32 v5, vcc, 0, v3, vcc
	v_add_co_u32_e32 v6, vcc, s30, v2
	s_nop 1
	v_addc_co_u32_e32 v7, vcc, 0, v3, vcc
	global_load_dwordx4 v[30:33], v[4:5], off nt
	global_load_dwordx4 v[26:29], v[6:7], off nt
	v_add_co_u32_e32 v4, vcc, s31, v2
	s_nop 1
	v_addc_co_u32_e32 v5, vcc, 0, v3, vcc
	v_add_co_u32_e32 v6, vcc, s33, v2
	s_nop 1
	v_addc_co_u32_e32 v7, vcc, 0, v3, vcc
	global_load_dwordx4 v[22:25], v[4:5], off nt
	global_load_dwordx4 v[18:21], v[6:7], off nt
	v_add_co_u32_e32 v4, vcc, s34, v2
	s_nop 1
	v_addc_co_u32_e32 v5, vcc, 0, v3, vcc
	v_add_co_u32_e32 v6, vcc, s35, v2
	s_nop 1
	v_addc_co_u32_e32 v7, vcc, 0, v3, vcc
	global_load_dwordx4 v[14:17], v[4:5], off nt
	global_load_dwordx4 v[10:13], v[6:7], off nt
	v_add_co_u32_e32 v4, vcc, 0x38000, v2
	s_nop 1
	v_addc_co_u32_e32 v5, vcc, 0, v3, vcc
	v_add_co_u32_e32 v2, vcc, 0x3c000, v2
	s_nop 1
	v_addc_co_u32_e32 v3, vcc, 0, v3, vcc
	global_load_dwordx4 v[6:9], v[4:5], off nt
	s_nop 0
	global_load_dwordx4 v[2:5], v[2:3], off nt
	s_addk_i32 s40, 0x80
	s_add_i32 s39, s39, 64
	s_add_i32 s2, s2, 1
	v_cmp_lt_i32_e32 vcc, s36, v129
	s_and_saveexec_b64 s[10:11], vcc
	s_xor_b64 s[10:11], exec, s[10:11]
	v_add_u32_e32 v150, 0x7ffff000, v128
	v_and_b32_e32 v150, 0x7fffff00, v150
	v_or3_b32 v150, v151, v150, s37
	s_andn2_saveexec_b64 s[10:11], s[10:11]
	v_and_or_b32 v150, v128, s38, v151
	s_or_b64 exec, exec, s[10:11]
	s_waitcnt vmcnt(35)
; __device__ __forceinline__ unsigned pk4_fp8(float a, float b, float c, float d) {
;     a = __builtin_fminf(__builtin_fmaxf(a, -448.f), 448.f); b = __builtin_fminf(__builtin_fmaxf(b, -448.f), 448.f); c = __builtin_fminf(__builtin_fmaxf(c, -448.f), 448.f); d = __builtin_fminf(__builtin_fmaxf(d, -448.f), 448.f);
;     int w = 0; w = __builtin_amdgcn_cvt_pk_fp8_f32(a, b, w, false); w = __builtin_amdgcn_cvt_pk_fp8_f32(c, d, w, true); return (unsigned)w;
; template <int MODE> __device__ __forceinline__ void cv_finish(const f32x4 (&tv)[16], int K, int nblk, unsigned char* WT, int item, int lane) {
;     const int kb = item / nblk, nb = item - kb * nblk, k0 = 64 * kb + 16 * (lane >> 4), n0 = 64 * nb + 4 * (lane & 15);
;     unsigned D[16];
; #pragma unroll
;     for (int i = 0; i < 16; ++i) { const f32x2 a = (f32x2){tv[i].x, tv[i].y} * (f32x2){1024.f, 1024.f}, b = (f32x2){tv[i].z, tv[i].w} * (f32x2){1024.f, 1024.f};
;         D[i] = pk4_fp8(a.x, a.y, b.x, b.y); }
	v_pk_mul_f32 v[144:145], v[144:145], s[4:5] op_sel_hi:[1,0]
	v_pk_mul_f32 v[146:147], v[146:147], s[4:5] op_sel_hi:[1,0]
	v_med3_f32 v151, v144, s24, v72
	v_med3_f32 v145, v145, s24, v72
	v_mov_b32_e32 v144, v67
	v_cvt_pk_fp8_f32 v144, v151, v145
	v_med3_f32 v145, v146, s24, v72
	v_med3_f32 v146, v147, s24, v72
	s_waitcnt vmcnt(34)
	v_pk_mul_f32 v[140:141], v[140:141], s[4:5] op_sel_hi:[1,0]
	v_cvt_pk_fp8_f32 v144, v145, v146 op_sel:[0,0,1]
	v_med3_f32 v145, v140, s24, v72
	v_med3_f32 v141, v141, s24, v72
	v_mov_b32_e32 v140, v67
	v_cvt_pk_fp8_f32 v140, v145, v141
	v_pk_mul_f32 v[142:143], v[142:143], s[4:5] op_sel_hi:[1,0]
	s_waitcnt vmcnt(33)
	v_pk_mul_f32 v[136:137], v[136:137], s[4:5] op_sel_hi:[1,0]
	v_med3_f32 v141, v142, s24, v72
	v_med3_f32 v142, v143, s24, v72
	v_cvt_pk_fp8_f32 v140, v141, v142 op_sel:[0,0,1]
	v_med3_f32 v141, v136, s24, v72
	v_med3_f32 v137, v137, s24, v72
	v_mov_b32_e32 v136, v67
	v_cvt_pk_fp8_f32 v136, v141, v137
	v_pk_mul_f32 v[138:139], v[138:139], s[4:5] op_sel_hi:[1,0]
	s_waitcnt vmcnt(32)
	v_pk_mul_f32 v[132:133], v[132:133], s[4:5] op_sel_hi:[1,0]
	v_med3_f32 v137, v138, s24, v72
	v_med3_f32 v138, v139, s24, v72
	v_cvt_pk_fp8_f32 v136, v137, v138 op_sel:[0,0,1]
	v_med3_f32 v137, v132, s24, v72
	v_med3_f32 v133, v133, s24, v72
	v_mov_b32_e32 v132, v67
	v_cvt_pk_fp8_f32 v132, v137, v133
	v_pk_mul_f32 v[134:135], v[134:135], s[4:5] op_sel_hi:[1,0]
	s_waitcnt vmcnt(31)
	v_pk_mul_f32 v[124:125], v[124:125], s[4:5] op_sel_hi:[1,0]
	v_med3_f32 v133, v134, s24, v72
	v_med3_f32 v134, v135, s24, v72
	v_cvt_pk_fp8_f32 v132, v133, v134 op_sel:[0,0,1]
	v_med3_f32 v133, v124, s24, v72
	v_med3_f32 v125, v125, s24, v72
	v_mov_b32_e32 v124, v67
	v_cvt_pk_fp8_f32 v124, v133, v125
	v_pk_mul_f32 v[126:127], v[126:127], s[4:5] op_sel_hi:[1,0]
	s_waitcnt vmcnt(30)
	v_pk_mul_f32 v[120:121], v[120:121], s[4:5] op_sel_hi:[1,0]
	v_med3_f32 v125, v126, s24, v72
	v_med3_f32 v126, v127, s24, v72
	v_cvt_pk_fp8_f32 v124, v125, v126 op_sel:[0,0,1]
	v_med3_f32 v125, v120, s24, v72
	v_med3_f32 v121, v121, s24, v72
	v_mov_b32_e32 v120, v67
	v_cvt_pk_fp8_f32 v120, v125, v121
	v_pk_mul_f32 v[122:123], v[122:123], s[4:5] op_sel_hi:[1,0]
	s_waitcnt vmcnt(29)
	v_pk_mul_f32 v[116:117], v[116:117], s[4:5] op_sel_hi:[1,0]
	v_med3_f32 v121, v122, s24, v72
	v_med3_f32 v122, v123, s24, v72
	v_cvt_pk_fp8_f32 v120, v121, v122 op_sel:[0,0,1]
	v_med3_f32 v121, v116, s24, v72
	v_med3_f32 v117, v117, s24, v72
	v_mov_b32_e32 v116, v67
	v_cvt_pk_fp8_f32 v116, v121, v117
	v_pk_mul_f32 v[118:119], v[118:119], s[4:5] op_sel_hi:[1,0]
	s_waitcnt vmcnt(28)
	v_pk_mul_f32 v[112:113], v[112:113], s[4:5] op_sel_hi:[1,0]
	v_med3_f32 v117, v118, s24, v72
	v_med3_f32 v118, v119, s24, v72
	v_cvt_pk_fp8_f32 v116, v117, v118 op_sel:[0,0,1]
	v_med3_f32 v117, v112, s24, v72
	v_med3_f32 v113, v113, s24, v72
	v_mov_b32_e32 v112, v67
	v_cvt_pk_fp8_f32 v112, v117, v113
	v_pk_mul_f32 v[114:115], v[114:115], s[4:5] op_sel_hi:[1,0]
	s_waitcnt vmcnt(27)
	v_pk_mul_f32 v[108:109], v[108:109], s[4:5] op_sel_hi:[1,0]
	v_med3_f32 v113, v114, s24, v72
	v_med3_f32 v114, v115, s24, v72
	v_cvt_pk_fp8_f32 v112, v113, v114 op_sel:[0,0,1]
	v_med3_f32 v113, v108, s24, v72
	v_med3_f32 v109, v109, s24, v72
	v_mov_b32_e32 v108, v67
	v_cvt_pk_fp8_f32 v108, v113, v109
	v_pk_mul_f32 v[110:111], v[110:111], s[4:5] op_sel_hi:[1,0]
	s_waitcnt vmcnt(26)
	v_pk_mul_f32 v[104:105], v[104:105], s[4:5] op_sel_hi:[1,0]
	v_med3_f32 v109, v110, s24, v72
	v_med3_f32 v110, v111, s24, v72
	v_cvt_pk_fp8_f32 v108, v109, v110 op_sel:[0,0,1]
	v_med3_f32 v109, v104, s24, v72
	v_med3_f32 v105, v105, s24, v72
	v_mov_b32_e32 v104, v67
	v_cvt_pk_fp8_f32 v104, v109, v105
	v_pk_mul_f32 v[106:107], v[106:107], s[4:5] op_sel_hi:[1,0]
	s_waitcnt vmcnt(25)
	v_pk_mul_f32 v[100:101], v[100:101], s[4:5] op_sel_hi:[1,0]
	v_med3_f32 v105, v106, s24, v72
	v_med3_f32 v106, v107, s24, v72
	v_cvt_pk_fp8_f32 v104, v105, v106 op_sel:[0,0,1]
	v_med3_f32 v105, v100, s24, v72
	v_med3_f32 v101, v101, s24, v72
	v_mov_b32_e32 v100, v67
	v_cvt_pk_fp8_f32 v100, v105, v101
	v_pk_mul_f32 v[102:103], v[102:103], s[4:5] op_sel_hi:[1,0]
	s_waitcnt vmcnt(24)
	v_pk_mul_f32 v[96:97], v[96:97], s[4:5] op_sel_hi:[1,0]
	v_med3_f32 v101, v102, s24, v72
	v_med3_f32 v102, v103, s24, v72
	v_cvt_pk_fp8_f32 v100, v101, v102 op_sel:[0,0,1]
	v_med3_f32 v101, v96, s24, v72
	v_med3_f32 v97, v97, s24, v72
	v_mov_b32_e32 v96, v67
	v_cvt_pk_fp8_f32 v96, v101, v97
	v_pk_mul_f32 v[98:99], v[98:99], s[4:5] op_sel_hi:[1,0]
	s_waitcnt vmcnt(23)
	v_pk_mul_f32 v[92:93], v[92:93], s[4:5] op_sel_hi:[1,0]
	v_med3_f32 v97, v98, s24, v72
	v_med3_f32 v98, v99, s24, v72
	v_cvt_pk_fp8_f32 v96, v97, v98 op_sel:[0,0,1]
	v_med3_f32 v97, v92, s24, v72
	v_med3_f32 v93, v93, s24, v72
	v_mov_b32_e32 v92, v67
	v_cvt_pk_fp8_f32 v92, v97, v93
	v_pk_mul_f32 v[94:95], v[94:95], s[4:5] op_sel_hi:[1,0]
	s_waitcnt vmcnt(22)
	v_pk_mul_f32 v[88:89], v[88:89], s[4:5] op_sel_hi:[1,0]
	v_med3_f32 v93, v94, s24, v72
	v_med3_f32 v94, v95, s24, v72
	v_cvt_pk_fp8_f32 v92, v93, v94 op_sel:[0,0,1]
	v_med3_f32 v93, v88, s24, v72
	v_med3_f32 v89, v89, s24, v72
	v_mov_b32_e32 v88, v67
	v_cvt_pk_fp8_f32 v88, v93, v89
	v_pk_mul_f32 v[90:91], v[90:91], s[4:5] op_sel_hi:[1,0]
	s_waitcnt vmcnt(21)
	v_pk_mul_f32 v[84:85], v[84:85], s[4:5] op_sel_hi:[1,0]
	v_med3_f32 v89, v90, s24, v72
	v_med3_f32 v90, v91, s24, v72
	v_cvt_pk_fp8_f32 v88, v89, v90 op_sel:[0,0,1]
	v_med3_f32 v89, v84, s24, v72
	v_med3_f32 v85, v85, s24, v72
	v_mov_b32_e32 v84, v67
	v_cvt_pk_fp8_f32 v84, v89, v85
	v_pk_mul_f32 v[86:87], v[86:87], s[4:5] op_sel_hi:[1,0]
	s_waitcnt vmcnt(20)
; template <int MODE> __device__ __forceinline__ int drow(int n) {
;     if (MODE == 1) { const int h = n / 192, nl = n - h * 192; return nl < 128 ? n : h * 192 + 128 + ((nl - 128) & 31) * 2 + ((nl - 128) >> 5); }
;     if (MODE == 2) { return n < FF ? ((n >> 7) * 256 + (n & 127)) : (((n - FF) >> 7) * 256 + 128 + ((n - FF) & 127)); }
; __device__ __forceinline__ void cv_load(const float* W, int N, int nblk, int item, int lane, f32x4 (&tv)[16]) {
;     const int kb = item / nblk, nb = item - kb * nblk; const float* p = W + (size_t)(64 * kb + 16 * (lane >> 4)) * N + 64 * nb + 4 * (lane & 15);
; #pragma unroll
;     for (int i = 0; i < 16; ++i) tv[i] = __builtin_nontemporal_load((const f32x4*)(p + (size_t)i * N));
; }
; template <int MODE> __device__ __forceinline__ void cv_finish(const f32x4 (&tv)[16], int K, int nblk, unsigned char* WT, int item, int lane) {
;     const int kb = item / nblk, nb = item - kb * nblk, k0 = 64 * kb + 16 * (lane >> 4), n0 = 64 * nb + 4 * (lane & 15);
;     unsigned D[16];
; #pragma unroll
;     for (int i = 0; i < 16; ++i) { const f32x2 a = (f32x2){tv[i].x, tv[i].y} * (f32x2){1024.f, 1024.f}, b = (f32x2){tv[i].z, tv[i].w} * (f32x2){1024.f, 1024.f};
;         D[i] = pk4_fp8(a.x, a.y, b.x, b.y); }
;     unsigned O[4][4];
; #pragma unroll
;     for (int q = 0; q < 4; ++q) { const unsigned a = D[4 * q], b = D[4 * q + 1], c = D[4 * q + 2], d = D[4 * q + 3];
;         const unsigned t0 = __builtin_amdgcn_perm(b, a, 0x05010400u), t1 = __builtin_amdgcn_perm(b, a, 0x07030602u), u0 = __builtin_amdgcn_perm(d, c, 0x05010400u), u1 = __builtin_amdgcn_perm(d, c, 0x07030602u);
;         O[0][q] = __builtin_amdgcn_perm(u0, t0, 0x05040100u); O[1][q] = __builtin_amdgcn_perm(u0, t0, 0x07060302u); O[2][q] = __builtin_amdgcn_perm(u1, t1, 0x05040100u); O[3][q] = __builtin_amdgcn_perm(u1, t1, 0x07060302u); }
; #pragma unroll
;     for (int j = 0; j < 4; ++j) { u32x4 o; o.x = O[j][0]; o.y = O[j][1]; o.z = O[j][2]; o.w = O[j][3];
;         __builtin_nontemporal_store(o, (u32x4*)(WT + (size_t)drow<MODE>(n0 + j) * K + k0)); }
; }
; template <int MODE> __device__ __forceinline__ void cv_run4(const float* W, int K, int N, unsigned char* WT, int item0, int lane) {
;     const int nblk = N / 64; f32x4 ta[16];
; #pragma unroll 1
;     for (int j = 0; j < 4; ++j) { cv_load(W, N, nblk, item0 + j, lane, ta); cv_finish<MODE>(ta, K, nblk, WT, item0 + j, lane); }
	v_pk_mul_f32 v[80:81], v[80:81], s[4:5] op_sel_hi:[1,0]
	v_med3_f32 v85, v86, s24, v72
	v_med3_f32 v86, v87, s24, v72
	v_cvt_pk_fp8_f32 v84, v85, v86 op_sel:[0,0,1]
	v_med3_f32 v80, v80, s24, v72
	v_med3_f32 v81, v81, s24, v72
	v_mov_b32_e32 v85, v67
	v_cvt_pk_fp8_f32 v85, v80, v81
	v_pk_mul_f32 v[80:81], v[82:83], s[4:5] op_sel_hi:[1,0]
	v_ashrrev_i32_e32 v151, 31, v150
	v_med3_f32 v80, v80, s24, v72
	v_med3_f32 v81, v81, s24, v72
	v_cvt_pk_fp8_f32 v85, v80, v81 op_sel:[0,0,1]
	v_perm_b32 v83, v140, v144, s25
	v_perm_b32 v86, v132, v136, s25
	v_perm_b32 v87, v120, v124, s25
	v_perm_b32 v89, v112, v116, s25
	v_perm_b32 v90, v104, v108, s25
	v_perm_b32 v91, v96, v100, s25
	v_perm_b32 v93, v88, v92, s25
	v_perm_b32 v94, v85, v84, s25
	v_lshl_add_u64 v[80:81], s[8:9], 0, v[148:149]
	v_lshlrev_b64 v[98:99], 11, v[150:151]
	v_add_u32_e32 v82, 1, v129
	v_perm_b32 v152, v86, v83, s27
	v_perm_b32 v153, v89, v87, s27
	v_perm_b32 v154, v91, v90, s27
	v_perm_b32 v155, v94, v93, s27
	v_lshl_add_u64 v[98:99], v[80:81], 0, v[98:99]
	v_cmp_lt_i32_e32 vcc, s36, v82
	v_and_b32_e32 v95, 0x7d, v82
	global_store_dwordx4 v[98:99], v[152:155], off nt
	s_and_saveexec_b64 s[10:11], vcc
	s_xor_b64 s[10:11], exec, s[10:11]
	v_add_u32_e32 v82, 0x7ffff002, v128
	v_and_b32_e32 v82, 0x7fffff00, v82
	v_or3_b32 v82, v95, v82, s37
	s_andn2_saveexec_b64 s[10:11], s[10:11]
	v_add_u32_e32 v82, 2, v128
	v_and_or_b32 v82, v82, s38, v95
	s_or_b64 exec, exec, s[10:11]
	v_perm_b32 v148, v86, v83, s28
	v_ashrrev_i32_e32 v83, 31, v82
	v_lshlrev_b64 v[82:83], 11, v[82:83]
	v_perm_b32 v149, v89, v87, s28
	v_perm_b32 v150, v91, v90, s28
	v_perm_b32 v151, v94, v93, s28
	v_lshl_add_u64 v[82:83], v[80:81], 0, v[82:83]
	global_store_dwordx4 v[82:83], v[148:151], off nt
	v_add_u32_e32 v82, 2, v129
	v_cmp_lt_i32_e32 vcc, s36, v82
	v_and_b32_e32 v83, 0x7e, v82
	s_and_saveexec_b64 s[10:11], vcc
	s_xor_b64 s[10:11], exec, s[10:11]
	v_add_u32_e32 v82, 0x7ffff004, v128
	v_and_b32_e32 v82, 0x7fffff00, v82
	v_or3_b32 v82, v83, v82, s37
	s_andn2_saveexec_b64 s[10:11], s[10:11]
	v_add_u32_e32 v82, 4, v128
	v_and_or_b32 v82, v82, s38, v83
	s_or_b64 exec, exec, s[10:11]
	v_ashrrev_i32_e32 v83, 31, v82
	v_perm_b32 v86, v140, v144, s26
	v_perm_b32 v87, v132, v136, s26
	v_perm_b32 v89, v120, v124, s26
	v_perm_b32 v90, v112, v116, s26
	v_perm_b32 v91, v104, v108, s26
	v_perm_b32 v93, v96, v100, s26
	v_perm_b32 v88, v88, v92, s26
	v_perm_b32 v84, v85, v84, s26
	v_lshlrev_b64 v[82:83], 11, v[82:83]
	v_perm_b32 v94, v87, v86, s27
	v_perm_b32 v95, v90, v89, s27
	v_perm_b32 v96, v93, v91, s27
	v_perm_b32 v97, v84, v88, s27
	v_lshl_add_u64 v[82:83], v[80:81], 0, v[82:83]
	global_store_dwordx4 v[82:83], v[94:97], off nt
	v_add_u32_e32 v82, 3, v129
	v_cmp_lt_i32_e32 vcc, s36, v82
	v_and_b32_e32 v83, 0x7f, v82
	s_and_saveexec_b64 s[10:11], vcc
	s_xor_b64 s[10:11], exec, s[10:11]
	v_add_u32_e32 v82, 0x7ffff006, v128
	v_and_b32_e32 v82, 0x7fffff00, v82
	v_or3_b32 v82, v83, v82, s37
	s_andn2_saveexec_b64 s[10:11], s[10:11]
	v_add_u32_e32 v82, 6, v128
	v_and_or_b32 v82, v82, s38, v83
	s_or_b64 exec, exec, s[10:11]
	v_ashrrev_i32_e32 v83, 31, v82
	v_lshlrev_b64 v[82:83], 11, v[82:83]
	v_perm_b32 v94, v87, v86, s28
	v_perm_b32 v95, v90, v89, s28
	v_perm_b32 v96, v93, v91, s28
	v_perm_b32 v97, v84, v88, s28
	v_lshl_add_u64 v[80:81], v[80:81], 0, v[82:83]
	global_store_dwordx4 v[80:81], v[94:97], off nt
	s_ashr_i32 s10, s2, 31
	s_lshr_b32 s10, s10, 26
	s_add_i32 s10, s2, s10
	s_ashr_i32 s41, s10, 6
	s_andn2_b32 s10, s10, 63
	v_or_b32_e32 v148, s10, v1
	v_ashrrev_i32_e32 v149, 31, v148
	s_lshl_b32 s10, s41, 12
	v_lshlrev_b64 v[80:81], 14, v[148:149]
	s_sub_i32 s10, s39, s10
	v_lshl_add_u64 v[80:81], s[6:7], 0, v[80:81]
	s_ashr_i32 s11, s10, 31
	v_lshl_add_u64 v[80:81], s[10:11], 2, v[80:81]
	v_lshl_add_u64 v[80:81], v[80:81], 0, v[66:67]
	v_add_co_u32_e32 v82, vcc, s1, v80
	v_add_u32_e32 v129, s10, v130
	s_nop 0
	v_addc_co_u32_e32 v83, vcc, 0, v81, vcc
	global_load_dwordx4 v[144:147], v[80:81], off nt
	global_load_dwordx4 v[140:143], v[82:83], off nt
	v_add_co_u32_e32 v82, vcc, s12, v80
	v_add_u32_e32 v150, s40, v73
	s_nop 0
	v_addc_co_u32_e32 v83, vcc, 0, v81, vcc
	v_add_co_u32_e32 v84, vcc, s14, v80
	s_lshl_b32 s10, s41, 13
	s_nop 0
	v_addc_co_u32_e32 v85, vcc, 0, v81, vcc
	global_load_dwordx4 v[136:139], v[82:83], off nt
	global_load_dwordx4 v[132:135], v[84:85], off nt
	v_add_co_u32_e32 v82, vcc, s16, v80
	v_subrev_u32_e32 v128, s10, v150
	s_nop 0
	v_addc_co_u32_e32 v83, vcc, 0, v81, vcc
	v_add_co_u32_e32 v84, vcc, s18, v80
	v_and_b32_e32 v151, 0x7c, v129
	s_nop 0
	v_addc_co_u32_e32 v85, vcc, 0, v81, vcc
	global_load_dwordx4 v[124:127], v[82:83], off nt
	global_load_dwordx4 v[120:123], v[84:85], off nt
	v_add_co_u32_e32 v82, vcc, s20, v80
	s_nop 1
	v_addc_co_u32_e32 v83, vcc, 0, v81, vcc
	v_add_co_u32_e32 v84, vcc, s22, v80
	s_nop 1
	v_addc_co_u32_e32 v85, vcc, 0, v81, vcc
	global_load_dwordx4 v[116:119], v[82:83], off nt
	global_load_dwordx4 v[112:115], v[84:85], off nt
	v_add_co_u32_e32 v82, vcc, s29, v80
	s_nop 1
	v_addc_co_u32_e32 v83, vcc, 0, v81, vcc
	v_add_co_u32_e32 v84, vcc, s30, v80
	s_nop 1
	v_addc_co_u32_e32 v85, vcc, 0, v81, vcc
	global_load_dwordx4 v[108:111], v[82:83], off nt
	global_load_dwordx4 v[104:107], v[84:85], off nt
	v_add_co_u32_e32 v82, vcc, s31, v80
	s_nop 1
	v_addc_co_u32_e32 v83, vcc, 0, v81, vcc
	v_add_co_u32_e32 v84, vcc, s33, v80
	s_nop 1
	v_addc_co_u32_e32 v85, vcc, 0, v81, vcc
	global_load_dwordx4 v[100:103], v[82:83], off nt
	global_load_dwordx4 v[96:99], v[84:85], off nt
	v_add_co_u32_e32 v82, vcc, s34, v80
	s_nop 1
	v_addc_co_u32_e32 v83, vcc, 0, v81, vcc
	v_add_co_u32_e32 v84, vcc, s35, v80
	s_nop 1
	v_addc_co_u32_e32 v85, vcc, 0, v81, vcc
	global_load_dwordx4 v[92:95], v[82:83], off nt
	global_load_dwordx4 v[88:91], v[84:85], off nt
	v_add_co_u32_e32 v82, vcc, 0x38000, v80
	s_nop 1
	v_addc_co_u32_e32 v83, vcc, 0, v81, vcc
	v_add_co_u32_e32 v80, vcc, 0x3c000, v80
	s_nop 1
	v_addc_co_u32_e32 v81, vcc, 0, v81, vcc
	global_load_dwordx4 v[84:87], v[82:83], off nt
	s_nop 0
	global_load_dwordx4 v[80:83], v[80:81], off nt
	s_addk_i32 s40, 0x80
	s_add_i32 s39, s39, 64
	s_add_i32 s2, s2, 1
	v_cmp_lt_i32_e32 vcc, s36, v75
	s_and_saveexec_b64 s[10:11], vcc
	s_xor_b64 s[10:11], exec, s[10:11]
	v_add_u32_e32 v70, 0x7ffff000, v74
	v_and_b32_e32 v70, 0x7fffff00, v70
	v_or3_b32 v70, v71, v70, s37
	s_andn2_saveexec_b64 s[10:11], s[10:11]
	v_and_or_b32 v70, v74, s38, v71
	s_or_b64 exec, exec, s[10:11]
	s_waitcnt vmcnt(35)
; __device__ __forceinline__ unsigned pk4_fp8(float a, float b, float c, float d) {
;     a = __builtin_fminf(__builtin_fmaxf(a, -448.f), 448.f); b = __builtin_fminf(__builtin_fmaxf(b, -448.f), 448.f); c = __builtin_fminf(__builtin_fmaxf(c, -448.f), 448.f); d = __builtin_fminf(__builtin_fmaxf(d, -448.f), 448.f);
;     int w = 0; w = __builtin_amdgcn_cvt_pk_fp8_f32(a, b, w, false); w = __builtin_amdgcn_cvt_pk_fp8_f32(c, d, w, true); return (unsigned)w;
; }
; template <int MODE> __device__ __forceinline__ void cv_finish(const f32x4 (&tv)[16], int K, int nblk, unsigned char* WT, int item, int lane) {
;     const int kb = item / nblk, nb = item - kb * nblk, k0 = 64 * kb + 16 * (lane >> 4), n0 = 64 * nb + 4 * (lane & 15);
;     unsigned D[16];
; #pragma unroll
;     for (int i = 0; i < 16; ++i) { const f32x2 a = (f32x2){tv[i].x, tv[i].y} * (f32x2){1024.f, 1024.f}, b = (f32x2){tv[i].z, tv[i].w} * (f32x2){1024.f, 1024.f};
;         D[i] = pk4_fp8(a.x, a.y, b.x, b.y); }
	v_pk_mul_f32 v[62:63], v[62:63], s[4:5] op_sel_hi:[1,0]
	v_pk_mul_f32 v[64:65], v[64:65], s[4:5] op_sel_hi:[1,0]
	v_med3_f32 v71, v62, s24, v72
	v_med3_f32 v63, v63, s24, v72
	v_mov_b32_e32 v62, v67
	v_cvt_pk_fp8_f32 v62, v71, v63
	v_med3_f32 v63, v64, s24, v72
	v_med3_f32 v64, v65, s24, v72
	s_waitcnt vmcnt(34)
	v_pk_mul_f32 v[58:59], v[58:59], s[4:5] op_sel_hi:[1,0]
	v_cvt_pk_fp8_f32 v62, v63, v64 op_sel:[0,0,1]
	v_med3_f32 v63, v58, s24, v72
	v_med3_f32 v59, v59, s24, v72
	v_mov_b32_e32 v58, v67
	v_cvt_pk_fp8_f32 v58, v63, v59
	v_pk_mul_f32 v[60:61], v[60:61], s[4:5] op_sel_hi:[1,0]
	s_waitcnt vmcnt(33)
	v_pk_mul_f32 v[54:55], v[54:55], s[4:5] op_sel_hi:[1,0]
	v_med3_f32 v59, v60, s24, v72
	v_med3_f32 v60, v61, s24, v72
	v_cvt_pk_fp8_f32 v58, v59, v60 op_sel:[0,0,1]
	v_med3_f32 v59, v54, s24, v72
	v_med3_f32 v55, v55, s24, v72
	v_mov_b32_e32 v54, v67
	v_cvt_pk_fp8_f32 v54, v59, v55
	v_pk_mul_f32 v[56:57], v[56:57], s[4:5] op_sel_hi:[1,0]
	s_waitcnt vmcnt(32)
	v_pk_mul_f32 v[50:51], v[50:51], s[4:5] op_sel_hi:[1,0]
	v_med3_f32 v55, v56, s24, v72
	v_med3_f32 v56, v57, s24, v72
	v_cvt_pk_fp8_f32 v54, v55, v56 op_sel:[0,0,1]
	v_med3_f32 v55, v50, s24, v72
	v_med3_f32 v51, v51, s24, v72
	v_mov_b32_e32 v50, v67
	v_cvt_pk_fp8_f32 v50, v55, v51
	v_pk_mul_f32 v[52:53], v[52:53], s[4:5] op_sel_hi:[1,0]
	s_waitcnt vmcnt(31)
	v_pk_mul_f32 v[46:47], v[46:47], s[4:5] op_sel_hi:[1,0]
	v_med3_f32 v51, v52, s24, v72
	v_med3_f32 v52, v53, s24, v72
	v_cvt_pk_fp8_f32 v50, v51, v52 op_sel:[0,0,1]
	v_med3_f32 v51, v46, s24, v72
	v_med3_f32 v47, v47, s24, v72
	v_mov_b32_e32 v46, v67
	v_cvt_pk_fp8_f32 v46, v51, v47
	v_pk_mul_f32 v[48:49], v[48:49], s[4:5] op_sel_hi:[1,0]
	s_waitcnt vmcnt(30)
	v_pk_mul_f32 v[42:43], v[42:43], s[4:5] op_sel_hi:[1,0]
	v_med3_f32 v47, v48, s24, v72
	v_med3_f32 v48, v49, s24, v72
	v_cvt_pk_fp8_f32 v46, v47, v48 op_sel:[0,0,1]
	v_med3_f32 v47, v42, s24, v72
	v_med3_f32 v43, v43, s24, v72
	v_mov_b32_e32 v42, v67
	v_cvt_pk_fp8_f32 v42, v47, v43
	v_pk_mul_f32 v[44:45], v[44:45], s[4:5] op_sel_hi:[1,0]
	s_waitcnt vmcnt(29)
	v_pk_mul_f32 v[38:39], v[38:39], s[4:5] op_sel_hi:[1,0]
	v_med3_f32 v43, v44, s24, v72
	v_med3_f32 v44, v45, s24, v72
	v_cvt_pk_fp8_f32 v42, v43, v44 op_sel:[0,0,1]
	v_med3_f32 v43, v38, s24, v72
	v_med3_f32 v39, v39, s24, v72
	v_mov_b32_e32 v38, v67
	v_cvt_pk_fp8_f32 v38, v43, v39
	v_pk_mul_f32 v[40:41], v[40:41], s[4:5] op_sel_hi:[1,0]
	s_waitcnt vmcnt(28)
	v_pk_mul_f32 v[34:35], v[34:35], s[4:5] op_sel_hi:[1,0]
	v_med3_f32 v39, v40, s24, v72
	v_med3_f32 v40, v41, s24, v72
	v_cvt_pk_fp8_f32 v38, v39, v40 op_sel:[0,0,1]
	v_med3_f32 v39, v34, s24, v72
	v_med3_f32 v35, v35, s24, v72
	v_mov_b32_e32 v34, v67
	v_cvt_pk_fp8_f32 v34, v39, v35
	v_pk_mul_f32 v[36:37], v[36:37], s[4:5] op_sel_hi:[1,0]
	s_waitcnt vmcnt(27)
	v_pk_mul_f32 v[30:31], v[30:31], s[4:5] op_sel_hi:[1,0]
	v_med3_f32 v35, v36, s24, v72
	v_med3_f32 v36, v37, s24, v72
	v_cvt_pk_fp8_f32 v34, v35, v36 op_sel:[0,0,1]
	v_med3_f32 v35, v30, s24, v72
	v_med3_f32 v31, v31, s24, v72
	v_mov_b32_e32 v30, v67
	v_cvt_pk_fp8_f32 v30, v35, v31
	v_pk_mul_f32 v[32:33], v[32:33], s[4:5] op_sel_hi:[1,0]
	s_waitcnt vmcnt(26)
	v_pk_mul_f32 v[26:27], v[26:27], s[4:5] op_sel_hi:[1,0]
	v_med3_f32 v31, v32, s24, v72
	v_med3_f32 v32, v33, s24, v72
	v_cvt_pk_fp8_f32 v30, v31, v32 op_sel:[0,0,1]
	v_med3_f32 v31, v26, s24, v72
	v_med3_f32 v27, v27, s24, v72
	v_mov_b32_e32 v26, v67
	v_cvt_pk_fp8_f32 v26, v31, v27
	v_pk_mul_f32 v[28:29], v[28:29], s[4:5] op_sel_hi:[1,0]
	s_waitcnt vmcnt(25)
	v_pk_mul_f32 v[22:23], v[22:23], s[4:5] op_sel_hi:[1,0]
	v_med3_f32 v27, v28, s24, v72
	v_med3_f32 v28, v29, s24, v72
	v_cvt_pk_fp8_f32 v26, v27, v28 op_sel:[0,0,1]
	v_med3_f32 v27, v22, s24, v72
	v_med3_f32 v23, v23, s24, v72
	v_mov_b32_e32 v22, v67
	v_cvt_pk_fp8_f32 v22, v27, v23
	v_pk_mul_f32 v[24:25], v[24:25], s[4:5] op_sel_hi:[1,0]
	s_waitcnt vmcnt(24)
	v_pk_mul_f32 v[18:19], v[18:19], s[4:5] op_sel_hi:[1,0]
	v_med3_f32 v23, v24, s24, v72
	v_med3_f32 v24, v25, s24, v72
	v_cvt_pk_fp8_f32 v22, v23, v24 op_sel:[0,0,1]
	v_med3_f32 v23, v18, s24, v72
	v_med3_f32 v19, v19, s24, v72
	v_mov_b32_e32 v18, v67
	v_cvt_pk_fp8_f32 v18, v23, v19
	v_pk_mul_f32 v[20:21], v[20:21], s[4:5] op_sel_hi:[1,0]
	s_waitcnt vmcnt(23)
	v_pk_mul_f32 v[14:15], v[14:15], s[4:5] op_sel_hi:[1,0]
	v_med3_f32 v19, v20, s24, v72
	v_med3_f32 v20, v21, s24, v72
	v_cvt_pk_fp8_f32 v18, v19, v20 op_sel:[0,0,1]
	v_med3_f32 v19, v14, s24, v72
	v_med3_f32 v15, v15, s24, v72
	v_mov_b32_e32 v14, v67
	v_cvt_pk_fp8_f32 v14, v19, v15
	v_pk_mul_f32 v[16:17], v[16:17], s[4:5] op_sel_hi:[1,0]
	s_waitcnt vmcnt(22)
	v_pk_mul_f32 v[10:11], v[10:11], s[4:5] op_sel_hi:[1,0]
	v_med3_f32 v15, v16, s24, v72
	v_med3_f32 v16, v17, s24, v72
	v_cvt_pk_fp8_f32 v14, v15, v16 op_sel:[0,0,1]
	v_med3_f32 v15, v10, s24, v72
	v_med3_f32 v11, v11, s24, v72
	v_mov_b32_e32 v10, v67
	v_cvt_pk_fp8_f32 v10, v15, v11
	v_pk_mul_f32 v[12:13], v[12:13], s[4:5] op_sel_hi:[1,0]
	s_waitcnt vmcnt(21)
	v_pk_mul_f32 v[6:7], v[6:7], s[4:5] op_sel_hi:[1,0]
	v_med3_f32 v11, v12, s24, v72
	v_med3_f32 v12, v13, s24, v72
	v_cvt_pk_fp8_f32 v10, v11, v12 op_sel:[0,0,1]
	v_med3_f32 v11, v6, s24, v72
	v_med3_f32 v7, v7, s24, v72
	v_mov_b32_e32 v6, v67
	v_cvt_pk_fp8_f32 v6, v11, v7
	v_pk_mul_f32 v[8:9], v[8:9], s[4:5] op_sel_hi:[1,0]
	s_waitcnt vmcnt(20)
; template <int MODE> __device__ __forceinline__ int drow(int n) {
;     if (MODE == 1) { const int h = n / 192, nl = n - h * 192; return nl < 128 ? n : h * 192 + 128 + ((nl - 128) & 31) * 2 + ((nl - 128) >> 5); }
;     if (MODE == 2) { return n < FF ? ((n >> 7) * 256 + (n & 127)) : (((n - FF) >> 7) * 256 + 128 + ((n - FF) & 127)); }
;     return n;
; }
; template <int MODE> __device__ __forceinline__ void cv_finish(const f32x4 (&tv)[16], int K, int nblk, unsigned char* WT, int item, int lane) {
;     const int kb = item / nblk, nb = item - kb * nblk, k0 = 64 * kb + 16 * (lane >> 4), n0 = 64 * nb + 4 * (lane & 15);
;     unsigned D[16];
; #pragma unroll
;     for (int i = 0; i < 16; ++i) { const f32x2 a = (f32x2){tv[i].x, tv[i].y} * (f32x2){1024.f, 1024.f}, b = (f32x2){tv[i].z, tv[i].w} * (f32x2){1024.f, 1024.f};
;         D[i] = pk4_fp8(a.x, a.y, b.x, b.y); }
;     unsigned O[4][4];
; #pragma unroll
;     for (int q = 0; q < 4; ++q) { const unsigned a = D[4 * q], b = D[4 * q + 1], c = D[4 * q + 2], d = D[4 * q + 3];
;         const unsigned t0 = __builtin_amdgcn_perm(b, a, 0x05010400u), t1 = __builtin_amdgcn_perm(b, a, 0x07030602u), u0 = __builtin_amdgcn_perm(d, c, 0x05010400u), u1 = __builtin_amdgcn_perm(d, c, 0x07030602u);
;         O[0][q] = __builtin_amdgcn_perm(u0, t0, 0x05040100u); O[1][q] = __builtin_amdgcn_perm(u0, t0, 0x07060302u); O[2][q] = __builtin_amdgcn_perm(u1, t1, 0x05040100u); O[3][q] = __builtin_amdgcn_perm(u1, t1, 0x07060302u); }
; #pragma unroll
;     for (int j = 0; j < 4; ++j) { u32x4 o; o.x = O[j][0]; o.y = O[j][1]; o.z = O[j][2]; o.w = O[j][3];
;         __builtin_nontemporal_store(o, (u32x4*)(WT + (size_t)drow<MODE>(n0 + j) * K + k0)); }
; }
	v_pk_mul_f32 v[2:3], v[2:3], s[4:5] op_sel_hi:[1,0]
	v_med3_f32 v7, v8, s24, v72
	v_med3_f32 v8, v9, s24, v72
	v_cvt_pk_fp8_f32 v6, v7, v8 op_sel:[0,0,1]
	v_med3_f32 v2, v2, s24, v72
	v_med3_f32 v3, v3, s24, v72
	v_mov_b32_e32 v7, v67
	v_cvt_pk_fp8_f32 v7, v2, v3
	v_pk_mul_f32 v[2:3], v[4:5], s[4:5] op_sel_hi:[1,0]
	v_ashrrev_i32_e32 v71, 31, v70
	v_med3_f32 v2, v2, s24, v72
	v_med3_f32 v3, v3, s24, v72
	v_cvt_pk_fp8_f32 v7, v2, v3 op_sel:[0,0,1]
	v_perm_b32 v5, v58, v62, s25
	v_perm_b32 v8, v50, v54, s25
	v_perm_b32 v9, v42, v46, s25
	v_perm_b32 v11, v34, v38, s25
	v_perm_b32 v12, v26, v30, s25
	v_perm_b32 v13, v18, v22, s25
	v_perm_b32 v15, v10, v14, s25
	v_perm_b32 v16, v7, v6, s25
	v_lshl_add_u64 v[2:3], s[8:9], 0, v[68:69]
	v_lshlrev_b64 v[20:21], 11, v[70:71]
	v_add_u32_e32 v4, 1, v75
	v_perm_b32 v76, v8, v5, s27
	v_perm_b32 v77, v11, v9, s27
	v_perm_b32 v78, v13, v12, s27
	v_perm_b32 v79, v16, v15, s27
	v_lshl_add_u64 v[20:21], v[2:3], 0, v[20:21]
	v_cmp_lt_i32_e32 vcc, s36, v4
	v_and_b32_e32 v17, 0x7d, v4
	global_store_dwordx4 v[20:21], v[76:79], off nt
	s_and_saveexec_b64 s[10:11], vcc
	s_xor_b64 s[10:11], exec, s[10:11]
	v_add_u32_e32 v4, 0x7ffff002, v74
	v_and_b32_e32 v4, 0x7fffff00, v4
	v_or3_b32 v4, v17, v4, s37
	s_andn2_saveexec_b64 s[10:11], s[10:11]
	v_add_u32_e32 v4, 2, v74
	v_and_or_b32 v4, v4, s38, v17
	s_or_b64 exec, exec, s[10:11]
	v_perm_b32 v68, v8, v5, s28
	v_ashrrev_i32_e32 v5, 31, v4
	v_lshlrev_b64 v[4:5], 11, v[4:5]
	v_perm_b32 v69, v11, v9, s28
	v_perm_b32 v70, v13, v12, s28
	v_perm_b32 v71, v16, v15, s28
	v_lshl_add_u64 v[4:5], v[2:3], 0, v[4:5]
	global_store_dwordx4 v[4:5], v[68:71], off nt
	v_add_u32_e32 v4, 2, v75
	v_cmp_lt_i32_e32 vcc, s36, v4
	v_and_b32_e32 v5, 0x7e, v4
	s_and_saveexec_b64 s[10:11], vcc
	s_xor_b64 s[10:11], exec, s[10:11]
	v_add_u32_e32 v4, 0x7ffff004, v74
	v_and_b32_e32 v4, 0x7fffff00, v4
	v_or3_b32 v4, v5, v4, s37
	s_andn2_saveexec_b64 s[10:11], s[10:11]
	v_add_u32_e32 v4, 4, v74
	v_and_or_b32 v4, v4, s38, v5
	s_or_b64 exec, exec, s[10:11]
	v_ashrrev_i32_e32 v5, 31, v4
	v_perm_b32 v8, v58, v62, s26
	v_perm_b32 v9, v50, v54, s26
	v_perm_b32 v11, v42, v46, s26
	v_perm_b32 v12, v34, v38, s26
	v_perm_b32 v13, v26, v30, s26
	v_perm_b32 v15, v18, v22, s26
	v_perm_b32 v10, v10, v14, s26
	v_perm_b32 v6, v7, v6, s26
	v_lshlrev_b64 v[4:5], 11, v[4:5]
	v_perm_b32 v16, v9, v8, s27
	v_perm_b32 v17, v12, v11, s27
	v_perm_b32 v18, v15, v13, s27
	v_perm_b32 v19, v6, v10, s27
	v_lshl_add_u64 v[4:5], v[2:3], 0, v[4:5]
	global_store_dwordx4 v[4:5], v[16:19], off nt
	v_add_u32_e32 v4, 3, v75
	v_cmp_lt_i32_e32 vcc, s36, v4
	v_and_b32_e32 v5, 0x7f, v4
	s_and_saveexec_b64 s[10:11], vcc
	s_xor_b64 s[10:11], exec, s[10:11]
	v_add_u32_e32 v4, 0x7ffff006, v74
	v_and_b32_e32 v4, 0x7fffff00, v4
	v_or3_b32 v4, v5, v4, s37
	s_andn2_saveexec_b64 s[10:11], s[10:11]
	v_add_u32_e32 v4, 6, v74
	v_and_or_b32 v4, v4, s38, v5
	s_or_b64 exec, exec, s[10:11]
	v_ashrrev_i32_e32 v5, 31, v4
	v_lshlrev_b64 v[4:5], 11, v[4:5]
	v_perm_b32 v16, v9, v8, s28
	v_perm_b32 v17, v12, v11, s28
	v_perm_b32 v18, v15, v13, s28
	v_perm_b32 v19, v6, v10, s28
	v_lshl_add_u64 v[2:3], v[2:3], 0, v[4:5]
	global_store_dwordx4 v[2:3], v[16:19], off nt
	v_cmp_lt_i32_e32 vcc, s36, v129
	s_and_saveexec_b64 s[10:11], vcc
	s_xor_b64 s[10:11], exec, s[10:11]
	v_add_u32_e32 v150, 0x7ffff000, v128
	v_and_b32_e32 v150, 0x7fffff00, v150
	v_or3_b32 v150, v151, v150, s37
	s_andn2_saveexec_b64 s[10:11], s[10:11]
	v_and_or_b32 v150, v128, s38, v151
	s_or_b64 exec, exec, s[10:11]
	s_waitcnt vmcnt(19)
	v_pk_mul_f32 v[144:145], v[144:145], s[4:5] op_sel_hi:[1,0]
	v_pk_mul_f32 v[146:147], v[146:147], s[4:5] op_sel_hi:[1,0]
	v_med3_f32 v151, v144, s24, v72
	v_med3_f32 v145, v145, s24, v72
	v_mov_b32_e32 v144, v67
	v_cvt_pk_fp8_f32 v144, v151, v145
	v_med3_f32 v145, v146, s24, v72
	v_med3_f32 v146, v147, s24, v72
	s_waitcnt vmcnt(18)
	v_pk_mul_f32 v[140:141], v[140:141], s[4:5] op_sel_hi:[1,0]
	v_cvt_pk_fp8_f32 v144, v145, v146 op_sel:[0,0,1]
	v_med3_f32 v145, v140, s24, v72
	v_med3_f32 v141, v141, s24, v72
	v_mov_b32_e32 v140, v67
	v_cvt_pk_fp8_f32 v140, v145, v141
	v_pk_mul_f32 v[142:143], v[142:143], s[4:5] op_sel_hi:[1,0]
	s_waitcnt vmcnt(17)
	v_pk_mul_f32 v[136:137], v[136:137], s[4:5] op_sel_hi:[1,0]
	v_med3_f32 v141, v142, s24, v72
	v_med3_f32 v142, v143, s24, v72
	v_cvt_pk_fp8_f32 v140, v141, v142 op_sel:[0,0,1]
	v_med3_f32 v141, v136, s24, v72
	v_med3_f32 v137, v137, s24, v72
	v_mov_b32_e32 v136, v67
	v_cvt_pk_fp8_f32 v136, v141, v137
	v_pk_mul_f32 v[138:139], v[138:139], s[4:5] op_sel_hi:[1,0]
	s_waitcnt vmcnt(16)
	v_pk_mul_f32 v[132:133], v[132:133], s[4:5] op_sel_hi:[1,0]
	v_med3_f32 v137, v138, s24, v72
	v_med3_f32 v138, v139, s24, v72
	v_cvt_pk_fp8_f32 v136, v137, v138 op_sel:[0,0,1]
	v_med3_f32 v137, v132, s24, v72
	v_med3_f32 v133, v133, s24, v72
	v_mov_b32_e32 v132, v67
	v_cvt_pk_fp8_f32 v132, v137, v133
	v_pk_mul_f32 v[134:135], v[134:135], s[4:5] op_sel_hi:[1,0]
	s_waitcnt vmcnt(15)
	v_pk_mul_f32 v[124:125], v[124:125], s[4:5] op_sel_hi:[1,0]
	v_med3_f32 v133, v134, s24, v72
	v_med3_f32 v134, v135, s24, v72
	v_cvt_pk_fp8_f32 v132, v133, v134 op_sel:[0,0,1]
	v_med3_f32 v133, v124, s24, v72
	v_med3_f32 v125, v125, s24, v72
	v_mov_b32_e32 v124, v67
	v_cvt_pk_fp8_f32 v124, v133, v125
	v_pk_mul_f32 v[126:127], v[126:127], s[4:5] op_sel_hi:[1,0]
	s_waitcnt vmcnt(14)
	v_pk_mul_f32 v[120:121], v[120:121], s[4:5] op_sel_hi:[1,0]
	v_med3_f32 v125, v126, s24, v72
	v_med3_f32 v126, v127, s24, v72
	v_cvt_pk_fp8_f32 v124, v125, v126 op_sel:[0,0,1]
	v_med3_f32 v125, v120, s24, v72
	v_med3_f32 v121, v121, s24, v72
	v_mov_b32_e32 v120, v67
	v_cvt_pk_fp8_f32 v120, v125, v121
	v_pk_mul_f32 v[122:123], v[122:123], s[4:5] op_sel_hi:[1,0]
	s_waitcnt vmcnt(13)
; template <int MODE> __device__ __forceinline__ void cv_finish(const f32x4 (&tv)[16], int K, int nblk, unsigned char* WT, int item, int lane) {
;     const int kb = item / nblk, nb = item - kb * nblk, k0 = 64 * kb + 16 * (lane >> 4), n0 = 64 * nb + 4 * (lane & 15);
;     unsigned D[16];
; #pragma unroll
;     for (int i = 0; i < 16; ++i) { const f32x2 a = (f32x2){tv[i].x, tv[i].y} * (f32x2){1024.f, 1024.f}, b = (f32x2){tv[i].z, tv[i].w} * (f32x2){1024.f, 1024.f};
;         D[i] = pk4_fp8(a.x, a.y, b.x, b.y); }
;     unsigned O[4][4];
; #pragma unroll
;     for (int q = 0; q < 4; ++q) { const unsigned a = D[4 * q], b = D[4 * q + 1], c = D[4 * q + 2], d = D[4 * q + 3];
;         const unsigned t0 = __builtin_amdgcn_perm(b, a, 0x05010400u), t1 = __builtin_amdgcn_perm(b, a, 0x07030602u), u0 = __builtin_amdgcn_perm(d, c, 0x05010400u), u1 = __builtin_amdgcn_perm(d, c, 0x07030602u);
;         O[0][q] = __builtin_amdgcn_perm(u0, t0, 0x05040100u); O[1][q] = __builtin_amdgcn_perm(u0, t0, 0x07060302u); O[2][q] = __builtin_amdgcn_perm(u1, t1, 0x05040100u); O[3][q] = __builtin_amdgcn_perm(u1, t1, 0x07060302u); }
; #pragma unroll
;     for (int j = 0; j < 4; ++j) { u32x4 o; o.x = O[j][0]; o.y = O[j][1]; o.z = O[j][2]; o.w = O[j][3];
;         __builtin_nontemporal_store(o, (u32x4*)(WT + (size_t)drow<MODE>(n0 + j) * K + k0)); }
; }
; template <int MODE> __device__ __forceinline__ void cv_run4(const float* W, int K, int N, unsigned char* WT, int item0, int lane) {
;     const int nblk = N / 64; f32x4 ta[16];
; #pragma unroll 1
;     for (int j = 0; j < 4; ++j) { cv_load(W, N, nblk, item0 + j, lane, ta); cv_finish<MODE>(ta, K, nblk, WT, item0 + j, lane); }
	v_pk_mul_f32 v[116:117], v[116:117], s[4:5] op_sel_hi:[1,0]
	v_med3_f32 v121, v122, s24, v72
	v_med3_f32 v122, v123, s24, v72
	v_cvt_pk_fp8_f32 v120, v121, v122 op_sel:[0,0,1]
	v_med3_f32 v121, v116, s24, v72
	v_med3_f32 v117, v117, s24, v72
	v_mov_b32_e32 v116, v67
	v_cvt_pk_fp8_f32 v116, v121, v117
	v_pk_mul_f32 v[118:119], v[118:119], s[4:5] op_sel_hi:[1,0]
	s_waitcnt vmcnt(12)
	v_pk_mul_f32 v[112:113], v[112:113], s[4:5] op_sel_hi:[1,0]
	v_med3_f32 v117, v118, s24, v72
	v_med3_f32 v118, v119, s24, v72
	v_cvt_pk_fp8_f32 v116, v117, v118 op_sel:[0,0,1]
	v_med3_f32 v117, v112, s24, v72
	v_med3_f32 v113, v113, s24, v72
	v_mov_b32_e32 v112, v67
	v_cvt_pk_fp8_f32 v112, v117, v113
	v_pk_mul_f32 v[114:115], v[114:115], s[4:5] op_sel_hi:[1,0]
	s_waitcnt vmcnt(11)
	v_pk_mul_f32 v[108:109], v[108:109], s[4:5] op_sel_hi:[1,0]
	v_med3_f32 v113, v114, s24, v72
	v_med3_f32 v114, v115, s24, v72
	v_cvt_pk_fp8_f32 v112, v113, v114 op_sel:[0,0,1]
	v_med3_f32 v113, v108, s24, v72
	v_med3_f32 v109, v109, s24, v72
	v_mov_b32_e32 v108, v67
	v_cvt_pk_fp8_f32 v108, v113, v109
	v_pk_mul_f32 v[110:111], v[110:111], s[4:5] op_sel_hi:[1,0]
	s_waitcnt vmcnt(10)
	v_pk_mul_f32 v[104:105], v[104:105], s[4:5] op_sel_hi:[1,0]
	v_med3_f32 v109, v110, s24, v72
	v_med3_f32 v110, v111, s24, v72
	v_cvt_pk_fp8_f32 v108, v109, v110 op_sel:[0,0,1]
	v_med3_f32 v109, v104, s24, v72
	v_med3_f32 v105, v105, s24, v72
	v_mov_b32_e32 v104, v67
	v_cvt_pk_fp8_f32 v104, v109, v105
	v_pk_mul_f32 v[106:107], v[106:107], s[4:5] op_sel_hi:[1,0]
	s_waitcnt vmcnt(9)
	v_pk_mul_f32 v[100:101], v[100:101], s[4:5] op_sel_hi:[1,0]
	v_med3_f32 v105, v106, s24, v72
	v_med3_f32 v106, v107, s24, v72
	v_cvt_pk_fp8_f32 v104, v105, v106 op_sel:[0,0,1]
	v_med3_f32 v105, v100, s24, v72
	v_med3_f32 v101, v101, s24, v72
	v_mov_b32_e32 v100, v67
	v_cvt_pk_fp8_f32 v100, v105, v101
	v_pk_mul_f32 v[102:103], v[102:103], s[4:5] op_sel_hi:[1,0]
	s_waitcnt vmcnt(8)
	v_pk_mul_f32 v[96:97], v[96:97], s[4:5] op_sel_hi:[1,0]
	v_med3_f32 v101, v102, s24, v72
	v_med3_f32 v102, v103, s24, v72
	v_cvt_pk_fp8_f32 v100, v101, v102 op_sel:[0,0,1]
	v_med3_f32 v101, v96, s24, v72
	v_med3_f32 v97, v97, s24, v72
	v_mov_b32_e32 v96, v67
	v_cvt_pk_fp8_f32 v96, v101, v97
	v_pk_mul_f32 v[98:99], v[98:99], s[4:5] op_sel_hi:[1,0]
	s_waitcnt vmcnt(7)
	v_pk_mul_f32 v[92:93], v[92:93], s[4:5] op_sel_hi:[1,0]
	v_med3_f32 v97, v98, s24, v72
	v_med3_f32 v98, v99, s24, v72
	v_cvt_pk_fp8_f32 v96, v97, v98 op_sel:[0,0,1]
	v_med3_f32 v97, v92, s24, v72
	v_med3_f32 v93, v93, s24, v72
	v_mov_b32_e32 v92, v67
	v_cvt_pk_fp8_f32 v92, v97, v93
	v_pk_mul_f32 v[94:95], v[94:95], s[4:5] op_sel_hi:[1,0]
	s_waitcnt vmcnt(6)
	v_pk_mul_f32 v[88:89], v[88:89], s[4:5] op_sel_hi:[1,0]
	v_med3_f32 v93, v94, s24, v72
	v_med3_f32 v94, v95, s24, v72
	v_cvt_pk_fp8_f32 v92, v93, v94 op_sel:[0,0,1]
	v_med3_f32 v93, v88, s24, v72
	v_med3_f32 v89, v89, s24, v72
	v_mov_b32_e32 v88, v67
	v_cvt_pk_fp8_f32 v88, v93, v89
	v_pk_mul_f32 v[90:91], v[90:91], s[4:5] op_sel_hi:[1,0]
	s_waitcnt vmcnt(5)
	v_pk_mul_f32 v[84:85], v[84:85], s[4:5] op_sel_hi:[1,0]
	v_med3_f32 v89, v90, s24, v72
	v_med3_f32 v90, v91, s24, v72
	v_cvt_pk_fp8_f32 v88, v89, v90 op_sel:[0,0,1]
	v_med3_f32 v89, v84, s24, v72
	v_med3_f32 v85, v85, s24, v72
	v_mov_b32_e32 v84, v67
	v_cvt_pk_fp8_f32 v84, v89, v85
	v_pk_mul_f32 v[86:87], v[86:87], s[4:5] op_sel_hi:[1,0]
	s_waitcnt vmcnt(4)
	v_pk_mul_f32 v[80:81], v[80:81], s[4:5] op_sel_hi:[1,0]
	v_med3_f32 v85, v86, s24, v72
	v_med3_f32 v86, v87, s24, v72
	v_cvt_pk_fp8_f32 v84, v85, v86 op_sel:[0,0,1]
	v_med3_f32 v80, v80, s24, v72
	v_med3_f32 v81, v81, s24, v72
	v_mov_b32_e32 v85, v67
	v_cvt_pk_fp8_f32 v85, v80, v81
	v_pk_mul_f32 v[80:81], v[82:83], s[4:5] op_sel_hi:[1,0]
	v_ashrrev_i32_e32 v151, 31, v150
	v_med3_f32 v80, v80, s24, v72
	v_med3_f32 v81, v81, s24, v72
	v_cvt_pk_fp8_f32 v85, v80, v81 op_sel:[0,0,1]
	v_perm_b32 v83, v140, v144, s25
	v_perm_b32 v86, v132, v136, s25
	v_perm_b32 v87, v120, v124, s25
	v_perm_b32 v89, v112, v116, s25
	v_perm_b32 v90, v104, v108, s25
	v_perm_b32 v91, v96, v100, s25
	v_perm_b32 v93, v88, v92, s25
	v_perm_b32 v94, v85, v84, s25
	v_lshl_add_u64 v[80:81], s[8:9], 0, v[148:149]
	v_lshlrev_b64 v[98:99], 11, v[150:151]
	v_add_u32_e32 v82, 1, v129
	v_perm_b32 v152, v86, v83, s27
	v_perm_b32 v153, v89, v87, s27
	v_perm_b32 v154, v91, v90, s27
	v_perm_b32 v155, v94, v93, s27
	v_lshl_add_u64 v[98:99], v[80:81], 0, v[98:99]
	v_cmp_lt_i32_e32 vcc, s36, v82
	v_and_b32_e32 v95, 0x7d, v82
	global_store_dwordx4 v[98:99], v[152:155], off nt
	s_and_saveexec_b64 s[10:11], vcc
	s_xor_b64 s[10:11], exec, s[10:11]
	v_add_u32_e32 v82, 0x7ffff002, v128
	v_and_b32_e32 v82, 0x7fffff00, v82
	v_or3_b32 v82, v95, v82, s37
	s_andn2_saveexec_b64 s[10:11], s[10:11]
	v_add_u32_e32 v82, 2, v128
	v_and_or_b32 v82, v82, s38, v95
	s_or_b64 exec, exec, s[10:11]
	v_perm_b32 v148, v86, v83, s28
	v_ashrrev_i32_e32 v83, 31, v82
	v_lshlrev_b64 v[82:83], 11, v[82:83]
	v_perm_b32 v149, v89, v87, s28
	v_perm_b32 v150, v91, v90, s28
	v_perm_b32 v151, v94, v93, s28
	v_lshl_add_u64 v[82:83], v[80:81], 0, v[82:83]
	global_store_dwordx4 v[82:83], v[148:151], off nt
	v_add_u32_e32 v82, 2, v129
	v_cmp_lt_i32_e32 vcc, s36, v82
	v_and_b32_e32 v83, 0x7e, v82
	s_and_saveexec_b64 s[10:11], vcc
	s_xor_b64 s[10:11], exec, s[10:11]
	v_add_u32_e32 v82, 0x7ffff004, v128
	v_and_b32_e32 v82, 0x7fffff00, v82
	v_or3_b32 v82, v83, v82, s37
	s_andn2_saveexec_b64 s[10:11], s[10:11]
	v_add_u32_e32 v82, 4, v128
	v_and_or_b32 v82, v82, s38, v83
	s_or_b64 exec, exec, s[10:11]
	v_ashrrev_i32_e32 v83, 31, v82
	v_perm_b32 v86, v140, v144, s26
	v_perm_b32 v87, v132, v136, s26
	v_perm_b32 v89, v120, v124, s26
	v_perm_b32 v90, v112, v116, s26
	v_perm_b32 v91, v104, v108, s26
	v_perm_b32 v93, v96, v100, s26
	v_perm_b32 v88, v88, v92, s26
	v_perm_b32 v84, v85, v84, s26
	v_lshlrev_b64 v[82:83], 11, v[82:83]
	v_perm_b32 v94, v87, v86, s27
	v_perm_b32 v95, v90, v89, s27
	v_perm_b32 v96, v93, v91, s27
	v_perm_b32 v97, v84, v88, s27
	v_lshl_add_u64 v[82:83], v[80:81], 0, v[82:83]
	global_store_dwordx4 v[82:83], v[94:97], off nt
	v_add_u32_e32 v82, 3, v129
	v_cmp_lt_i32_e32 vcc, s36, v82
	v_and_b32_e32 v83, 0x7f, v82
	s_and_saveexec_b64 s[10:11], vcc
	s_xor_b64 s[10:11], exec, s[10:11]
	v_add_u32_e32 v82, 0x7ffff006, v128
	v_and_b32_e32 v82, 0x7fffff00, v82
	v_or3_b32 v82, v83, v82, s37
	s_andn2_saveexec_b64 s[10:11], s[10:11]
	v_add_u32_e32 v82, 6, v128
	v_and_or_b32 v82, v82, s38, v83
	s_or_b64 exec, exec, s[10:11]
	v_ashrrev_i32_e32 v83, 31, v82
	v_lshlrev_b64 v[82:83], 11, v[82:83]
	v_perm_b32 v94, v87, v86, s28
	v_perm_b32 v95, v90, v89, s28
	v_perm_b32 v96, v93, v91, s28
	v_perm_b32 v97, v84, v88, s28
	v_lshl_add_u64 v[80:81], v[80:81], 0, v[82:83]
	global_store_dwordx4 v[80:81], v[94:97], off nt
	s_cmpk_eq_i32 s40, 0x200
	s_cbranch_scc0 .LBB0_766
	s_branch .LBB0_752

; __device__ __forceinline__ void cv_load(const float* W, int N, int nblk, int item, int lane, f32x4 (&tv)[16]) {
;     const int kb = item / nblk, nb = item - kb * nblk; const float* p = W + (size_t)(64 * kb + 16 * (lane >> 4)) * N + 64 * nb + 4 * (lane & 15);
; #pragma unroll
;     for (int i = 0; i < 16; ++i) tv[i] = __builtin_nontemporal_load((const f32x4*)(p + (size_t)i * N));
; }
; template <int MODE> __device__ __forceinline__ void cv_run4(const float* W, int K, int N, unsigned char* WT, int item0, int lane) {
;     const int nblk = N / 64; f32x4 ta[16];
; #pragma unroll 1
;     for (int j = 0; j < 4; ++j) { cv_load(W, N, nblk, item0 + j, lane, ta); cv_finish<MODE>(ta, K, nblk, WT, item0 + j, lane); }
.LBB0_979:
	s_lshr_b32 s49, s4, 5
	s_lshl_b32 s50, s49, 11
	v_mov_b32_e32 v3, v69
	v_lshl_or_b32 v2, s49, 6, v1
	s_sub_i32 s49, s47, s50
	s_waitcnt lgkmcnt(1)
	v_subrev_u32_e32 v8, s50, v4
	s_waitcnt lgkmcnt(0)
	v_lshlrev_b64 v[6:7], 13, v[2:3]
	s_add_i32 s50, s48, s49
	v_lshl_add_u64 v[6:7], s[8:9], 0, v[6:7]
	s_ashr_i32 s51, s50, 31
	v_lshl_add_u64 v[6:7], s[50:51], 2, v[6:7]
	v_lshl_add_u64 v[16:17], v[6:7], 0, v[68:69]
	v_add_co_u32_e32 v18, vcc, s17, v16
	v_add_u32_e32 v8, s48, v8
	s_nop 0
	v_addc_co_u32_e32 v19, vcc, 0, v17, vcc
	v_add_co_u32_e32 v20, vcc, s18, v16
	v_ashrrev_i32_e32 v9, 31, v8
	s_nop 0
	v_addc_co_u32_e32 v21, vcc, 0, v17, vcc
	v_add_co_u32_e32 v22, vcc, s19, v16
	v_add_u32_e32 v10, 1, v8
	s_nop 0
	v_addc_co_u32_e32 v23, vcc, 0, v17, vcc
	v_add_co_u32_e32 v24, vcc, s20, v16
	s_waitcnt vmcnt(2)
	v_add_u32_e32 v12, 2, v8
	v_addc_co_u32_e32 v25, vcc, 0, v17, vcc
	v_add_co_u32_e32 v26, vcc, s21, v16
	v_add_u32_e32 v14, 3, v8
	s_nop 0
	v_addc_co_u32_e32 v27, vcc, 0, v17, vcc
	v_add_co_u32_e32 v30, vcc, s22, v16
	v_lshl_add_u64 v[2:3], s[10:11], 0, v[2:3]
	s_nop 0
	v_addc_co_u32_e32 v31, vcc, 0, v17, vcc
	v_add_co_u32_e32 v34, vcc, s23, v16
	v_lshlrev_b64 v[8:9], 11, v[8:9]
	s_nop 0
	v_addc_co_u32_e32 v35, vcc, 0, v17, vcc
	v_add_co_u32_e32 v38, vcc, s24, v16
	v_ashrrev_i32_e32 v11, 31, v10
	s_nop 0
	v_addc_co_u32_e32 v39, vcc, 0, v17, vcc
	v_add_co_u32_e32 v42, vcc, s25, v16
	v_ashrrev_i32_e32 v13, 31, v12
	s_nop 0
	v_addc_co_u32_e32 v43, vcc, 0, v17, vcc
	v_add_co_u32_e32 v46, vcc, s26, v16
	v_ashrrev_i32_e32 v15, 31, v14
	s_nop 0
	v_addc_co_u32_e32 v47, vcc, 0, v17, vcc
	v_add_co_u32_e32 v50, vcc, s27, v16
	v_lshl_add_u64 v[76:77], v[2:3], 0, v[8:9]
	s_nop 0
	v_addc_co_u32_e32 v51, vcc, 0, v17, vcc
	v_add_co_u32_e32 v54, vcc, s28, v16
	v_lshlrev_b64 v[10:11], 11, v[10:11]
	s_nop 0
	v_addc_co_u32_e32 v55, vcc, 0, v17, vcc
	v_add_co_u32_e32 v58, vcc, s29, v16
	v_lshlrev_b64 v[12:13], 11, v[12:13]
	s_nop 0
	v_addc_co_u32_e32 v59, vcc, 0, v17, vcc
	v_add_co_u32_e32 v62, vcc, s30, v16
	v_lshlrev_b64 v[14:15], 11, v[14:15]
	s_nop 0
	v_addc_co_u32_e32 v63, vcc, 0, v17, vcc
	v_add_co_u32_e32 v70, vcc, s31, v16
	global_load_dwordx4 v[6:9], v[16:17], off nt
	s_nop 0
	v_addc_co_u32_e32 v71, vcc, 0, v17, vcc
	v_lshl_add_u64 v[78:79], v[2:3], 0, v[10:11]
	v_lshl_add_u64 v[80:81], v[2:3], 0, v[12:13]
	v_lshl_add_u64 v[2:3], v[2:3], 0, v[14:15]
	global_load_dwordx4 v[10:13], v[18:19], off nt
	global_load_dwordx4 v[14:17], v[20:21], off nt
	s_nop 0
	global_load_dwordx4 v[18:21], v[22:23], off nt
	s_nop 0
	global_load_dwordx4 v[22:25], v[24:25], off nt
	s_nop 0
	global_load_dwordx4 v[26:29], v[26:27], off nt
	s_nop 0
	global_load_dwordx4 v[30:33], v[30:31], off nt
	s_nop 0
	global_load_dwordx4 v[34:37], v[34:35], off nt
	s_nop 0
	global_load_dwordx4 v[38:41], v[38:39], off nt
	s_nop 0
	global_load_dwordx4 v[42:45], v[42:43], off nt
	s_nop 0
	global_load_dwordx4 v[46:49], v[46:47], off nt
	s_nop 0
	global_load_dwordx4 v[50:53], v[50:51], off nt
	s_nop 0
	global_load_dwordx4 v[54:57], v[54:55], off nt
	s_nop 0
	global_load_dwordx4 v[58:61], v[58:59], off nt
	s_nop 0
	global_load_dwordx4 v[62:65], v[62:63], off nt
	s_nop 0
	global_load_dwordx4 v[70:73], v[70:71], off nt
	v_mov_b32_e32 v5, v69
	v_mov_b32_e32 v75, v69
	v_mov_b32_e32 v82, v69
	v_mov_b32_e32 v83, v69
	v_mov_b32_e32 v84, v69
	v_mov_b32_e32 v85, v69
	v_mov_b32_e32 v86, v69
	v_mov_b32_e32 v87, v69
	v_mov_b32_e32 v88, v69
	v_mov_b32_e32 v89, v69
	v_mov_b32_e32 v90, v69
	v_mov_b32_e32 v91, v69
	v_mov_b32_e32 v92, v69
	v_mov_b32_e32 v93, v69
	v_mov_b32_e32 v94, v69
	v_mov_b32_e32 v95, v69
	s_add_i32 s4, s4, 1
	s_add_i32 s48, s48, 64
	s_lshr_b32 s49, s4, 5
	s_lshl_b32 s50, s49, 11
	v_mov_b32_e32 v101, v69
	v_lshl_or_b32 v100, s49, 6, v1
	s_sub_i32 s49, s47, s50
	s_waitcnt lgkmcnt(1)
	v_subrev_u32_e32 v106, s50, v4
	s_waitcnt lgkmcnt(0)
	v_lshlrev_b64 v[104:105], 13, v[100:101]
	s_add_i32 s50, s48, s49
	v_lshl_add_u64 v[104:105], s[8:9], 0, v[104:105]
	s_ashr_i32 s51, s50, 31
	v_lshl_add_u64 v[104:105], s[50:51], 2, v[104:105]
	v_lshl_add_u64 v[114:115], v[104:105], 0, v[68:69]
	v_add_co_u32_e32 v116, vcc, s17, v114
	v_add_u32_e32 v106, s48, v106
	s_nop 0
	v_addc_co_u32_e32 v117, vcc, 0, v115, vcc
	v_add_co_u32_e32 v118, vcc, s18, v114
	v_ashrrev_i32_e32 v107, 31, v106
	s_nop 0
	v_addc_co_u32_e32 v119, vcc, 0, v115, vcc
	v_add_co_u32_e32 v120, vcc, s19, v114
	v_add_u32_e32 v108, 1, v106
	s_nop 0
	v_addc_co_u32_e32 v121, vcc, 0, v115, vcc
	v_add_co_u32_e32 v122, vcc, s20, v114
	s_waitcnt vmcnt(2)
; __device__ __forceinline__ unsigned pk4_fp8(float a, float b, float c, float d) {
;     a = __builtin_fminf(__builtin_fmaxf(a, -448.f), 448.f); b = __builtin_fminf(__builtin_fmaxf(b, -448.f), 448.f); c = __builtin_fminf(__builtin_fmaxf(c, -448.f), 448.f); d = __builtin_fminf(__builtin_fmaxf(d, -448.f), 448.f);
;     int w = 0; w = __builtin_amdgcn_cvt_pk_fp8_f32(a, b, w, false); w = __builtin_amdgcn_cvt_pk_fp8_f32(c, d, w, true); return (unsigned)w;
; }
; __device__ __forceinline__ void cv_load(const float* W, int N, int nblk, int item, int lane, f32x4 (&tv)[16]) {
;     const int kb = item / nblk, nb = item - kb * nblk; const float* p = W + (size_t)(64 * kb + 16 * (lane >> 4)) * N + 64 * nb + 4 * (lane & 15);
; #pragma unroll
;     for (int i = 0; i < 16; ++i) tv[i] = __builtin_nontemporal_load((const f32x4*)(p + (size_t)i * N));
; }
; template <int MODE> __device__ __forceinline__ void cv_finish(const f32x4 (&tv)[16], int K, int nblk, unsigned char* WT, int item, int lane) {
;     const int kb = item / nblk, nb = item - kb * nblk, k0 = 64 * kb + 16 * (lane >> 4), n0 = 64 * nb + 4 * (lane & 15);
;     unsigned D[16];
; #pragma unroll
;     for (int i = 0; i < 16; ++i) { const f32x2 a = (f32x2){tv[i].x, tv[i].y} * (f32x2){1024.f, 1024.f}, b = (f32x2){tv[i].z, tv[i].w} * (f32x2){1024.f, 1024.f};
;         D[i] = pk4_fp8(a.x, a.y, b.x, b.y); }
	v_add_u32_e32 v110, 2, v106
	v_addc_co_u32_e32 v123, vcc, 0, v115, vcc
	v_add_co_u32_e32 v124, vcc, s21, v114
	v_add_u32_e32 v112, 3, v106
	s_nop 0
	v_addc_co_u32_e32 v125, vcc, 0, v115, vcc
	v_add_co_u32_e32 v128, vcc, s22, v114
	v_lshl_add_u64 v[100:101], s[10:11], 0, v[100:101]
	s_nop 0
	v_addc_co_u32_e32 v129, vcc, 0, v115, vcc
	v_add_co_u32_e32 v132, vcc, s23, v114
	v_lshlrev_b64 v[106:107], 11, v[106:107]
	s_nop 0
	v_addc_co_u32_e32 v133, vcc, 0, v115, vcc
	v_add_co_u32_e32 v136, vcc, s24, v114
	v_ashrrev_i32_e32 v109, 31, v108
	s_nop 0
	v_addc_co_u32_e32 v137, vcc, 0, v115, vcc
	v_add_co_u32_e32 v140, vcc, s25, v114
	v_ashrrev_i32_e32 v111, 31, v110
	s_nop 0
	v_addc_co_u32_e32 v141, vcc, 0, v115, vcc
	v_add_co_u32_e32 v144, vcc, s26, v114
	v_ashrrev_i32_e32 v113, 31, v112
	s_nop 0
	v_addc_co_u32_e32 v145, vcc, 0, v115, vcc
	v_add_co_u32_e32 v148, vcc, s27, v114
	v_lshl_add_u64 v[170:171], v[100:101], 0, v[106:107]
	s_nop 0
	v_addc_co_u32_e32 v149, vcc, 0, v115, vcc
	v_add_co_u32_e32 v152, vcc, s28, v114
	v_lshlrev_b64 v[108:109], 11, v[108:109]
	s_nop 0
	v_addc_co_u32_e32 v153, vcc, 0, v115, vcc
	v_add_co_u32_e32 v156, vcc, s29, v114
	v_lshlrev_b64 v[110:111], 11, v[110:111]
	s_nop 0
	v_addc_co_u32_e32 v157, vcc, 0, v115, vcc
	v_add_co_u32_e32 v160, vcc, s30, v114
	v_lshlrev_b64 v[112:113], 11, v[112:113]
	s_nop 0
	v_addc_co_u32_e32 v161, vcc, 0, v115, vcc
	v_add_co_u32_e32 v164, vcc, s31, v114
	global_load_dwordx4 v[104:107], v[114:115], off nt
	s_nop 0
	v_addc_co_u32_e32 v165, vcc, 0, v115, vcc
	v_lshl_add_u64 v[172:173], v[100:101], 0, v[108:109]
	v_lshl_add_u64 v[174:175], v[100:101], 0, v[110:111]
	v_lshl_add_u64 v[100:101], v[100:101], 0, v[112:113]
	global_load_dwordx4 v[108:111], v[116:117], off nt
	global_load_dwordx4 v[112:115], v[118:119], off nt
	s_nop 0
	global_load_dwordx4 v[116:119], v[120:121], off nt
	s_nop 0
	global_load_dwordx4 v[120:123], v[122:123], off nt
	s_nop 0
	global_load_dwordx4 v[124:127], v[124:125], off nt
	s_nop 0
	global_load_dwordx4 v[128:131], v[128:129], off nt
	s_nop 0
	global_load_dwordx4 v[132:135], v[132:133], off nt
	s_nop 0
	global_load_dwordx4 v[136:139], v[136:137], off nt
	s_nop 0
	global_load_dwordx4 v[140:143], v[140:141], off nt
	s_nop 0
	global_load_dwordx4 v[144:147], v[144:145], off nt
	s_nop 0
	global_load_dwordx4 v[148:151], v[148:149], off nt
	s_nop 0
	global_load_dwordx4 v[152:155], v[152:153], off nt
	s_nop 0
	global_load_dwordx4 v[156:159], v[156:157], off nt
	s_nop 0
	global_load_dwordx4 v[160:163], v[160:161], off nt
	s_nop 0
	global_load_dwordx4 v[164:167], v[164:165], off nt
	v_mov_b32_e32 v103, v69
	v_mov_b32_e32 v169, v69
	v_mov_b32_e32 v102, v69
	v_mov_b32_e32 v177, v69
	v_mov_b32_e32 v168, v69
	v_mov_b32_e32 v179, v69
	v_mov_b32_e32 v176, v69
	v_mov_b32_e32 v181, v69
	v_mov_b32_e32 v178, v69
	v_mov_b32_e32 v183, v69
	v_mov_b32_e32 v180, v69
	v_mov_b32_e32 v185, v69
	v_mov_b32_e32 v182, v69
	v_mov_b32_e32 v187, v69
	v_mov_b32_e32 v184, v69
	v_mov_b32_e32 v189, v69
	s_add_i32 s4, s4, 1
	s_add_i32 s48, s48, 64
	s_waitcnt vmcnt(31)
	v_pk_mul_f32 v[6:7], v[6:7], s[6:7] op_sel_hi:[1,0]
	s_nop 0
	v_med3_f32 v96, v6, s33, v74
	v_med3_f32 v97, v7, s33, v74
	s_waitcnt vmcnt(30)
	v_pk_mul_f32 v[6:7], v[10:11], s[6:7] op_sel_hi:[1,0]
	s_waitcnt vmcnt(29)
	v_pk_mul_f32 v[10:11], v[14:15], s[6:7] op_sel_hi:[1,0]
	s_waitcnt vmcnt(28)
	v_pk_mul_f32 v[14:15], v[18:19], s[6:7] op_sel_hi:[1,0]
	s_waitcnt vmcnt(27)
	v_pk_mul_f32 v[18:19], v[22:23], s[6:7] op_sel_hi:[1,0]
	s_waitcnt vmcnt(26)
	v_pk_mul_f32 v[22:23], v[26:27], s[6:7] op_sel_hi:[1,0]
	s_waitcnt vmcnt(25)
	v_pk_mul_f32 v[26:27], v[30:31], s[6:7] op_sel_hi:[1,0]
	s_waitcnt vmcnt(24)
	v_pk_mul_f32 v[30:31], v[34:35], s[6:7] op_sel_hi:[1,0]
	s_waitcnt vmcnt(23)
	v_pk_mul_f32 v[34:35], v[38:39], s[6:7] op_sel_hi:[1,0]
	s_waitcnt vmcnt(22)
	v_pk_mul_f32 v[38:39], v[42:43], s[6:7] op_sel_hi:[1,0]
	s_waitcnt vmcnt(21)
	v_pk_mul_f32 v[42:43], v[46:47], s[6:7] op_sel_hi:[1,0]
	s_waitcnt vmcnt(20)
	v_pk_mul_f32 v[46:47], v[50:51], s[6:7] op_sel_hi:[1,0]
	s_waitcnt vmcnt(19)
	v_pk_mul_f32 v[50:51], v[54:55], s[6:7] op_sel_hi:[1,0]
	s_waitcnt vmcnt(18)
	v_pk_mul_f32 v[54:55], v[58:59], s[6:7] op_sel_hi:[1,0]
	s_waitcnt vmcnt(17)
	v_pk_mul_f32 v[58:59], v[62:63], s[6:7] op_sel_hi:[1,0]
	s_waitcnt vmcnt(16)
; __device__ __forceinline__ unsigned pk4_fp8(float a, float b, float c, float d) {
;     a = __builtin_fminf(__builtin_fmaxf(a, -448.f), 448.f); b = __builtin_fminf(__builtin_fmaxf(b, -448.f), 448.f); c = __builtin_fminf(__builtin_fmaxf(c, -448.f), 448.f); d = __builtin_fminf(__builtin_fmaxf(d, -448.f), 448.f);
;     int w = 0; w = __builtin_amdgcn_cvt_pk_fp8_f32(a, b, w, false); w = __builtin_amdgcn_cvt_pk_fp8_f32(c, d, w, true); return (unsigned)w;
; }
; template <int MODE> __device__ __forceinline__ void cv_finish(const f32x4 (&tv)[16], int K, int nblk, unsigned char* WT, int item, int lane) {
;     const int kb = item / nblk, nb = item - kb * nblk, k0 = 64 * kb + 16 * (lane >> 4), n0 = 64 * nb + 4 * (lane & 15);
;     unsigned D[16];
; #pragma unroll
;     for (int i = 0; i < 16; ++i) { const f32x2 a = (f32x2){tv[i].x, tv[i].y} * (f32x2){1024.f, 1024.f}, b = (f32x2){tv[i].z, tv[i].w} * (f32x2){1024.f, 1024.f};
;         D[i] = pk4_fp8(a.x, a.y, b.x, b.y); }
;     unsigned O[4][4];
; #pragma unroll
;     for (int q = 0; q < 4; ++q) { const unsigned a = D[4 * q], b = D[4 * q + 1], c = D[4 * q + 2], d = D[4 * q + 3];
;         const unsigned t0 = __builtin_amdgcn_perm(b, a, 0x05010400u), t1 = __builtin_amdgcn_perm(b, a, 0x07030602u), u0 = __builtin_amdgcn_perm(d, c, 0x05010400u), u1 = __builtin_amdgcn_perm(d, c, 0x07030602u);
;         O[0][q] = __builtin_amdgcn_perm(u0, t0, 0x05040100u); O[1][q] = __builtin_amdgcn_perm(u0, t0, 0x07060302u); O[2][q] = __builtin_amdgcn_perm(u1, t1, 0x05040100u); O[3][q] = __builtin_amdgcn_perm(u1, t1, 0x07060302u); }
; #pragma unroll
;     for (int j = 0; j < 4; ++j) { u32x4 o; o.x = O[j][0]; o.y = O[j][1]; o.z = O[j][2]; o.w = O[j][3];
;         __builtin_nontemporal_store(o, (u32x4*)(WT + (size_t)drow<MODE>(n0 + j) * K + k0)); }
; }
	v_pk_mul_f32 v[62:63], v[70:71], s[6:7] op_sel_hi:[1,0]
	v_med3_f32 v6, v6, s33, v74
	v_med3_f32 v7, v7, s33, v74
	v_med3_f32 v10, v10, s33, v74
	v_med3_f32 v11, v11, s33, v74
	v_med3_f32 v14, v14, s33, v74
	v_med3_f32 v15, v15, s33, v74
	v_med3_f32 v18, v18, s33, v74
	v_med3_f32 v19, v19, s33, v74
	v_med3_f32 v22, v22, s33, v74
	v_med3_f32 v23, v23, s33, v74
	v_med3_f32 v26, v26, s33, v74
	v_med3_f32 v27, v27, s33, v74
	v_med3_f32 v30, v30, s33, v74
	v_med3_f32 v31, v31, s33, v74
	v_med3_f32 v34, v34, s33, v74
	v_med3_f32 v35, v35, s33, v74
	v_med3_f32 v38, v38, s33, v74
	v_med3_f32 v39, v39, s33, v74
	v_med3_f32 v42, v42, s33, v74
	v_med3_f32 v43, v43, s33, v74
	v_med3_f32 v46, v46, s33, v74
	v_med3_f32 v47, v47, s33, v74
	v_med3_f32 v50, v50, s33, v74
	v_med3_f32 v51, v51, s33, v74
	v_med3_f32 v54, v54, s33, v74
	v_med3_f32 v55, v55, s33, v74
	v_med3_f32 v58, v58, s33, v74
	v_med3_f32 v59, v59, s33, v74
	v_med3_f32 v62, v62, s33, v74
	v_med3_f32 v63, v63, s33, v74
	v_cvt_pk_fp8_f32 v5, v96, v97
	v_cvt_pk_fp8_f32 v75, v6, v7
	v_cvt_pk_fp8_f32 v82, v10, v11
	v_cvt_pk_fp8_f32 v83, v14, v15
	v_cvt_pk_fp8_f32 v84, v18, v19
	v_cvt_pk_fp8_f32 v85, v22, v23
	v_cvt_pk_fp8_f32 v86, v26, v27
	v_cvt_pk_fp8_f32 v87, v30, v31
	v_cvt_pk_fp8_f32 v88, v34, v35
	v_cvt_pk_fp8_f32 v89, v38, v39
	v_cvt_pk_fp8_f32 v90, v42, v43
	v_cvt_pk_fp8_f32 v91, v46, v47
	v_cvt_pk_fp8_f32 v92, v50, v51
	v_cvt_pk_fp8_f32 v93, v54, v55
	v_cvt_pk_fp8_f32 v94, v58, v59
	v_cvt_pk_fp8_f32 v95, v62, v63
	v_pk_mul_f32 v[8:9], v[8:9], s[6:7] op_sel_hi:[1,0]
	s_nop 0
	v_med3_f32 v98, v8, s33, v74
	v_med3_f32 v99, v9, s33, v74
	v_pk_mul_f32 v[8:9], v[12:13], s[6:7] op_sel_hi:[1,0]
	v_pk_mul_f32 v[12:13], v[16:17], s[6:7] op_sel_hi:[1,0]
	v_pk_mul_f32 v[16:17], v[20:21], s[6:7] op_sel_hi:[1,0]
	v_pk_mul_f32 v[20:21], v[24:25], s[6:7] op_sel_hi:[1,0]
	v_pk_mul_f32 v[24:25], v[28:29], s[6:7] op_sel_hi:[1,0]
	v_pk_mul_f32 v[28:29], v[32:33], s[6:7] op_sel_hi:[1,0]
	v_pk_mul_f32 v[32:33], v[36:37], s[6:7] op_sel_hi:[1,0]
	v_pk_mul_f32 v[36:37], v[40:41], s[6:7] op_sel_hi:[1,0]
	v_pk_mul_f32 v[40:41], v[44:45], s[6:7] op_sel_hi:[1,0]
	v_pk_mul_f32 v[44:45], v[48:49], s[6:7] op_sel_hi:[1,0]
	v_pk_mul_f32 v[48:49], v[52:53], s[6:7] op_sel_hi:[1,0]
	v_pk_mul_f32 v[52:53], v[56:57], s[6:7] op_sel_hi:[1,0]
	v_pk_mul_f32 v[56:57], v[60:61], s[6:7] op_sel_hi:[1,0]
	v_pk_mul_f32 v[60:61], v[64:65], s[6:7] op_sel_hi:[1,0]
	v_pk_mul_f32 v[64:65], v[72:73], s[6:7] op_sel_hi:[1,0]
	v_med3_f32 v8, v8, s33, v74
	v_med3_f32 v9, v9, s33, v74
	v_med3_f32 v12, v12, s33, v74
	v_med3_f32 v13, v13, s33, v74
	v_med3_f32 v16, v16, s33, v74
	v_med3_f32 v17, v17, s33, v74
	v_med3_f32 v20, v20, s33, v74
	v_med3_f32 v21, v21, s33, v74
	v_med3_f32 v24, v24, s33, v74
	v_med3_f32 v25, v25, s33, v74
	v_med3_f32 v28, v28, s33, v74
	v_med3_f32 v29, v29, s33, v74
	v_med3_f32 v32, v32, s33, v74
	v_med3_f32 v33, v33, s33, v74
	v_med3_f32 v36, v36, s33, v74
	v_med3_f32 v37, v37, s33, v74
	v_med3_f32 v40, v40, s33, v74
	v_med3_f32 v41, v41, s33, v74
	v_med3_f32 v44, v44, s33, v74
	v_med3_f32 v45, v45, s33, v74
	v_med3_f32 v48, v48, s33, v74
	v_med3_f32 v49, v49, s33, v74
	v_med3_f32 v52, v52, s33, v74
	v_med3_f32 v53, v53, s33, v74
	v_med3_f32 v56, v56, s33, v74
	v_med3_f32 v57, v57, s33, v74
	v_med3_f32 v60, v60, s33, v74
	v_med3_f32 v61, v61, s33, v74
	v_med3_f32 v64, v64, s33, v74
	v_med3_f32 v65, v65, s33, v74
	v_cvt_pk_fp8_f32 v5, v98, v99 op_sel:[0,0,1]
	v_cvt_pk_fp8_f32 v75, v8, v9 op_sel:[0,0,1]
	v_cvt_pk_fp8_f32 v82, v12, v13 op_sel:[0,0,1]
	v_cvt_pk_fp8_f32 v83, v16, v17 op_sel:[0,0,1]
	v_cvt_pk_fp8_f32 v84, v20, v21 op_sel:[0,0,1]
	v_cvt_pk_fp8_f32 v85, v24, v25 op_sel:[0,0,1]
	v_cvt_pk_fp8_f32 v86, v28, v29 op_sel:[0,0,1]
	v_cvt_pk_fp8_f32 v87, v32, v33 op_sel:[0,0,1]
	v_cvt_pk_fp8_f32 v88, v36, v37 op_sel:[0,0,1]
	v_cvt_pk_fp8_f32 v89, v40, v41 op_sel:[0,0,1]
	v_cvt_pk_fp8_f32 v90, v44, v45 op_sel:[0,0,1]
	v_cvt_pk_fp8_f32 v91, v48, v49 op_sel:[0,0,1]
	v_cvt_pk_fp8_f32 v92, v52, v53 op_sel:[0,0,1]
	v_cvt_pk_fp8_f32 v93, v56, v57 op_sel:[0,0,1]
	v_cvt_pk_fp8_f32 v94, v60, v61 op_sel:[0,0,1]
	v_cvt_pk_fp8_f32 v95, v64, v65 op_sel:[0,0,1]
	v_perm_b32 v7, v75, v5, s34
	v_perm_b32 v5, v75, v5, s35
	v_perm_b32 v8, v83, v82, s34
	v_perm_b32 v9, v83, v82, s35
	v_perm_b32 v11, v85, v84, s34
	v_perm_b32 v13, v87, v86, s34
	v_perm_b32 v17, v89, v88, s34
	v_perm_b32 v21, v91, v90, s34
	v_perm_b32 v23, v93, v92, s34
	v_perm_b32 v25, v95, v94, s34
	v_perm_b32 v12, v85, v84, s35
	v_perm_b32 v16, v87, v86, s35
	v_perm_b32 v20, v89, v88, s35
	v_perm_b32 v22, v91, v90, s35
	v_perm_b32 v24, v93, v92, s35
	v_perm_b32 v26, v95, v94, s35
	v_perm_b32 v6, v8, v7, s36
	v_perm_b32 v10, v8, v7, s37
	v_perm_b32 v14, v9, v5, s36
	v_perm_b32 v18, v9, v5, s37
	v_perm_b32 v7, v13, v11, s36
	v_perm_b32 v8, v21, v17, s36
	v_perm_b32 v9, v25, v23, s36
	v_perm_b32 v11, v13, v11, s37
	v_perm_b32 v15, v16, v12, s36
	v_perm_b32 v19, v16, v12, s37
	v_perm_b32 v12, v21, v17, s37
	v_perm_b32 v16, v22, v20, s36
	v_perm_b32 v20, v22, v20, s37
	v_perm_b32 v13, v25, v23, s37
	v_perm_b32 v17, v26, v24, s36
	v_perm_b32 v21, v26, v24, s37
	global_store_dwordx4 v[76:77], v[6:9], off nt
	global_store_dwordx4 v[78:79], v[10:13], off nt
	global_store_dwordx4 v[80:81], v[14:17], off nt
	global_store_dwordx4 v[2:3], v[18:21], off nt
	s_lshr_b32 s49, s4, 5
	s_lshl_b32 s50, s49, 11
	v_mov_b32_e32 v3, v69
	v_lshl_or_b32 v2, s49, 6, v1
	s_sub_i32 s49, s47, s50
	s_waitcnt lgkmcnt(1)
	v_subrev_u32_e32 v8, s50, v4
	s_waitcnt lgkmcnt(0)
; __device__ __forceinline__ void cv_load(const float* W, int N, int nblk, int item, int lane, f32x4 (&tv)[16]) {
;     const int kb = item / nblk, nb = item - kb * nblk; const float* p = W + (size_t)(64 * kb + 16 * (lane >> 4)) * N + 64 * nb + 4 * (lane & 15);
; #pragma unroll
;     for (int i = 0; i < 16; ++i) tv[i] = __builtin_nontemporal_load((const f32x4*)(p + (size_t)i * N));
; }
; template <int MODE> __device__ __forceinline__ void cv_finish(const f32x4 (&tv)[16], int K, int nblk, unsigned char* WT, int item, int lane) {
;     const int kb = item / nblk, nb = item - kb * nblk, k0 = 64 * kb + 16 * (lane >> 4), n0 = 64 * nb + 4 * (lane & 15);
;     unsigned D[16];
; #pragma unroll
;     for (int i = 0; i < 16; ++i) { const f32x2 a = (f32x2){tv[i].x, tv[i].y} * (f32x2){1024.f, 1024.f}, b = (f32x2){tv[i].z, tv[i].w} * (f32x2){1024.f, 1024.f};
;         D[i] = pk4_fp8(a.x, a.y, b.x, b.y); }
	v_lshlrev_b64 v[6:7], 13, v[2:3]
	s_add_i32 s50, s48, s49
	v_lshl_add_u64 v[6:7], s[8:9], 0, v[6:7]
	s_ashr_i32 s51, s50, 31
	v_lshl_add_u64 v[6:7], s[50:51], 2, v[6:7]
	v_lshl_add_u64 v[16:17], v[6:7], 0, v[68:69]
	v_add_co_u32_e32 v18, vcc, s17, v16
	v_add_u32_e32 v8, s48, v8
	s_nop 0
	v_addc_co_u32_e32 v19, vcc, 0, v17, vcc
	v_add_co_u32_e32 v20, vcc, s18, v16
	v_ashrrev_i32_e32 v9, 31, v8
	s_nop 0
	v_addc_co_u32_e32 v21, vcc, 0, v17, vcc
	v_add_co_u32_e32 v22, vcc, s19, v16
	v_add_u32_e32 v10, 1, v8
	s_nop 0
	v_addc_co_u32_e32 v23, vcc, 0, v17, vcc
	v_add_co_u32_e32 v24, vcc, s20, v16
	s_waitcnt vmcnt(2)
	v_add_u32_e32 v12, 2, v8
	v_addc_co_u32_e32 v25, vcc, 0, v17, vcc
	v_add_co_u32_e32 v26, vcc, s21, v16
	v_add_u32_e32 v14, 3, v8
	s_nop 0
	v_addc_co_u32_e32 v27, vcc, 0, v17, vcc
	v_add_co_u32_e32 v30, vcc, s22, v16
	v_lshl_add_u64 v[2:3], s[10:11], 0, v[2:3]
	s_nop 0
	v_addc_co_u32_e32 v31, vcc, 0, v17, vcc
	v_add_co_u32_e32 v34, vcc, s23, v16
	v_lshlrev_b64 v[8:9], 11, v[8:9]
	s_nop 0
	v_addc_co_u32_e32 v35, vcc, 0, v17, vcc
	v_add_co_u32_e32 v38, vcc, s24, v16
	v_ashrrev_i32_e32 v11, 31, v10
	s_nop 0
	v_addc_co_u32_e32 v39, vcc, 0, v17, vcc
	v_add_co_u32_e32 v42, vcc, s25, v16
	v_ashrrev_i32_e32 v13, 31, v12
	s_nop 0
	v_addc_co_u32_e32 v43, vcc, 0, v17, vcc
	v_add_co_u32_e32 v46, vcc, s26, v16
	v_ashrrev_i32_e32 v15, 31, v14
	s_nop 0
	v_addc_co_u32_e32 v47, vcc, 0, v17, vcc
	v_add_co_u32_e32 v50, vcc, s27, v16
	v_lshl_add_u64 v[76:77], v[2:3], 0, v[8:9]
	s_nop 0
	v_addc_co_u32_e32 v51, vcc, 0, v17, vcc
	v_add_co_u32_e32 v54, vcc, s28, v16
	v_lshlrev_b64 v[10:11], 11, v[10:11]
	s_nop 0
	v_addc_co_u32_e32 v55, vcc, 0, v17, vcc
	v_add_co_u32_e32 v58, vcc, s29, v16
	v_lshlrev_b64 v[12:13], 11, v[12:13]
	s_nop 0
	v_addc_co_u32_e32 v59, vcc, 0, v17, vcc
	v_add_co_u32_e32 v62, vcc, s30, v16
	v_lshlrev_b64 v[14:15], 11, v[14:15]
	s_nop 0
	v_addc_co_u32_e32 v63, vcc, 0, v17, vcc
	v_add_co_u32_e32 v70, vcc, s31, v16
	global_load_dwordx4 v[6:9], v[16:17], off nt
	s_nop 0
	v_addc_co_u32_e32 v71, vcc, 0, v17, vcc
	v_lshl_add_u64 v[78:79], v[2:3], 0, v[10:11]
	v_lshl_add_u64 v[80:81], v[2:3], 0, v[12:13]
	v_lshl_add_u64 v[2:3], v[2:3], 0, v[14:15]
	global_load_dwordx4 v[10:13], v[18:19], off nt
	global_load_dwordx4 v[14:17], v[20:21], off nt
	s_nop 0
	global_load_dwordx4 v[18:21], v[22:23], off nt
	s_nop 0
	global_load_dwordx4 v[22:25], v[24:25], off nt
	s_nop 0
	global_load_dwordx4 v[26:29], v[26:27], off nt
	s_nop 0
	global_load_dwordx4 v[30:33], v[30:31], off nt
	s_nop 0
	global_load_dwordx4 v[34:37], v[34:35], off nt
	s_nop 0
	global_load_dwordx4 v[38:41], v[38:39], off nt
	s_nop 0
	global_load_dwordx4 v[42:45], v[42:43], off nt
	s_nop 0
	global_load_dwordx4 v[46:49], v[46:47], off nt
	s_nop 0
	global_load_dwordx4 v[50:53], v[50:51], off nt
	s_nop 0
	global_load_dwordx4 v[54:57], v[54:55], off nt
	s_nop 0
	global_load_dwordx4 v[58:61], v[58:59], off nt
	s_nop 0
	global_load_dwordx4 v[62:65], v[62:63], off nt
	s_nop 0
	global_load_dwordx4 v[70:73], v[70:71], off nt
	v_mov_b32_e32 v5, v69
	v_mov_b32_e32 v75, v69
	v_mov_b32_e32 v82, v69
	v_mov_b32_e32 v83, v69
	v_mov_b32_e32 v84, v69
	v_mov_b32_e32 v85, v69
	v_mov_b32_e32 v86, v69
	v_mov_b32_e32 v87, v69
	v_mov_b32_e32 v88, v69
	v_mov_b32_e32 v89, v69
	v_mov_b32_e32 v90, v69
	v_mov_b32_e32 v91, v69
	v_mov_b32_e32 v92, v69
	v_mov_b32_e32 v93, v69
	v_mov_b32_e32 v94, v69
	v_mov_b32_e32 v95, v69
	s_add_i32 s4, s4, 1
	s_add_i32 s48, s48, 64
	s_waitcnt vmcnt(35)
	v_pk_mul_f32 v[104:105], v[104:105], s[6:7] op_sel_hi:[1,0]
	s_nop 0
	v_med3_f32 v186, v104, s33, v74
	v_med3_f32 v191, v105, s33, v74
	s_waitcnt vmcnt(34)
	v_pk_mul_f32 v[104:105], v[108:109], s[6:7] op_sel_hi:[1,0]
	s_waitcnt vmcnt(33)
	v_pk_mul_f32 v[108:109], v[112:113], s[6:7] op_sel_hi:[1,0]
	s_waitcnt vmcnt(32)
	v_pk_mul_f32 v[112:113], v[116:117], s[6:7] op_sel_hi:[1,0]
	s_waitcnt vmcnt(31)
	v_pk_mul_f32 v[116:117], v[120:121], s[6:7] op_sel_hi:[1,0]
	s_waitcnt vmcnt(30)
	v_pk_mul_f32 v[120:121], v[124:125], s[6:7] op_sel_hi:[1,0]
	s_waitcnt vmcnt(29)
	v_pk_mul_f32 v[124:125], v[128:129], s[6:7] op_sel_hi:[1,0]
	s_waitcnt vmcnt(28)
	v_pk_mul_f32 v[128:129], v[132:133], s[6:7] op_sel_hi:[1,0]
	s_waitcnt vmcnt(27)
	v_pk_mul_f32 v[132:133], v[136:137], s[6:7] op_sel_hi:[1,0]
	s_waitcnt vmcnt(26)
	v_pk_mul_f32 v[136:137], v[140:141], s[6:7] op_sel_hi:[1,0]
	s_waitcnt vmcnt(25)
	v_pk_mul_f32 v[140:141], v[144:145], s[6:7] op_sel_hi:[1,0]
	s_waitcnt vmcnt(24)
	v_pk_mul_f32 v[144:145], v[148:149], s[6:7] op_sel_hi:[1,0]
	s_waitcnt vmcnt(23)
	v_pk_mul_f32 v[148:149], v[152:153], s[6:7] op_sel_hi:[1,0]
	s_waitcnt vmcnt(22)
	v_pk_mul_f32 v[152:153], v[156:157], s[6:7] op_sel_hi:[1,0]
	s_waitcnt vmcnt(21)
	v_pk_mul_f32 v[156:157], v[160:161], s[6:7] op_sel_hi:[1,0]
	s_waitcnt vmcnt(20)
; __device__ __forceinline__ unsigned pk4_fp8(float a, float b, float c, float d) {
;     a = __builtin_fminf(__builtin_fmaxf(a, -448.f), 448.f); b = __builtin_fminf(__builtin_fmaxf(b, -448.f), 448.f); c = __builtin_fminf(__builtin_fmaxf(c, -448.f), 448.f); d = __builtin_fminf(__builtin_fmaxf(d, -448.f), 448.f);
;     int w = 0; w = __builtin_amdgcn_cvt_pk_fp8_f32(a, b, w, false); w = __builtin_amdgcn_cvt_pk_fp8_f32(c, d, w, true); return (unsigned)w;
; }
; template <int MODE> __device__ __forceinline__ void cv_finish(const f32x4 (&tv)[16], int K, int nblk, unsigned char* WT, int item, int lane) {
;     const int kb = item / nblk, nb = item - kb * nblk, k0 = 64 * kb + 16 * (lane >> 4), n0 = 64 * nb + 4 * (lane & 15);
;     unsigned D[16];
; #pragma unroll
;     for (int i = 0; i < 16; ++i) { const f32x2 a = (f32x2){tv[i].x, tv[i].y} * (f32x2){1024.f, 1024.f}, b = (f32x2){tv[i].z, tv[i].w} * (f32x2){1024.f, 1024.f};
;         D[i] = pk4_fp8(a.x, a.y, b.x, b.y); }
;     unsigned O[4][4];
; #pragma unroll
;     for (int q = 0; q < 4; ++q) { const unsigned a = D[4 * q], b = D[4 * q + 1], c = D[4 * q + 2], d = D[4 * q + 3];
;         const unsigned t0 = __builtin_amdgcn_perm(b, a, 0x05010400u), t1 = __builtin_amdgcn_perm(b, a, 0x07030602u), u0 = __builtin_amdgcn_perm(d, c, 0x05010400u), u1 = __builtin_amdgcn_perm(d, c, 0x07030602u);
;         O[0][q] = __builtin_amdgcn_perm(u0, t0, 0x05040100u); O[1][q] = __builtin_amdgcn_perm(u0, t0, 0x07060302u); O[2][q] = __builtin_amdgcn_perm(u1, t1, 0x05040100u); O[3][q] = __builtin_amdgcn_perm(u1, t1, 0x07060302u); }
; #pragma unroll
;     for (int j = 0; j < 4; ++j) { u32x4 o; o.x = O[j][0]; o.y = O[j][1]; o.z = O[j][2]; o.w = O[j][3];
;         __builtin_nontemporal_store(o, (u32x4*)(WT + (size_t)drow<MODE>(n0 + j) * K + k0)); }
; }
	v_pk_mul_f32 v[160:161], v[164:165], s[6:7] op_sel_hi:[1,0]
	v_med3_f32 v104, v104, s33, v74
	v_med3_f32 v105, v105, s33, v74
	v_med3_f32 v108, v108, s33, v74
	v_med3_f32 v109, v109, s33, v74
	v_med3_f32 v112, v112, s33, v74
	v_med3_f32 v113, v113, s33, v74
	v_med3_f32 v116, v116, s33, v74
	v_med3_f32 v117, v117, s33, v74
	v_med3_f32 v120, v120, s33, v74
	v_med3_f32 v121, v121, s33, v74
	v_med3_f32 v124, v124, s33, v74
	v_med3_f32 v125, v125, s33, v74
	v_med3_f32 v128, v128, s33, v74
	v_med3_f32 v129, v129, s33, v74
	v_med3_f32 v132, v132, s33, v74
	v_med3_f32 v133, v133, s33, v74
	v_med3_f32 v136, v136, s33, v74
	v_med3_f32 v137, v137, s33, v74
	v_med3_f32 v140, v140, s33, v74
	v_med3_f32 v141, v141, s33, v74
	v_med3_f32 v144, v144, s33, v74
	v_med3_f32 v145, v145, s33, v74
	v_med3_f32 v148, v148, s33, v74
	v_med3_f32 v149, v149, s33, v74
	v_med3_f32 v152, v152, s33, v74
	v_med3_f32 v153, v153, s33, v74
	v_med3_f32 v156, v156, s33, v74
	v_med3_f32 v157, v157, s33, v74
	v_med3_f32 v160, v160, s33, v74
	v_med3_f32 v161, v161, s33, v74
	v_cvt_pk_fp8_f32 v103, v186, v191
	v_cvt_pk_fp8_f32 v169, v104, v105
	v_cvt_pk_fp8_f32 v102, v108, v109
	v_cvt_pk_fp8_f32 v177, v112, v113
	v_cvt_pk_fp8_f32 v168, v116, v117
	v_cvt_pk_fp8_f32 v179, v120, v121
	v_cvt_pk_fp8_f32 v176, v124, v125
	v_cvt_pk_fp8_f32 v181, v128, v129
	v_cvt_pk_fp8_f32 v178, v132, v133
	v_cvt_pk_fp8_f32 v183, v136, v137
	v_cvt_pk_fp8_f32 v180, v140, v141
	v_cvt_pk_fp8_f32 v185, v144, v145
	v_cvt_pk_fp8_f32 v182, v148, v149
	v_cvt_pk_fp8_f32 v187, v152, v153
	v_cvt_pk_fp8_f32 v184, v156, v157
	v_cvt_pk_fp8_f32 v189, v160, v161
	v_pk_mul_f32 v[106:107], v[106:107], s[6:7] op_sel_hi:[1,0]
	s_nop 0
	v_med3_f32 v188, v106, s33, v74
	v_med3_f32 v193, v107, s33, v74
	v_pk_mul_f32 v[106:107], v[110:111], s[6:7] op_sel_hi:[1,0]
	v_pk_mul_f32 v[110:111], v[114:115], s[6:7] op_sel_hi:[1,0]
	v_pk_mul_f32 v[114:115], v[118:119], s[6:7] op_sel_hi:[1,0]
	v_pk_mul_f32 v[118:119], v[122:123], s[6:7] op_sel_hi:[1,0]
	v_pk_mul_f32 v[122:123], v[126:127], s[6:7] op_sel_hi:[1,0]
	v_pk_mul_f32 v[126:127], v[130:131], s[6:7] op_sel_hi:[1,0]
	v_pk_mul_f32 v[130:131], v[134:135], s[6:7] op_sel_hi:[1,0]
	v_pk_mul_f32 v[134:135], v[138:139], s[6:7] op_sel_hi:[1,0]
	v_pk_mul_f32 v[138:139], v[142:143], s[6:7] op_sel_hi:[1,0]
	v_pk_mul_f32 v[142:143], v[146:147], s[6:7] op_sel_hi:[1,0]
	v_pk_mul_f32 v[146:147], v[150:151], s[6:7] op_sel_hi:[1,0]
	v_pk_mul_f32 v[150:151], v[154:155], s[6:7] op_sel_hi:[1,0]
	v_pk_mul_f32 v[154:155], v[158:159], s[6:7] op_sel_hi:[1,0]
	v_pk_mul_f32 v[158:159], v[162:163], s[6:7] op_sel_hi:[1,0]
	v_pk_mul_f32 v[162:163], v[166:167], s[6:7] op_sel_hi:[1,0]
	v_med3_f32 v106, v106, s33, v74
	v_med3_f32 v107, v107, s33, v74
	v_med3_f32 v110, v110, s33, v74
	v_med3_f32 v111, v111, s33, v74
	v_med3_f32 v114, v114, s33, v74
	v_med3_f32 v115, v115, s33, v74
	v_med3_f32 v118, v118, s33, v74
	v_med3_f32 v119, v119, s33, v74
	v_med3_f32 v122, v122, s33, v74
	v_med3_f32 v123, v123, s33, v74
	v_med3_f32 v126, v126, s33, v74
	v_med3_f32 v127, v127, s33, v74
	v_med3_f32 v130, v130, s33, v74
	v_med3_f32 v131, v131, s33, v74
	v_med3_f32 v134, v134, s33, v74
	v_med3_f32 v135, v135, s33, v74
	v_med3_f32 v138, v138, s33, v74
	v_med3_f32 v139, v139, s33, v74
	v_med3_f32 v142, v142, s33, v74
	v_med3_f32 v143, v143, s33, v74
	v_med3_f32 v146, v146, s33, v74
	v_med3_f32 v147, v147, s33, v74
	v_med3_f32 v150, v150, s33, v74
	v_med3_f32 v151, v151, s33, v74
	v_med3_f32 v154, v154, s33, v74
	v_med3_f32 v155, v155, s33, v74
	v_med3_f32 v158, v158, s33, v74
	v_med3_f32 v159, v159, s33, v74
	v_med3_f32 v162, v162, s33, v74
	v_med3_f32 v163, v163, s33, v74
	v_cvt_pk_fp8_f32 v103, v188, v193 op_sel:[0,0,1]
	v_cvt_pk_fp8_f32 v169, v106, v107 op_sel:[0,0,1]
	v_cvt_pk_fp8_f32 v102, v110, v111 op_sel:[0,0,1]
	v_cvt_pk_fp8_f32 v177, v114, v115 op_sel:[0,0,1]
	v_cvt_pk_fp8_f32 v168, v118, v119 op_sel:[0,0,1]
	v_cvt_pk_fp8_f32 v179, v122, v123 op_sel:[0,0,1]
	v_cvt_pk_fp8_f32 v176, v126, v127 op_sel:[0,0,1]
	v_cvt_pk_fp8_f32 v181, v130, v131 op_sel:[0,0,1]
	v_cvt_pk_fp8_f32 v178, v134, v135 op_sel:[0,0,1]
	v_cvt_pk_fp8_f32 v183, v138, v139 op_sel:[0,0,1]
	v_cvt_pk_fp8_f32 v180, v142, v143 op_sel:[0,0,1]
	v_cvt_pk_fp8_f32 v185, v146, v147 op_sel:[0,0,1]
	v_cvt_pk_fp8_f32 v182, v150, v151 op_sel:[0,0,1]
	v_cvt_pk_fp8_f32 v187, v154, v155 op_sel:[0,0,1]
	v_cvt_pk_fp8_f32 v184, v158, v159 op_sel:[0,0,1]
	v_cvt_pk_fp8_f32 v189, v162, v163 op_sel:[0,0,1]
	v_perm_b32 v105, v169, v103, s34
	v_perm_b32 v103, v169, v103, s35
	v_perm_b32 v106, v177, v102, s34
	v_perm_b32 v107, v177, v102, s35
	v_perm_b32 v109, v179, v168, s34
	v_perm_b32 v111, v181, v176, s34
	v_perm_b32 v115, v183, v178, s34
	v_perm_b32 v119, v185, v180, s34
	v_perm_b32 v121, v187, v182, s34
	v_perm_b32 v123, v189, v184, s34
	v_perm_b32 v110, v179, v168, s35
	v_perm_b32 v114, v181, v176, s35
	v_perm_b32 v118, v183, v178, s35
	v_perm_b32 v120, v185, v180, s35
	v_perm_b32 v122, v187, v182, s35
	v_perm_b32 v124, v189, v184, s35
	v_perm_b32 v104, v106, v105, s36
	v_perm_b32 v108, v106, v105, s37
	v_perm_b32 v112, v107, v103, s36
	v_perm_b32 v116, v107, v103, s37
	v_perm_b32 v105, v111, v109, s36
	v_perm_b32 v106, v119, v115, s36
	v_perm_b32 v107, v123, v121, s36
	v_perm_b32 v109, v111, v109, s37
	v_perm_b32 v113, v114, v110, s36
	v_perm_b32 v117, v114, v110, s37
	v_perm_b32 v110, v119, v115, s37
	v_perm_b32 v114, v120, v118, s36
	v_perm_b32 v118, v120, v118, s37
	v_perm_b32 v111, v123, v121, s37
	v_perm_b32 v115, v124, v122, s36
	v_perm_b32 v119, v124, v122, s37
	global_store_dwordx4 v[170:171], v[104:107], off nt
	global_store_dwordx4 v[172:173], v[108:111], off nt
	global_store_dwordx4 v[174:175], v[112:115], off nt
	global_store_dwordx4 v[100:101], v[116:119], off nt
	s_lshr_b32 s49, s4, 5
	s_lshl_b32 s50, s49, 11
	v_mov_b32_e32 v101, v69
	v_lshl_or_b32 v100, s49, 6, v1
	s_sub_i32 s49, s47, s50
	s_waitcnt lgkmcnt(1)
; __device__ __forceinline__ void cv_load(const float* W, int N, int nblk, int item, int lane, f32x4 (&tv)[16]) {
;     const int kb = item / nblk, nb = item - kb * nblk; const float* p = W + (size_t)(64 * kb + 16 * (lane >> 4)) * N + 64 * nb + 4 * (lane & 15);
; #pragma unroll
;     for (int i = 0; i < 16; ++i) tv[i] = __builtin_nontemporal_load((const f32x4*)(p + (size_t)i * N));
; }
; template <int MODE> __device__ __forceinline__ void cv_finish(const f32x4 (&tv)[16], int K, int nblk, unsigned char* WT, int item, int lane) {
;     const int kb = item / nblk, nb = item - kb * nblk, k0 = 64 * kb + 16 * (lane >> 4), n0 = 64 * nb + 4 * (lane & 15);
;     unsigned D[16];
; #pragma unroll
;     for (int i = 0; i < 16; ++i) { const f32x2 a = (f32x2){tv[i].x, tv[i].y} * (f32x2){1024.f, 1024.f}, b = (f32x2){tv[i].z, tv[i].w} * (f32x2){1024.f, 1024.f};
;         D[i] = pk4_fp8(a.x, a.y, b.x, b.y); }
	v_subrev_u32_e32 v106, s50, v4
	s_waitcnt lgkmcnt(0)
	v_lshlrev_b64 v[104:105], 13, v[100:101]
	s_add_i32 s50, s48, s49
	v_lshl_add_u64 v[104:105], s[8:9], 0, v[104:105]
	s_ashr_i32 s51, s50, 31
	v_lshl_add_u64 v[104:105], s[50:51], 2, v[104:105]
	v_lshl_add_u64 v[114:115], v[104:105], 0, v[68:69]
	v_add_co_u32_e32 v116, vcc, s17, v114
	v_add_u32_e32 v106, s48, v106
	s_nop 0
	v_addc_co_u32_e32 v117, vcc, 0, v115, vcc
	v_add_co_u32_e32 v118, vcc, s18, v114
	v_ashrrev_i32_e32 v107, 31, v106
	s_nop 0
	v_addc_co_u32_e32 v119, vcc, 0, v115, vcc
	v_add_co_u32_e32 v120, vcc, s19, v114
	v_add_u32_e32 v108, 1, v106
	s_nop 0
	v_addc_co_u32_e32 v121, vcc, 0, v115, vcc
	v_add_co_u32_e32 v122, vcc, s20, v114
	s_waitcnt vmcnt(2)
	v_add_u32_e32 v110, 2, v106
	v_addc_co_u32_e32 v123, vcc, 0, v115, vcc
	v_add_co_u32_e32 v124, vcc, s21, v114
	v_add_u32_e32 v112, 3, v106
	s_nop 0
	v_addc_co_u32_e32 v125, vcc, 0, v115, vcc
	v_add_co_u32_e32 v128, vcc, s22, v114
	v_lshl_add_u64 v[100:101], s[10:11], 0, v[100:101]
	s_nop 0
	v_addc_co_u32_e32 v129, vcc, 0, v115, vcc
	v_add_co_u32_e32 v132, vcc, s23, v114
	v_lshlrev_b64 v[106:107], 11, v[106:107]
	s_nop 0
	v_addc_co_u32_e32 v133, vcc, 0, v115, vcc
	v_add_co_u32_e32 v136, vcc, s24, v114
	v_ashrrev_i32_e32 v109, 31, v108
	s_nop 0
	v_addc_co_u32_e32 v137, vcc, 0, v115, vcc
	v_add_co_u32_e32 v140, vcc, s25, v114
	v_ashrrev_i32_e32 v111, 31, v110
	s_nop 0
	v_addc_co_u32_e32 v141, vcc, 0, v115, vcc
	v_add_co_u32_e32 v144, vcc, s26, v114
	v_ashrrev_i32_e32 v113, 31, v112
	s_nop 0
	v_addc_co_u32_e32 v145, vcc, 0, v115, vcc
	v_add_co_u32_e32 v148, vcc, s27, v114
	v_lshl_add_u64 v[170:171], v[100:101], 0, v[106:107]
	s_nop 0
	v_addc_co_u32_e32 v149, vcc, 0, v115, vcc
	v_add_co_u32_e32 v152, vcc, s28, v114
	v_lshlrev_b64 v[108:109], 11, v[108:109]
	s_nop 0
	v_addc_co_u32_e32 v153, vcc, 0, v115, vcc
	v_add_co_u32_e32 v156, vcc, s29, v114
	v_lshlrev_b64 v[110:111], 11, v[110:111]
	s_nop 0
	v_addc_co_u32_e32 v157, vcc, 0, v115, vcc
	v_add_co_u32_e32 v160, vcc, s30, v114
	v_lshlrev_b64 v[112:113], 11, v[112:113]
	s_nop 0
	v_addc_co_u32_e32 v161, vcc, 0, v115, vcc
	v_add_co_u32_e32 v164, vcc, s31, v114
	global_load_dwordx4 v[104:107], v[114:115], off nt
	s_nop 0
	v_addc_co_u32_e32 v165, vcc, 0, v115, vcc
	v_lshl_add_u64 v[172:173], v[100:101], 0, v[108:109]
	v_lshl_add_u64 v[174:175], v[100:101], 0, v[110:111]
	v_lshl_add_u64 v[100:101], v[100:101], 0, v[112:113]
	global_load_dwordx4 v[108:111], v[116:117], off nt
	global_load_dwordx4 v[112:115], v[118:119], off nt
	s_nop 0
	global_load_dwordx4 v[116:119], v[120:121], off nt
	s_nop 0
	global_load_dwordx4 v[120:123], v[122:123], off nt
	s_nop 0
	global_load_dwordx4 v[124:127], v[124:125], off nt
	s_nop 0
	global_load_dwordx4 v[128:131], v[128:129], off nt
	s_nop 0
	global_load_dwordx4 v[132:135], v[132:133], off nt
	s_nop 0
	global_load_dwordx4 v[136:139], v[136:137], off nt
	s_nop 0
	global_load_dwordx4 v[140:143], v[140:141], off nt
	s_nop 0
	global_load_dwordx4 v[144:147], v[144:145], off nt
	s_nop 0
	global_load_dwordx4 v[148:151], v[148:149], off nt
	s_nop 0
	global_load_dwordx4 v[152:155], v[152:153], off nt
	s_nop 0
	global_load_dwordx4 v[156:159], v[156:157], off nt
	s_nop 0
	global_load_dwordx4 v[160:163], v[160:161], off nt
	s_nop 0
	global_load_dwordx4 v[164:167], v[164:165], off nt
	v_mov_b32_e32 v103, v69
	v_mov_b32_e32 v169, v69
	v_mov_b32_e32 v102, v69
	v_mov_b32_e32 v177, v69
	v_mov_b32_e32 v168, v69
	v_mov_b32_e32 v179, v69
	v_mov_b32_e32 v176, v69
	v_mov_b32_e32 v181, v69
	v_mov_b32_e32 v178, v69
	v_mov_b32_e32 v183, v69
	v_mov_b32_e32 v180, v69
	v_mov_b32_e32 v185, v69
	v_mov_b32_e32 v182, v69
	v_mov_b32_e32 v187, v69
	v_mov_b32_e32 v184, v69
	v_mov_b32_e32 v189, v69
	s_add_i32 s4, s4, 1
	s_add_i32 s48, s48, 64
	s_cmpk_eq_i32 s48, 0x100
	s_waitcnt vmcnt(35)
	v_pk_mul_f32 v[6:7], v[6:7], s[6:7] op_sel_hi:[1,0]
	s_nop 0
	v_med3_f32 v96, v6, s33, v74
	v_med3_f32 v97, v7, s33, v74
	s_waitcnt vmcnt(34)
	v_pk_mul_f32 v[6:7], v[10:11], s[6:7] op_sel_hi:[1,0]
	s_waitcnt vmcnt(33)
	v_pk_mul_f32 v[10:11], v[14:15], s[6:7] op_sel_hi:[1,0]
	s_waitcnt vmcnt(32)
	v_pk_mul_f32 v[14:15], v[18:19], s[6:7] op_sel_hi:[1,0]
	s_waitcnt vmcnt(31)
	v_pk_mul_f32 v[18:19], v[22:23], s[6:7] op_sel_hi:[1,0]
	s_waitcnt vmcnt(30)
	v_pk_mul_f32 v[22:23], v[26:27], s[6:7] op_sel_hi:[1,0]
	s_waitcnt vmcnt(29)
	v_pk_mul_f32 v[26:27], v[30:31], s[6:7] op_sel_hi:[1,0]
	s_waitcnt vmcnt(28)
	v_pk_mul_f32 v[30:31], v[34:35], s[6:7] op_sel_hi:[1,0]
	s_waitcnt vmcnt(27)
	v_pk_mul_f32 v[34:35], v[38:39], s[6:7] op_sel_hi:[1,0]
	s_waitcnt vmcnt(26)
	v_pk_mul_f32 v[38:39], v[42:43], s[6:7] op_sel_hi:[1,0]
	s_waitcnt vmcnt(25)
	v_pk_mul_f32 v[42:43], v[46:47], s[6:7] op_sel_hi:[1,0]
	s_waitcnt vmcnt(24)
	v_pk_mul_f32 v[46:47], v[50:51], s[6:7] op_sel_hi:[1,0]
	s_waitcnt vmcnt(23)
	v_pk_mul_f32 v[50:51], v[54:55], s[6:7] op_sel_hi:[1,0]
	s_waitcnt vmcnt(22)
	v_pk_mul_f32 v[54:55], v[58:59], s[6:7] op_sel_hi:[1,0]
	s_waitcnt vmcnt(21)
	v_pk_mul_f32 v[58:59], v[62:63], s[6:7] op_sel_hi:[1,0]
	s_waitcnt vmcnt(20)
; __device__ __forceinline__ unsigned pk4_fp8(float a, float b, float c, float d) {
;     a = __builtin_fminf(__builtin_fmaxf(a, -448.f), 448.f); b = __builtin_fminf(__builtin_fmaxf(b, -448.f), 448.f); c = __builtin_fminf(__builtin_fmaxf(c, -448.f), 448.f); d = __builtin_fminf(__builtin_fmaxf(d, -448.f), 448.f);
;     int w = 0; w = __builtin_amdgcn_cvt_pk_fp8_f32(a, b, w, false); w = __builtin_amdgcn_cvt_pk_fp8_f32(c, d, w, true); return (unsigned)w;
; }
; template <int MODE> __device__ __forceinline__ void cv_finish(const f32x4 (&tv)[16], int K, int nblk, unsigned char* WT, int item, int lane) {
;     const int kb = item / nblk, nb = item - kb * nblk, k0 = 64 * kb + 16 * (lane >> 4), n0 = 64 * nb + 4 * (lane & 15);
;     unsigned D[16];
; #pragma unroll
;     for (int i = 0; i < 16; ++i) { const f32x2 a = (f32x2){tv[i].x, tv[i].y} * (f32x2){1024.f, 1024.f}, b = (f32x2){tv[i].z, tv[i].w} * (f32x2){1024.f, 1024.f};
;         D[i] = pk4_fp8(a.x, a.y, b.x, b.y); }
;     unsigned O[4][4];
; #pragma unroll
;     for (int q = 0; q < 4; ++q) { const unsigned a = D[4 * q], b = D[4 * q + 1], c = D[4 * q + 2], d = D[4 * q + 3];
;         const unsigned t0 = __builtin_amdgcn_perm(b, a, 0x05010400u), t1 = __builtin_amdgcn_perm(b, a, 0x07030602u), u0 = __builtin_amdgcn_perm(d, c, 0x05010400u), u1 = __builtin_amdgcn_perm(d, c, 0x07030602u);
;         O[0][q] = __builtin_amdgcn_perm(u0, t0, 0x05040100u); O[1][q] = __builtin_amdgcn_perm(u0, t0, 0x07060302u); O[2][q] = __builtin_amdgcn_perm(u1, t1, 0x05040100u); O[3][q] = __builtin_amdgcn_perm(u1, t1, 0x07060302u); }
; #pragma unroll
;     for (int j = 0; j < 4; ++j) { u32x4 o; o.x = O[j][0]; o.y = O[j][1]; o.z = O[j][2]; o.w = O[j][3];
;         __builtin_nontemporal_store(o, (u32x4*)(WT + (size_t)drow<MODE>(n0 + j) * K + k0)); }
; }
	v_pk_mul_f32 v[62:63], v[70:71], s[6:7] op_sel_hi:[1,0]
	v_med3_f32 v6, v6, s33, v74
	v_med3_f32 v7, v7, s33, v74
	v_med3_f32 v10, v10, s33, v74
	v_med3_f32 v11, v11, s33, v74
	v_med3_f32 v14, v14, s33, v74
	v_med3_f32 v15, v15, s33, v74
	v_med3_f32 v18, v18, s33, v74
	v_med3_f32 v19, v19, s33, v74
	v_med3_f32 v22, v22, s33, v74
	v_med3_f32 v23, v23, s33, v74
	v_med3_f32 v26, v26, s33, v74
	v_med3_f32 v27, v27, s33, v74
	v_med3_f32 v30, v30, s33, v74
	v_med3_f32 v31, v31, s33, v74
	v_med3_f32 v34, v34, s33, v74
	v_med3_f32 v35, v35, s33, v74
	v_med3_f32 v38, v38, s33, v74
	v_med3_f32 v39, v39, s33, v74
	v_med3_f32 v42, v42, s33, v74
	v_med3_f32 v43, v43, s33, v74
	v_med3_f32 v46, v46, s33, v74
	v_med3_f32 v47, v47, s33, v74
	v_med3_f32 v50, v50, s33, v74
	v_med3_f32 v51, v51, s33, v74
	v_med3_f32 v54, v54, s33, v74
	v_med3_f32 v55, v55, s33, v74
	v_med3_f32 v58, v58, s33, v74
	v_med3_f32 v59, v59, s33, v74
	v_med3_f32 v62, v62, s33, v74
	v_med3_f32 v63, v63, s33, v74
	v_cvt_pk_fp8_f32 v5, v96, v97
	v_cvt_pk_fp8_f32 v75, v6, v7
	v_cvt_pk_fp8_f32 v82, v10, v11
	v_cvt_pk_fp8_f32 v83, v14, v15
	v_cvt_pk_fp8_f32 v84, v18, v19
	v_cvt_pk_fp8_f32 v85, v22, v23
	v_cvt_pk_fp8_f32 v86, v26, v27
	v_cvt_pk_fp8_f32 v87, v30, v31
	v_cvt_pk_fp8_f32 v88, v34, v35
	v_cvt_pk_fp8_f32 v89, v38, v39
	v_cvt_pk_fp8_f32 v90, v42, v43
	v_cvt_pk_fp8_f32 v91, v46, v47
	v_cvt_pk_fp8_f32 v92, v50, v51
	v_cvt_pk_fp8_f32 v93, v54, v55
	v_cvt_pk_fp8_f32 v94, v58, v59
	v_cvt_pk_fp8_f32 v95, v62, v63
	v_pk_mul_f32 v[8:9], v[8:9], s[6:7] op_sel_hi:[1,0]
	s_nop 0
	v_med3_f32 v98, v8, s33, v74
	v_med3_f32 v99, v9, s33, v74
	v_pk_mul_f32 v[8:9], v[12:13], s[6:7] op_sel_hi:[1,0]
	v_pk_mul_f32 v[12:13], v[16:17], s[6:7] op_sel_hi:[1,0]
	v_pk_mul_f32 v[16:17], v[20:21], s[6:7] op_sel_hi:[1,0]
	v_pk_mul_f32 v[20:21], v[24:25], s[6:7] op_sel_hi:[1,0]
	v_pk_mul_f32 v[24:25], v[28:29], s[6:7] op_sel_hi:[1,0]
	v_pk_mul_f32 v[28:29], v[32:33], s[6:7] op_sel_hi:[1,0]
	v_pk_mul_f32 v[32:33], v[36:37], s[6:7] op_sel_hi:[1,0]
	v_pk_mul_f32 v[36:37], v[40:41], s[6:7] op_sel_hi:[1,0]
	v_pk_mul_f32 v[40:41], v[44:45], s[6:7] op_sel_hi:[1,0]
	v_pk_mul_f32 v[44:45], v[48:49], s[6:7] op_sel_hi:[1,0]
	v_pk_mul_f32 v[48:49], v[52:53], s[6:7] op_sel_hi:[1,0]
	v_pk_mul_f32 v[52:53], v[56:57], s[6:7] op_sel_hi:[1,0]
	v_pk_mul_f32 v[56:57], v[60:61], s[6:7] op_sel_hi:[1,0]
	v_pk_mul_f32 v[60:61], v[64:65], s[6:7] op_sel_hi:[1,0]
	v_pk_mul_f32 v[64:65], v[72:73], s[6:7] op_sel_hi:[1,0]
	v_med3_f32 v8, v8, s33, v74
	v_med3_f32 v9, v9, s33, v74
	v_med3_f32 v12, v12, s33, v74
	v_med3_f32 v13, v13, s33, v74
	v_med3_f32 v16, v16, s33, v74
	v_med3_f32 v17, v17, s33, v74
	v_med3_f32 v20, v20, s33, v74
	v_med3_f32 v21, v21, s33, v74
	v_med3_f32 v24, v24, s33, v74
	v_med3_f32 v25, v25, s33, v74
	v_med3_f32 v28, v28, s33, v74
	v_med3_f32 v29, v29, s33, v74
	v_med3_f32 v32, v32, s33, v74
	v_med3_f32 v33, v33, s33, v74
	v_med3_f32 v36, v36, s33, v74
	v_med3_f32 v37, v37, s33, v74
	v_med3_f32 v40, v40, s33, v74
	v_med3_f32 v41, v41, s33, v74
	v_med3_f32 v44, v44, s33, v74
	v_med3_f32 v45, v45, s33, v74
	v_med3_f32 v48, v48, s33, v74
	v_med3_f32 v49, v49, s33, v74
	v_med3_f32 v52, v52, s33, v74
	v_med3_f32 v53, v53, s33, v74
	v_med3_f32 v56, v56, s33, v74
	v_med3_f32 v57, v57, s33, v74
	v_med3_f32 v60, v60, s33, v74
	v_med3_f32 v61, v61, s33, v74
	v_med3_f32 v64, v64, s33, v74
	v_med3_f32 v65, v65, s33, v74
	v_cvt_pk_fp8_f32 v5, v98, v99 op_sel:[0,0,1]
	v_cvt_pk_fp8_f32 v75, v8, v9 op_sel:[0,0,1]
	v_cvt_pk_fp8_f32 v82, v12, v13 op_sel:[0,0,1]
	v_cvt_pk_fp8_f32 v83, v16, v17 op_sel:[0,0,1]
	v_cvt_pk_fp8_f32 v84, v20, v21 op_sel:[0,0,1]
	v_cvt_pk_fp8_f32 v85, v24, v25 op_sel:[0,0,1]
	v_cvt_pk_fp8_f32 v86, v28, v29 op_sel:[0,0,1]
	v_cvt_pk_fp8_f32 v87, v32, v33 op_sel:[0,0,1]
	v_cvt_pk_fp8_f32 v88, v36, v37 op_sel:[0,0,1]
	v_cvt_pk_fp8_f32 v89, v40, v41 op_sel:[0,0,1]
	v_cvt_pk_fp8_f32 v90, v44, v45 op_sel:[0,0,1]
	v_cvt_pk_fp8_f32 v91, v48, v49 op_sel:[0,0,1]
	v_cvt_pk_fp8_f32 v92, v52, v53 op_sel:[0,0,1]
	v_cvt_pk_fp8_f32 v93, v56, v57 op_sel:[0,0,1]
	v_cvt_pk_fp8_f32 v94, v60, v61 op_sel:[0,0,1]
	v_cvt_pk_fp8_f32 v95, v64, v65 op_sel:[0,0,1]
	v_perm_b32 v7, v75, v5, s34
	v_perm_b32 v5, v75, v5, s35
	v_perm_b32 v8, v83, v82, s34
	v_perm_b32 v9, v83, v82, s35
	v_perm_b32 v11, v85, v84, s34
	v_perm_b32 v13, v87, v86, s34
	v_perm_b32 v17, v89, v88, s34
	v_perm_b32 v21, v91, v90, s34
	v_perm_b32 v23, v93, v92, s34
	v_perm_b32 v25, v95, v94, s34
	v_perm_b32 v12, v85, v84, s35
	v_perm_b32 v16, v87, v86, s35
	v_perm_b32 v20, v89, v88, s35
	v_perm_b32 v22, v91, v90, s35
	v_perm_b32 v24, v93, v92, s35
	v_perm_b32 v26, v95, v94, s35
	v_perm_b32 v6, v8, v7, s36
	v_perm_b32 v10, v8, v7, s37
	v_perm_b32 v14, v9, v5, s36
	v_perm_b32 v18, v9, v5, s37
	v_perm_b32 v7, v13, v11, s36
	v_perm_b32 v8, v21, v17, s36
	v_perm_b32 v9, v25, v23, s36
	v_perm_b32 v11, v13, v11, s37
	v_perm_b32 v15, v16, v12, s36
	v_perm_b32 v19, v16, v12, s37
	v_perm_b32 v12, v21, v17, s37
	v_perm_b32 v16, v22, v20, s36
	v_perm_b32 v20, v22, v20, s37
	v_perm_b32 v13, v25, v23, s37
	v_perm_b32 v17, v26, v24, s36
	v_perm_b32 v21, v26, v24, s37
	global_store_dwordx4 v[76:77], v[6:9], off nt
	global_store_dwordx4 v[78:79], v[10:13], off nt
	global_store_dwordx4 v[80:81], v[14:17], off nt
	global_store_dwordx4 v[2:3], v[18:21], off nt
	s_waitcnt vmcnt(19)
	v_pk_mul_f32 v[104:105], v[104:105], s[6:7] op_sel_hi:[1,0]
	s_nop 0
	v_med3_f32 v186, v104, s33, v74
	v_med3_f32 v191, v105, s33, v74
	s_waitcnt vmcnt(18)
	v_pk_mul_f32 v[104:105], v[108:109], s[6:7] op_sel_hi:[1,0]
	s_waitcnt vmcnt(17)
	v_pk_mul_f32 v[108:109], v[112:113], s[6:7] op_sel_hi:[1,0]
	s_waitcnt vmcnt(16)
; template <int MODE> __device__ __forceinline__ void cv_finish(const f32x4 (&tv)[16], int K, int nblk, unsigned char* WT, int item, int lane) {
;     const int kb = item / nblk, nb = item - kb * nblk, k0 = 64 * kb + 16 * (lane >> 4), n0 = 64 * nb + 4 * (lane & 15);
;     unsigned D[16];
; #pragma unroll
;     for (int i = 0; i < 16; ++i) { const f32x2 a = (f32x2){tv[i].x, tv[i].y} * (f32x2){1024.f, 1024.f}, b = (f32x2){tv[i].z, tv[i].w} * (f32x2){1024.f, 1024.f};
;         D[i] = pk4_fp8(a.x, a.y, b.x, b.y); }
;     unsigned O[4][4];
; #pragma unroll
;     for (int q = 0; q < 4; ++q) { const unsigned a = D[4 * q], b = D[4 * q + 1], c = D[4 * q + 2], d = D[4 * q + 3];
;         const unsigned t0 = __builtin_amdgcn_perm(b, a, 0x05010400u), t1 = __builtin_amdgcn_perm(b, a, 0x07030602u), u0 = __builtin_amdgcn_perm(d, c, 0x05010400u), u1 = __builtin_amdgcn_perm(d, c, 0x07030602u);
;         O[0][q] = __builtin_amdgcn_perm(u0, t0, 0x05040100u); O[1][q] = __builtin_amdgcn_perm(u0, t0, 0x07060302u); O[2][q] = __builtin_amdgcn_perm(u1, t1, 0x05040100u); O[3][q] = __builtin_amdgcn_perm(u1, t1, 0x07060302u); }
; #pragma unroll
;     for (int j = 0; j < 4; ++j) { u32x4 o; o.x = O[j][0]; o.y = O[j][1]; o.z = O[j][2]; o.w = O[j][3];
;         __builtin_nontemporal_store(o, (u32x4*)(WT + (size_t)drow<MODE>(n0 + j) * K + k0)); }
; }
; template <int MODE> __device__ __forceinline__ void cv_run4(const float* W, int K, int N, unsigned char* WT, int item0, int lane) {
;     const int nblk = N / 64; f32x4 ta[16];
; #pragma unroll 1
;     for (int j = 0; j < 4; ++j) { cv_load(W, N, nblk, item0 + j, lane, ta); cv_finish<MODE>(ta, K, nblk, WT, item0 + j, lane); }
	v_pk_mul_f32 v[112:113], v[116:117], s[6:7] op_sel_hi:[1,0]
	s_waitcnt vmcnt(15)
	v_pk_mul_f32 v[116:117], v[120:121], s[6:7] op_sel_hi:[1,0]
	s_waitcnt vmcnt(14)
	v_pk_mul_f32 v[120:121], v[124:125], s[6:7] op_sel_hi:[1,0]
	s_waitcnt vmcnt(13)
	v_pk_mul_f32 v[124:125], v[128:129], s[6:7] op_sel_hi:[1,0]
	s_waitcnt vmcnt(12)
	v_pk_mul_f32 v[128:129], v[132:133], s[6:7] op_sel_hi:[1,0]
	s_waitcnt vmcnt(11)
	v_pk_mul_f32 v[132:133], v[136:137], s[6:7] op_sel_hi:[1,0]
	s_waitcnt vmcnt(10)
	v_pk_mul_f32 v[136:137], v[140:141], s[6:7] op_sel_hi:[1,0]
	s_waitcnt vmcnt(9)
	v_pk_mul_f32 v[140:141], v[144:145], s[6:7] op_sel_hi:[1,0]
	s_waitcnt vmcnt(8)
	v_pk_mul_f32 v[144:145], v[148:149], s[6:7] op_sel_hi:[1,0]
	s_waitcnt vmcnt(7)
	v_pk_mul_f32 v[148:149], v[152:153], s[6:7] op_sel_hi:[1,0]
	s_waitcnt vmcnt(6)
	v_pk_mul_f32 v[152:153], v[156:157], s[6:7] op_sel_hi:[1,0]
	s_waitcnt vmcnt(5)
	v_pk_mul_f32 v[156:157], v[160:161], s[6:7] op_sel_hi:[1,0]
	s_waitcnt vmcnt(4)
	v_pk_mul_f32 v[160:161], v[164:165], s[6:7] op_sel_hi:[1,0]
	v_med3_f32 v104, v104, s33, v74
	v_med3_f32 v105, v105, s33, v74
	v_med3_f32 v108, v108, s33, v74
	v_med3_f32 v109, v109, s33, v74
	v_med3_f32 v112, v112, s33, v74
	v_med3_f32 v113, v113, s33, v74
	v_med3_f32 v116, v116, s33, v74
	v_med3_f32 v117, v117, s33, v74
	v_med3_f32 v120, v120, s33, v74
	v_med3_f32 v121, v121, s33, v74
	v_med3_f32 v124, v124, s33, v74
	v_med3_f32 v125, v125, s33, v74
	v_med3_f32 v128, v128, s33, v74
	v_med3_f32 v129, v129, s33, v74
	v_med3_f32 v132, v132, s33, v74
	v_med3_f32 v133, v133, s33, v74
	v_med3_f32 v136, v136, s33, v74
	v_med3_f32 v137, v137, s33, v74
	v_med3_f32 v140, v140, s33, v74
	v_med3_f32 v141, v141, s33, v74
	v_med3_f32 v144, v144, s33, v74
	v_med3_f32 v145, v145, s33, v74
	v_med3_f32 v148, v148, s33, v74
	v_med3_f32 v149, v149, s33, v74
	v_med3_f32 v152, v152, s33, v74
	v_med3_f32 v153, v153, s33, v74
	v_med3_f32 v156, v156, s33, v74
	v_med3_f32 v157, v157, s33, v74
	v_med3_f32 v160, v160, s33, v74
	v_med3_f32 v161, v161, s33, v74
	v_cvt_pk_fp8_f32 v103, v186, v191
	v_cvt_pk_fp8_f32 v169, v104, v105
	v_cvt_pk_fp8_f32 v102, v108, v109
	v_cvt_pk_fp8_f32 v177, v112, v113
	v_cvt_pk_fp8_f32 v168, v116, v117
	v_cvt_pk_fp8_f32 v179, v120, v121
	v_cvt_pk_fp8_f32 v176, v124, v125
	v_cvt_pk_fp8_f32 v181, v128, v129
	v_cvt_pk_fp8_f32 v178, v132, v133
	v_cvt_pk_fp8_f32 v183, v136, v137
	v_cvt_pk_fp8_f32 v180, v140, v141
	v_cvt_pk_fp8_f32 v185, v144, v145
	v_cvt_pk_fp8_f32 v182, v148, v149
	v_cvt_pk_fp8_f32 v187, v152, v153
	v_cvt_pk_fp8_f32 v184, v156, v157
	v_cvt_pk_fp8_f32 v189, v160, v161
	v_pk_mul_f32 v[106:107], v[106:107], s[6:7] op_sel_hi:[1,0]
	s_nop 0
	v_med3_f32 v188, v106, s33, v74
	v_med3_f32 v193, v107, s33, v74
	v_pk_mul_f32 v[106:107], v[110:111], s[6:7] op_sel_hi:[1,0]
	v_pk_mul_f32 v[110:111], v[114:115], s[6:7] op_sel_hi:[1,0]
	v_pk_mul_f32 v[114:115], v[118:119], s[6:7] op_sel_hi:[1,0]
	v_pk_mul_f32 v[118:119], v[122:123], s[6:7] op_sel_hi:[1,0]
	v_pk_mul_f32 v[122:123], v[126:127], s[6:7] op_sel_hi:[1,0]
	v_pk_mul_f32 v[126:127], v[130:131], s[6:7] op_sel_hi:[1,0]
	v_pk_mul_f32 v[130:131], v[134:135], s[6:7] op_sel_hi:[1,0]
	v_pk_mul_f32 v[134:135], v[138:139], s[6:7] op_sel_hi:[1,0]
	v_pk_mul_f32 v[138:139], v[142:143], s[6:7] op_sel_hi:[1,0]
	v_pk_mul_f32 v[142:143], v[146:147], s[6:7] op_sel_hi:[1,0]
	v_pk_mul_f32 v[146:147], v[150:151], s[6:7] op_sel_hi:[1,0]
	v_pk_mul_f32 v[150:151], v[154:155], s[6:7] op_sel_hi:[1,0]
	v_pk_mul_f32 v[154:155], v[158:159], s[6:7] op_sel_hi:[1,0]
	v_pk_mul_f32 v[158:159], v[162:163], s[6:7] op_sel_hi:[1,0]
	v_pk_mul_f32 v[162:163], v[166:167], s[6:7] op_sel_hi:[1,0]
	v_med3_f32 v106, v106, s33, v74
	v_med3_f32 v107, v107, s33, v74
	v_med3_f32 v110, v110, s33, v74
	v_med3_f32 v111, v111, s33, v74
	v_med3_f32 v114, v114, s33, v74
	v_med3_f32 v115, v115, s33, v74
	v_med3_f32 v118, v118, s33, v74
	v_med3_f32 v119, v119, s33, v74
	v_med3_f32 v122, v122, s33, v74
	v_med3_f32 v123, v123, s33, v74
	v_med3_f32 v126, v126, s33, v74
	v_med3_f32 v127, v127, s33, v74
	v_med3_f32 v130, v130, s33, v74
	v_med3_f32 v131, v131, s33, v74
	v_med3_f32 v134, v134, s33, v74
	v_med3_f32 v135, v135, s33, v74
	v_med3_f32 v138, v138, s33, v74
	v_med3_f32 v139, v139, s33, v74
	v_med3_f32 v142, v142, s33, v74
	v_med3_f32 v143, v143, s33, v74
	v_med3_f32 v146, v146, s33, v74
	v_med3_f32 v147, v147, s33, v74
	v_med3_f32 v150, v150, s33, v74
	v_med3_f32 v151, v151, s33, v74
	v_med3_f32 v154, v154, s33, v74
	v_med3_f32 v155, v155, s33, v74
	v_med3_f32 v158, v158, s33, v74
	v_med3_f32 v159, v159, s33, v74
	v_med3_f32 v162, v162, s33, v74
	v_med3_f32 v163, v163, s33, v74
	v_cvt_pk_fp8_f32 v103, v188, v193 op_sel:[0,0,1]
	v_cvt_pk_fp8_f32 v169, v106, v107 op_sel:[0,0,1]
	v_cvt_pk_fp8_f32 v102, v110, v111 op_sel:[0,0,1]
	v_cvt_pk_fp8_f32 v177, v114, v115 op_sel:[0,0,1]
	v_cvt_pk_fp8_f32 v168, v118, v119 op_sel:[0,0,1]
	v_cvt_pk_fp8_f32 v179, v122, v123 op_sel:[0,0,1]
	v_cvt_pk_fp8_f32 v176, v126, v127 op_sel:[0,0,1]
	v_cvt_pk_fp8_f32 v181, v130, v131 op_sel:[0,0,1]
	v_cvt_pk_fp8_f32 v178, v134, v135 op_sel:[0,0,1]
	v_cvt_pk_fp8_f32 v183, v138, v139 op_sel:[0,0,1]
	v_cvt_pk_fp8_f32 v180, v142, v143 op_sel:[0,0,1]
	v_cvt_pk_fp8_f32 v185, v146, v147 op_sel:[0,0,1]
	v_cvt_pk_fp8_f32 v182, v150, v151 op_sel:[0,0,1]
	v_cvt_pk_fp8_f32 v187, v154, v155 op_sel:[0,0,1]
	v_cvt_pk_fp8_f32 v184, v158, v159 op_sel:[0,0,1]
	v_cvt_pk_fp8_f32 v189, v162, v163 op_sel:[0,0,1]
	v_perm_b32 v105, v169, v103, s34
	v_perm_b32 v103, v169, v103, s35
	v_perm_b32 v106, v177, v102, s34
	v_perm_b32 v107, v177, v102, s35
	v_perm_b32 v109, v179, v168, s34
	v_perm_b32 v111, v181, v176, s34
	v_perm_b32 v115, v183, v178, s34
	v_perm_b32 v119, v185, v180, s34
	v_perm_b32 v121, v187, v182, s34
	v_perm_b32 v123, v189, v184, s34
	v_perm_b32 v110, v179, v168, s35
	v_perm_b32 v114, v181, v176, s35
	v_perm_b32 v118, v183, v178, s35
	v_perm_b32 v120, v185, v180, s35
	v_perm_b32 v122, v187, v182, s35
	v_perm_b32 v124, v189, v184, s35
	v_perm_b32 v104, v106, v105, s36
	v_perm_b32 v108, v106, v105, s37
	v_perm_b32 v112, v107, v103, s36
	v_perm_b32 v116, v107, v103, s37
	v_perm_b32 v105, v111, v109, s36
	v_perm_b32 v106, v119, v115, s36
	v_perm_b32 v107, v123, v121, s36
	v_perm_b32 v109, v111, v109, s37
	v_perm_b32 v113, v114, v110, s36
	v_perm_b32 v117, v114, v110, s37
	v_perm_b32 v110, v119, v115, s37
	v_perm_b32 v114, v120, v118, s36
	v_perm_b32 v118, v120, v118, s37
	v_perm_b32 v111, v123, v121, s37
	v_perm_b32 v115, v124, v122, s36
	v_perm_b32 v119, v124, v122, s37
	global_store_dwordx4 v[170:171], v[104:107], off nt
	global_store_dwordx4 v[172:173], v[108:111], off nt
	global_store_dwordx4 v[174:175], v[112:115], off nt
	global_store_dwordx4 v[100:101], v[116:119], off nt
	s_cbranch_scc0 .LBB0_979
	s_mov_b64 s[8:9], 0

; template <int MODE> __device__ __forceinline__ int drow(int n) {
;     if (MODE == 1) { const int h = n / 192, nl = n - h * 192; return nl < 128 ? n : h * 192 + 128 + ((nl - 128) & 31) * 2 + ((nl - 128) >> 5); }
;     if (MODE == 2) { return n < FF ? ((n >> 7) * 256 + (n & 127)) : (((n - FF) >> 7) * 256 + 128 + ((n - FF) & 127)); }
;     return n;
; }
; __device__ __forceinline__ void cv_load(const float* W, int N, int nblk, int item, int lane, f32x4 (&tv)[16]) {
;     const int kb = item / nblk, nb = item - kb * nblk; const float* p = W + (size_t)(64 * kb + 16 * (lane >> 4)) * N + 64 * nb + 4 * (lane & 15);
; #pragma unroll
;     for (int i = 0; i < 16; ++i) tv[i] = __builtin_nontemporal_load((const f32x4*)(p + (size_t)i * N));
; }
; template <int MODE> __device__ __forceinline__ void cv_run4(const float* W, int K, int N, unsigned char* WT, int item0, int lane) {
;     const int nblk = N / 64; f32x4 ta[16];
; #pragma unroll 1
;     for (int j = 0; j < 4; ++j) { cv_load(W, N, nblk, item0 + j, lane, ta); cv_finish<MODE>(ta, K, nblk, WT, item0 + j, lane); }
.LBB0_984:
	s_ashr_i32 s12, s4, 31
	s_lshr_b32 s12, s12, 26
	s_add_i32 s12, s4, s12
	s_ashr_i32 s49, s12, 6
	s_andn2_b32 s12, s12, 63
	v_or_b32_e32 v70, s12, v1
	v_ashrrev_i32_e32 v71, 31, v70
	s_lshl_b32 s12, s49, 12
	v_lshlrev_b64 v[2:3], 14, v[70:71]
	s_sub_i32 s12, s47, s12
	v_lshl_add_u64 v[2:3], s[8:9], 0, v[2:3]
	s_ashr_i32 s13, s12, 31
	v_lshl_add_u64 v[2:3], s[12:13], 2, v[2:3]
	v_lshl_add_u64 v[2:3], v[2:3], 0, v[68:69]
	v_add_co_u32_e32 v4, vcc, s18, v2
	v_add_u32_e32 v77, s12, v66
	s_nop 0
	v_addc_co_u32_e32 v5, vcc, 0, v3, vcc
	global_load_dwordx4 v[62:65], v[2:3], off nt
	global_load_dwordx4 v[58:61], v[4:5], off nt
	v_add_co_u32_e32 v4, vcc, s20, v2
	v_add_u32_e32 v72, s48, v75
	s_nop 0
	v_addc_co_u32_e32 v5, vcc, 0, v3, vcc
	s_waitcnt lgkmcnt(0)
	v_add_co_u32_e32 v6, vcc, s22, v2
	s_lshl_b32 s12, s49, 13
	s_nop 0
	v_addc_co_u32_e32 v7, vcc, 0, v3, vcc
	global_load_dwordx4 v[54:57], v[4:5], off nt
	global_load_dwordx4 v[50:53], v[6:7], off nt
	v_add_co_u32_e32 v4, vcc, s24, v2
	v_subrev_u32_e32 v76, s12, v72
	s_nop 0
	v_addc_co_u32_e32 v5, vcc, 0, v3, vcc
	v_add_co_u32_e32 v6, vcc, s26, v2
	v_and_b32_e32 v73, 0x7c, v77
	s_nop 0
	v_addc_co_u32_e32 v7, vcc, 0, v3, vcc
	global_load_dwordx4 v[46:49], v[4:5], off nt
	global_load_dwordx4 v[42:45], v[6:7], off nt
	v_add_co_u32_e32 v4, vcc, s28, v2
	s_nop 1
	v_addc_co_u32_e32 v5, vcc, 0, v3, vcc
	v_add_co_u32_e32 v6, vcc, s30, v2
	s_nop 1
	v_addc_co_u32_e32 v7, vcc, 0, v3, vcc
	global_load_dwordx4 v[38:41], v[4:5], off nt
	global_load_dwordx4 v[34:37], v[6:7], off nt
	v_add_co_u32_e32 v4, vcc, s38, v2
	s_nop 1
	v_addc_co_u32_e32 v5, vcc, 0, v3, vcc
	v_add_co_u32_e32 v6, vcc, s39, v2
	s_nop 1
	v_addc_co_u32_e32 v7, vcc, 0, v3, vcc
	global_load_dwordx4 v[30:33], v[4:5], off nt
	global_load_dwordx4 v[26:29], v[6:7], off nt
	v_add_co_u32_e32 v4, vcc, s40, v2
	s_nop 1
	v_addc_co_u32_e32 v5, vcc, 0, v3, vcc
	v_add_co_u32_e32 v6, vcc, s41, v2
	s_nop 1
	v_addc_co_u32_e32 v7, vcc, 0, v3, vcc
	global_load_dwordx4 v[22:25], v[4:5], off nt
	global_load_dwordx4 v[18:21], v[6:7], off nt
	v_add_co_u32_e32 v4, vcc, s42, v2
	s_nop 1
	v_addc_co_u32_e32 v5, vcc, 0, v3, vcc
	v_add_co_u32_e32 v6, vcc, s43, v2
	s_nop 1
	v_addc_co_u32_e32 v7, vcc, 0, v3, vcc
	global_load_dwordx4 v[14:17], v[4:5], off nt
	global_load_dwordx4 v[10:13], v[6:7], off nt
	v_add_co_u32_e32 v4, vcc, 0x38000, v2
	s_nop 1
	v_addc_co_u32_e32 v5, vcc, 0, v3, vcc
	v_add_co_u32_e32 v2, vcc, 0x3c000, v2
	s_nop 1
	v_addc_co_u32_e32 v3, vcc, 0, v3, vcc
	global_load_dwordx4 v[6:9], v[4:5], off nt
	s_nop 0
	global_load_dwordx4 v[2:5], v[2:3], off nt
	s_addk_i32 s48, 0x80
	s_add_i32 s47, s47, 64
	s_add_i32 s4, s4, 1
	s_ashr_i32 s12, s4, 31
	s_lshr_b32 s12, s12, 26
	s_add_i32 s12, s4, s12
	s_ashr_i32 s49, s12, 6
	s_andn2_b32 s12, s12, 63
	v_or_b32_e32 v146, s12, v1
	v_ashrrev_i32_e32 v147, 31, v146
	s_lshl_b32 s12, s49, 12
	v_lshlrev_b64 v[82:83], 14, v[146:147]
	s_sub_i32 s12, s47, s12
	v_lshl_add_u64 v[82:83], s[8:9], 0, v[82:83]
	s_ashr_i32 s13, s12, 31
	v_lshl_add_u64 v[82:83], s[12:13], 2, v[82:83]
	v_lshl_add_u64 v[82:83], v[82:83], 0, v[68:69]
	v_add_co_u32_e32 v84, vcc, s18, v82
	v_add_u32_e32 v151, s12, v66
	s_nop 0
	v_addc_co_u32_e32 v85, vcc, 0, v83, vcc
	global_load_dwordx4 v[142:145], v[82:83], off nt
	global_load_dwordx4 v[138:141], v[84:85], off nt
	v_add_co_u32_e32 v84, vcc, s20, v82
	v_add_u32_e32 v148, s48, v75
	s_nop 0
	v_addc_co_u32_e32 v85, vcc, 0, v83, vcc
	s_waitcnt lgkmcnt(0)
	v_add_co_u32_e32 v86, vcc, s22, v82
	s_lshl_b32 s12, s49, 13
	s_nop 0
	v_addc_co_u32_e32 v87, vcc, 0, v83, vcc
	global_load_dwordx4 v[134:137], v[84:85], off nt
	global_load_dwordx4 v[130:133], v[86:87], off nt
	v_add_co_u32_e32 v84, vcc, s24, v82
	v_subrev_u32_e32 v150, s12, v148
	s_nop 0
	v_addc_co_u32_e32 v85, vcc, 0, v83, vcc
	v_add_co_u32_e32 v86, vcc, s26, v82
	v_and_b32_e32 v149, 0x7c, v151
	s_nop 0
	v_addc_co_u32_e32 v87, vcc, 0, v83, vcc
	global_load_dwordx4 v[126:129], v[84:85], off nt
	global_load_dwordx4 v[122:125], v[86:87], off nt
	v_add_co_u32_e32 v84, vcc, s28, v82
	s_nop 1
	v_addc_co_u32_e32 v85, vcc, 0, v83, vcc
	v_add_co_u32_e32 v86, vcc, s30, v82
	s_nop 1
	v_addc_co_u32_e32 v87, vcc, 0, v83, vcc
	global_load_dwordx4 v[118:121], v[84:85], off nt
	global_load_dwordx4 v[114:117], v[86:87], off nt
	v_add_co_u32_e32 v84, vcc, s38, v82
	s_nop 1
	v_addc_co_u32_e32 v85, vcc, 0, v83, vcc
	v_add_co_u32_e32 v86, vcc, s39, v82
	s_nop 1
	v_addc_co_u32_e32 v87, vcc, 0, v83, vcc
	global_load_dwordx4 v[110:113], v[84:85], off nt
	global_load_dwordx4 v[106:109], v[86:87], off nt
	v_add_co_u32_e32 v84, vcc, s40, v82
	s_nop 1
	v_addc_co_u32_e32 v85, vcc, 0, v83, vcc
	v_add_co_u32_e32 v86, vcc, s41, v82
	s_nop 1
	v_addc_co_u32_e32 v87, vcc, 0, v83, vcc
	global_load_dwordx4 v[102:105], v[84:85], off nt
	global_load_dwordx4 v[98:101], v[86:87], off nt
	v_add_co_u32_e32 v84, vcc, s42, v82
	s_nop 1
	v_addc_co_u32_e32 v85, vcc, 0, v83, vcc
	v_add_co_u32_e32 v86, vcc, s43, v82
	s_nop 1
	v_addc_co_u32_e32 v87, vcc, 0, v83, vcc
	global_load_dwordx4 v[94:97], v[84:85], off nt
	global_load_dwordx4 v[90:93], v[86:87], off nt
	v_add_co_u32_e32 v84, vcc, 0x38000, v82
	s_nop 1
	v_addc_co_u32_e32 v85, vcc, 0, v83, vcc
	v_add_co_u32_e32 v82, vcc, 0x3c000, v82
	s_nop 1
	v_addc_co_u32_e32 v83, vcc, 0, v83, vcc
	global_load_dwordx4 v[86:89], v[84:85], off nt
	s_nop 0
	global_load_dwordx4 v[82:85], v[82:83], off nt
	s_addk_i32 s48, 0x80
	s_add_i32 s47, s47, 64
	s_add_i32 s4, s4, 1
	v_cmp_lt_i32_e32 vcc, s44, v77
	s_and_saveexec_b64 s[12:13], vcc
	s_xor_b64 s[12:13], exec, s[12:13]
	v_add_u32_e32 v72, 0x7ffff000, v76
	v_and_b32_e32 v72, 0x7fffff00, v72
	v_or3_b32 v72, v73, v72, s45
	s_andn2_saveexec_b64 s[12:13], s[12:13]
	v_and_or_b32 v72, v76, s46, v73
	s_or_b64 exec, exec, s[12:13]
	s_waitcnt vmcnt(31)
; __device__ __forceinline__ unsigned pk4_fp8(float a, float b, float c, float d) {
;     a = __builtin_fminf(__builtin_fmaxf(a, -448.f), 448.f); b = __builtin_fminf(__builtin_fmaxf(b, -448.f), 448.f); c = __builtin_fminf(__builtin_fmaxf(c, -448.f), 448.f); d = __builtin_fminf(__builtin_fmaxf(d, -448.f), 448.f);
;     int w = 0; w = __builtin_amdgcn_cvt_pk_fp8_f32(a, b, w, false); w = __builtin_amdgcn_cvt_pk_fp8_f32(c, d, w, true); return (unsigned)w;
; }
; template <int MODE> __device__ __forceinline__ void cv_finish(const f32x4 (&tv)[16], int K, int nblk, unsigned char* WT, int item, int lane) {
;     const int kb = item / nblk, nb = item - kb * nblk, k0 = 64 * kb + 16 * (lane >> 4), n0 = 64 * nb + 4 * (lane & 15);
;     unsigned D[16];
; #pragma unroll
;     for (int i = 0; i < 16; ++i) { const f32x2 a = (f32x2){tv[i].x, tv[i].y} * (f32x2){1024.f, 1024.f}, b = (f32x2){tv[i].z, tv[i].w} * (f32x2){1024.f, 1024.f};
;         D[i] = pk4_fp8(a.x, a.y, b.x, b.y); }
	v_pk_mul_f32 v[62:63], v[62:63], s[6:7] op_sel_hi:[1,0]
	v_pk_mul_f32 v[64:65], v[64:65], s[6:7] op_sel_hi:[1,0]
	v_med3_f32 v73, v62, s33, v74
	v_med3_f32 v63, v63, s33, v74
	v_mov_b32_e32 v62, v69
	v_cvt_pk_fp8_f32 v62, v73, v63
	v_med3_f32 v63, v64, s33, v74
	v_med3_f32 v64, v65, s33, v74
	s_waitcnt vmcnt(30)
	v_pk_mul_f32 v[58:59], v[58:59], s[6:7] op_sel_hi:[1,0]
	v_cvt_pk_fp8_f32 v62, v63, v64 op_sel:[0,0,1]
	v_med3_f32 v63, v58, s33, v74
	v_med3_f32 v59, v59, s33, v74
	v_mov_b32_e32 v58, v69
	v_cvt_pk_fp8_f32 v58, v63, v59
	v_pk_mul_f32 v[60:61], v[60:61], s[6:7] op_sel_hi:[1,0]
	s_waitcnt vmcnt(29)
	v_pk_mul_f32 v[54:55], v[54:55], s[6:7] op_sel_hi:[1,0]
	v_med3_f32 v59, v60, s33, v74
	v_med3_f32 v60, v61, s33, v74
	v_cvt_pk_fp8_f32 v58, v59, v60 op_sel:[0,0,1]
	v_med3_f32 v59, v54, s33, v74
	v_med3_f32 v55, v55, s33, v74
	v_mov_b32_e32 v54, v69
	v_cvt_pk_fp8_f32 v54, v59, v55
	v_pk_mul_f32 v[56:57], v[56:57], s[6:7] op_sel_hi:[1,0]
	s_waitcnt vmcnt(28)
	v_pk_mul_f32 v[50:51], v[50:51], s[6:7] op_sel_hi:[1,0]
	v_med3_f32 v55, v56, s33, v74
	v_med3_f32 v56, v57, s33, v74
	v_cvt_pk_fp8_f32 v54, v55, v56 op_sel:[0,0,1]
	v_med3_f32 v55, v50, s33, v74
	v_med3_f32 v51, v51, s33, v74
	v_mov_b32_e32 v50, v69
	v_cvt_pk_fp8_f32 v50, v55, v51
	v_pk_mul_f32 v[52:53], v[52:53], s[6:7] op_sel_hi:[1,0]
	s_waitcnt vmcnt(27)
	v_pk_mul_f32 v[46:47], v[46:47], s[6:7] op_sel_hi:[1,0]
	v_med3_f32 v51, v52, s33, v74
	v_med3_f32 v52, v53, s33, v74
	v_cvt_pk_fp8_f32 v50, v51, v52 op_sel:[0,0,1]
	v_med3_f32 v51, v46, s33, v74
	v_med3_f32 v47, v47, s33, v74
	v_mov_b32_e32 v46, v69
	v_cvt_pk_fp8_f32 v46, v51, v47
	v_pk_mul_f32 v[48:49], v[48:49], s[6:7] op_sel_hi:[1,0]
	s_waitcnt vmcnt(26)
	v_pk_mul_f32 v[42:43], v[42:43], s[6:7] op_sel_hi:[1,0]
	v_med3_f32 v47, v48, s33, v74
	v_med3_f32 v48, v49, s33, v74
	v_cvt_pk_fp8_f32 v46, v47, v48 op_sel:[0,0,1]
	v_med3_f32 v47, v42, s33, v74
	v_med3_f32 v43, v43, s33, v74
	v_mov_b32_e32 v42, v69
	v_cvt_pk_fp8_f32 v42, v47, v43
	v_pk_mul_f32 v[44:45], v[44:45], s[6:7] op_sel_hi:[1,0]
	s_waitcnt vmcnt(25)
	v_pk_mul_f32 v[38:39], v[38:39], s[6:7] op_sel_hi:[1,0]
	v_med3_f32 v43, v44, s33, v74
	v_med3_f32 v44, v45, s33, v74
	v_cvt_pk_fp8_f32 v42, v43, v44 op_sel:[0,0,1]
	v_med3_f32 v43, v38, s33, v74
	v_med3_f32 v39, v39, s33, v74
	v_mov_b32_e32 v38, v69
	v_cvt_pk_fp8_f32 v38, v43, v39
	v_pk_mul_f32 v[40:41], v[40:41], s[6:7] op_sel_hi:[1,0]
	s_waitcnt vmcnt(24)
	v_pk_mul_f32 v[34:35], v[34:35], s[6:7] op_sel_hi:[1,0]
	v_med3_f32 v39, v40, s33, v74
	v_med3_f32 v40, v41, s33, v74
	v_cvt_pk_fp8_f32 v38, v39, v40 op_sel:[0,0,1]
	v_med3_f32 v39, v34, s33, v74
	v_med3_f32 v35, v35, s33, v74
	v_mov_b32_e32 v34, v69
	v_cvt_pk_fp8_f32 v34, v39, v35
	v_pk_mul_f32 v[36:37], v[36:37], s[6:7] op_sel_hi:[1,0]
	s_waitcnt vmcnt(23)
	v_pk_mul_f32 v[30:31], v[30:31], s[6:7] op_sel_hi:[1,0]
	v_med3_f32 v35, v36, s33, v74
	v_med3_f32 v36, v37, s33, v74
	v_cvt_pk_fp8_f32 v34, v35, v36 op_sel:[0,0,1]
	v_med3_f32 v35, v30, s33, v74
	v_med3_f32 v31, v31, s33, v74
	v_mov_b32_e32 v30, v69
	v_cvt_pk_fp8_f32 v30, v35, v31
	v_pk_mul_f32 v[32:33], v[32:33], s[6:7] op_sel_hi:[1,0]
	s_waitcnt vmcnt(22)
	v_pk_mul_f32 v[26:27], v[26:27], s[6:7] op_sel_hi:[1,0]
	v_med3_f32 v31, v32, s33, v74
	v_med3_f32 v32, v33, s33, v74
	v_cvt_pk_fp8_f32 v30, v31, v32 op_sel:[0,0,1]
	v_med3_f32 v31, v26, s33, v74
	v_med3_f32 v27, v27, s33, v74
	v_mov_b32_e32 v26, v69
	v_cvt_pk_fp8_f32 v26, v31, v27
	v_pk_mul_f32 v[28:29], v[28:29], s[6:7] op_sel_hi:[1,0]
	s_waitcnt vmcnt(21)
	v_pk_mul_f32 v[22:23], v[22:23], s[6:7] op_sel_hi:[1,0]
	v_med3_f32 v27, v28, s33, v74
	v_med3_f32 v28, v29, s33, v74
	v_cvt_pk_fp8_f32 v26, v27, v28 op_sel:[0,0,1]
	v_med3_f32 v27, v22, s33, v74
	v_med3_f32 v23, v23, s33, v74
	v_mov_b32_e32 v22, v69
	v_cvt_pk_fp8_f32 v22, v27, v23
	v_pk_mul_f32 v[24:25], v[24:25], s[6:7] op_sel_hi:[1,0]
	s_waitcnt vmcnt(20)
	v_pk_mul_f32 v[18:19], v[18:19], s[6:7] op_sel_hi:[1,0]
	v_med3_f32 v23, v24, s33, v74
	v_med3_f32 v24, v25, s33, v74
	v_cvt_pk_fp8_f32 v22, v23, v24 op_sel:[0,0,1]
	v_med3_f32 v23, v18, s33, v74
	v_med3_f32 v19, v19, s33, v74
	v_mov_b32_e32 v18, v69
	v_cvt_pk_fp8_f32 v18, v23, v19
	v_pk_mul_f32 v[20:21], v[20:21], s[6:7] op_sel_hi:[1,0]
	s_waitcnt vmcnt(19)
	v_pk_mul_f32 v[14:15], v[14:15], s[6:7] op_sel_hi:[1,0]
	v_med3_f32 v19, v20, s33, v74
	v_med3_f32 v20, v21, s33, v74
	v_cvt_pk_fp8_f32 v18, v19, v20 op_sel:[0,0,1]
	v_med3_f32 v19, v14, s33, v74
	v_med3_f32 v15, v15, s33, v74
	v_mov_b32_e32 v14, v69
	v_cvt_pk_fp8_f32 v14, v19, v15
	v_pk_mul_f32 v[16:17], v[16:17], s[6:7] op_sel_hi:[1,0]
	s_waitcnt vmcnt(18)
	v_pk_mul_f32 v[10:11], v[10:11], s[6:7] op_sel_hi:[1,0]
	v_med3_f32 v15, v16, s33, v74
	v_med3_f32 v16, v17, s33, v74
	v_cvt_pk_fp8_f32 v14, v15, v16 op_sel:[0,0,1]
	v_med3_f32 v15, v10, s33, v74
	v_med3_f32 v11, v11, s33, v74
	v_mov_b32_e32 v10, v69
	v_cvt_pk_fp8_f32 v10, v15, v11
	v_pk_mul_f32 v[12:13], v[12:13], s[6:7] op_sel_hi:[1,0]
	s_waitcnt vmcnt(17)
	v_pk_mul_f32 v[6:7], v[6:7], s[6:7] op_sel_hi:[1,0]
	v_med3_f32 v11, v12, s33, v74
	v_med3_f32 v12, v13, s33, v74
	v_cvt_pk_fp8_f32 v10, v11, v12 op_sel:[0,0,1]
	v_med3_f32 v11, v6, s33, v74
	v_med3_f32 v7, v7, s33, v74
	v_mov_b32_e32 v6, v69
	v_cvt_pk_fp8_f32 v6, v11, v7
	v_pk_mul_f32 v[8:9], v[8:9], s[6:7] op_sel_hi:[1,0]
	s_waitcnt vmcnt(16)
; template <int MODE> __device__ __forceinline__ int drow(int n) {
;     if (MODE == 1) { const int h = n / 192, nl = n - h * 192; return nl < 128 ? n : h * 192 + 128 + ((nl - 128) & 31) * 2 + ((nl - 128) >> 5); }
;     if (MODE == 2) { return n < FF ? ((n >> 7) * 256 + (n & 127)) : (((n - FF) >> 7) * 256 + 128 + ((n - FF) & 127)); }
;     return n;
; }
; template <int MODE> __device__ __forceinline__ void cv_finish(const f32x4 (&tv)[16], int K, int nblk, unsigned char* WT, int item, int lane) {
;     const int kb = item / nblk, nb = item - kb * nblk, k0 = 64 * kb + 16 * (lane >> 4), n0 = 64 * nb + 4 * (lane & 15);
;     unsigned D[16];
; #pragma unroll
;     for (int i = 0; i < 16; ++i) { const f32x2 a = (f32x2){tv[i].x, tv[i].y} * (f32x2){1024.f, 1024.f}, b = (f32x2){tv[i].z, tv[i].w} * (f32x2){1024.f, 1024.f};
;         D[i] = pk4_fp8(a.x, a.y, b.x, b.y); }
;     unsigned O[4][4];
; #pragma unroll
;     for (int q = 0; q < 4; ++q) { const unsigned a = D[4 * q], b = D[4 * q + 1], c = D[4 * q + 2], d = D[4 * q + 3];
;         const unsigned t0 = __builtin_amdgcn_perm(b, a, 0x05010400u), t1 = __builtin_amdgcn_perm(b, a, 0x07030602u), u0 = __builtin_amdgcn_perm(d, c, 0x05010400u), u1 = __builtin_amdgcn_perm(d, c, 0x07030602u);
;         O[0][q] = __builtin_amdgcn_perm(u0, t0, 0x05040100u); O[1][q] = __builtin_amdgcn_perm(u0, t0, 0x07060302u); O[2][q] = __builtin_amdgcn_perm(u1, t1, 0x05040100u); O[3][q] = __builtin_amdgcn_perm(u1, t1, 0x07060302u); }
; #pragma unroll
;     for (int j = 0; j < 4; ++j) { u32x4 o; o.x = O[j][0]; o.y = O[j][1]; o.z = O[j][2]; o.w = O[j][3];
;         __builtin_nontemporal_store(o, (u32x4*)(WT + (size_t)drow<MODE>(n0 + j) * K + k0)); }
; }
; template <int MODE> __device__ __forceinline__ void cv_run4(const float* W, int K, int N, unsigned char* WT, int item0, int lane) {
;     const int nblk = N / 64; f32x4 ta[16];
; #pragma unroll 1
;     for (int j = 0; j < 4; ++j) { cv_load(W, N, nblk, item0 + j, lane, ta); cv_finish<MODE>(ta, K, nblk, WT, item0 + j, lane); }
	v_pk_mul_f32 v[2:3], v[2:3], s[6:7] op_sel_hi:[1,0]
	v_med3_f32 v7, v8, s33, v74
	v_med3_f32 v8, v9, s33, v74
	v_cvt_pk_fp8_f32 v6, v7, v8 op_sel:[0,0,1]
	v_med3_f32 v2, v2, s33, v74
	v_med3_f32 v3, v3, s33, v74
	v_mov_b32_e32 v7, v69
	v_cvt_pk_fp8_f32 v7, v2, v3
	v_pk_mul_f32 v[2:3], v[4:5], s[6:7] op_sel_hi:[1,0]
	v_ashrrev_i32_e32 v73, 31, v72
	v_med3_f32 v2, v2, s33, v74
	v_med3_f32 v3, v3, s33, v74
	v_cvt_pk_fp8_f32 v7, v2, v3 op_sel:[0,0,1]
	v_perm_b32 v5, v58, v62, s34
	v_perm_b32 v8, v50, v54, s34
	v_perm_b32 v9, v42, v46, s34
	v_perm_b32 v11, v34, v38, s34
	v_perm_b32 v12, v26, v30, s34
	v_perm_b32 v13, v18, v22, s34
	v_perm_b32 v15, v10, v14, s34
	v_perm_b32 v16, v7, v6, s34
	v_lshl_add_u64 v[2:3], s[10:11], 0, v[70:71]
	v_lshlrev_b64 v[20:21], 11, v[72:73]
	v_add_u32_e32 v4, 1, v77
	v_perm_b32 v78, v8, v5, s36
	v_perm_b32 v79, v11, v9, s36
	v_perm_b32 v80, v13, v12, s36
	v_perm_b32 v81, v16, v15, s36
	v_lshl_add_u64 v[20:21], v[2:3], 0, v[20:21]
	v_cmp_lt_i32_e32 vcc, s44, v4
	v_and_b32_e32 v17, 0x7d, v4
	global_store_dwordx4 v[20:21], v[78:81], off nt
	s_and_saveexec_b64 s[12:13], vcc
	s_xor_b64 s[12:13], exec, s[12:13]
	v_add_u32_e32 v4, 0x7ffff002, v76
	v_and_b32_e32 v4, 0x7fffff00, v4
	v_or3_b32 v4, v17, v4, s45
	s_andn2_saveexec_b64 s[12:13], s[12:13]
	v_add_u32_e32 v4, 2, v76
	v_and_or_b32 v4, v4, s46, v17
	s_or_b64 exec, exec, s[12:13]
	v_perm_b32 v70, v8, v5, s37
	v_ashrrev_i32_e32 v5, 31, v4
	v_lshlrev_b64 v[4:5], 11, v[4:5]
	v_perm_b32 v71, v11, v9, s37
	v_perm_b32 v72, v13, v12, s37
	v_perm_b32 v73, v16, v15, s37
	v_lshl_add_u64 v[4:5], v[2:3], 0, v[4:5]
	global_store_dwordx4 v[4:5], v[70:73], off nt
	v_add_u32_e32 v4, 2, v77
	v_cmp_lt_i32_e32 vcc, s44, v4
	v_and_b32_e32 v5, 0x7e, v4
	s_and_saveexec_b64 s[12:13], vcc
	s_xor_b64 s[12:13], exec, s[12:13]
	v_add_u32_e32 v4, 0x7ffff004, v76
	v_and_b32_e32 v4, 0x7fffff00, v4
	v_or3_b32 v4, v5, v4, s45
	s_andn2_saveexec_b64 s[12:13], s[12:13]
	v_add_u32_e32 v4, 4, v76
	v_and_or_b32 v4, v4, s46, v5
	s_or_b64 exec, exec, s[12:13]
	v_ashrrev_i32_e32 v5, 31, v4
	v_perm_b32 v8, v58, v62, s35
	v_perm_b32 v9, v50, v54, s35
	v_perm_b32 v11, v42, v46, s35
	v_perm_b32 v12, v34, v38, s35
	v_perm_b32 v13, v26, v30, s35
	v_perm_b32 v15, v18, v22, s35
	v_perm_b32 v10, v10, v14, s35
	v_perm_b32 v6, v7, v6, s35
	v_lshlrev_b64 v[4:5], 11, v[4:5]
	v_perm_b32 v16, v9, v8, s36
	v_perm_b32 v17, v12, v11, s36
	v_perm_b32 v18, v15, v13, s36
	v_perm_b32 v19, v6, v10, s36
	v_lshl_add_u64 v[4:5], v[2:3], 0, v[4:5]
	global_store_dwordx4 v[4:5], v[16:19], off nt
	v_add_u32_e32 v4, 3, v77
	v_cmp_lt_i32_e32 vcc, s44, v4
	v_and_b32_e32 v5, 0x7f, v4
	s_and_saveexec_b64 s[12:13], vcc
	s_xor_b64 s[12:13], exec, s[12:13]
	v_add_u32_e32 v4, 0x7ffff006, v76
	v_and_b32_e32 v4, 0x7fffff00, v4
	v_or3_b32 v4, v5, v4, s45
	s_andn2_saveexec_b64 s[12:13], s[12:13]
	v_add_u32_e32 v4, 6, v76
	v_and_or_b32 v4, v4, s46, v5
	s_or_b64 exec, exec, s[12:13]
	v_ashrrev_i32_e32 v5, 31, v4
	v_lshlrev_b64 v[4:5], 11, v[4:5]
	v_perm_b32 v16, v9, v8, s37
	v_perm_b32 v17, v12, v11, s37
	v_perm_b32 v18, v15, v13, s37
	v_perm_b32 v19, v6, v10, s37
	v_lshl_add_u64 v[2:3], v[2:3], 0, v[4:5]
	global_store_dwordx4 v[2:3], v[16:19], off nt
	s_ashr_i32 s12, s4, 31
	s_lshr_b32 s12, s12, 26
	s_add_i32 s12, s4, s12
	s_ashr_i32 s49, s12, 6
	s_andn2_b32 s12, s12, 63
	v_or_b32_e32 v70, s12, v1
	v_ashrrev_i32_e32 v71, 31, v70
	s_lshl_b32 s12, s49, 12
	v_lshlrev_b64 v[2:3], 14, v[70:71]
	s_sub_i32 s12, s47, s12
	v_lshl_add_u64 v[2:3], s[8:9], 0, v[2:3]
	s_ashr_i32 s13, s12, 31
	v_lshl_add_u64 v[2:3], s[12:13], 2, v[2:3]
	v_lshl_add_u64 v[2:3], v[2:3], 0, v[68:69]
	v_add_co_u32_e32 v4, vcc, s18, v2
	v_add_u32_e32 v77, s12, v66
	s_nop 0
	v_addc_co_u32_e32 v5, vcc, 0, v3, vcc
	global_load_dwordx4 v[62:65], v[2:3], off nt
	global_load_dwordx4 v[58:61], v[4:5], off nt
	v_add_co_u32_e32 v4, vcc, s20, v2
	v_add_u32_e32 v72, s48, v75
	s_nop 0
	v_addc_co_u32_e32 v5, vcc, 0, v3, vcc
	s_waitcnt lgkmcnt(0)
	v_add_co_u32_e32 v6, vcc, s22, v2
	s_lshl_b32 s12, s49, 13
	s_nop 0
	v_addc_co_u32_e32 v7, vcc, 0, v3, vcc
	global_load_dwordx4 v[54:57], v[4:5], off nt
	global_load_dwordx4 v[50:53], v[6:7], off nt
	v_add_co_u32_e32 v4, vcc, s24, v2
	v_subrev_u32_e32 v76, s12, v72
	s_nop 0
	v_addc_co_u32_e32 v5, vcc, 0, v3, vcc
	v_add_co_u32_e32 v6, vcc, s26, v2
	v_and_b32_e32 v73, 0x7c, v77
	s_nop 0
	v_addc_co_u32_e32 v7, vcc, 0, v3, vcc
	global_load_dwordx4 v[46:49], v[4:5], off nt
	global_load_dwordx4 v[42:45], v[6:7], off nt
	v_add_co_u32_e32 v4, vcc, s28, v2
	s_nop 1
	v_addc_co_u32_e32 v5, vcc, 0, v3, vcc
	v_add_co_u32_e32 v6, vcc, s30, v2
	s_nop 1
	v_addc_co_u32_e32 v7, vcc, 0, v3, vcc
	global_load_dwordx4 v[38:41], v[4:5], off nt
	global_load_dwordx4 v[34:37], v[6:7], off nt
	v_add_co_u32_e32 v4, vcc, s38, v2
	s_nop 1
	v_addc_co_u32_e32 v5, vcc, 0, v3, vcc
	v_add_co_u32_e32 v6, vcc, s39, v2
	s_nop 1
	v_addc_co_u32_e32 v7, vcc, 0, v3, vcc
	global_load_dwordx4 v[30:33], v[4:5], off nt
	global_load_dwordx4 v[26:29], v[6:7], off nt
	v_add_co_u32_e32 v4, vcc, s40, v2
	s_nop 1
	v_addc_co_u32_e32 v5, vcc, 0, v3, vcc
	v_add_co_u32_e32 v6, vcc, s41, v2
	s_nop 1
	v_addc_co_u32_e32 v7, vcc, 0, v3, vcc
	global_load_dwordx4 v[22:25], v[4:5], off nt
	global_load_dwordx4 v[18:21], v[6:7], off nt
	v_add_co_u32_e32 v4, vcc, s42, v2
	s_nop 1
	v_addc_co_u32_e32 v5, vcc, 0, v3, vcc
	v_add_co_u32_e32 v6, vcc, s43, v2
	s_nop 1
	v_addc_co_u32_e32 v7, vcc, 0, v3, vcc
	global_load_dwordx4 v[14:17], v[4:5], off nt
	global_load_dwordx4 v[10:13], v[6:7], off nt
	v_add_co_u32_e32 v4, vcc, 0x38000, v2
	s_nop 1
	v_addc_co_u32_e32 v5, vcc, 0, v3, vcc
	v_add_co_u32_e32 v2, vcc, 0x3c000, v2
	s_nop 1
	v_addc_co_u32_e32 v3, vcc, 0, v3, vcc
	global_load_dwordx4 v[6:9], v[4:5], off nt
	s_nop 0
	global_load_dwordx4 v[2:5], v[2:3], off nt
	s_addk_i32 s48, 0x80
	s_add_i32 s47, s47, 64
	s_add_i32 s4, s4, 1
	v_cmp_lt_i32_e32 vcc, s44, v151
	s_and_saveexec_b64 s[12:13], vcc
	s_xor_b64 s[12:13], exec, s[12:13]
	v_add_u32_e32 v148, 0x7ffff000, v150
	v_and_b32_e32 v148, 0x7fffff00, v148
	v_or3_b32 v148, v149, v148, s45
	s_andn2_saveexec_b64 s[12:13], s[12:13]
	v_and_or_b32 v148, v150, s46, v149
	s_or_b64 exec, exec, s[12:13]
	s_waitcnt vmcnt(35)
; __device__ __forceinline__ unsigned pk4_fp8(float a, float b, float c, float d) {
;     a = __builtin_fminf(__builtin_fmaxf(a, -448.f), 448.f); b = __builtin_fminf(__builtin_fmaxf(b, -448.f), 448.f); c = __builtin_fminf(__builtin_fmaxf(c, -448.f), 448.f); d = __builtin_fminf(__builtin_fmaxf(d, -448.f), 448.f);
;     int w = 0; w = __builtin_amdgcn_cvt_pk_fp8_f32(a, b, w, false); w = __builtin_amdgcn_cvt_pk_fp8_f32(c, d, w, true); return (unsigned)w;
; }
; template <int MODE> __device__ __forceinline__ void cv_finish(const f32x4 (&tv)[16], int K, int nblk, unsigned char* WT, int item, int lane) {
;     const int kb = item / nblk, nb = item - kb * nblk, k0 = 64 * kb + 16 * (lane >> 4), n0 = 64 * nb + 4 * (lane & 15);
;     unsigned D[16];
; #pragma unroll
;     for (int i = 0; i < 16; ++i) { const f32x2 a = (f32x2){tv[i].x, tv[i].y} * (f32x2){1024.f, 1024.f}, b = (f32x2){tv[i].z, tv[i].w} * (f32x2){1024.f, 1024.f};
;         D[i] = pk4_fp8(a.x, a.y, b.x, b.y); }
	v_pk_mul_f32 v[142:143], v[142:143], s[6:7] op_sel_hi:[1,0]
	v_pk_mul_f32 v[144:145], v[144:145], s[6:7] op_sel_hi:[1,0]
	v_med3_f32 v149, v142, s33, v74
	v_med3_f32 v143, v143, s33, v74
	v_mov_b32_e32 v142, v69
	v_cvt_pk_fp8_f32 v142, v149, v143
	v_med3_f32 v143, v144, s33, v74
	v_med3_f32 v144, v145, s33, v74
	s_waitcnt vmcnt(34)
	v_pk_mul_f32 v[138:139], v[138:139], s[6:7] op_sel_hi:[1,0]
	v_cvt_pk_fp8_f32 v142, v143, v144 op_sel:[0,0,1]
	v_med3_f32 v143, v138, s33, v74
	v_med3_f32 v139, v139, s33, v74
	v_mov_b32_e32 v138, v69
	v_cvt_pk_fp8_f32 v138, v143, v139
	v_pk_mul_f32 v[140:141], v[140:141], s[6:7] op_sel_hi:[1,0]
	s_waitcnt vmcnt(33)
	v_pk_mul_f32 v[134:135], v[134:135], s[6:7] op_sel_hi:[1,0]
	v_med3_f32 v139, v140, s33, v74
	v_med3_f32 v140, v141, s33, v74
	v_cvt_pk_fp8_f32 v138, v139, v140 op_sel:[0,0,1]
	v_med3_f32 v139, v134, s33, v74
	v_med3_f32 v135, v135, s33, v74
	v_mov_b32_e32 v134, v69
	v_cvt_pk_fp8_f32 v134, v139, v135
	v_pk_mul_f32 v[136:137], v[136:137], s[6:7] op_sel_hi:[1,0]
	s_waitcnt vmcnt(32)
	v_pk_mul_f32 v[130:131], v[130:131], s[6:7] op_sel_hi:[1,0]
	v_med3_f32 v135, v136, s33, v74
	v_med3_f32 v136, v137, s33, v74
	v_cvt_pk_fp8_f32 v134, v135, v136 op_sel:[0,0,1]
	v_med3_f32 v135, v130, s33, v74
	v_med3_f32 v131, v131, s33, v74
	v_mov_b32_e32 v130, v69
	v_cvt_pk_fp8_f32 v130, v135, v131
	v_pk_mul_f32 v[132:133], v[132:133], s[6:7] op_sel_hi:[1,0]
	s_waitcnt vmcnt(31)
	v_pk_mul_f32 v[126:127], v[126:127], s[6:7] op_sel_hi:[1,0]
	v_med3_f32 v131, v132, s33, v74
	v_med3_f32 v132, v133, s33, v74
	v_cvt_pk_fp8_f32 v130, v131, v132 op_sel:[0,0,1]
	v_med3_f32 v131, v126, s33, v74
	v_med3_f32 v127, v127, s33, v74
	v_mov_b32_e32 v126, v69
	v_cvt_pk_fp8_f32 v126, v131, v127
	v_pk_mul_f32 v[128:129], v[128:129], s[6:7] op_sel_hi:[1,0]
	s_waitcnt vmcnt(30)
	v_pk_mul_f32 v[122:123], v[122:123], s[6:7] op_sel_hi:[1,0]
	v_med3_f32 v127, v128, s33, v74
	v_med3_f32 v128, v129, s33, v74
	v_cvt_pk_fp8_f32 v126, v127, v128 op_sel:[0,0,1]
	v_med3_f32 v127, v122, s33, v74
	v_med3_f32 v123, v123, s33, v74
	v_mov_b32_e32 v122, v69
	v_cvt_pk_fp8_f32 v122, v127, v123
	v_pk_mul_f32 v[124:125], v[124:125], s[6:7] op_sel_hi:[1,0]
	s_waitcnt vmcnt(29)
	v_pk_mul_f32 v[118:119], v[118:119], s[6:7] op_sel_hi:[1,0]
	v_med3_f32 v123, v124, s33, v74
	v_med3_f32 v124, v125, s33, v74
	v_cvt_pk_fp8_f32 v122, v123, v124 op_sel:[0,0,1]
	v_med3_f32 v123, v118, s33, v74
	v_med3_f32 v119, v119, s33, v74
	v_mov_b32_e32 v118, v69
	v_cvt_pk_fp8_f32 v118, v123, v119
	v_pk_mul_f32 v[120:121], v[120:121], s[6:7] op_sel_hi:[1,0]
	s_waitcnt vmcnt(28)
	v_pk_mul_f32 v[114:115], v[114:115], s[6:7] op_sel_hi:[1,0]
	v_med3_f32 v119, v120, s33, v74
	v_med3_f32 v120, v121, s33, v74
	v_cvt_pk_fp8_f32 v118, v119, v120 op_sel:[0,0,1]
	v_med3_f32 v119, v114, s33, v74
	v_med3_f32 v115, v115, s33, v74
	v_mov_b32_e32 v114, v69
	v_cvt_pk_fp8_f32 v114, v119, v115
	v_pk_mul_f32 v[116:117], v[116:117], s[6:7] op_sel_hi:[1,0]
	s_waitcnt vmcnt(27)
	v_pk_mul_f32 v[110:111], v[110:111], s[6:7] op_sel_hi:[1,0]
	v_med3_f32 v115, v116, s33, v74
	v_med3_f32 v116, v117, s33, v74
	v_cvt_pk_fp8_f32 v114, v115, v116 op_sel:[0,0,1]
	v_med3_f32 v115, v110, s33, v74
	v_med3_f32 v111, v111, s33, v74
	v_mov_b32_e32 v110, v69
	v_cvt_pk_fp8_f32 v110, v115, v111
	v_pk_mul_f32 v[112:113], v[112:113], s[6:7] op_sel_hi:[1,0]
	s_waitcnt vmcnt(26)
	v_pk_mul_f32 v[106:107], v[106:107], s[6:7] op_sel_hi:[1,0]
	v_med3_f32 v111, v112, s33, v74
	v_med3_f32 v112, v113, s33, v74
	v_cvt_pk_fp8_f32 v110, v111, v112 op_sel:[0,0,1]
	v_med3_f32 v111, v106, s33, v74
	v_med3_f32 v107, v107, s33, v74
	v_mov_b32_e32 v106, v69
	v_cvt_pk_fp8_f32 v106, v111, v107
	v_pk_mul_f32 v[108:109], v[108:109], s[6:7] op_sel_hi:[1,0]
	s_waitcnt vmcnt(25)
	v_pk_mul_f32 v[102:103], v[102:103], s[6:7] op_sel_hi:[1,0]
	v_med3_f32 v107, v108, s33, v74
	v_med3_f32 v108, v109, s33, v74
	v_cvt_pk_fp8_f32 v106, v107, v108 op_sel:[0,0,1]
	v_med3_f32 v107, v102, s33, v74
	v_med3_f32 v103, v103, s33, v74
	v_mov_b32_e32 v102, v69
	v_cvt_pk_fp8_f32 v102, v107, v103
	v_pk_mul_f32 v[104:105], v[104:105], s[6:7] op_sel_hi:[1,0]
	s_waitcnt vmcnt(24)
	v_pk_mul_f32 v[98:99], v[98:99], s[6:7] op_sel_hi:[1,0]
	v_med3_f32 v103, v104, s33, v74
	v_med3_f32 v104, v105, s33, v74
	v_cvt_pk_fp8_f32 v102, v103, v104 op_sel:[0,0,1]
	v_med3_f32 v103, v98, s33, v74
	v_med3_f32 v99, v99, s33, v74
	v_mov_b32_e32 v98, v69
	v_cvt_pk_fp8_f32 v98, v103, v99
	v_pk_mul_f32 v[100:101], v[100:101], s[6:7] op_sel_hi:[1,0]
	s_waitcnt vmcnt(23)
	v_pk_mul_f32 v[94:95], v[94:95], s[6:7] op_sel_hi:[1,0]
	v_med3_f32 v99, v100, s33, v74
	v_med3_f32 v100, v101, s33, v74
	v_cvt_pk_fp8_f32 v98, v99, v100 op_sel:[0,0,1]
	v_med3_f32 v99, v94, s33, v74
	v_med3_f32 v95, v95, s33, v74
	v_mov_b32_e32 v94, v69
	v_cvt_pk_fp8_f32 v94, v99, v95
	v_pk_mul_f32 v[96:97], v[96:97], s[6:7] op_sel_hi:[1,0]
	s_waitcnt vmcnt(22)
	v_pk_mul_f32 v[90:91], v[90:91], s[6:7] op_sel_hi:[1,0]
	v_med3_f32 v95, v96, s33, v74
	v_med3_f32 v96, v97, s33, v74
	v_cvt_pk_fp8_f32 v94, v95, v96 op_sel:[0,0,1]
	v_med3_f32 v95, v90, s33, v74
	v_med3_f32 v91, v91, s33, v74
	v_mov_b32_e32 v90, v69
	v_cvt_pk_fp8_f32 v90, v95, v91
	v_pk_mul_f32 v[92:93], v[92:93], s[6:7] op_sel_hi:[1,0]
	s_waitcnt vmcnt(21)
	v_pk_mul_f32 v[86:87], v[86:87], s[6:7] op_sel_hi:[1,0]
	v_med3_f32 v91, v92, s33, v74
	v_med3_f32 v92, v93, s33, v74
	v_cvt_pk_fp8_f32 v90, v91, v92 op_sel:[0,0,1]
	v_med3_f32 v91, v86, s33, v74
	v_med3_f32 v87, v87, s33, v74
	v_mov_b32_e32 v86, v69
	v_cvt_pk_fp8_f32 v86, v91, v87
	v_pk_mul_f32 v[88:89], v[88:89], s[6:7] op_sel_hi:[1,0]
	s_waitcnt vmcnt(20)
; template <int MODE> __device__ __forceinline__ int drow(int n) {
;     if (MODE == 1) { const int h = n / 192, nl = n - h * 192; return nl < 128 ? n : h * 192 + 128 + ((nl - 128) & 31) * 2 + ((nl - 128) >> 5); }
;     if (MODE == 2) { return n < FF ? ((n >> 7) * 256 + (n & 127)) : (((n - FF) >> 7) * 256 + 128 + ((n - FF) & 127)); }
;     return n;
; }
; template <int MODE> __device__ __forceinline__ void cv_finish(const f32x4 (&tv)[16], int K, int nblk, unsigned char* WT, int item, int lane) {
;     const int kb = item / nblk, nb = item - kb * nblk, k0 = 64 * kb + 16 * (lane >> 4), n0 = 64 * nb + 4 * (lane & 15);
;     unsigned D[16];
; #pragma unroll
;     for (int i = 0; i < 16; ++i) { const f32x2 a = (f32x2){tv[i].x, tv[i].y} * (f32x2){1024.f, 1024.f}, b = (f32x2){tv[i].z, tv[i].w} * (f32x2){1024.f, 1024.f};
;         D[i] = pk4_fp8(a.x, a.y, b.x, b.y); }
;     unsigned O[4][4];
; #pragma unroll
;     for (int q = 0; q < 4; ++q) { const unsigned a = D[4 * q], b = D[4 * q + 1], c = D[4 * q + 2], d = D[4 * q + 3];
;         const unsigned t0 = __builtin_amdgcn_perm(b, a, 0x05010400u), t1 = __builtin_amdgcn_perm(b, a, 0x07030602u), u0 = __builtin_amdgcn_perm(d, c, 0x05010400u), u1 = __builtin_amdgcn_perm(d, c, 0x07030602u);
;         O[0][q] = __builtin_amdgcn_perm(u0, t0, 0x05040100u); O[1][q] = __builtin_amdgcn_perm(u0, t0, 0x07060302u); O[2][q] = __builtin_amdgcn_perm(u1, t1, 0x05040100u); O[3][q] = __builtin_amdgcn_perm(u1, t1, 0x07060302u); }
; #pragma unroll
;     for (int j = 0; j < 4; ++j) { u32x4 o; o.x = O[j][0]; o.y = O[j][1]; o.z = O[j][2]; o.w = O[j][3];
;         __builtin_nontemporal_store(o, (u32x4*)(WT + (size_t)drow<MODE>(n0 + j) * K + k0)); }
; }
; template <int MODE> __device__ __forceinline__ void cv_run4(const float* W, int K, int N, unsigned char* WT, int item0, int lane) {
;     const int nblk = N / 64; f32x4 ta[16];
; #pragma unroll 1
;     for (int j = 0; j < 4; ++j) { cv_load(W, N, nblk, item0 + j, lane, ta); cv_finish<MODE>(ta, K, nblk, WT, item0 + j, lane); }
	v_pk_mul_f32 v[82:83], v[82:83], s[6:7] op_sel_hi:[1,0]
	v_med3_f32 v87, v88, s33, v74
	v_med3_f32 v88, v89, s33, v74
	v_cvt_pk_fp8_f32 v86, v87, v88 op_sel:[0,0,1]
	v_med3_f32 v82, v82, s33, v74
	v_med3_f32 v83, v83, s33, v74
	v_mov_b32_e32 v87, v69
	v_cvt_pk_fp8_f32 v87, v82, v83
	v_pk_mul_f32 v[82:83], v[84:85], s[6:7] op_sel_hi:[1,0]
	v_ashrrev_i32_e32 v149, 31, v148
	v_med3_f32 v82, v82, s33, v74
	v_med3_f32 v83, v83, s33, v74
	v_cvt_pk_fp8_f32 v87, v82, v83 op_sel:[0,0,1]
	v_perm_b32 v85, v138, v142, s34
	v_perm_b32 v88, v130, v134, s34
	v_perm_b32 v89, v122, v126, s34
	v_perm_b32 v91, v114, v118, s34
	v_perm_b32 v92, v106, v110, s34
	v_perm_b32 v93, v98, v102, s34
	v_perm_b32 v95, v90, v94, s34
	v_perm_b32 v96, v87, v86, s34
	v_lshl_add_u64 v[82:83], s[10:11], 0, v[146:147]
	v_lshlrev_b64 v[100:101], 11, v[148:149]
	v_add_u32_e32 v84, 1, v151
	v_perm_b32 v152, v88, v85, s36
	v_perm_b32 v153, v91, v89, s36
	v_perm_b32 v154, v93, v92, s36
	v_perm_b32 v155, v96, v95, s36
	v_lshl_add_u64 v[100:101], v[82:83], 0, v[100:101]
	v_cmp_lt_i32_e32 vcc, s44, v84
	v_and_b32_e32 v97, 0x7d, v84
	global_store_dwordx4 v[100:101], v[152:155], off nt
	s_and_saveexec_b64 s[12:13], vcc
	s_xor_b64 s[12:13], exec, s[12:13]
	v_add_u32_e32 v84, 0x7ffff002, v150
	v_and_b32_e32 v84, 0x7fffff00, v84
	v_or3_b32 v84, v97, v84, s45
	s_andn2_saveexec_b64 s[12:13], s[12:13]
	v_add_u32_e32 v84, 2, v150
	v_and_or_b32 v84, v84, s46, v97
	s_or_b64 exec, exec, s[12:13]
	v_perm_b32 v146, v88, v85, s37
	v_ashrrev_i32_e32 v85, 31, v84
	v_lshlrev_b64 v[84:85], 11, v[84:85]
	v_perm_b32 v147, v91, v89, s37
	v_perm_b32 v148, v93, v92, s37
	v_perm_b32 v149, v96, v95, s37
	v_lshl_add_u64 v[84:85], v[82:83], 0, v[84:85]
	global_store_dwordx4 v[84:85], v[146:149], off nt
	v_add_u32_e32 v84, 2, v151
	v_cmp_lt_i32_e32 vcc, s44, v84
	v_and_b32_e32 v85, 0x7e, v84
	s_and_saveexec_b64 s[12:13], vcc
	s_xor_b64 s[12:13], exec, s[12:13]
	v_add_u32_e32 v84, 0x7ffff004, v150
	v_and_b32_e32 v84, 0x7fffff00, v84
	v_or3_b32 v84, v85, v84, s45
	s_andn2_saveexec_b64 s[12:13], s[12:13]
	v_add_u32_e32 v84, 4, v150
	v_and_or_b32 v84, v84, s46, v85
	s_or_b64 exec, exec, s[12:13]
	v_ashrrev_i32_e32 v85, 31, v84
	v_perm_b32 v88, v138, v142, s35
	v_perm_b32 v89, v130, v134, s35
	v_perm_b32 v91, v122, v126, s35
	v_perm_b32 v92, v114, v118, s35
	v_perm_b32 v93, v106, v110, s35
	v_perm_b32 v95, v98, v102, s35
	v_perm_b32 v90, v90, v94, s35
	v_perm_b32 v86, v87, v86, s35
	v_lshlrev_b64 v[84:85], 11, v[84:85]
	v_perm_b32 v96, v89, v88, s36
	v_perm_b32 v97, v92, v91, s36
	v_perm_b32 v98, v95, v93, s36
	v_perm_b32 v99, v86, v90, s36
	v_lshl_add_u64 v[84:85], v[82:83], 0, v[84:85]
	global_store_dwordx4 v[84:85], v[96:99], off nt
	v_add_u32_e32 v84, 3, v151
	v_cmp_lt_i32_e32 vcc, s44, v84
	v_and_b32_e32 v85, 0x7f, v84
	s_and_saveexec_b64 s[12:13], vcc
	s_xor_b64 s[12:13], exec, s[12:13]
	v_add_u32_e32 v84, 0x7ffff006, v150
	v_and_b32_e32 v84, 0x7fffff00, v84
	v_or3_b32 v84, v85, v84, s45
	s_andn2_saveexec_b64 s[12:13], s[12:13]
	v_add_u32_e32 v84, 6, v150
	v_and_or_b32 v84, v84, s46, v85
	s_or_b64 exec, exec, s[12:13]
	v_ashrrev_i32_e32 v85, 31, v84
	v_lshlrev_b64 v[84:85], 11, v[84:85]
	v_perm_b32 v96, v89, v88, s37
	v_perm_b32 v97, v92, v91, s37
	v_perm_b32 v98, v95, v93, s37
	v_perm_b32 v99, v86, v90, s37
	v_lshl_add_u64 v[82:83], v[82:83], 0, v[84:85]
	global_store_dwordx4 v[82:83], v[96:99], off nt
	s_ashr_i32 s12, s4, 31
	s_lshr_b32 s12, s12, 26
	s_add_i32 s12, s4, s12
	s_ashr_i32 s49, s12, 6
	s_andn2_b32 s12, s12, 63
	v_or_b32_e32 v146, s12, v1
	v_ashrrev_i32_e32 v147, 31, v146
	s_lshl_b32 s12, s49, 12
	v_lshlrev_b64 v[82:83], 14, v[146:147]
	s_sub_i32 s12, s47, s12
	v_lshl_add_u64 v[82:83], s[8:9], 0, v[82:83]
	s_ashr_i32 s13, s12, 31
	v_lshl_add_u64 v[82:83], s[12:13], 2, v[82:83]
	v_lshl_add_u64 v[82:83], v[82:83], 0, v[68:69]
	v_add_co_u32_e32 v84, vcc, s18, v82
	v_add_u32_e32 v151, s12, v66
	s_nop 0
	v_addc_co_u32_e32 v85, vcc, 0, v83, vcc
	global_load_dwordx4 v[142:145], v[82:83], off nt
	global_load_dwordx4 v[138:141], v[84:85], off nt
	v_add_co_u32_e32 v84, vcc, s20, v82
	v_add_u32_e32 v148, s48, v75
	s_nop 0
	v_addc_co_u32_e32 v85, vcc, 0, v83, vcc
	s_waitcnt lgkmcnt(0)
	v_add_co_u32_e32 v86, vcc, s22, v82
	s_lshl_b32 s12, s49, 13
	s_nop 0
	v_addc_co_u32_e32 v87, vcc, 0, v83, vcc
	global_load_dwordx4 v[134:137], v[84:85], off nt
	global_load_dwordx4 v[130:133], v[86:87], off nt
	v_add_co_u32_e32 v84, vcc, s24, v82
	v_subrev_u32_e32 v150, s12, v148
	s_nop 0
	v_addc_co_u32_e32 v85, vcc, 0, v83, vcc
	v_add_co_u32_e32 v86, vcc, s26, v82
	v_and_b32_e32 v149, 0x7c, v151
	s_nop 0
	v_addc_co_u32_e32 v87, vcc, 0, v83, vcc
	global_load_dwordx4 v[126:129], v[84:85], off nt
	global_load_dwordx4 v[122:125], v[86:87], off nt
	v_add_co_u32_e32 v84, vcc, s28, v82
	s_nop 1
	v_addc_co_u32_e32 v85, vcc, 0, v83, vcc
	v_add_co_u32_e32 v86, vcc, s30, v82
	s_nop 1
	v_addc_co_u32_e32 v87, vcc, 0, v83, vcc
	global_load_dwordx4 v[118:121], v[84:85], off nt
	global_load_dwordx4 v[114:117], v[86:87], off nt
	v_add_co_u32_e32 v84, vcc, s38, v82
	s_nop 1
	v_addc_co_u32_e32 v85, vcc, 0, v83, vcc
	v_add_co_u32_e32 v86, vcc, s39, v82
	s_nop 1
	v_addc_co_u32_e32 v87, vcc, 0, v83, vcc
	global_load_dwordx4 v[110:113], v[84:85], off nt
	global_load_dwordx4 v[106:109], v[86:87], off nt
	v_add_co_u32_e32 v84, vcc, s40, v82
	s_nop 1
	v_addc_co_u32_e32 v85, vcc, 0, v83, vcc
	v_add_co_u32_e32 v86, vcc, s41, v82
	s_nop 1
	v_addc_co_u32_e32 v87, vcc, 0, v83, vcc
	global_load_dwordx4 v[102:105], v[84:85], off nt
	global_load_dwordx4 v[98:101], v[86:87], off nt
	v_add_co_u32_e32 v84, vcc, s42, v82
	s_nop 1
	v_addc_co_u32_e32 v85, vcc, 0, v83, vcc
	v_add_co_u32_e32 v86, vcc, s43, v82
	s_nop 1
	v_addc_co_u32_e32 v87, vcc, 0, v83, vcc
	global_load_dwordx4 v[94:97], v[84:85], off nt
	global_load_dwordx4 v[90:93], v[86:87], off nt
	v_add_co_u32_e32 v84, vcc, 0x38000, v82
	s_nop 1
	v_addc_co_u32_e32 v85, vcc, 0, v83, vcc
	v_add_co_u32_e32 v82, vcc, 0x3c000, v82
	s_nop 1
	v_addc_co_u32_e32 v83, vcc, 0, v83, vcc
	global_load_dwordx4 v[86:89], v[84:85], off nt
	s_nop 0
	global_load_dwordx4 v[82:85], v[82:83], off nt
	s_addk_i32 s48, 0x80
	s_add_i32 s47, s47, 64
	s_add_i32 s4, s4, 1
	v_cmp_lt_i32_e32 vcc, s44, v77
	s_and_saveexec_b64 s[12:13], vcc
	s_xor_b64 s[12:13], exec, s[12:13]
	v_add_u32_e32 v72, 0x7ffff000, v76
	v_and_b32_e32 v72, 0x7fffff00, v72
	v_or3_b32 v72, v73, v72, s45
	s_andn2_saveexec_b64 s[12:13], s[12:13]
	v_and_or_b32 v72, v76, s46, v73
	s_or_b64 exec, exec, s[12:13]
	s_waitcnt vmcnt(35)
; __device__ __forceinline__ unsigned pk4_fp8(float a, float b, float c, float d) {
;     a = __builtin_fminf(__builtin_fmaxf(a, -448.f), 448.f); b = __builtin_fminf(__builtin_fmaxf(b, -448.f), 448.f); c = __builtin_fminf(__builtin_fmaxf(c, -448.f), 448.f); d = __builtin_fminf(__builtin_fmaxf(d, -448.f), 448.f);
;     int w = 0; w = __builtin_amdgcn_cvt_pk_fp8_f32(a, b, w, false); w = __builtin_amdgcn_cvt_pk_fp8_f32(c, d, w, true); return (unsigned)w;
; }
; template <int MODE> __device__ __forceinline__ void cv_finish(const f32x4 (&tv)[16], int K, int nblk, unsigned char* WT, int item, int lane) {
;     const int kb = item / nblk, nb = item - kb * nblk, k0 = 64 * kb + 16 * (lane >> 4), n0 = 64 * nb + 4 * (lane & 15);
;     unsigned D[16];
; #pragma unroll
;     for (int i = 0; i < 16; ++i) { const f32x2 a = (f32x2){tv[i].x, tv[i].y} * (f32x2){1024.f, 1024.f}, b = (f32x2){tv[i].z, tv[i].w} * (f32x2){1024.f, 1024.f};
;         D[i] = pk4_fp8(a.x, a.y, b.x, b.y); }
	v_pk_mul_f32 v[62:63], v[62:63], s[6:7] op_sel_hi:[1,0]
	v_pk_mul_f32 v[64:65], v[64:65], s[6:7] op_sel_hi:[1,0]
	v_med3_f32 v73, v62, s33, v74
	v_med3_f32 v63, v63, s33, v74
	v_mov_b32_e32 v62, v69
	v_cvt_pk_fp8_f32 v62, v73, v63
	v_med3_f32 v63, v64, s33, v74
	v_med3_f32 v64, v65, s33, v74
	s_waitcnt vmcnt(34)
	v_pk_mul_f32 v[58:59], v[58:59], s[6:7] op_sel_hi:[1,0]
	v_cvt_pk_fp8_f32 v62, v63, v64 op_sel:[0,0,1]
	v_med3_f32 v63, v58, s33, v74
	v_med3_f32 v59, v59, s33, v74
	v_mov_b32_e32 v58, v69
	v_cvt_pk_fp8_f32 v58, v63, v59
	v_pk_mul_f32 v[60:61], v[60:61], s[6:7] op_sel_hi:[1,0]
	s_waitcnt vmcnt(33)
	v_pk_mul_f32 v[54:55], v[54:55], s[6:7] op_sel_hi:[1,0]
	v_med3_f32 v59, v60, s33, v74
	v_med3_f32 v60, v61, s33, v74
	v_cvt_pk_fp8_f32 v58, v59, v60 op_sel:[0,0,1]
	v_med3_f32 v59, v54, s33, v74
	v_med3_f32 v55, v55, s33, v74
	v_mov_b32_e32 v54, v69
	v_cvt_pk_fp8_f32 v54, v59, v55
	v_pk_mul_f32 v[56:57], v[56:57], s[6:7] op_sel_hi:[1,0]
	s_waitcnt vmcnt(32)
	v_pk_mul_f32 v[50:51], v[50:51], s[6:7] op_sel_hi:[1,0]
	v_med3_f32 v55, v56, s33, v74
	v_med3_f32 v56, v57, s33, v74
	v_cvt_pk_fp8_f32 v54, v55, v56 op_sel:[0,0,1]
	v_med3_f32 v55, v50, s33, v74
	v_med3_f32 v51, v51, s33, v74
	v_mov_b32_e32 v50, v69
	v_cvt_pk_fp8_f32 v50, v55, v51
	v_pk_mul_f32 v[52:53], v[52:53], s[6:7] op_sel_hi:[1,0]
	s_waitcnt vmcnt(31)
	v_pk_mul_f32 v[46:47], v[46:47], s[6:7] op_sel_hi:[1,0]
	v_med3_f32 v51, v52, s33, v74
	v_med3_f32 v52, v53, s33, v74
	v_cvt_pk_fp8_f32 v50, v51, v52 op_sel:[0,0,1]
	v_med3_f32 v51, v46, s33, v74
	v_med3_f32 v47, v47, s33, v74
	v_mov_b32_e32 v46, v69
	v_cvt_pk_fp8_f32 v46, v51, v47
	v_pk_mul_f32 v[48:49], v[48:49], s[6:7] op_sel_hi:[1,0]
	s_waitcnt vmcnt(30)
	v_pk_mul_f32 v[42:43], v[42:43], s[6:7] op_sel_hi:[1,0]
	v_med3_f32 v47, v48, s33, v74
	v_med3_f32 v48, v49, s33, v74
	v_cvt_pk_fp8_f32 v46, v47, v48 op_sel:[0,0,1]
	v_med3_f32 v47, v42, s33, v74
	v_med3_f32 v43, v43, s33, v74
	v_mov_b32_e32 v42, v69
	v_cvt_pk_fp8_f32 v42, v47, v43
	v_pk_mul_f32 v[44:45], v[44:45], s[6:7] op_sel_hi:[1,0]
	s_waitcnt vmcnt(29)
	v_pk_mul_f32 v[38:39], v[38:39], s[6:7] op_sel_hi:[1,0]
	v_med3_f32 v43, v44, s33, v74
	v_med3_f32 v44, v45, s33, v74
	v_cvt_pk_fp8_f32 v42, v43, v44 op_sel:[0,0,1]
	v_med3_f32 v43, v38, s33, v74
	v_med3_f32 v39, v39, s33, v74
	v_mov_b32_e32 v38, v69
	v_cvt_pk_fp8_f32 v38, v43, v39
	v_pk_mul_f32 v[40:41], v[40:41], s[6:7] op_sel_hi:[1,0]
	s_waitcnt vmcnt(28)
	v_pk_mul_f32 v[34:35], v[34:35], s[6:7] op_sel_hi:[1,0]
	v_med3_f32 v39, v40, s33, v74
	v_med3_f32 v40, v41, s33, v74
	v_cvt_pk_fp8_f32 v38, v39, v40 op_sel:[0,0,1]
	v_med3_f32 v39, v34, s33, v74
	v_med3_f32 v35, v35, s33, v74
	v_mov_b32_e32 v34, v69
	v_cvt_pk_fp8_f32 v34, v39, v35
	v_pk_mul_f32 v[36:37], v[36:37], s[6:7] op_sel_hi:[1,0]
	s_waitcnt vmcnt(27)
	v_pk_mul_f32 v[30:31], v[30:31], s[6:7] op_sel_hi:[1,0]
	v_med3_f32 v35, v36, s33, v74
	v_med3_f32 v36, v37, s33, v74
	v_cvt_pk_fp8_f32 v34, v35, v36 op_sel:[0,0,1]
	v_med3_f32 v35, v30, s33, v74
	v_med3_f32 v31, v31, s33, v74
	v_mov_b32_e32 v30, v69
	v_cvt_pk_fp8_f32 v30, v35, v31
	v_pk_mul_f32 v[32:33], v[32:33], s[6:7] op_sel_hi:[1,0]
	s_waitcnt vmcnt(26)
	v_pk_mul_f32 v[26:27], v[26:27], s[6:7] op_sel_hi:[1,0]
	v_med3_f32 v31, v32, s33, v74
	v_med3_f32 v32, v33, s33, v74
	v_cvt_pk_fp8_f32 v30, v31, v32 op_sel:[0,0,1]
	v_med3_f32 v31, v26, s33, v74
	v_med3_f32 v27, v27, s33, v74
	v_mov_b32_e32 v26, v69
	v_cvt_pk_fp8_f32 v26, v31, v27
	v_pk_mul_f32 v[28:29], v[28:29], s[6:7] op_sel_hi:[1,0]
	s_waitcnt vmcnt(25)
	v_pk_mul_f32 v[22:23], v[22:23], s[6:7] op_sel_hi:[1,0]
	v_med3_f32 v27, v28, s33, v74
	v_med3_f32 v28, v29, s33, v74
	v_cvt_pk_fp8_f32 v26, v27, v28 op_sel:[0,0,1]
	v_med3_f32 v27, v22, s33, v74
	v_med3_f32 v23, v23, s33, v74
	v_mov_b32_e32 v22, v69
	v_cvt_pk_fp8_f32 v22, v27, v23
	v_pk_mul_f32 v[24:25], v[24:25], s[6:7] op_sel_hi:[1,0]
	s_waitcnt vmcnt(24)
	v_pk_mul_f32 v[18:19], v[18:19], s[6:7] op_sel_hi:[1,0]
	v_med3_f32 v23, v24, s33, v74
	v_med3_f32 v24, v25, s33, v74
	v_cvt_pk_fp8_f32 v22, v23, v24 op_sel:[0,0,1]
	v_med3_f32 v23, v18, s33, v74
	v_med3_f32 v19, v19, s33, v74
	v_mov_b32_e32 v18, v69
	v_cvt_pk_fp8_f32 v18, v23, v19
	v_pk_mul_f32 v[20:21], v[20:21], s[6:7] op_sel_hi:[1,0]
	s_waitcnt vmcnt(23)
	v_pk_mul_f32 v[14:15], v[14:15], s[6:7] op_sel_hi:[1,0]
	v_med3_f32 v19, v20, s33, v74
	v_med3_f32 v20, v21, s33, v74
	v_cvt_pk_fp8_f32 v18, v19, v20 op_sel:[0,0,1]
	v_med3_f32 v19, v14, s33, v74
	v_med3_f32 v15, v15, s33, v74
	v_mov_b32_e32 v14, v69
	v_cvt_pk_fp8_f32 v14, v19, v15
	v_pk_mul_f32 v[16:17], v[16:17], s[6:7] op_sel_hi:[1,0]
	s_waitcnt vmcnt(22)
	v_pk_mul_f32 v[10:11], v[10:11], s[6:7] op_sel_hi:[1,0]
	v_med3_f32 v15, v16, s33, v74
	v_med3_f32 v16, v17, s33, v74
	v_cvt_pk_fp8_f32 v14, v15, v16 op_sel:[0,0,1]
	v_med3_f32 v15, v10, s33, v74
	v_med3_f32 v11, v11, s33, v74
	v_mov_b32_e32 v10, v69
	v_cvt_pk_fp8_f32 v10, v15, v11
	v_pk_mul_f32 v[12:13], v[12:13], s[6:7] op_sel_hi:[1,0]
	s_waitcnt vmcnt(21)
	v_pk_mul_f32 v[6:7], v[6:7], s[6:7] op_sel_hi:[1,0]
	v_med3_f32 v11, v12, s33, v74
	v_med3_f32 v12, v13, s33, v74
	v_cvt_pk_fp8_f32 v10, v11, v12 op_sel:[0,0,1]
	v_med3_f32 v11, v6, s33, v74
	v_med3_f32 v7, v7, s33, v74
	v_mov_b32_e32 v6, v69
	v_cvt_pk_fp8_f32 v6, v11, v7
	v_pk_mul_f32 v[8:9], v[8:9], s[6:7] op_sel_hi:[1,0]
	s_waitcnt vmcnt(20)
; template <int MODE> __device__ __forceinline__ int drow(int n) {
;     if (MODE == 1) { const int h = n / 192, nl = n - h * 192; return nl < 128 ? n : h * 192 + 128 + ((nl - 128) & 31) * 2 + ((nl - 128) >> 5); }
;     if (MODE == 2) { return n < FF ? ((n >> 7) * 256 + (n & 127)) : (((n - FF) >> 7) * 256 + 128 + ((n - FF) & 127)); }
;     return n;
; }
; template <int MODE> __device__ __forceinline__ void cv_finish(const f32x4 (&tv)[16], int K, int nblk, unsigned char* WT, int item, int lane) {
;     const int kb = item / nblk, nb = item - kb * nblk, k0 = 64 * kb + 16 * (lane >> 4), n0 = 64 * nb + 4 * (lane & 15);
;     unsigned D[16];
; #pragma unroll
;     for (int i = 0; i < 16; ++i) { const f32x2 a = (f32x2){tv[i].x, tv[i].y} * (f32x2){1024.f, 1024.f}, b = (f32x2){tv[i].z, tv[i].w} * (f32x2){1024.f, 1024.f};
;         D[i] = pk4_fp8(a.x, a.y, b.x, b.y); }
;     unsigned O[4][4];
; #pragma unroll
;     for (int q = 0; q < 4; ++q) { const unsigned a = D[4 * q], b = D[4 * q + 1], c = D[4 * q + 2], d = D[4 * q + 3];
;         const unsigned t0 = __builtin_amdgcn_perm(b, a, 0x05010400u), t1 = __builtin_amdgcn_perm(b, a, 0x07030602u), u0 = __builtin_amdgcn_perm(d, c, 0x05010400u), u1 = __builtin_amdgcn_perm(d, c, 0x07030602u);
;         O[0][q] = __builtin_amdgcn_perm(u0, t0, 0x05040100u); O[1][q] = __builtin_amdgcn_perm(u0, t0, 0x07060302u); O[2][q] = __builtin_amdgcn_perm(u1, t1, 0x05040100u); O[3][q] = __builtin_amdgcn_perm(u1, t1, 0x07060302u); }
; #pragma unroll
;     for (int j = 0; j < 4; ++j) { u32x4 o; o.x = O[j][0]; o.y = O[j][1]; o.z = O[j][2]; o.w = O[j][3];
;         __builtin_nontemporal_store(o, (u32x4*)(WT + (size_t)drow<MODE>(n0 + j) * K + k0)); }
; }
	v_pk_mul_f32 v[2:3], v[2:3], s[6:7] op_sel_hi:[1,0]
	v_med3_f32 v7, v8, s33, v74
	v_med3_f32 v8, v9, s33, v74
	v_cvt_pk_fp8_f32 v6, v7, v8 op_sel:[0,0,1]
	v_med3_f32 v2, v2, s33, v74
	v_med3_f32 v3, v3, s33, v74
	v_mov_b32_e32 v7, v69
	v_cvt_pk_fp8_f32 v7, v2, v3
	v_pk_mul_f32 v[2:3], v[4:5], s[6:7] op_sel_hi:[1,0]
	v_ashrrev_i32_e32 v73, 31, v72
	v_med3_f32 v2, v2, s33, v74
	v_med3_f32 v3, v3, s33, v74
	v_cvt_pk_fp8_f32 v7, v2, v3 op_sel:[0,0,1]
	v_perm_b32 v5, v58, v62, s34
	v_perm_b32 v8, v50, v54, s34
	v_perm_b32 v9, v42, v46, s34
	v_perm_b32 v11, v34, v38, s34
	v_perm_b32 v12, v26, v30, s34
	v_perm_b32 v13, v18, v22, s34
	v_perm_b32 v15, v10, v14, s34
	v_perm_b32 v16, v7, v6, s34
	v_lshl_add_u64 v[2:3], s[10:11], 0, v[70:71]
	v_lshlrev_b64 v[20:21], 11, v[72:73]
	v_add_u32_e32 v4, 1, v77
	v_perm_b32 v78, v8, v5, s36
	v_perm_b32 v79, v11, v9, s36
	v_perm_b32 v80, v13, v12, s36
	v_perm_b32 v81, v16, v15, s36
	v_lshl_add_u64 v[20:21], v[2:3], 0, v[20:21]
	v_cmp_lt_i32_e32 vcc, s44, v4
	v_and_b32_e32 v17, 0x7d, v4
	global_store_dwordx4 v[20:21], v[78:81], off nt
	s_and_saveexec_b64 s[12:13], vcc
	s_xor_b64 s[12:13], exec, s[12:13]
	v_add_u32_e32 v4, 0x7ffff002, v76
	v_and_b32_e32 v4, 0x7fffff00, v4
	v_or3_b32 v4, v17, v4, s45
	s_andn2_saveexec_b64 s[12:13], s[12:13]
	v_add_u32_e32 v4, 2, v76
	v_and_or_b32 v4, v4, s46, v17
	s_or_b64 exec, exec, s[12:13]
	v_perm_b32 v70, v8, v5, s37
	v_ashrrev_i32_e32 v5, 31, v4
	v_lshlrev_b64 v[4:5], 11, v[4:5]
	v_perm_b32 v71, v11, v9, s37
	v_perm_b32 v72, v13, v12, s37
	v_perm_b32 v73, v16, v15, s37
	v_lshl_add_u64 v[4:5], v[2:3], 0, v[4:5]
	global_store_dwordx4 v[4:5], v[70:73], off nt
	v_add_u32_e32 v4, 2, v77
	v_cmp_lt_i32_e32 vcc, s44, v4
	v_and_b32_e32 v5, 0x7e, v4
	s_and_saveexec_b64 s[12:13], vcc
	s_xor_b64 s[12:13], exec, s[12:13]
	v_add_u32_e32 v4, 0x7ffff004, v76
	v_and_b32_e32 v4, 0x7fffff00, v4
	v_or3_b32 v4, v5, v4, s45
	s_andn2_saveexec_b64 s[12:13], s[12:13]
	v_add_u32_e32 v4, 4, v76
	v_and_or_b32 v4, v4, s46, v5
	s_or_b64 exec, exec, s[12:13]
	v_ashrrev_i32_e32 v5, 31, v4
	v_perm_b32 v8, v58, v62, s35
	v_perm_b32 v9, v50, v54, s35
	v_perm_b32 v11, v42, v46, s35
	v_perm_b32 v12, v34, v38, s35
	v_perm_b32 v13, v26, v30, s35
	v_perm_b32 v15, v18, v22, s35
	v_perm_b32 v10, v10, v14, s35
	v_perm_b32 v6, v7, v6, s35
	v_lshlrev_b64 v[4:5], 11, v[4:5]
	v_perm_b32 v16, v9, v8, s36
	v_perm_b32 v17, v12, v11, s36
	v_perm_b32 v18, v15, v13, s36
	v_perm_b32 v19, v6, v10, s36
	v_lshl_add_u64 v[4:5], v[2:3], 0, v[4:5]
	global_store_dwordx4 v[4:5], v[16:19], off nt
	v_add_u32_e32 v4, 3, v77
	v_cmp_lt_i32_e32 vcc, s44, v4
	v_and_b32_e32 v5, 0x7f, v4
	s_and_saveexec_b64 s[12:13], vcc
	s_xor_b64 s[12:13], exec, s[12:13]
	v_add_u32_e32 v4, 0x7ffff006, v76
	v_and_b32_e32 v4, 0x7fffff00, v4
	v_or3_b32 v4, v5, v4, s45
	s_andn2_saveexec_b64 s[12:13], s[12:13]
	v_add_u32_e32 v4, 6, v76
	v_and_or_b32 v4, v4, s46, v5
	s_or_b64 exec, exec, s[12:13]
	v_ashrrev_i32_e32 v5, 31, v4
	v_lshlrev_b64 v[4:5], 11, v[4:5]
	v_perm_b32 v16, v9, v8, s37
	v_perm_b32 v17, v12, v11, s37
	v_perm_b32 v18, v15, v13, s37
	v_perm_b32 v19, v6, v10, s37
	v_lshl_add_u64 v[2:3], v[2:3], 0, v[4:5]
	global_store_dwordx4 v[2:3], v[16:19], off nt
	v_cmp_lt_i32_e32 vcc, s44, v151
	s_and_saveexec_b64 s[12:13], vcc
	s_xor_b64 s[12:13], exec, s[12:13]
	v_add_u32_e32 v148, 0x7ffff000, v150
	v_and_b32_e32 v148, 0x7fffff00, v148
	v_or3_b32 v148, v149, v148, s45
	s_andn2_saveexec_b64 s[12:13], s[12:13]
	v_and_or_b32 v148, v150, s46, v149
	s_or_b64 exec, exec, s[12:13]
	s_waitcnt vmcnt(19)
	v_pk_mul_f32 v[142:143], v[142:143], s[6:7] op_sel_hi:[1,0]
	v_pk_mul_f32 v[144:145], v[144:145], s[6:7] op_sel_hi:[1,0]
	v_med3_f32 v149, v142, s33, v74
	v_med3_f32 v143, v143, s33, v74
	v_mov_b32_e32 v142, v69
	v_cvt_pk_fp8_f32 v142, v149, v143
	v_med3_f32 v143, v144, s33, v74
	v_med3_f32 v144, v145, s33, v74
	s_waitcnt vmcnt(18)
	v_pk_mul_f32 v[138:139], v[138:139], s[6:7] op_sel_hi:[1,0]
	v_cvt_pk_fp8_f32 v142, v143, v144 op_sel:[0,0,1]
	v_med3_f32 v143, v138, s33, v74
	v_med3_f32 v139, v139, s33, v74
	v_mov_b32_e32 v138, v69
	v_cvt_pk_fp8_f32 v138, v143, v139
	v_pk_mul_f32 v[140:141], v[140:141], s[6:7] op_sel_hi:[1,0]
	s_waitcnt vmcnt(17)
	v_pk_mul_f32 v[134:135], v[134:135], s[6:7] op_sel_hi:[1,0]
	v_med3_f32 v139, v140, s33, v74
	v_med3_f32 v140, v141, s33, v74
	v_cvt_pk_fp8_f32 v138, v139, v140 op_sel:[0,0,1]
	v_med3_f32 v139, v134, s33, v74
	v_med3_f32 v135, v135, s33, v74
	v_mov_b32_e32 v134, v69
	v_cvt_pk_fp8_f32 v134, v139, v135
	v_pk_mul_f32 v[136:137], v[136:137], s[6:7] op_sel_hi:[1,0]
	s_waitcnt vmcnt(16)
	v_pk_mul_f32 v[130:131], v[130:131], s[6:7] op_sel_hi:[1,0]
	v_med3_f32 v135, v136, s33, v74
	v_med3_f32 v136, v137, s33, v74
	v_cvt_pk_fp8_f32 v134, v135, v136 op_sel:[0,0,1]
	v_med3_f32 v135, v130, s33, v74
	v_med3_f32 v131, v131, s33, v74
	v_mov_b32_e32 v130, v69
	v_cvt_pk_fp8_f32 v130, v135, v131
	v_pk_mul_f32 v[132:133], v[132:133], s[6:7] op_sel_hi:[1,0]
	s_waitcnt vmcnt(15)
	v_pk_mul_f32 v[126:127], v[126:127], s[6:7] op_sel_hi:[1,0]
	v_med3_f32 v131, v132, s33, v74
	v_med3_f32 v132, v133, s33, v74
	v_cvt_pk_fp8_f32 v130, v131, v132 op_sel:[0,0,1]
	v_med3_f32 v131, v126, s33, v74
	v_med3_f32 v127, v127, s33, v74
	v_mov_b32_e32 v126, v69
	v_cvt_pk_fp8_f32 v126, v131, v127
	v_pk_mul_f32 v[128:129], v[128:129], s[6:7] op_sel_hi:[1,0]
	s_waitcnt vmcnt(14)
	v_pk_mul_f32 v[122:123], v[122:123], s[6:7] op_sel_hi:[1,0]
	v_med3_f32 v127, v128, s33, v74
	v_med3_f32 v128, v129, s33, v74
	v_cvt_pk_fp8_f32 v126, v127, v128 op_sel:[0,0,1]
	v_med3_f32 v127, v122, s33, v74
	v_med3_f32 v123, v123, s33, v74
	v_mov_b32_e32 v122, v69
	v_cvt_pk_fp8_f32 v122, v127, v123
	v_pk_mul_f32 v[124:125], v[124:125], s[6:7] op_sel_hi:[1,0]
	s_waitcnt vmcnt(13)
; template <int MODE> __device__ __forceinline__ int drow(int n) {
;     if (MODE == 1) { const int h = n / 192, nl = n - h * 192; return nl < 128 ? n : h * 192 + 128 + ((nl - 128) & 31) * 2 + ((nl - 128) >> 5); }
;     if (MODE == 2) { return n < FF ? ((n >> 7) * 256 + (n & 127)) : (((n - FF) >> 7) * 256 + 128 + ((n - FF) & 127)); }
;     return n;
; }
; template <int MODE> __device__ __forceinline__ void cv_finish(const f32x4 (&tv)[16], int K, int nblk, unsigned char* WT, int item, int lane) {
;     const int kb = item / nblk, nb = item - kb * nblk, k0 = 64 * kb + 16 * (lane >> 4), n0 = 64 * nb + 4 * (lane & 15);
;     unsigned D[16];
; #pragma unroll
;     for (int i = 0; i < 16; ++i) { const f32x2 a = (f32x2){tv[i].x, tv[i].y} * (f32x2){1024.f, 1024.f}, b = (f32x2){tv[i].z, tv[i].w} * (f32x2){1024.f, 1024.f};
;         D[i] = pk4_fp8(a.x, a.y, b.x, b.y); }
;     unsigned O[4][4];
; #pragma unroll
;     for (int q = 0; q < 4; ++q) { const unsigned a = D[4 * q], b = D[4 * q + 1], c = D[4 * q + 2], d = D[4 * q + 3];
;         const unsigned t0 = __builtin_amdgcn_perm(b, a, 0x05010400u), t1 = __builtin_amdgcn_perm(b, a, 0x07030602u), u0 = __builtin_amdgcn_perm(d, c, 0x05010400u), u1 = __builtin_amdgcn_perm(d, c, 0x07030602u);
;         O[0][q] = __builtin_amdgcn_perm(u0, t0, 0x05040100u); O[1][q] = __builtin_amdgcn_perm(u0, t0, 0x07060302u); O[2][q] = __builtin_amdgcn_perm(u1, t1, 0x05040100u); O[3][q] = __builtin_amdgcn_perm(u1, t1, 0x07060302u); }
; #pragma unroll
;     for (int j = 0; j < 4; ++j) { u32x4 o; o.x = O[j][0]; o.y = O[j][1]; o.z = O[j][2]; o.w = O[j][3];
;         __builtin_nontemporal_store(o, (u32x4*)(WT + (size_t)drow<MODE>(n0 + j) * K + k0)); }
; }
; template <int MODE> __device__ __forceinline__ void cv_run4(const float* W, int K, int N, unsigned char* WT, int item0, int lane) {
;     const int nblk = N / 64; f32x4 ta[16];
; #pragma unroll 1
;     for (int j = 0; j < 4; ++j) { cv_load(W, N, nblk, item0 + j, lane, ta); cv_finish<MODE>(ta, K, nblk, WT, item0 + j, lane); }
	v_pk_mul_f32 v[118:119], v[118:119], s[6:7] op_sel_hi:[1,0]
	v_med3_f32 v123, v124, s33, v74
	v_med3_f32 v124, v125, s33, v74
	v_cvt_pk_fp8_f32 v122, v123, v124 op_sel:[0,0,1]
	v_med3_f32 v123, v118, s33, v74
	v_med3_f32 v119, v119, s33, v74
	v_mov_b32_e32 v118, v69
	v_cvt_pk_fp8_f32 v118, v123, v119
	v_pk_mul_f32 v[120:121], v[120:121], s[6:7] op_sel_hi:[1,0]
	s_waitcnt vmcnt(12)
	v_pk_mul_f32 v[114:115], v[114:115], s[6:7] op_sel_hi:[1,0]
	v_med3_f32 v119, v120, s33, v74
	v_med3_f32 v120, v121, s33, v74
	v_cvt_pk_fp8_f32 v118, v119, v120 op_sel:[0,0,1]
	v_med3_f32 v119, v114, s33, v74
	v_med3_f32 v115, v115, s33, v74
	v_mov_b32_e32 v114, v69
	v_cvt_pk_fp8_f32 v114, v119, v115
	v_pk_mul_f32 v[116:117], v[116:117], s[6:7] op_sel_hi:[1,0]
	s_waitcnt vmcnt(11)
	v_pk_mul_f32 v[110:111], v[110:111], s[6:7] op_sel_hi:[1,0]
	v_med3_f32 v115, v116, s33, v74
	v_med3_f32 v116, v117, s33, v74
	v_cvt_pk_fp8_f32 v114, v115, v116 op_sel:[0,0,1]
	v_med3_f32 v115, v110, s33, v74
	v_med3_f32 v111, v111, s33, v74
	v_mov_b32_e32 v110, v69
	v_cvt_pk_fp8_f32 v110, v115, v111
	v_pk_mul_f32 v[112:113], v[112:113], s[6:7] op_sel_hi:[1,0]
	s_waitcnt vmcnt(10)
	v_pk_mul_f32 v[106:107], v[106:107], s[6:7] op_sel_hi:[1,0]
	v_med3_f32 v111, v112, s33, v74
	v_med3_f32 v112, v113, s33, v74
	v_cvt_pk_fp8_f32 v110, v111, v112 op_sel:[0,0,1]
	v_med3_f32 v111, v106, s33, v74
	v_med3_f32 v107, v107, s33, v74
	v_mov_b32_e32 v106, v69
	v_cvt_pk_fp8_f32 v106, v111, v107
	v_pk_mul_f32 v[108:109], v[108:109], s[6:7] op_sel_hi:[1,0]
	s_waitcnt vmcnt(9)
	v_pk_mul_f32 v[102:103], v[102:103], s[6:7] op_sel_hi:[1,0]
	v_med3_f32 v107, v108, s33, v74
	v_med3_f32 v108, v109, s33, v74
	v_cvt_pk_fp8_f32 v106, v107, v108 op_sel:[0,0,1]
	v_med3_f32 v107, v102, s33, v74
	v_med3_f32 v103, v103, s33, v74
	v_mov_b32_e32 v102, v69
	v_cvt_pk_fp8_f32 v102, v107, v103
	v_pk_mul_f32 v[104:105], v[104:105], s[6:7] op_sel_hi:[1,0]
	s_waitcnt vmcnt(8)
	v_pk_mul_f32 v[98:99], v[98:99], s[6:7] op_sel_hi:[1,0]
	v_med3_f32 v103, v104, s33, v74
	v_med3_f32 v104, v105, s33, v74
	v_cvt_pk_fp8_f32 v102, v103, v104 op_sel:[0,0,1]
	v_med3_f32 v103, v98, s33, v74
	v_med3_f32 v99, v99, s33, v74
	v_mov_b32_e32 v98, v69
	v_cvt_pk_fp8_f32 v98, v103, v99
	v_pk_mul_f32 v[100:101], v[100:101], s[6:7] op_sel_hi:[1,0]
	s_waitcnt vmcnt(7)
	v_pk_mul_f32 v[94:95], v[94:95], s[6:7] op_sel_hi:[1,0]
	v_med3_f32 v99, v100, s33, v74
	v_med3_f32 v100, v101, s33, v74
	v_cvt_pk_fp8_f32 v98, v99, v100 op_sel:[0,0,1]
	v_med3_f32 v99, v94, s33, v74
	v_med3_f32 v95, v95, s33, v74
	v_mov_b32_e32 v94, v69
	v_cvt_pk_fp8_f32 v94, v99, v95
	v_pk_mul_f32 v[96:97], v[96:97], s[6:7] op_sel_hi:[1,0]
	s_waitcnt vmcnt(6)
	v_pk_mul_f32 v[90:91], v[90:91], s[6:7] op_sel_hi:[1,0]
	v_med3_f32 v95, v96, s33, v74
	v_med3_f32 v96, v97, s33, v74
	v_cvt_pk_fp8_f32 v94, v95, v96 op_sel:[0,0,1]
	v_med3_f32 v95, v90, s33, v74
	v_med3_f32 v91, v91, s33, v74
	v_mov_b32_e32 v90, v69
	v_cvt_pk_fp8_f32 v90, v95, v91
	v_pk_mul_f32 v[92:93], v[92:93], s[6:7] op_sel_hi:[1,0]
	s_waitcnt vmcnt(5)
	v_pk_mul_f32 v[86:87], v[86:87], s[6:7] op_sel_hi:[1,0]
	v_med3_f32 v91, v92, s33, v74
	v_med3_f32 v92, v93, s33, v74
	v_cvt_pk_fp8_f32 v90, v91, v92 op_sel:[0,0,1]
	v_med3_f32 v91, v86, s33, v74
	v_med3_f32 v87, v87, s33, v74
	v_mov_b32_e32 v86, v69
	v_cvt_pk_fp8_f32 v86, v91, v87
	v_pk_mul_f32 v[88:89], v[88:89], s[6:7] op_sel_hi:[1,0]
	s_waitcnt vmcnt(4)
	v_pk_mul_f32 v[82:83], v[82:83], s[6:7] op_sel_hi:[1,0]
	v_med3_f32 v87, v88, s33, v74
	v_med3_f32 v88, v89, s33, v74
	v_cvt_pk_fp8_f32 v86, v87, v88 op_sel:[0,0,1]
	v_med3_f32 v82, v82, s33, v74
	v_med3_f32 v83, v83, s33, v74
	v_mov_b32_e32 v87, v69
	v_cvt_pk_fp8_f32 v87, v82, v83
	v_pk_mul_f32 v[82:83], v[84:85], s[6:7] op_sel_hi:[1,0]
	v_ashrrev_i32_e32 v149, 31, v148
	v_med3_f32 v82, v82, s33, v74
	v_med3_f32 v83, v83, s33, v74
	v_cvt_pk_fp8_f32 v87, v82, v83 op_sel:[0,0,1]
	v_perm_b32 v85, v138, v142, s34
	v_perm_b32 v88, v130, v134, s34
	v_perm_b32 v89, v122, v126, s34
	v_perm_b32 v91, v114, v118, s34
	v_perm_b32 v92, v106, v110, s34
	v_perm_b32 v93, v98, v102, s34
	v_perm_b32 v95, v90, v94, s34
	v_perm_b32 v96, v87, v86, s34
	v_lshl_add_u64 v[82:83], s[10:11], 0, v[146:147]
	v_lshlrev_b64 v[100:101], 11, v[148:149]
	v_add_u32_e32 v84, 1, v151
	v_perm_b32 v152, v88, v85, s36
	v_perm_b32 v153, v91, v89, s36
	v_perm_b32 v154, v93, v92, s36
	v_perm_b32 v155, v96, v95, s36
	v_lshl_add_u64 v[100:101], v[82:83], 0, v[100:101]
	v_cmp_lt_i32_e32 vcc, s44, v84
	v_and_b32_e32 v97, 0x7d, v84
	global_store_dwordx4 v[100:101], v[152:155], off nt
	s_and_saveexec_b64 s[12:13], vcc
	s_xor_b64 s[12:13], exec, s[12:13]
	v_add_u32_e32 v84, 0x7ffff002, v150
	v_and_b32_e32 v84, 0x7fffff00, v84
	v_or3_b32 v84, v97, v84, s45
	s_andn2_saveexec_b64 s[12:13], s[12:13]
	v_add_u32_e32 v84, 2, v150
	v_and_or_b32 v84, v84, s46, v97
	s_or_b64 exec, exec, s[12:13]
	v_perm_b32 v146, v88, v85, s37
	v_ashrrev_i32_e32 v85, 31, v84
	v_lshlrev_b64 v[84:85], 11, v[84:85]
	v_perm_b32 v147, v91, v89, s37
	v_perm_b32 v148, v93, v92, s37
	v_perm_b32 v149, v96, v95, s37
	v_lshl_add_u64 v[84:85], v[82:83], 0, v[84:85]
	global_store_dwordx4 v[84:85], v[146:149], off nt
	v_add_u32_e32 v84, 2, v151
	v_cmp_lt_i32_e32 vcc, s44, v84
	v_and_b32_e32 v85, 0x7e, v84
	s_and_saveexec_b64 s[12:13], vcc
	s_xor_b64 s[12:13], exec, s[12:13]
	v_add_u32_e32 v84, 0x7ffff004, v150
	v_and_b32_e32 v84, 0x7fffff00, v84
	v_or3_b32 v84, v85, v84, s45
	s_andn2_saveexec_b64 s[12:13], s[12:13]
	v_add_u32_e32 v84, 4, v150
	v_and_or_b32 v84, v84, s46, v85
	s_or_b64 exec, exec, s[12:13]
	v_ashrrev_i32_e32 v85, 31, v84
	v_perm_b32 v88, v138, v142, s35
	v_perm_b32 v89, v130, v134, s35
	v_perm_b32 v91, v122, v126, s35
	v_perm_b32 v92, v114, v118, s35
	v_perm_b32 v93, v106, v110, s35
	v_perm_b32 v95, v98, v102, s35
	v_perm_b32 v90, v90, v94, s35
	v_perm_b32 v86, v87, v86, s35
	v_lshlrev_b64 v[84:85], 11, v[84:85]
	v_perm_b32 v96, v89, v88, s36
	v_perm_b32 v97, v92, v91, s36
	v_perm_b32 v98, v95, v93, s36
	v_perm_b32 v99, v86, v90, s36
	v_lshl_add_u64 v[84:85], v[82:83], 0, v[84:85]
	global_store_dwordx4 v[84:85], v[96:99], off nt
	v_add_u32_e32 v84, 3, v151
	v_cmp_lt_i32_e32 vcc, s44, v84
	v_and_b32_e32 v85, 0x7f, v84
	s_and_saveexec_b64 s[12:13], vcc
	s_xor_b64 s[12:13], exec, s[12:13]
	v_add_u32_e32 v84, 0x7ffff006, v150
	v_and_b32_e32 v84, 0x7fffff00, v84
	v_or3_b32 v84, v85, v84, s45
	s_andn2_saveexec_b64 s[12:13], s[12:13]
	v_add_u32_e32 v84, 6, v150
	v_and_or_b32 v84, v84, s46, v85
	s_or_b64 exec, exec, s[12:13]
	v_ashrrev_i32_e32 v85, 31, v84
	v_lshlrev_b64 v[84:85], 11, v[84:85]
	v_perm_b32 v96, v89, v88, s37
	v_perm_b32 v97, v92, v91, s37
	v_perm_b32 v98, v95, v93, s37
	v_perm_b32 v99, v86, v90, s37
	v_lshl_add_u64 v[82:83], v[82:83], 0, v[84:85]
	global_store_dwordx4 v[82:83], v[96:99], off nt
	s_cmpk_eq_i32 s48, 0x200
	s_cbranch_scc0 .LBB0_984
	s_branch .LBB0_970
